# m0 save/restore removed around every LDS-DMA piece; accumulator zero-init with v_mov_b64
# speedup vs baseline: 1.0057x; 1.0057x over previous
; __device__ __forceinline__ int opaque_tid(int wave) { int l; asm volatile("v_mbcnt_lo_u32_b32 %0, -1, 0\n\tv_mbcnt_hi_u32_b32 %0, -1, %0" : "=v"(l)); return wave * 64 + l; }
; template <class Epi, class Sched, bool ALIGN_EPI, bool FP8 = false>
; __device__ __forceinline__ void gemm_phase(LAS unsigned char* lds, const bf16_t* A, const bf16_t* Bt, const int K, const Sched& S, const Epi& E, const int wave_in) {
;     const int tid = opaque_tid(wave_in); const int wid = __builtin_amdgcn_readfirstlane(tid >> 6), lane = tid & 63, wr = wid >> 2, wc = wid & 3, fr = lane & 15, fq = lane >> 4;
;     const int nt = K / BK;
;     int sR[2], sC[2]; unsigned voffB[2];
; #pragma unroll
;     for (int i = 0; i < 2; ++i) { stage_rc(tid * 16 + i * 8192, sR[i], sC[i]); const int Rb = Epi::PERM ? ((sR[i] & ~31) + perm32(sR[i] & 31)) : sR[i];
;         voffB[i] = (unsigned)(Rb * K + sC[i]) * 2u; }
;     const size_t kstep = (size_t)(BK * 2);
;     const size_t hstep = (size_t)HALF * K * 2;
;     const unsigned ldsw = (unsigned)wid * 1024u;
;     const unsigned ldsbase = (unsigned)__builtin_amdgcn_readfirstlane((int)((unsigned)(uintptr_t)lds + ldsw));
;     const int aoff = lds_byte(wr * 64 + fr, fq * 8), boff = lds_byte(wc * 32 + fr, fq * 8);
;     ...
;     Unit cur, nxt; int ui = 0;
;     if (!S.next(0, cur)) return;
;     f32x4 acc[2][2][4][2];
; #pragma unroll
;     for (int a = 0; a < 2; ++a)
; #pragma unroll
;         for (int b = 0; b < 2; ++b)
; #pragma unroll
;             for (int m = 0; m < 4; ++m)
; #pragma unroll
;                 for (int n = 0; n < 2; ++n) acc[a][b][m][n] = (f32x4){0.f, 0.f, 0.f, 0.f};
;     bf16x8 At[4][2], B0[2][2], B1[2][2];
;     const int sclW = W8_E8M0, sclA = A8_E8M0;
;     unsigned vA[2][2], vN[2][2];
;     PG8_AOFF(vA, cur);
;     const char* const cA = (const char*)A;
;     const char* cB = (const char*)Bt + S.b_off(cur) * 2;
;     PG8_STAGE(PG8_SB(0, 0), cB, voffB[0], voffB[1]); PG8_STAGE(PG8_SB(0, 1), cB + hstep, voffB[0], voffB[1]); PG8_STAGE(PG8_SA(0, 0), cA, vA[0][0], vA[0][1]); PG8_STAGE(PG8_SA(0, 1), cA, vA[1][0], vA[1][1]);
;     if (wr == 1) PG8_BAR;
;     PG8_WAIT_V(2); PG8_BAR;
;     PG8_STAGE(PG8_SB(1, 0), cB + kstep, voffB[0], voffB[1]); PG8_STAGE(PG8_SA(1, 0), cA + kstep, vA[0][0], vA[0][1]); PG8_STAGE(PG8_SB(1, 1), cB + hstep + kstep, voffB[0], voffB[1]);
;     PG8_WAIT_V(6); PG8_BAR;
.LBB0_237:
	s_andn2_b64 vcc, exec, s[0:1]
	s_cbranch_vccnz .LBB0_287
	v_ashrrev_i32_e32 v4, 31, v0
	v_lshrrev_b32_e32 v4, 26, v4
	v_lshlrev_b32_e32 v3, 4, v0
	v_add_u32_e32 v4, v0, v4
	v_bfe_i32 v0, v0, 27, 1
	v_lshrrev_b32_e32 v0, 22, v0
	v_add_u32_e32 v0, v3, v0
	v_and_b32_e32 v0, 0xfffffc00, v0
	v_sub_u32_e32 v0, v3, v0
	v_lshrrev_b32_e32 v5, 4, v0
	v_bitop3_b32 v0, v5, v0, 32 bitop3:0x6c
	s_waitcnt vmcnt(5)
	v_ashrrev_i32_e32 v6, 31, v0
	v_ashrrev_i32_e32 v4, 6, v4
	v_lshrrev_b32_e32 v6, 26, v6
	v_lshlrev_b32_e32 v5, 3, v4
	v_add_u32_e32 v6, v0, v6
	v_and_b32_e32 v5, -16, v5
	v_ashrrev_i32_e32 v7, 6, v6
	v_and_b32_e32 v6, 0xc0, v6
	v_add_u32_e32 v5, v7, v5
	v_sub_u32_e32 v0, v0, v6
	v_lshlrev_b32_e32 v4, 5, v4
	v_ashrrev_i16_sdwa v0, v185, sext(v0) dst_sel:DWORD dst_unused:UNUSED_PAD src0_sel:DWORD src1_sel:BYTE_0
	v_lshlrev_b32_e32 v6, 1, v5
	v_lshrrev_b32_e32 v8, 2, v5
	v_and_b32_e32 v7, 3, v7
	s_mov_b32 s1, 0x1fffe0
	v_and_b32_e32 v4, 32, v4
	v_bfe_i32 v0, v0, 0, 16
	v_and_b32_e32 v6, 24, v6
	v_and_b32_e32 v8, 4, v8
	v_and_or_b32 v7, v5, s1, v7
	v_or3_b32 v6, v7, v8, v6
	v_add_lshl_u32 v4, v4, v0, 1
	v_add_u32_e32 v3, 0x2000, v3
	v_lshl_add_u32 v0, v6, 11, v4
	v_ashrrev_i32_e32 v6, 31, v3
	v_lshrrev_b32_e32 v6, 22, v6
	v_add_u32_e32 v6, v3, v6
	v_ashrrev_i32_e32 v6, 10, v6
	v_mul_i32_i24_e32 v7, 0x400, v6
	v_sub_u32_e32 v3, v3, v7
	v_lshrrev_b32_e32 v7, 4, v3
	v_bitop3_b32 v3, v7, v3, 32 bitop3:0x6c
	v_ashrrev_i32_e32 v8, 31, v3
	v_lshrrev_b32_e32 v8, 26, v8
	v_lshlrev_b32_e32 v7, 3, v6
	v_add_u32_e32 v8, v3, v8
	v_and_b32_e32 v7, -16, v7
	v_ashrrev_i32_e32 v9, 6, v8
	v_and_b32_e32 v8, 0xc0, v8
	s_add_u32 s24, s94, 0x3900000
	v_add_u32_e32 v7, v9, v7
	v_sub_u32_e32 v3, v3, v8
	v_and_b32_e32 v9, 3, v9
	s_addc_u32 s25, s95, 0
	v_lshlrev_b32_e32 v6, 5, v6
	v_ashrrev_i16_sdwa v3, v185, sext(v3) dst_sel:DWORD dst_unused:UNUSED_PAD src0_sel:DWORD src1_sel:BYTE_0
	v_and_or_b32 v9, v7, s1, v9
	s_lshl_b32 s1, s3, 10
	s_ashr_i32 s0, s2, 8
	v_and_b32_e32 v6, 32, v6
	v_bfe_i32 v3, v3, 0, 16
	s_add_i32 s28, s1, 0
	v_add_lshl_u32 v3, v6, v3, 1
	s_add_u32 s6, s94, 0x44c00000
	s_addc_u32 s7, s95, 0
	s_lshl_b32 s1, s18, 19
	v_lshl_add_u32 v145, v5, 11, v4
	v_lshl_add_u32 v147, v7, 11, v3
	s_ashr_i32 s27, s26, 31
	v_lshlrev_b32_e32 v8, 1, v7
	s_waitcnt vmcnt(4)
	v_lshrrev_b32_e32 v10, 2, v7
	v_add_u32_e32 v130, s1, v145
	v_add_u32_e32 v131, s1, v147
	s_bitset1_b32 s1, 18
	s_lshl_b64 s[4:5], s[26:27], 19
	v_and_b32_e32 v8, 24, v8
	v_and_b32_e32 v10, 4, v10
	s_add_u32 s10, s24, s4
	v_or3_b32 v8, v9, v10, v8
	v_add_u32_e32 v133, s1, v145
	v_add_u32_e32 v132, s1, v147
	s_addc_u32 s11, s25, s5
	s_add_i32 s50, s28, 0x10000
	s_mov_b32 m0, s50
	s_nop 0
	global_load_lds_dwordx4 v0, s[10:11]
	s_add_i32 s51, s28, 0x12000
	v_lshl_add_u32 v144, v8, 11, v3
	s_mov_b32 m0, s51
	s_nop 0
	global_load_lds_dwordx4 v144, s[10:11]
	s_add_u32 s4, s10, 0x40000
	s_addc_u32 s5, s11, 0
	s_add_i32 s52, s28, 0x14000
	s_mov_b32 m0, s52
	s_nop 0
	global_load_lds_dwordx4 v0, s[4:5]
	s_add_i32 s53, s28, 0x16000
	s_mov_b32 m0, s53
	s_nop 0
	global_load_lds_dwordx4 v144, s[4:5]
	s_add_i32 s54, s28, 0x2000
	s_mov_b32 m0, s28
	s_nop 0
	global_load_lds_dwordx4 v130, s[6:7]
	s_add_i32 s55, s28, 0x4000
	s_mov_b32 m0, s54
	s_nop 0
	global_load_lds_dwordx4 v131, s[6:7]
	s_add_i32 s56, s28, 0x6000
	s_mov_b32 m0, s55
	s_nop 0
	global_load_lds_dwordx4 v133, s[6:7]
	s_cmp_eq_u32 s0, 1
	s_mov_b32 m0, s56
	s_nop 0
	global_load_lds_dwordx4 v132, s[6:7]
	v_writelane_b32 v232, s76, 22
	s_cselect_b64 s[74:75], -1, 0
	s_cmp_lg_u32 s0, 1
	v_writelane_b32 v232, s77, 23
	s_cbranch_scc1 .LBB0_240
	s_barrier
.LBB0_240:
	v_bfe_u32 v149, v2, 4, 2
	s_add_u32 s82, s94, 0x5dc00000
	v_and_b32_e32 v148, 15, v2
	v_lshlrev_b32_e32 v3, 4, v149
	v_lshlrev_b32_e32 v2, 2, v2
	v_writelane_b32 v232, s92, 18
	s_addc_u32 s83, s95, 0
	s_lshl_b32 s57, s0, 6
	v_lshl_or_b32 v3, v148, 6, v3
	s_lshl_b32 s0, s0, 13
	v_and_b32_e32 v2, 32, v2
	v_bitop3_b32 v4, v3, s0, v2 bitop3:0xde
	s_lshl_b32 s0, s3, 5
	s_and_b32 s58, s0, 0x60
	s_lshl_b32 s0, s58, 7
	v_bitop3_b32 v2, v3, s0, v2 bitop3:0xde
	s_add_u32 s0, s10, 0x80
	s_waitcnt vmcnt(2)
	s_barrier
	s_addc_u32 s1, s11, 0
	s_add_i32 s59, s28, 0x18000
	s_mov_b32 m0, s59
	s_nop 0
	global_load_lds_dwordx4 v0, s[0:1]
	s_add_i32 s64, s28, 0x1a000
	s_mov_b32 m0, s64
	s_nop 0
	global_load_lds_dwordx4 v144, s[0:1]
	s_add_u32 s0, s6, 0x80
	s_addc_u32 s1, s7, 0
	s_add_i32 s65, s28, 0x8000
	s_mov_b32 m0, s65
	s_nop 0
	global_load_lds_dwordx4 v130, s[0:1]
	s_add_i32 s66, s28, 0xa000
	s_mov_b32 m0, s66
	s_nop 0
	global_load_lds_dwordx4 v131, s[0:1]
	s_add_u32 s0, s10, 0x40080
	s_addc_u32 s1, s11, 0
	s_add_i32 s67, s28, 0x1c000
	s_mov_b32 m0, s67
	s_nop 0
	global_load_lds_dwordx4 v0, s[0:1]
	s_add_i32 s72, s28, 0x1e000
	s_mov_b32 m0, s72
	s_nop 0
	global_load_lds_dwordx4 v144, s[0:1]
	v_writelane_b32 v232, s93, 19
	s_waitcnt vmcnt(6)
	s_add_i32 s73, s28, 0xc000
	s_add_i32 s76, s28, 0xe000
	v_writelane_b32 v232, s94, 20
	s_cmpk_lt_u32 s2, 0x100
	s_mov_b32 s81, s19
	v_writelane_b32 v232, s95, 21
	s_cselect_b64 s[84:85], -1, 0
	s_ashr_i32 s77, s29, 31
	s_ashr_i32 s90, s38, 31
	s_lshr_b32 s91, s80, 3
	s_mov_b32 s92, 0
	v_mov_b64_e32 v[134:135], s[80:81]
	v_add_u32_e32 v150, 0, v2
	v_add_u32_e32 v151, 0, v4
	s_mov_b64 s[48:49], 0x100
	s_barrier
	s_branch .LBB0_243

; #define PG8_STAGE(bufoff, gbase, v0, v1) do { glds16_s((gbase), (v0), ldsbase + (unsigned)(bufoff)); glds16_s((gbase), (v1), ldsbase + (unsigned)(bufoff) + 8192u); } while (0)
; #define PG8_LDA(dst, b, h) do { _Pragma("unroll") for (int m = 0; m < 4; ++m) _Pragma("unroll") for (int k = 0; k < 2; ++k) dst[m][k] = *(const LAS bf16x8*)(lds + PG8_SA(b, h) + aoff + m * 2048 + k * 1024); } while (0)
; #define PG8_LDB(dst, b, h) do { _Pragma("unroll") for (int n = 0; n < 2; ++n) _Pragma("unroll") for (int k = 0; k < 2; ++k) dst[n][k] = *(const LAS bf16x8*)(lds + PG8_SB(b, h) + boff + n * 2048 + k * 1024); } while (0)
; #define PG8_WAIT_V(n) asm volatile("s_waitcnt vmcnt(" #n ")" ::: "memory")
; #define PG8_WAIT_L(n) asm volatile("s_waitcnt lgkmcnt(" #n ")" ::: "memory")
; #define PG8_BAR __builtin_amdgcn_s_barrier()
; #define PG8_SCHED __builtin_amdgcn_sched_barrier(0)
; template <class Epi, class Sched, bool ALIGN_EPI, bool FP8 = false>
; __device__ __forceinline__ void gemm_phase(LAS unsigned char* lds, const bf16_t* A, const bf16_t* Bt, const int K, const Sched& S, const Epi& E, const int wave_in) {
;     ...
;             const unsigned w00 = last ? vN[0][0] : vA[0][0], w01 = last ? vN[0][1] : vA[0][1], w10 = last ? vN[1][0] : vA[1][0], w11 = last ? vN[1][1] : vA[1][1];
;             PG8_LDB(B0, 0, 0); PG8_LDB(B1, 0, 1); PG8_SCHED; PG8_LDA(At, 0, 0); PG8_STAGE(PG8_SA(1, 1), a1, vA[1][0], vA[1][1]);
;             PG8_WAIT_V(8); PG8_WAIT_L(0); PG8_BAR; PG8_MMA(0, 0, At, B0); PG8_MMA(0, 1, At, B1); PG8_BAR; PG8_SCHED;
;     ...
; #pragma unroll
;         for (int a = 0; a < 2; ++a)
; #pragma unroll
;             for (int b = 0; b < 2; ++b)
; #pragma unroll
;                 for (int m = 0; m < 4; ++m)
; #pragma unroll
;                     for (int n = 0; n < 2; ++n) acc[a][b][m][n] = (f32x4){0.f, 0.f, 0.f, 0.f};
.LBB0_247:
	s_add_u32 s0, s10, 0x100
	v_mov_b32_e32 v2, 0
	s_addc_u32 s1, s11, 0
	s_mov_b32 s27, -2
	s_mov_b64 s[4:5], s[6:7]
	v_mov_b32_e32 v3, 0
	v_mov_b64_e32 v[4:5], 0
	v_mov_b64_e32 v[6:7], 0
	v_mov_b64_e32 v[8:9], 0
	s_waitcnt vmcnt(2)
	v_mov_b64_e32 v[18:19], 0
	v_mov_b64_e32 v[20:21], 0
	s_waitcnt vmcnt(1)
	v_mov_b64_e32 v[22:23], 0
	v_mov_b64_e32 v[24:25], 0
	v_mov_b64_e32 v[34:35], 0
	v_mov_b64_e32 v[36:37], 0
	v_mov_b64_e32 v[38:39], 0
	v_mov_b64_e32 v[40:41], 0
	v_mov_b64_e32 v[50:51], 0
	v_mov_b64_e32 v[52:53], 0
	v_mov_b64_e32 v[54:55], 0
	v_mov_b64_e32 v[56:57], 0
	v_mov_b64_e32 v[10:11], 0
	v_mov_b64_e32 v[12:13], 0
	v_mov_b64_e32 v[14:15], 0
	v_mov_b64_e32 v[16:17], 0
	s_waitcnt vmcnt(0)
	v_mov_b64_e32 v[26:27], 0
	v_mov_b64_e32 v[28:29], 0
	v_mov_b64_e32 v[30:31], 0
	v_mov_b64_e32 v[32:33], 0
	v_mov_b64_e32 v[42:43], 0
	v_mov_b64_e32 v[44:45], 0
	v_mov_b64_e32 v[46:47], 0
	v_mov_b64_e32 v[48:49], 0
	v_mov_b64_e32 v[58:59], 0
	v_mov_b64_e32 v[60:61], 0
	v_mov_b64_e32 v[62:63], 0
	v_mov_b64_e32 v[64:65], 0
	v_mov_b64_e32 v[66:67], 0
	v_mov_b64_e32 v[68:69], 0
	v_mov_b64_e32 v[70:71], 0
	v_mov_b64_e32 v[72:73], 0
	v_mov_b64_e32 v[82:83], 0
	v_mov_b64_e32 v[84:85], 0
	v_mov_b64_e32 v[86:87], 0
	v_mov_b64_e32 v[88:89], 0
	v_mov_b64_e32 v[98:99], 0
	v_mov_b64_e32 v[100:101], 0
	v_mov_b64_e32 v[102:103], 0
	v_mov_b64_e32 v[104:105], 0
	v_mov_b64_e32 v[114:115], 0
	v_mov_b64_e32 v[116:117], 0
	v_mov_b64_e32 v[118:119], 0
	v_mov_b64_e32 v[120:121], 0
	v_mov_b64_e32 v[74:75], 0
	v_mov_b64_e32 v[76:77], 0
	v_mov_b64_e32 v[78:79], 0
	v_mov_b64_e32 v[80:81], 0
	v_mov_b64_e32 v[90:91], 0
	v_mov_b64_e32 v[92:93], 0
	v_mov_b64_e32 v[94:95], 0
	v_mov_b64_e32 v[96:97], 0
	v_mov_b64_e32 v[106:107], 0
	v_mov_b64_e32 v[108:109], 0
	v_mov_b64_e32 v[110:111], 0
	v_mov_b64_e32 v[112:113], 0
	v_mov_b64_e32 v[122:123], 0
	v_mov_b64_e32 v[124:125], 0
	v_mov_b64_e32 v[126:127], 0
	v_mov_b64_e32 v[128:129], 0
.LBB0_248:
	s_add_u32 s10, s4, 0x100
	s_addc_u32 s11, s5, 0
	v_add_u32_e32 v160, 0x10000, v150
	v_add_u32_e32 v176, 0x14000, v150
	s_cmp_eq_u32 s27, 12
	ds_read_b128 v[136:139], v160
	ds_read_b128 v[140:143], v160 offset:1024
	ds_read_b128 v[156:159], v160 offset:2048
	ds_read_b128 v[160:163], v160 offset:3072
	ds_read_b128 v[164:167], v176
	ds_read_b128 v[168:171], v176 offset:1024
	ds_read_b128 v[172:175], v176 offset:2048
	ds_read_b128 v[176:179], v176 offset:3072
	s_cselect_b64 vcc, -1, 0
	s_and_b64 s[8:9], vcc, exec
	s_cselect_b32 s22, s6, s10
	s_cselect_b32 s23, s7, s11
	s_cselect_b32 s16, s88, s0
	s_cselect_b32 s17, s89, s1
	s_add_u32 s8, s22, 0x80
	s_addc_u32 s9, s23, 0
	s_add_u32 s20, s16, 0x80
	v_cndmask_b32_e32 v180, v130, v152, vcc
	v_cndmask_b32_e32 v181, v133, v154, vcc
	v_cndmask_b32_e32 v197, v131, v153, vcc
	s_addc_u32 s21, s17, 0
	ds_read_b128 v[198:201], v151
	ds_read_b128 v[202:205], v151 offset:1024
	ds_read_b128 v[206:209], v151 offset:2048
	ds_read_b128 v[210:213], v151 offset:3072
	ds_read_b128 v[214:217], v151 offset:4096
	ds_read_b128 v[218:221], v151 offset:5120
	ds_read_b128 v[222:225], v151 offset:6144
	ds_read_b128 v[226:229], v151 offset:7168
	s_add_u32 s4, s4, 0x80
	s_addc_u32 s5, s5, 0
	s_mov_b32 m0, s73
	s_nop 0
	global_load_lds_dwordx4 v133, s[4:5]
	s_nop 0
	s_mov_b32 m0, s76
	s_nop 0
	global_load_lds_dwordx4 v132, s[4:5]
	s_waitcnt vmcnt(8)
	s_waitcnt lgkmcnt(0)
	s_barrier
	s_setprio 1
	s_waitcnt lgkmcnt(7)
	v_mfma_f32_16x16x32_bf16 v[126:129], v[136:139], v[198:201], v[126:129]
	v_mfma_f32_16x16x32_bf16 v[122:125], v[156:159], v[198:201], v[122:125]
	s_waitcnt lgkmcnt(5)
	v_mfma_f32_16x16x32_bf16 v[110:113], v[136:139], v[206:209], v[110:113]
	v_mfma_f32_16x16x32_bf16 v[106:109], v[156:159], v[206:209], v[106:109]
	s_waitcnt lgkmcnt(3)
	v_mfma_f32_16x16x32_bf16 v[94:97], v[136:139], v[214:217], v[94:97]
	v_mfma_f32_16x16x32_bf16 v[90:93], v[156:159], v[214:217], v[90:93]
	s_waitcnt lgkmcnt(1)
	v_mfma_f32_16x16x32_bf16 v[78:81], v[136:139], v[222:225], v[78:81]
	v_mfma_f32_16x16x32_bf16 v[74:77], v[156:159], v[222:225], v[74:77]
	v_mfma_f32_16x16x32_bf16 v[126:129], v[140:143], v[202:205], v[126:129]
	v_mfma_f32_16x16x32_bf16 v[122:125], v[160:163], v[202:205], v[122:125]
	v_mfma_f32_16x16x32_bf16 v[110:113], v[140:143], v[210:213], v[110:113]
	v_mfma_f32_16x16x32_bf16 v[106:109], v[160:163], v[210:213], v[106:109]
	v_mfma_f32_16x16x32_bf16 v[94:97], v[140:143], v[218:221], v[94:97]
	v_mfma_f32_16x16x32_bf16 v[90:93], v[160:163], v[218:221], v[90:93]
	s_waitcnt lgkmcnt(0)
	v_mfma_f32_16x16x32_bf16 v[78:81], v[140:143], v[226:229], v[78:81]
	v_mfma_f32_16x16x32_bf16 v[74:77], v[160:163], v[226:229], v[74:77]
	s_setprio 0
	s_setprio 1
	v_mfma_f32_16x16x32_bf16 v[118:121], v[164:167], v[198:201], v[118:121]
	v_mfma_f32_16x16x32_bf16 v[114:117], v[172:175], v[198:201], v[114:117]
	v_mfma_f32_16x16x32_bf16 v[102:105], v[164:167], v[206:209], v[102:105]
	v_mfma_f32_16x16x32_bf16 v[98:101], v[172:175], v[206:209], v[98:101]
	v_mfma_f32_16x16x32_bf16 v[86:89], v[164:167], v[214:217], v[86:89]
	v_mfma_f32_16x16x32_bf16 v[82:85], v[172:175], v[214:217], v[82:85]
	v_mfma_f32_16x16x32_bf16 v[70:73], v[164:167], v[222:225], v[70:73]
	v_mfma_f32_16x16x32_bf16 v[66:69], v[172:175], v[222:225], v[66:69]
	v_mfma_f32_16x16x32_bf16 v[118:121], v[168:171], v[202:205], v[118:121]
	v_mfma_f32_16x16x32_bf16 v[114:117], v[176:179], v[202:205], v[114:117]
	v_mfma_f32_16x16x32_bf16 v[102:105], v[168:171], v[210:213], v[102:105]
	v_mfma_f32_16x16x32_bf16 v[98:101], v[176:179], v[210:213], v[98:101]
	v_mfma_f32_16x16x32_bf16 v[86:89], v[168:171], v[218:221], v[86:89]
	v_mfma_f32_16x16x32_bf16 v[82:85], v[176:179], v[218:221], v[82:85]
	v_mfma_f32_16x16x32_bf16 v[70:73], v[168:171], v[226:229], v[70:73]
	v_mfma_f32_16x16x32_bf16 v[66:69], v[176:179], v[226:229], v[66:69]
	s_setprio 0
	s_barrier
; #define PG8_STAGE(bufoff, gbase, v0, v1) do { glds16_s((gbase), (v0), ldsbase + (unsigned)(bufoff)); glds16_s((gbase), (v1), ldsbase + (unsigned)(bufoff) + 8192u); } while (0)
; #define PG8_LDA(dst, b, h) do { _Pragma("unroll") for (int m = 0; m < 4; ++m) _Pragma("unroll") for (int k = 0; k < 2; ++k) dst[m][k] = *(const LAS bf16x8*)(lds + PG8_SA(b, h) + aoff + m * 2048 + k * 1024); } while (0)
; #define PG8_LDB(dst, b, h) do { _Pragma("unroll") for (int n = 0; n < 2; ++n) _Pragma("unroll") for (int k = 0; k < 2; ++k) dst[n][k] = *(const LAS bf16x8*)(lds + PG8_SB(b, h) + boff + n * 2048 + k * 1024); } while (0)
; #define PG8_WAIT_V(n) asm volatile("s_waitcnt vmcnt(" #n ")" ::: "memory")
; #define PG8_WAIT_L(n) asm volatile("s_waitcnt lgkmcnt(" #n ")" ::: "memory")
; #define PG8_BAR __builtin_amdgcn_s_barrier()
; #define PG8_SCHED __builtin_amdgcn_sched_barrier(0)
; template <class Epi, class Sched, bool ALIGN_EPI, bool FP8 = false>
; __device__ __forceinline__ void gemm_phase(LAS unsigned char* lds, const bf16_t* A, const bf16_t* Bt, const int K, const Sched& S, const Epi& E, const int wave_in) {
;     ...
;             PG8_WAIT_V(8); PG8_WAIT_L(0); PG8_BAR; PG8_MMA(0, 0, At, B0); PG8_MMA(0, 1, At, B1); PG8_BAR; PG8_SCHED;
;             PG8_LDA(At, 0, 1); PG8_STAGE(PG8_SB(0, 0), b2, voffB[0], voffB[1]); PG8_STAGE(PG8_SB(0, 1), b2 + hstep, voffB[0], voffB[1]); PG8_STAGE(PG8_SA(0, 0), a2, w00, w01);
;             PG8_WAIT_V(8); PG8_WAIT_L(0); PG8_BAR; PG8_MMA(1, 0, At, B0); PG8_MMA(1, 1, At, B1); PG8_BAR; PG8_SCHED;
;             PG8_LDB(B0, 1, 0); PG8_LDB(B1, 1, 1); PG8_SCHED; PG8_LDA(At, 1, 0); PG8_STAGE(PG8_SA(0, 1), a2, w10, w11);
;             PG8_WAIT_V(8); PG8_WAIT_L(0); PG8_BAR; PG8_MMA(0, 0, At, B0); PG8_MMA(0, 1, At, B1); PG8_BAR; PG8_SCHED;
	ds_read_b128 v[198:201], v151 offset:16384
	ds_read_b128 v[202:205], v151 offset:17408
	ds_read_b128 v[206:209], v151 offset:18432
	ds_read_b128 v[210:213], v151 offset:19456
	ds_read_b128 v[214:217], v151 offset:20480
	ds_read_b128 v[218:221], v151 offset:21504
	ds_read_b128 v[222:225], v151 offset:22528
	ds_read_b128 v[226:229], v151 offset:23552
	s_mov_b32 m0, s50
	s_nop 0
	global_load_lds_dwordx4 v0, s[16:17]
	s_nop 0
	s_mov_b32 m0, s51
	s_nop 0
	global_load_lds_dwordx4 v144, s[16:17]
	s_add_u32 s4, s16, 0x40000
	s_addc_u32 s5, s17, 0
	s_mov_b32 m0, s52
	s_nop 0
	global_load_lds_dwordx4 v0, s[4:5]
	s_nop 0
	s_mov_b32 m0, s53
	s_nop 0
	global_load_lds_dwordx4 v144, s[4:5]
	s_mov_b32 m0, s28
	s_nop 0
	global_load_lds_dwordx4 v180, s[22:23]
	s_nop 0
	s_mov_b32 m0, s54
	s_nop 0
	global_load_lds_dwordx4 v197, s[22:23]
	s_waitcnt vmcnt(8)
	s_waitcnt lgkmcnt(0)
	s_barrier
	s_setprio 1
	s_waitcnt lgkmcnt(7)
	v_mfma_f32_16x16x32_bf16 v[62:65], v[136:139], v[198:201], v[62:65]
	v_mfma_f32_16x16x32_bf16 v[58:61], v[156:159], v[198:201], v[58:61]
	s_waitcnt lgkmcnt(5)
	v_mfma_f32_16x16x32_bf16 v[46:49], v[136:139], v[206:209], v[46:49]
	v_mfma_f32_16x16x32_bf16 v[42:45], v[156:159], v[206:209], v[42:45]
	s_waitcnt lgkmcnt(3)
	v_mfma_f32_16x16x32_bf16 v[30:33], v[136:139], v[214:217], v[30:33]
	v_mfma_f32_16x16x32_bf16 v[26:29], v[156:159], v[214:217], v[26:29]
	s_waitcnt lgkmcnt(1)
	v_mfma_f32_16x16x32_bf16 v[14:17], v[136:139], v[222:225], v[14:17]
	v_mfma_f32_16x16x32_bf16 v[10:13], v[156:159], v[222:225], v[10:13]
	v_mfma_f32_16x16x32_bf16 v[62:65], v[140:143], v[202:205], v[62:65]
	v_mfma_f32_16x16x32_bf16 v[58:61], v[160:163], v[202:205], v[58:61]
	v_mfma_f32_16x16x32_bf16 v[46:49], v[140:143], v[210:213], v[46:49]
	v_mfma_f32_16x16x32_bf16 v[42:45], v[160:163], v[210:213], v[42:45]
	v_mfma_f32_16x16x32_bf16 v[30:33], v[140:143], v[218:221], v[30:33]
	v_mfma_f32_16x16x32_bf16 v[26:29], v[160:163], v[218:221], v[26:29]
	s_waitcnt lgkmcnt(0)
	v_mfma_f32_16x16x32_bf16 v[14:17], v[140:143], v[226:229], v[14:17]
	v_mfma_f32_16x16x32_bf16 v[10:13], v[160:163], v[226:229], v[10:13]
	s_setprio 0
	s_setprio 1
	v_mfma_f32_16x16x32_bf16 v[54:57], v[164:167], v[198:201], v[54:57]
	v_mfma_f32_16x16x32_bf16 v[50:53], v[172:175], v[198:201], v[50:53]
	v_mfma_f32_16x16x32_bf16 v[38:41], v[164:167], v[206:209], v[38:41]
	v_mfma_f32_16x16x32_bf16 v[34:37], v[172:175], v[206:209], v[34:37]
	v_mfma_f32_16x16x32_bf16 v[22:25], v[164:167], v[214:217], v[22:25]
	v_mfma_f32_16x16x32_bf16 v[18:21], v[172:175], v[214:217], v[18:21]
	v_mfma_f32_16x16x32_bf16 v[6:9], v[164:167], v[222:225], v[6:9]
	v_mfma_f32_16x16x32_bf16 v[2:5], v[172:175], v[222:225], v[2:5]
	v_mfma_f32_16x16x32_bf16 v[54:57], v[168:171], v[202:205], v[54:57]
	v_mfma_f32_16x16x32_bf16 v[50:53], v[176:179], v[202:205], v[50:53]
	v_mfma_f32_16x16x32_bf16 v[38:41], v[168:171], v[210:213], v[38:41]
	v_mfma_f32_16x16x32_bf16 v[34:37], v[176:179], v[210:213], v[34:37]
	v_mfma_f32_16x16x32_bf16 v[22:25], v[168:171], v[218:221], v[22:25]
	v_mfma_f32_16x16x32_bf16 v[18:21], v[176:179], v[218:221], v[18:21]
	v_mfma_f32_16x16x32_bf16 v[6:9], v[168:171], v[226:229], v[6:9]
	v_mfma_f32_16x16x32_bf16 v[2:5], v[176:179], v[226:229], v[2:5]
	s_setprio 0
	s_barrier
	v_add_u32_e32 v160, 0x18000, v150
	v_add_u32_e32 v176, 0x1c000, v150
	ds_read_b128 v[136:139], v160
	ds_read_b128 v[140:143], v160 offset:1024
	ds_read_b128 v[156:159], v160 offset:2048
	ds_read_b128 v[160:163], v160 offset:3072
	ds_read_b128 v[164:167], v176
	ds_read_b128 v[168:171], v176 offset:1024
	ds_read_b128 v[172:175], v176 offset:2048
	ds_read_b128 v[176:179], v176 offset:3072
	ds_read_b128 v[198:201], v151 offset:32768
	ds_read_b128 v[202:205], v151 offset:33792
	ds_read_b128 v[206:209], v151 offset:34816
	ds_read_b128 v[210:213], v151 offset:35840
	ds_read_b128 v[214:217], v151 offset:36864
	ds_read_b128 v[218:221], v151 offset:37888
	ds_read_b128 v[222:225], v151 offset:38912
	ds_read_b128 v[226:229], v151 offset:39936
	s_mov_b32 m0, s55
	s_nop 0
	global_load_lds_dwordx4 v181, s[22:23]
	v_cndmask_b32_e32 v230, v132, v155, vcc
	s_mov_b32 m0, s56
	s_nop 0
	global_load_lds_dwordx4 v230, s[22:23]
	s_waitcnt vmcnt(8)
	s_waitcnt lgkmcnt(0)
	s_barrier
; #define PG8_STAGE(bufoff, gbase, v0, v1) do { glds16_s((gbase), (v0), ldsbase + (unsigned)(bufoff)); glds16_s((gbase), (v1), ldsbase + (unsigned)(bufoff) + 8192u); } while (0)
; #define PG8_LDA(dst, b, h) do { _Pragma("unroll") for (int m = 0; m < 4; ++m) _Pragma("unroll") for (int k = 0; k < 2; ++k) dst[m][k] = *(const LAS bf16x8*)(lds + PG8_SA(b, h) + aoff + m * 2048 + k * 1024); } while (0)
; #define PG8_WAIT_V(n) asm volatile("s_waitcnt vmcnt(" #n ")" ::: "memory")
; #define PG8_WAIT_L(n) asm volatile("s_waitcnt lgkmcnt(" #n ")" ::: "memory")
; #define PG8_BAR __builtin_amdgcn_s_barrier()
; #define PG8_SCHED __builtin_amdgcn_sched_barrier(0)
; template <class Epi, class Sched, bool ALIGN_EPI, bool FP8 = false>
; __device__ __forceinline__ void gemm_phase(LAS unsigned char* lds, const bf16_t* A, const bf16_t* Bt, const int K, const Sched& S, const Epi& E, const int wave_in) {
;     ...
;             PG8_WAIT_V(8); PG8_WAIT_L(0); PG8_BAR; PG8_MMA(0, 0, At, B0); PG8_MMA(0, 1, At, B1); PG8_BAR; PG8_SCHED;
;             PG8_LDA(At, 1, 1); PG8_STAGE(PG8_SB(1, 0), b3, voffB[0], voffB[1]); PG8_STAGE(PG8_SB(1, 1), b3 + hstep, voffB[0], voffB[1]); PG8_STAGE(PG8_SA(1, 0), a3, w00, w01);
;             PG8_WAIT_V(8); PG8_WAIT_L(0); PG8_BAR; PG8_MMA(1, 0, At, B0); PG8_MMA(1, 1, At, B1); PG8_BAR; PG8_SCHED;
;         }
;         if constexpr (FP8) asm volatile("s_nop 15\n\ts_nop 15" ::: "memory");
;         if constexpr (ALIGN_EPI) { if (wr == 0) PG8_BAR; }
	s_setprio 1
	s_waitcnt lgkmcnt(7)
	v_mfma_f32_16x16x32_bf16 v[126:129], v[136:139], v[198:201], v[126:129]
	v_mfma_f32_16x16x32_bf16 v[122:125], v[156:159], v[198:201], v[122:125]
	s_waitcnt lgkmcnt(5)
	v_mfma_f32_16x16x32_bf16 v[110:113], v[136:139], v[206:209], v[110:113]
	v_mfma_f32_16x16x32_bf16 v[106:109], v[156:159], v[206:209], v[106:109]
	s_waitcnt lgkmcnt(3)
	v_mfma_f32_16x16x32_bf16 v[94:97], v[136:139], v[214:217], v[94:97]
	v_mfma_f32_16x16x32_bf16 v[90:93], v[156:159], v[214:217], v[90:93]
	s_waitcnt lgkmcnt(1)
	v_mfma_f32_16x16x32_bf16 v[78:81], v[136:139], v[222:225], v[78:81]
	v_mfma_f32_16x16x32_bf16 v[74:77], v[156:159], v[222:225], v[74:77]
	v_mfma_f32_16x16x32_bf16 v[126:129], v[140:143], v[202:205], v[126:129]
	v_mfma_f32_16x16x32_bf16 v[122:125], v[160:163], v[202:205], v[122:125]
	v_mfma_f32_16x16x32_bf16 v[110:113], v[140:143], v[210:213], v[110:113]
	v_mfma_f32_16x16x32_bf16 v[106:109], v[160:163], v[210:213], v[106:109]
	v_mfma_f32_16x16x32_bf16 v[94:97], v[140:143], v[218:221], v[94:97]
	v_mfma_f32_16x16x32_bf16 v[90:93], v[160:163], v[218:221], v[90:93]
	s_waitcnt lgkmcnt(0)
	v_mfma_f32_16x16x32_bf16 v[78:81], v[140:143], v[226:229], v[78:81]
	v_mfma_f32_16x16x32_bf16 v[74:77], v[160:163], v[226:229], v[74:77]
	s_setprio 0
	s_setprio 1
	v_mfma_f32_16x16x32_bf16 v[118:121], v[164:167], v[198:201], v[118:121]
	v_mfma_f32_16x16x32_bf16 v[114:117], v[172:175], v[198:201], v[114:117]
	v_mfma_f32_16x16x32_bf16 v[102:105], v[164:167], v[206:209], v[102:105]
	v_mfma_f32_16x16x32_bf16 v[98:101], v[172:175], v[206:209], v[98:101]
	v_mfma_f32_16x16x32_bf16 v[86:89], v[164:167], v[214:217], v[86:89]
	v_mfma_f32_16x16x32_bf16 v[82:85], v[172:175], v[214:217], v[82:85]
	v_mfma_f32_16x16x32_bf16 v[70:73], v[164:167], v[222:225], v[70:73]
	v_mfma_f32_16x16x32_bf16 v[66:69], v[172:175], v[222:225], v[66:69]
	v_mfma_f32_16x16x32_bf16 v[118:121], v[168:171], v[202:205], v[118:121]
	v_mfma_f32_16x16x32_bf16 v[114:117], v[176:179], v[202:205], v[114:117]
	v_mfma_f32_16x16x32_bf16 v[102:105], v[168:171], v[210:213], v[102:105]
	v_mfma_f32_16x16x32_bf16 v[98:101], v[176:179], v[210:213], v[98:101]
	v_mfma_f32_16x16x32_bf16 v[86:89], v[168:171], v[218:221], v[86:89]
	v_mfma_f32_16x16x32_bf16 v[82:85], v[176:179], v[218:221], v[82:85]
	v_mfma_f32_16x16x32_bf16 v[70:73], v[168:171], v[226:229], v[70:73]
	v_mfma_f32_16x16x32_bf16 v[66:69], v[176:179], v[226:229], v[66:69]
	s_setprio 0
	s_barrier
	ds_read_b128 v[198:201], v151 offset:49152
	ds_read_b128 v[202:205], v151 offset:50176
	ds_read_b128 v[206:209], v151 offset:51200
	ds_read_b128 v[210:213], v151 offset:52224
	ds_read_b128 v[214:217], v151 offset:53248
	ds_read_b128 v[218:221], v151 offset:54272
	ds_read_b128 v[222:225], v151 offset:55296
	ds_read_b128 v[226:229], v151 offset:56320
	s_mov_b32 m0, s59
	s_nop 0
	global_load_lds_dwordx4 v0, s[20:21]
	s_nop 0
	s_mov_b32 m0, s64
	s_nop 0
	global_load_lds_dwordx4 v144, s[20:21]
	s_add_u32 s4, s16, 0x40080
	s_addc_u32 s5, s17, 0
	s_mov_b32 m0, s67
	s_nop 0
	global_load_lds_dwordx4 v0, s[4:5]
	s_nop 0
	s_mov_b32 m0, s72
	s_nop 0
	global_load_lds_dwordx4 v144, s[4:5]
	s_mov_b32 m0, s65
	s_nop 0
	global_load_lds_dwordx4 v180, s[8:9]
	s_nop 0
	s_mov_b32 m0, s66
	s_nop 0
	global_load_lds_dwordx4 v197, s[8:9]
	s_waitcnt vmcnt(8)
	s_waitcnt lgkmcnt(0)
	s_barrier
	s_setprio 1
	s_waitcnt lgkmcnt(7)
	v_mfma_f32_16x16x32_bf16 v[62:65], v[136:139], v[198:201], v[62:65]
	v_mfma_f32_16x16x32_bf16 v[58:61], v[156:159], v[198:201], v[58:61]
	s_waitcnt lgkmcnt(5)
	v_mfma_f32_16x16x32_bf16 v[46:49], v[136:139], v[206:209], v[46:49]
	v_mfma_f32_16x16x32_bf16 v[42:45], v[156:159], v[206:209], v[42:45]
	s_waitcnt lgkmcnt(3)
	v_mfma_f32_16x16x32_bf16 v[30:33], v[136:139], v[214:217], v[30:33]
	v_mfma_f32_16x16x32_bf16 v[26:29], v[156:159], v[214:217], v[26:29]
	s_waitcnt lgkmcnt(1)
	v_mfma_f32_16x16x32_bf16 v[14:17], v[136:139], v[222:225], v[14:17]
	v_mfma_f32_16x16x32_bf16 v[10:13], v[156:159], v[222:225], v[10:13]
	v_mfma_f32_16x16x32_bf16 v[62:65], v[140:143], v[202:205], v[62:65]
	v_mfma_f32_16x16x32_bf16 v[58:61], v[160:163], v[202:205], v[58:61]
	v_mfma_f32_16x16x32_bf16 v[46:49], v[140:143], v[210:213], v[46:49]
	v_mfma_f32_16x16x32_bf16 v[42:45], v[160:163], v[210:213], v[42:45]
	v_mfma_f32_16x16x32_bf16 v[30:33], v[140:143], v[218:221], v[30:33]
	v_mfma_f32_16x16x32_bf16 v[26:29], v[160:163], v[218:221], v[26:29]
	s_waitcnt lgkmcnt(0)
	v_mfma_f32_16x16x32_bf16 v[14:17], v[140:143], v[226:229], v[14:17]
	v_mfma_f32_16x16x32_bf16 v[10:13], v[160:163], v[226:229], v[10:13]
	s_setprio 0
	s_setprio 1
	v_mfma_f32_16x16x32_bf16 v[54:57], v[164:167], v[198:201], v[54:57]
	v_mfma_f32_16x16x32_bf16 v[50:53], v[172:175], v[198:201], v[50:53]
	v_mfma_f32_16x16x32_bf16 v[38:41], v[164:167], v[206:209], v[38:41]
	v_mfma_f32_16x16x32_bf16 v[34:37], v[172:175], v[206:209], v[34:37]
	v_mfma_f32_16x16x32_bf16 v[22:25], v[164:167], v[214:217], v[22:25]
	v_mfma_f32_16x16x32_bf16 v[18:21], v[172:175], v[214:217], v[18:21]
	v_mfma_f32_16x16x32_bf16 v[6:9], v[164:167], v[222:225], v[6:9]
	v_mfma_f32_16x16x32_bf16 v[2:5], v[172:175], v[222:225], v[2:5]
	v_mfma_f32_16x16x32_bf16 v[54:57], v[168:171], v[202:205], v[54:57]
	v_mfma_f32_16x16x32_bf16 v[50:53], v[176:179], v[202:205], v[50:53]
	v_mfma_f32_16x16x32_bf16 v[38:41], v[168:171], v[210:213], v[38:41]
	v_mfma_f32_16x16x32_bf16 v[34:37], v[176:179], v[210:213], v[34:37]
	v_mfma_f32_16x16x32_bf16 v[22:25], v[168:171], v[218:221], v[22:25]
	v_mfma_f32_16x16x32_bf16 v[18:21], v[176:179], v[218:221], v[18:21]
	v_mfma_f32_16x16x32_bf16 v[6:9], v[168:171], v[226:229], v[6:9]
	v_mfma_f32_16x16x32_bf16 v[2:5], v[176:179], v[226:229], v[2:5]
	s_setprio 0
	s_barrier
	s_add_i32 s27, s27, 2
	s_add_u32 s0, s0, 0x100
	s_addc_u32 s1, s1, 0
	s_cmp_gt_u32 s27, 13
	s_mov_b64 s[4:5], s[10:11]
	s_cbranch_scc0 .LBB0_248
	s_and_b64 vcc, exec, s[84:85]
	s_cbranch_vccz .LBB0_251
	s_barrier

; __device__ __forceinline__ int opaque_tid(int wave) { int l; asm volatile("v_mbcnt_lo_u32_b32 %0, -1, 0\n\tv_mbcnt_hi_u32_b32 %0, -1, %0" : "=v"(l)); return wave * 64 + l; }
; template <class Epi, class Sched, bool ALIGN_EPI, bool FP8 = false>
; __device__ __forceinline__ void gemm_phase(LAS unsigned char* lds, const bf16_t* A, const bf16_t* Bt, const int K, const Sched& S, const Epi& E, const int wave_in) {
;     const int tid = opaque_tid(wave_in); const int wid = __builtin_amdgcn_readfirstlane(tid >> 6), lane = tid & 63, wr = wid >> 2, wc = wid & 3, fr = lane & 15, fq = lane >> 4;
;     const int nt = K / BK;
;     int sR[2], sC[2]; unsigned voffB[2];
; #pragma unroll
;     for (int i = 0; i < 2; ++i) { stage_rc(tid * 16 + i * 8192, sR[i], sC[i]); const int Rb = Epi::PERM ? ((sR[i] & ~31) + perm32(sR[i] & 31)) : sR[i];
;         voffB[i] = (unsigned)(Rb * K + sC[i]) * 2u; }
;     const size_t kstep = (size_t)(BK * 2);
;     const size_t hstep = (size_t)HALF * K * 2;
;     const unsigned ldsw = (unsigned)wid * 1024u;
;     const unsigned ldsbase = (unsigned)__builtin_amdgcn_readfirstlane((int)((unsigned)(uintptr_t)lds + ldsw));
;     const int aoff = lds_byte(wr * 64 + fr, fq * 8), boff = lds_byte(wc * 32 + fr, fq * 8);
;     ...
;     Unit cur, nxt; int ui = 0;
;     if (!S.next(0, cur)) return;
;     f32x4 acc[2][2][4][2];
; #pragma unroll
;     for (int a = 0; a < 2; ++a)
; #pragma unroll
;         for (int b = 0; b < 2; ++b)
; #pragma unroll
;             for (int m = 0; m < 4; ++m)
; #pragma unroll
;                 for (int n = 0; n < 2; ++n) acc[a][b][m][n] = (f32x4){0.f, 0.f, 0.f, 0.f};
;     bf16x8 At[4][2], B0[2][2], B1[2][2];
;     const int sclW = W8_E8M0, sclA = A8_E8M0;
;     unsigned vA[2][2], vN[2][2];
;     PG8_AOFF(vA, cur);
;     const char* const cA = (const char*)A;
;     const char* cB = (const char*)Bt + S.b_off(cur) * 2;
;     PG8_STAGE(PG8_SB(0, 0), cB, voffB[0], voffB[1]); PG8_STAGE(PG8_SB(0, 1), cB + hstep, voffB[0], voffB[1]); PG8_STAGE(PG8_SA(0, 0), cA, vA[0][0], vA[0][1]); PG8_STAGE(PG8_SA(0, 1), cA, vA[1][0], vA[1][1]);
;     if (wr == 1) PG8_BAR;
;     PG8_WAIT_V(2); PG8_BAR;
;     PG8_STAGE(PG8_SB(1, 0), cB + kstep, voffB[0], voffB[1]); PG8_STAGE(PG8_SA(1, 0), cA + kstep, vA[0][0], vA[0][1]); PG8_STAGE(PG8_SB(1, 1), cB + hstep + kstep, voffB[0], voffB[1]);
;     PG8_WAIT_V(6); PG8_BAR;
.LBB0_404:
	s_andn2_b64 vcc, exec, s[0:1]
	s_cbranch_vccnz .LBB0_511
	v_ashrrev_i32_e32 v4, 31, v0
	v_lshrrev_b32_e32 v4, 26, v4
	v_lshlrev_b32_e32 v3, 4, v0
	v_add_u32_e32 v4, v0, v4
	v_bfe_i32 v0, v0, 27, 1
	v_lshrrev_b32_e32 v0, 22, v0
	v_add_u32_e32 v0, v3, v0
	v_and_b32_e32 v0, 0xfffffc00, v0
	v_sub_u32_e32 v0, v3, v0
	v_lshrrev_b32_e32 v5, 4, v0
	v_bitop3_b32 v0, v5, v0, 32 bitop3:0x6c
	s_waitcnt vmcnt(5)
	v_ashrrev_i32_e32 v6, 31, v0
	v_lshrrev_b32_e32 v6, 26, v6
	v_add_u32_e32 v6, v0, v6
	v_ashrrev_i32_e32 v4, 6, v4
	v_lshrrev_b32_e32 v7, 6, v6
	v_and_b32_e32 v6, 0xc0, v6
	v_lshlrev_b32_e32 v5, 3, v4
	v_lshlrev_b32_e32 v4, 5, v4
	v_sub_u32_e32 v0, v0, v6
	v_and_b32_e32 v5, 0x3ffff0, v5
	v_and_b32_e32 v4, 32, v4
	v_ashrrev_i16_sdwa v0, v185, sext(v0) dst_sel:DWORD dst_unused:UNUSED_PAD src0_sel:DWORD src1_sel:BYTE_0
	v_add_u32_sdwa v0, v4, sext(v0) dst_sel:DWORD dst_unused:UNUSED_PAD src0_sel:DWORD src1_sel:WORD_0
	v_add_lshl_u32 v4, v7, v5, 10
	v_lshl_add_u32 v147, v0, 1, v4
	v_add_u32_e32 v0, 0x2000, v3
	v_ashrrev_i32_e32 v3, 31, v0
	v_lshrrev_b32_e32 v3, 22, v3
	v_add_u32_e32 v3, v0, v3
	v_ashrrev_i32_e32 v3, 10, v3
	v_mul_i32_i24_e32 v4, 0x400, v3
	v_sub_u32_e32 v0, v0, v4
	v_lshrrev_b32_e32 v4, 4, v0
	v_bitop3_b32 v0, v4, v0, 32 bitop3:0x6c
	v_ashrrev_i32_e32 v5, 31, v0
	v_lshrrev_b32_e32 v5, 26, v5
	v_add_u32_e32 v5, v0, v5
	s_add_u32 s74, s94, 0x99000000
	v_lshrrev_b32_e32 v6, 6, v5
	v_and_b32_e32 v5, 0xc0, v5
	s_addc_u32 s75, s95, 0
	v_lshlrev_b32_e32 v4, 3, v3
	v_lshlrev_b32_e32 v3, 5, v3
	v_sub_u32_e32 v0, v0, v5
	v_writelane_b32 v232, s76, 22
	s_add_u32 s8, s94, 0x3100000
	v_and_b32_e32 v4, 0x3ffff0, v4
	v_and_b32_e32 v3, 32, v3
	v_ashrrev_i16_sdwa v0, v185, sext(v0) dst_sel:DWORD dst_unused:UNUSED_PAD src0_sel:DWORD src1_sel:BYTE_0
	v_writelane_b32 v232, s77, 23
	s_addc_u32 s9, s95, 0
	v_add_u32_sdwa v0, v3, sext(v0) dst_sel:DWORD dst_unused:UNUSED_PAD src0_sel:DWORD src1_sel:WORD_0
	v_add_lshl_u32 v3, v6, v4, 10
	s_lshl_b32 s1, s2, 10
	v_writelane_b32 v232, s97, 24
	v_lshl_add_u32 v164, v0, 1, v3
	s_add_i32 s18, s1, 0
	s_lshl_b32 s1, s28, 18
	s_ashr_i32 s97, s96, 31
	s_ashr_i32 s0, s4, 8
	v_add_u32_e32 v173, s1, v147
	v_add_u32_e32 v0, s1, v164
	s_bitset1_b32 s1, 17
	s_lshl_b64 s[6:7], s[96:97], 18
	s_add_u32 s10, s8, s6
	v_add_u32_e32 v175, s1, v147
	v_add_u32_e32 v174, s1, v164
	s_addc_u32 s11, s9, s7
	s_add_i32 s20, s18, 0x10000
	s_mov_b32 m0, s20
	s_nop 0
	global_load_lds_dwordx4 v147, s[10:11]
	s_add_i32 s21, s18, 0x12000
	s_mov_b32 m0, s21
	s_nop 0
	global_load_lds_dwordx4 v164, s[10:11]
	s_add_u32 s6, s10, 0x20000
	s_addc_u32 s7, s11, 0
	s_add_i32 s22, s18, 0x14000
	s_mov_b32 m0, s22
	s_nop 0
	global_load_lds_dwordx4 v147, s[6:7]
	s_add_i32 s23, s18, 0x16000
	s_mov_b32 m0, s23
	s_nop 0
	global_load_lds_dwordx4 v164, s[6:7]
	s_add_i32 s24, s18, 0x2000
	s_mov_b32 m0, s18
	s_nop 0
	global_load_lds_dwordx4 v173, s[74:75]
	s_add_i32 s25, s18, 0x4000
	s_mov_b32 m0, s24
	s_nop 0
	global_load_lds_dwordx4 v0, s[74:75]
	s_add_i32 s50, s18, 0x6000
	s_mov_b32 m0, s25
	s_nop 0
	global_load_lds_dwordx4 v175, s[74:75]
	s_cmp_eq_u32 s0, 1
	s_mov_b32 m0, s50
	s_nop 0
	global_load_lds_dwordx4 v174, s[74:75]
	s_cselect_b64 s[82:83], -1, 0
	s_cmp_lg_u32 s0, 1
	s_cbranch_scc1 .LBB0_407
	s_barrier
.LBB0_407:
	s_add_u32 s84, s94, 0x200000
	s_addc_u32 s85, s95, 0
	s_add_u32 s86, s94, 0x202000
	s_addc_u32 s87, s95, 0
	v_bfe_u32 v166, v2, 4, 2
	s_add_u32 s88, s94, 0x76800000
	v_and_b32_e32 v165, 15, v2
	v_lshlrev_b32_e32 v3, 4, v166
	v_lshlrev_b32_e32 v2, 2, v2
	s_addc_u32 s89, s95, 0
	s_and_b32 s5, s2, 3
	s_lshl_b32 s51, s0, 6
	v_lshl_or_b32 v3, v165, 6, v3
	s_lshl_b32 s0, s0, 13
	v_and_b32_e32 v2, 32, v2
	v_bitop3_b32 v4, v3, s0, v2 bitop3:0xde
	s_lshl_b32 s52, s5, 5
	s_lshl_b32 s0, s5, 12
	v_bitop3_b32 v2, v3, s0, v2 bitop3:0xde
	s_add_u32 s0, s10, 0x80
	s_waitcnt vmcnt(2)
	s_barrier
	s_addc_u32 s1, s11, 0
	s_add_i32 s53, s18, 0x18000
	s_mov_b32 m0, s53
	s_nop 0
	global_load_lds_dwordx4 v147, s[0:1]
	s_add_i32 s54, s18, 0x1a000
	s_mov_b32 m0, s54
	s_nop 0
	global_load_lds_dwordx4 v164, s[0:1]
	s_add_u32 s0, s94, 0x99000080
	v_writelane_b32 v232, s92, 18
	s_addc_u32 s1, s95, 0
	s_add_i32 s55, s18, 0x8000
	s_mov_b32 m0, s55
	s_nop 0
	global_load_lds_dwordx4 v173, s[0:1]
	s_add_i32 s56, s18, 0xa000
	s_mov_b32 m0, s56
	s_nop 0
	global_load_lds_dwordx4 v0, s[0:1]
	s_add_u32 s0, s10, 0x20080
	s_addc_u32 s1, s11, 0
	s_add_i32 s57, s18, 0x1c000
	s_mov_b32 m0, s57
	s_nop 0
	global_load_lds_dwordx4 v147, s[0:1]
	s_add_i32 s58, s18, 0x1e000
	s_mov_b32 m0, s58
	s_nop 0
	global_load_lds_dwordx4 v164, s[0:1]
	s_add_i32 s59, s18, 0xc000
	s_add_i32 s64, s18, 0xe000
	s_waitcnt vmcnt(6)
	s_cmpk_lt_u32 s4, 0x100
	v_writelane_b32 v232, s93, 19
	s_cselect_b64 s[90:91], -1, 0
	s_bitcmp0_b32 s4, 6
	v_writelane_b32 v232, s94, 20
	s_mov_b32 s65, 0
	s_cselect_b64 s[2:3], -1, 0
	s_lshl_b32 s66, s5, 11
	s_bfe_u32 s67, s4, 0x20008
	s_ashr_i32 s72, s29, 31
	s_ashr_i32 s73, s38, 31
	s_mov_b32 s81, s19
	s_lshr_b32 s97, s80, 3
	v_add_u32_e32 v167, 0, v2
	v_add_u32_e32 v168, 0, v4
	s_movk_i32 s47, 0x7ff
	v_writelane_b32 v232, s95, 21
	s_barrier
	s_branch .LBB0_410

; #define PG8_STAGE(bufoff, gbase, v0, v1) do { glds16_s((gbase), (v0), ldsbase + (unsigned)(bufoff)); glds16_s((gbase), (v1), ldsbase + (unsigned)(bufoff) + 8192u); } while (0)
; #define PG8_LDA(dst, b, h) do { _Pragma("unroll") for (int m = 0; m < 4; ++m) _Pragma("unroll") for (int k = 0; k < 2; ++k) dst[m][k] = *(const LAS bf16x8*)(lds + PG8_SA(b, h) + aoff + m * 2048 + k * 1024); } while (0)
; #define PG8_LDB(dst, b, h) do { _Pragma("unroll") for (int n = 0; n < 2; ++n) _Pragma("unroll") for (int k = 0; k < 2; ++k) dst[n][k] = *(const LAS bf16x8*)(lds + PG8_SB(b, h) + boff + n * 2048 + k * 1024); } while (0)
; #define PG8_WAIT_V(n) asm volatile("s_waitcnt vmcnt(" #n ")" ::: "memory")
; #define PG8_WAIT_L(n) asm volatile("s_waitcnt lgkmcnt(" #n ")" ::: "memory")
; #define PG8_BAR __builtin_amdgcn_s_barrier()
; #define PG8_SCHED __builtin_amdgcn_sched_barrier(0)
; template <class Epi, class Sched, bool ALIGN_EPI, bool FP8 = false>
; __device__ __forceinline__ void gemm_phase(LAS unsigned char* lds, const bf16_t* A, const bf16_t* Bt, const int K, const Sched& S, const Epi& E, const int wave_in) {
;     ...
;             const unsigned w00 = last ? vN[0][0] : vA[0][0], w01 = last ? vN[0][1] : vA[0][1], w10 = last ? vN[1][0] : vA[1][0], w11 = last ? vN[1][1] : vA[1][1];
;             PG8_LDB(B0, 0, 0); PG8_LDB(B1, 0, 1); PG8_SCHED; PG8_LDA(At, 0, 0); PG8_STAGE(PG8_SA(1, 1), a1, vA[1][0], vA[1][1]);
;             PG8_WAIT_V(8); PG8_WAIT_L(0); PG8_BAR; PG8_MMA(0, 0, At, B0); PG8_MMA(0, 1, At, B1); PG8_BAR; PG8_SCHED;
;     ...
; #pragma unroll
;         for (int a = 0; a < 2; ++a)
; #pragma unroll
;             for (int b = 0; b < 2; ++b)
; #pragma unroll
;                 for (int m = 0; m < 4; ++m)
; #pragma unroll
;                     for (int n = 0; n < 2; ++n) acc[a][b][m][n] = (f32x4){0.f, 0.f, 0.f, 0.f};
.LBB0_414:
	s_add_u32 s0, s10, 0x100
	s_waitcnt vmcnt(3)
	v_mov_b32_e32 v34, 0
	s_addc_u32 s1, s11, 0
	s_mov_b32 s77, -2
	s_mov_b64 s[26:27], s[74:75]
	v_mov_b32_e32 v35, 0
	s_waitcnt vmcnt(1)
	v_mov_b64_e32 v[36:37], 0
	v_mov_b64_e32 v[50:51], 0
	v_mov_b64_e32 v[52:53], 0
	v_mov_b64_e32 v[38:39], 0
	v_mov_b64_e32 v[40:41], 0
	v_mov_b64_e32 v[54:55], 0
	v_mov_b64_e32 v[56:57], 0
	v_mov_b64_e32 v[42:43], 0
	v_mov_b64_e32 v[44:45], 0
	v_mov_b64_e32 v[58:59], 0
	v_mov_b64_e32 v[60:61], 0
	v_mov_b64_e32 v[46:47], 0
	v_mov_b64_e32 v[48:49], 0
	v_mov_b64_e32 v[62:63], 0
	v_mov_b64_e32 v[64:65], 0
	v_mov_b64_e32 v[66:67], 0
	v_mov_b64_e32 v[68:69], 0
	v_mov_b64_e32 v[82:83], 0
	v_mov_b64_e32 v[84:85], 0
	v_mov_b64_e32 v[70:71], 0
	v_mov_b64_e32 v[72:73], 0
	v_mov_b64_e32 v[86:87], 0
	v_mov_b64_e32 v[88:89], 0
	v_mov_b64_e32 v[74:75], 0
	v_mov_b64_e32 v[76:77], 0
	v_mov_b64_e32 v[90:91], 0
	v_mov_b64_e32 v[92:93], 0
	v_mov_b64_e32 v[78:79], 0
	v_mov_b64_e32 v[80:81], 0
	v_mov_b64_e32 v[94:95], 0
	v_mov_b64_e32 v[96:97], 0
	v_mov_b64_e32 v[98:99], 0
	v_mov_b64_e32 v[100:101], 0
	v_mov_b64_e32 v[114:115], 0
	v_mov_b64_e32 v[116:117], 0
	v_mov_b64_e32 v[102:103], 0
	v_mov_b64_e32 v[104:105], 0
	v_mov_b64_e32 v[118:119], 0
	v_mov_b64_e32 v[120:121], 0
	v_mov_b64_e32 v[106:107], 0
	v_mov_b64_e32 v[108:109], 0
	v_mov_b64_e32 v[122:123], 0
	v_mov_b64_e32 v[124:125], 0
	v_mov_b64_e32 v[110:111], 0
	v_mov_b64_e32 v[112:113], 0
	v_mov_b64_e32 v[126:127], 0
	v_mov_b64_e32 v[128:129], 0
	v_mov_b64_e32 v[130:131], 0
	v_mov_b64_e32 v[132:133], 0
	v_mov_b64_e32 v[148:149], 0
	v_mov_b64_e32 v[150:151], 0
	v_mov_b64_e32 v[134:135], 0
	v_mov_b64_e32 v[136:137], 0
	v_mov_b64_e32 v[152:153], 0
	v_mov_b64_e32 v[154:155], 0
	v_mov_b64_e32 v[138:139], 0
	v_mov_b64_e32 v[140:141], 0
	v_mov_b64_e32 v[156:157], 0
	v_mov_b64_e32 v[158:159], 0
	v_mov_b64_e32 v[142:143], 0
	v_mov_b64_e32 v[144:145], 0
	v_mov_b64_e32 v[160:161], 0
	v_mov_b64_e32 v[162:163], 0
.LBB0_415:
	s_add_u32 s6, s26, 0x100
	s_addc_u32 s7, s27, 0
	v_add_u32_e32 v2, 0x10000, v167
	v_add_u32_e32 v6, 0x14000, v167
	s_cmp_eq_u32 s77, 4
	s_waitcnt vmcnt(0)
	ds_read_b128 v[26:29], v2
	ds_read_b128 v[30:33], v2 offset:1024
	ds_read_b128 v[18:21], v2 offset:2048
	ds_read_b128 v[22:25], v2 offset:3072
	ds_read_b128 v[10:13], v6
	ds_read_b128 v[14:17], v6 offset:1024
	ds_read_b128 v[2:5], v6 offset:2048
	ds_read_b128 v[6:9], v6 offset:3072
	s_cselect_b64 vcc, -1, 0
	s_and_b64 s[10:11], vcc, exec
	s_cselect_b32 s60, s74, s6
	s_cselect_b32 s61, s75, s7
	s_cselect_b32 s16, s94, s0
	s_cselect_b32 s17, s95, s1
	s_add_u32 s10, s60, 0x80
	s_addc_u32 s11, s61, 0
	s_add_u32 s48, s26, 0x80
	v_cndmask_b32_e32 v176, v173, v169, vcc
	v_cndmask_b32_e32 v178, v175, v171, vcc
	s_addc_u32 s49, s27, 0
	v_cndmask_b32_e32 v177, v0, v170, vcc
	ds_read_b128 v[198:201], v168
	ds_read_b128 v[202:205], v168 offset:1024
	ds_read_b128 v[206:209], v168 offset:2048
	ds_read_b128 v[210:213], v168 offset:3072
	ds_read_b128 v[214:217], v168 offset:4096
	ds_read_b128 v[218:221], v168 offset:5120
	ds_read_b128 v[222:225], v168 offset:6144
	ds_read_b128 v[226:229], v168 offset:7168
	s_mov_b32 m0, s59
	s_nop 0
	global_load_lds_dwordx4 v175, s[48:49]
	s_add_u32 s26, s16, 0x80
	s_mov_b32 m0, s64
	s_nop 0
	global_load_lds_dwordx4 v174, s[48:49]
	s_waitcnt vmcnt(8)
	s_waitcnt lgkmcnt(0)
	s_addc_u32 s27, s17, 0
	s_barrier
	s_setprio 1
	s_waitcnt lgkmcnt(6)
	v_mfma_scale_f32_16x16x128_f8f6f4 v[160:163], v[26:33], v[198:205], v[160:163], v186, v187 op_sel_hi:[0,0,0]
	v_mfma_scale_f32_16x16x128_f8f6f4 v[142:145], v[18:25], v[198:205], v[142:145], v186, v187 op_sel_hi:[0,0,0]
	s_waitcnt lgkmcnt(4)
	v_mfma_scale_f32_16x16x128_f8f6f4 v[156:159], v[26:33], v[206:213], v[156:159], v186, v187 op_sel_hi:[0,0,0]
	v_mfma_scale_f32_16x16x128_f8f6f4 v[138:141], v[18:25], v[206:213], v[138:141], v186, v187 op_sel_hi:[0,0,0]
	s_waitcnt lgkmcnt(2)
	v_mfma_scale_f32_16x16x128_f8f6f4 v[152:155], v[26:33], v[214:221], v[152:155], v186, v187 op_sel_hi:[0,0,0]
	v_mfma_scale_f32_16x16x128_f8f6f4 v[134:137], v[18:25], v[214:221], v[134:137], v186, v187 op_sel_hi:[0,0,0]
	s_waitcnt lgkmcnt(0)
	v_mfma_scale_f32_16x16x128_f8f6f4 v[148:151], v[26:33], v[222:229], v[148:151], v186, v187 op_sel_hi:[0,0,0]
	v_mfma_scale_f32_16x16x128_f8f6f4 v[130:133], v[18:25], v[222:229], v[130:133], v186, v187 op_sel_hi:[0,0,0]
	s_setprio 0
	s_setprio 1
	v_mfma_scale_f32_16x16x128_f8f6f4 v[126:129], v[10:17], v[198:205], v[126:129], v186, v187 op_sel_hi:[0,0,0]
	v_mfma_scale_f32_16x16x128_f8f6f4 v[110:113], v[2:9], v[198:205], v[110:113], v186, v187 op_sel_hi:[0,0,0]
	v_mfma_scale_f32_16x16x128_f8f6f4 v[122:125], v[10:17], v[206:213], v[122:125], v186, v187 op_sel_hi:[0,0,0]
	v_mfma_scale_f32_16x16x128_f8f6f4 v[106:109], v[2:9], v[206:213], v[106:109], v186, v187 op_sel_hi:[0,0,0]
	v_mfma_scale_f32_16x16x128_f8f6f4 v[118:121], v[10:17], v[214:221], v[118:121], v186, v187 op_sel_hi:[0,0,0]
	v_mfma_scale_f32_16x16x128_f8f6f4 v[102:105], v[2:9], v[214:221], v[102:105], v186, v187 op_sel_hi:[0,0,0]
	v_mfma_scale_f32_16x16x128_f8f6f4 v[114:117], v[10:17], v[222:229], v[114:117], v186, v187 op_sel_hi:[0,0,0]
	v_mfma_scale_f32_16x16x128_f8f6f4 v[98:101], v[2:9], v[222:229], v[98:101], v186, v187 op_sel_hi:[0,0,0]
	s_setprio 0
	s_barrier
; #define PG8_STAGE(bufoff, gbase, v0, v1) do { glds16_s((gbase), (v0), ldsbase + (unsigned)(bufoff)); glds16_s((gbase), (v1), ldsbase + (unsigned)(bufoff) + 8192u); } while (0)
; #define PG8_LDA(dst, b, h) do { _Pragma("unroll") for (int m = 0; m < 4; ++m) _Pragma("unroll") for (int k = 0; k < 2; ++k) dst[m][k] = *(const LAS bf16x8*)(lds + PG8_SA(b, h) + aoff + m * 2048 + k * 1024); } while (0)
; #define PG8_LDB(dst, b, h) do { _Pragma("unroll") for (int n = 0; n < 2; ++n) _Pragma("unroll") for (int k = 0; k < 2; ++k) dst[n][k] = *(const LAS bf16x8*)(lds + PG8_SB(b, h) + boff + n * 2048 + k * 1024); } while (0)
; #define PG8_WAIT_V(n) asm volatile("s_waitcnt vmcnt(" #n ")" ::: "memory")
; #define PG8_WAIT_L(n) asm volatile("s_waitcnt lgkmcnt(" #n ")" ::: "memory")
; #define PG8_BAR __builtin_amdgcn_s_barrier()
; #define PG8_SCHED __builtin_amdgcn_sched_barrier(0)
; template <class Epi, class Sched, bool ALIGN_EPI, bool FP8 = false>
; __device__ __forceinline__ void gemm_phase(LAS unsigned char* lds, const bf16_t* A, const bf16_t* Bt, const int K, const Sched& S, const Epi& E, const int wave_in) {
;     ...
;             PG8_WAIT_V(8); PG8_WAIT_L(0); PG8_BAR; PG8_MMA(0, 0, At, B0); PG8_MMA(0, 1, At, B1); PG8_BAR; PG8_SCHED;
;             PG8_LDA(At, 0, 1); PG8_STAGE(PG8_SB(0, 0), b2, voffB[0], voffB[1]); PG8_STAGE(PG8_SB(0, 1), b2 + hstep, voffB[0], voffB[1]); PG8_STAGE(PG8_SA(0, 0), a2, w00, w01);
;             PG8_WAIT_V(8); PG8_WAIT_L(0); PG8_BAR; PG8_MMA(1, 0, At, B0); PG8_MMA(1, 1, At, B1); PG8_BAR; PG8_SCHED;
;             PG8_LDB(B0, 1, 0); PG8_LDB(B1, 1, 1); PG8_SCHED; PG8_LDA(At, 1, 0); PG8_STAGE(PG8_SA(0, 1), a2, w10, w11);
;             PG8_WAIT_V(8); PG8_WAIT_L(0); PG8_BAR; PG8_MMA(0, 0, At, B0); PG8_MMA(0, 1, At, B1); PG8_BAR; PG8_SCHED;
	ds_read_b128 v[198:201], v168 offset:16384
	ds_read_b128 v[202:205], v168 offset:17408
	ds_read_b128 v[206:209], v168 offset:18432
	ds_read_b128 v[210:213], v168 offset:19456
	ds_read_b128 v[214:217], v168 offset:20480
	ds_read_b128 v[218:221], v168 offset:21504
	ds_read_b128 v[222:225], v168 offset:22528
	ds_read_b128 v[226:229], v168 offset:23552
	s_mov_b32 m0, s20
	s_nop 0
	global_load_lds_dwordx4 v147, s[16:17]
	s_add_u32 s48, s16, 0x20000
	s_mov_b32 m0, s21
	s_nop 0
	global_load_lds_dwordx4 v164, s[16:17]
	s_addc_u32 s49, s17, 0
	s_mov_b32 m0, s22
	s_nop 0
	global_load_lds_dwordx4 v147, s[48:49]
	s_nop 0
	s_mov_b32 m0, s23
	s_nop 0
	global_load_lds_dwordx4 v164, s[48:49]
	s_nop 0
	s_mov_b32 m0, s18
	s_nop 0
	global_load_lds_dwordx4 v176, s[60:61]
	s_nop 0
	s_mov_b32 m0, s24
	s_nop 0
	global_load_lds_dwordx4 v177, s[60:61]
	s_waitcnt vmcnt(8)
	s_waitcnt lgkmcnt(0)
	s_barrier
	s_setprio 1
	s_waitcnt lgkmcnt(6)
	v_mfma_scale_f32_16x16x128_f8f6f4 v[94:97], v[26:33], v[198:205], v[94:97], v186, v187 op_sel_hi:[0,0,0]
	v_mfma_scale_f32_16x16x128_f8f6f4 v[78:81], v[18:25], v[198:205], v[78:81], v186, v187 op_sel_hi:[0,0,0]
	s_waitcnt lgkmcnt(4)
	v_mfma_scale_f32_16x16x128_f8f6f4 v[90:93], v[26:33], v[206:213], v[90:93], v186, v187 op_sel_hi:[0,0,0]
	v_mfma_scale_f32_16x16x128_f8f6f4 v[74:77], v[18:25], v[206:213], v[74:77], v186, v187 op_sel_hi:[0,0,0]
	s_waitcnt lgkmcnt(2)
	v_mfma_scale_f32_16x16x128_f8f6f4 v[86:89], v[26:33], v[214:221], v[86:89], v186, v187 op_sel_hi:[0,0,0]
	v_mfma_scale_f32_16x16x128_f8f6f4 v[70:73], v[18:25], v[214:221], v[70:73], v186, v187 op_sel_hi:[0,0,0]
	s_waitcnt lgkmcnt(0)
	v_mfma_scale_f32_16x16x128_f8f6f4 v[82:85], v[26:33], v[222:229], v[82:85], v186, v187 op_sel_hi:[0,0,0]
	v_mfma_scale_f32_16x16x128_f8f6f4 v[66:69], v[18:25], v[222:229], v[66:69], v186, v187 op_sel_hi:[0,0,0]
	s_setprio 0
	s_setprio 1
	v_mfma_scale_f32_16x16x128_f8f6f4 v[62:65], v[10:17], v[198:205], v[62:65], v186, v187 op_sel_hi:[0,0,0]
	v_mfma_scale_f32_16x16x128_f8f6f4 v[46:49], v[2:9], v[198:205], v[46:49], v186, v187 op_sel_hi:[0,0,0]
	v_mfma_scale_f32_16x16x128_f8f6f4 v[58:61], v[10:17], v[206:213], v[58:61], v186, v187 op_sel_hi:[0,0,0]
	v_mfma_scale_f32_16x16x128_f8f6f4 v[42:45], v[2:9], v[206:213], v[42:45], v186, v187 op_sel_hi:[0,0,0]
	v_mfma_scale_f32_16x16x128_f8f6f4 v[54:57], v[10:17], v[214:221], v[54:57], v186, v187 op_sel_hi:[0,0,0]
	v_mfma_scale_f32_16x16x128_f8f6f4 v[38:41], v[2:9], v[214:221], v[38:41], v186, v187 op_sel_hi:[0,0,0]
	v_mfma_scale_f32_16x16x128_f8f6f4 v[50:53], v[10:17], v[222:229], v[50:53], v186, v187 op_sel_hi:[0,0,0]
	v_mfma_scale_f32_16x16x128_f8f6f4 v[34:37], v[2:9], v[222:229], v[34:37], v186, v187 op_sel_hi:[0,0,0]
	s_setprio 0
	s_barrier
	v_add_u32_e32 v14, 0x18000, v167
	v_add_u32_e32 v30, 0x1c000, v167
	ds_read_b128 v[2:5], v14
	ds_read_b128 v[6:9], v14 offset:1024
	ds_read_b128 v[10:13], v14 offset:2048
	ds_read_b128 v[14:17], v14 offset:3072
	ds_read_b128 v[18:21], v30
	ds_read_b128 v[22:25], v30 offset:1024
	ds_read_b128 v[26:29], v30 offset:2048
	ds_read_b128 v[30:33], v30 offset:3072
	ds_read_b128 v[198:201], v168 offset:32768
	ds_read_b128 v[202:205], v168 offset:33792
	ds_read_b128 v[206:209], v168 offset:34816
	ds_read_b128 v[210:213], v168 offset:35840
	ds_read_b128 v[214:217], v168 offset:36864
	ds_read_b128 v[218:221], v168 offset:37888
	ds_read_b128 v[222:225], v168 offset:38912
	ds_read_b128 v[226:229], v168 offset:39936
	s_mov_b32 m0, s25
	s_nop 0
	global_load_lds_dwordx4 v178, s[60:61]
	v_cndmask_b32_e32 v179, v174, v172, vcc
	s_mov_b32 m0, s50
	s_nop 0
	global_load_lds_dwordx4 v179, s[60:61]
	s_waitcnt vmcnt(8)
	s_waitcnt lgkmcnt(0)
	s_barrier
; #define PG8_STAGE(bufoff, gbase, v0, v1) do { glds16_s((gbase), (v0), ldsbase + (unsigned)(bufoff)); glds16_s((gbase), (v1), ldsbase + (unsigned)(bufoff) + 8192u); } while (0)
; #define PG8_LDA(dst, b, h) do { _Pragma("unroll") for (int m = 0; m < 4; ++m) _Pragma("unroll") for (int k = 0; k < 2; ++k) dst[m][k] = *(const LAS bf16x8*)(lds + PG8_SA(b, h) + aoff + m * 2048 + k * 1024); } while (0)
; #define PG8_WAIT_V(n) asm volatile("s_waitcnt vmcnt(" #n ")" ::: "memory")
; #define PG8_WAIT_L(n) asm volatile("s_waitcnt lgkmcnt(" #n ")" ::: "memory")
; #define PG8_BAR __builtin_amdgcn_s_barrier()
; #define PG8_SCHED __builtin_amdgcn_sched_barrier(0)
; template <class Epi, class Sched, bool ALIGN_EPI, bool FP8 = false>
; __device__ __forceinline__ void gemm_phase(LAS unsigned char* lds, const bf16_t* A, const bf16_t* Bt, const int K, const Sched& S, const Epi& E, const int wave_in) {
;     ...
;             PG8_WAIT_V(8); PG8_WAIT_L(0); PG8_BAR; PG8_MMA(0, 0, At, B0); PG8_MMA(0, 1, At, B1); PG8_BAR; PG8_SCHED;
;             PG8_LDA(At, 1, 1); PG8_STAGE(PG8_SB(1, 0), b3, voffB[0], voffB[1]); PG8_STAGE(PG8_SB(1, 1), b3 + hstep, voffB[0], voffB[1]); PG8_STAGE(PG8_SA(1, 0), a3, w00, w01);
;             PG8_WAIT_V(8); PG8_WAIT_L(0); PG8_BAR; PG8_MMA(1, 0, At, B0); PG8_MMA(1, 1, At, B1); PG8_BAR; PG8_SCHED;
;         }
;         if constexpr (FP8) asm volatile("s_nop 15\n\ts_nop 15" ::: "memory");
;         if constexpr (ALIGN_EPI) { if (wr == 0) PG8_BAR; }
	s_setprio 1
	s_waitcnt lgkmcnt(6)
	v_mfma_scale_f32_16x16x128_f8f6f4 v[160:163], v[2:9], v[198:205], v[160:163], v186, v187 op_sel_hi:[0,0,0]
	v_mfma_scale_f32_16x16x128_f8f6f4 v[142:145], v[10:17], v[198:205], v[142:145], v186, v187 op_sel_hi:[0,0,0]
	s_waitcnt lgkmcnt(4)
	v_mfma_scale_f32_16x16x128_f8f6f4 v[156:159], v[2:9], v[206:213], v[156:159], v186, v187 op_sel_hi:[0,0,0]
	v_mfma_scale_f32_16x16x128_f8f6f4 v[138:141], v[10:17], v[206:213], v[138:141], v186, v187 op_sel_hi:[0,0,0]
	s_waitcnt lgkmcnt(2)
	v_mfma_scale_f32_16x16x128_f8f6f4 v[152:155], v[2:9], v[214:221], v[152:155], v186, v187 op_sel_hi:[0,0,0]
	v_mfma_scale_f32_16x16x128_f8f6f4 v[134:137], v[10:17], v[214:221], v[134:137], v186, v187 op_sel_hi:[0,0,0]
	s_waitcnt lgkmcnt(0)
	v_mfma_scale_f32_16x16x128_f8f6f4 v[148:151], v[2:9], v[222:229], v[148:151], v186, v187 op_sel_hi:[0,0,0]
	v_mfma_scale_f32_16x16x128_f8f6f4 v[130:133], v[10:17], v[222:229], v[130:133], v186, v187 op_sel_hi:[0,0,0]
	s_setprio 0
	s_setprio 1
	v_mfma_scale_f32_16x16x128_f8f6f4 v[126:129], v[18:25], v[198:205], v[126:129], v186, v187 op_sel_hi:[0,0,0]
	v_mfma_scale_f32_16x16x128_f8f6f4 v[110:113], v[26:33], v[198:205], v[110:113], v186, v187 op_sel_hi:[0,0,0]
	v_mfma_scale_f32_16x16x128_f8f6f4 v[122:125], v[18:25], v[206:213], v[122:125], v186, v187 op_sel_hi:[0,0,0]
	v_mfma_scale_f32_16x16x128_f8f6f4 v[106:109], v[26:33], v[206:213], v[106:109], v186, v187 op_sel_hi:[0,0,0]
	v_mfma_scale_f32_16x16x128_f8f6f4 v[118:121], v[18:25], v[214:221], v[118:121], v186, v187 op_sel_hi:[0,0,0]
	v_mfma_scale_f32_16x16x128_f8f6f4 v[102:105], v[26:33], v[214:221], v[102:105], v186, v187 op_sel_hi:[0,0,0]
	v_mfma_scale_f32_16x16x128_f8f6f4 v[114:117], v[18:25], v[222:229], v[114:117], v186, v187 op_sel_hi:[0,0,0]
	v_mfma_scale_f32_16x16x128_f8f6f4 v[98:101], v[26:33], v[222:229], v[98:101], v186, v187 op_sel_hi:[0,0,0]
	s_setprio 0
	s_barrier
	ds_read_b128 v[198:201], v168 offset:49152
	ds_read_b128 v[202:205], v168 offset:50176
	ds_read_b128 v[206:209], v168 offset:51200
	ds_read_b128 v[210:213], v168 offset:52224
	ds_read_b128 v[214:217], v168 offset:53248
	ds_read_b128 v[218:221], v168 offset:54272
	ds_read_b128 v[222:225], v168 offset:55296
	ds_read_b128 v[226:229], v168 offset:56320
	s_mov_b32 m0, s53
	s_nop 0
	global_load_lds_dwordx4 v147, s[26:27]
	s_add_u32 s16, s16, 0x20080
	s_mov_b32 m0, s54
	s_nop 0
	global_load_lds_dwordx4 v164, s[26:27]
	s_addc_u32 s17, s17, 0
	s_mov_b32 m0, s57
	s_nop 0
	global_load_lds_dwordx4 v147, s[16:17]
	s_nop 0
	s_mov_b32 m0, s58
	s_nop 0
	global_load_lds_dwordx4 v164, s[16:17]
	s_nop 0
	s_mov_b32 m0, s55
	s_nop 0
	global_load_lds_dwordx4 v176, s[10:11]
	s_nop 0
	s_mov_b32 m0, s56
	s_nop 0
	global_load_lds_dwordx4 v177, s[10:11]
	s_waitcnt vmcnt(8)
	s_waitcnt lgkmcnt(0)
	s_barrier
	s_setprio 1
	s_waitcnt lgkmcnt(6)
	v_mfma_scale_f32_16x16x128_f8f6f4 v[94:97], v[2:9], v[198:205], v[94:97], v186, v187 op_sel_hi:[0,0,0]
	v_mfma_scale_f32_16x16x128_f8f6f4 v[78:81], v[10:17], v[198:205], v[78:81], v186, v187 op_sel_hi:[0,0,0]
	s_waitcnt lgkmcnt(4)
	v_mfma_scale_f32_16x16x128_f8f6f4 v[90:93], v[2:9], v[206:213], v[90:93], v186, v187 op_sel_hi:[0,0,0]
	v_mfma_scale_f32_16x16x128_f8f6f4 v[74:77], v[10:17], v[206:213], v[74:77], v186, v187 op_sel_hi:[0,0,0]
	s_waitcnt lgkmcnt(2)
	v_mfma_scale_f32_16x16x128_f8f6f4 v[86:89], v[2:9], v[214:221], v[86:89], v186, v187 op_sel_hi:[0,0,0]
	v_mfma_scale_f32_16x16x128_f8f6f4 v[70:73], v[10:17], v[214:221], v[70:73], v186, v187 op_sel_hi:[0,0,0]
	s_waitcnt lgkmcnt(0)
	v_mfma_scale_f32_16x16x128_f8f6f4 v[82:85], v[2:9], v[222:229], v[82:85], v186, v187 op_sel_hi:[0,0,0]
	v_mfma_scale_f32_16x16x128_f8f6f4 v[66:69], v[10:17], v[222:229], v[66:69], v186, v187 op_sel_hi:[0,0,0]
	s_setprio 0
	s_setprio 1
	v_mfma_scale_f32_16x16x128_f8f6f4 v[62:65], v[18:25], v[198:205], v[62:65], v186, v187 op_sel_hi:[0,0,0]
	v_mfma_scale_f32_16x16x128_f8f6f4 v[46:49], v[26:33], v[198:205], v[46:49], v186, v187 op_sel_hi:[0,0,0]
	v_mfma_scale_f32_16x16x128_f8f6f4 v[58:61], v[18:25], v[206:213], v[58:61], v186, v187 op_sel_hi:[0,0,0]
	v_mfma_scale_f32_16x16x128_f8f6f4 v[42:45], v[26:33], v[206:213], v[42:45], v186, v187 op_sel_hi:[0,0,0]
	v_mfma_scale_f32_16x16x128_f8f6f4 v[54:57], v[18:25], v[214:221], v[54:57], v186, v187 op_sel_hi:[0,0,0]
	v_mfma_scale_f32_16x16x128_f8f6f4 v[38:41], v[26:33], v[214:221], v[38:41], v186, v187 op_sel_hi:[0,0,0]
	v_mfma_scale_f32_16x16x128_f8f6f4 v[50:53], v[18:25], v[222:229], v[50:53], v186, v187 op_sel_hi:[0,0,0]
	v_mfma_scale_f32_16x16x128_f8f6f4 v[34:37], v[26:33], v[222:229], v[34:37], v186, v187 op_sel_hi:[0,0,0]
	s_setprio 0
	s_barrier
	s_add_i32 s77, s77, 2
	s_add_u32 s0, s0, 0x100
	s_addc_u32 s1, s1, 0
	s_cmp_gt_u32 s77, 5
	s_mov_b64 s[26:27], s[6:7]
	s_cbranch_scc0 .LBB0_415
	s_nop 15
	s_nop 15
	s_and_b64 vcc, exec, s[90:91]
	s_cbranch_vccz .LBB0_418
	s_barrier

; __device__ __forceinline__ int opaque_tid(int wave) { int l; asm volatile("v_mbcnt_lo_u32_b32 %0, -1, 0\n\tv_mbcnt_hi_u32_b32 %0, -1, %0" : "=v"(l)); return wave * 64 + l; }
; template <class Epi, class Sched, bool ALIGN_EPI, bool FP8 = false>
; __device__ __forceinline__ void gemm_phase(LAS unsigned char* lds, const bf16_t* A, const bf16_t* Bt, const int K, const Sched& S, const Epi& E, const int wave_in) {
;     const int tid = opaque_tid(wave_in); const int wid = __builtin_amdgcn_readfirstlane(tid >> 6), lane = tid & 63, wr = wid >> 2, wc = wid & 3, fr = lane & 15, fq = lane >> 4;
;     const int nt = K / BK;
;     int sR[2], sC[2]; unsigned voffB[2];
; #pragma unroll
;     for (int i = 0; i < 2; ++i) { stage_rc(tid * 16 + i * 8192, sR[i], sC[i]); const int Rb = Epi::PERM ? ((sR[i] & ~31) + perm32(sR[i] & 31)) : sR[i];
;         voffB[i] = (unsigned)(Rb * K + sC[i]) * 2u; }
;     const size_t kstep = (size_t)(BK * 2);
;     const size_t hstep = (size_t)HALF * K * 2;
;     const unsigned ldsw = (unsigned)wid * 1024u;
;     const unsigned ldsbase = (unsigned)__builtin_amdgcn_readfirstlane((int)((unsigned)(uintptr_t)lds + ldsw));
;     const int aoff = lds_byte(wr * 64 + fr, fq * 8), boff = lds_byte(wc * 32 + fr, fq * 8);
;     ...
;     Unit cur, nxt; int ui = 0;
;     if (!S.next(0, cur)) return;
;     f32x4 acc[2][2][4][2];
; #pragma unroll
;     for (int a = 0; a < 2; ++a)
; #pragma unroll
;         for (int b = 0; b < 2; ++b)
; #pragma unroll
;             for (int m = 0; m < 4; ++m)
; #pragma unroll
;                 for (int n = 0; n < 2; ++n) acc[a][b][m][n] = (f32x4){0.f, 0.f, 0.f, 0.f};
;     bf16x8 At[4][2], B0[2][2], B1[2][2];
;     const int sclW = W8_E8M0, sclA = A8_E8M0;
;     unsigned vA[2][2], vN[2][2];
;     PG8_AOFF(vA, cur);
;     const char* const cA = (const char*)A;
;     const char* cB = (const char*)Bt + S.b_off(cur) * 2;
;     PG8_STAGE(PG8_SB(0, 0), cB, voffB[0], voffB[1]); PG8_STAGE(PG8_SB(0, 1), cB + hstep, voffB[0], voffB[1]); PG8_STAGE(PG8_SA(0, 0), cA, vA[0][0], vA[0][1]); PG8_STAGE(PG8_SA(0, 1), cA, vA[1][0], vA[1][1]);
;     if (wr == 1) PG8_BAR;
;     PG8_WAIT_V(2); PG8_BAR;
;     PG8_STAGE(PG8_SB(1, 0), cB + kstep, voffB[0], voffB[1]); PG8_STAGE(PG8_SA(1, 0), cA + kstep, vA[0][0], vA[0][1]); PG8_STAGE(PG8_SB(1, 1), cB + hstep + kstep, voffB[0], voffB[1]);
;     PG8_WAIT_V(6); PG8_BAR;
.LBB0_449:
	s_and_b64 s[4:5], s[76:77], exec
	s_cselect_b32 s50, 0x400000, 0
	s_andn2_b64 vcc, exec, s[0:1]
	s_movk_i32 s56, 0x80
	s_mov_b32 s14, 0xbf3a00e3
	s_cbranch_vccnz .LBB0_499
	v_ashrrev_i32_e32 v4, 31, v0
	v_lshrrev_b32_e32 v4, 26, v4
	v_lshlrev_b32_e32 v3, 4, v0
	v_add_u32_e32 v4, v0, v4
	v_bfe_i32 v0, v0, 27, 1
	v_lshrrev_b32_e32 v0, 22, v0
	v_add_u32_e32 v0, v3, v0
	v_and_b32_e32 v0, 0xfffffc00, v0
	v_sub_u32_e32 v0, v3, v0
	v_lshrrev_b32_e32 v5, 4, v0
	v_bitop3_b32 v0, v5, v0, 32 bitop3:0x6c
	s_waitcnt vmcnt(5)
	v_ashrrev_i32_e32 v6, 31, v0
	s_add_u32 s80, s94, 0x99000000
	v_ashrrev_i32_e32 v4, 6, v4
	v_lshrrev_b32_e32 v6, 26, v6
	s_addc_u32 s81, s95, 0
	v_lshlrev_b32_e32 v5, 3, v4
	v_add_u32_e32 v6, v0, v6
	s_add_u32 s0, s94, s50
	v_and_b32_e32 v5, -16, v5
	v_ashrrev_i32_e32 v7, 6, v6
	v_and_b32_e32 v6, 0xc0, v6
	s_addc_u32 s1, s95, 0
	v_add_u32_e32 v5, v7, v5
	v_sub_u32_e32 v0, v0, v6
	s_add_u32 s20, s0, 0x1800000
	v_lshlrev_b32_e32 v4, 5, v4
	v_ashrrev_i16_sdwa v0, v185, sext(v0) dst_sel:DWORD dst_unused:UNUSED_PAD src0_sel:DWORD src1_sel:BYTE_0
	v_lshlrev_b32_e32 v6, 1, v5
	v_lshrrev_b32_e32 v8, 2, v5
	v_and_b32_e32 v7, 3, v7
	s_mov_b32 s0, 0x3fffe0
	v_and_b32_e32 v4, 32, v4
	v_bfe_i32 v0, v0, 0, 16
	v_and_b32_e32 v6, 24, v6
	v_and_b32_e32 v8, 4, v8
	v_and_or_b32 v7, v5, s0, v7
	v_or3_b32 v6, v7, v8, v6
	v_add_lshl_u32 v4, v4, v0, 1
	v_add_u32_e32 v3, 0x2000, v3
	v_lshl_add_u32 v0, v6, 10, v4
	v_ashrrev_i32_e32 v6, 31, v3
	v_lshrrev_b32_e32 v6, 22, v6
	v_add_u32_e32 v6, v3, v6
	v_ashrrev_i32_e32 v6, 10, v6
	v_mul_i32_i24_e32 v7, 0x400, v6
	v_sub_u32_e32 v3, v3, v7
	v_lshrrev_b32_e32 v7, 4, v3
	v_bitop3_b32 v3, v7, v3, 32 bitop3:0x6c
	v_ashrrev_i32_e32 v8, 31, v3
	v_lshrrev_b32_e32 v8, 26, v8
	v_add_u32_e32 v8, v3, v8
	v_ashrrev_i32_e32 v9, 6, v8
	v_and_b32_e32 v8, 0xc0, v8
	v_sub_u32_e32 v3, v3, v8
	v_lshlrev_b32_e32 v7, 3, v6
	v_lshlrev_b32_e32 v6, 5, v6
	v_ashrrev_i16_sdwa v3, v185, sext(v3) dst_sel:DWORD dst_unused:UNUSED_PAD src0_sel:DWORD src1_sel:BYTE_0
	v_and_b32_e32 v7, -16, v7
	v_and_b32_e32 v6, 32, v6
	v_bfe_i32 v3, v3, 0, 16
	s_addc_u32 s21, s1, 0
	v_add_u32_e32 v7, v9, v7
	v_add_lshl_u32 v3, v6, v3, 1
	s_lshl_b32 s1, s3, 10
	v_and_b32_e32 v9, 3, v9
	s_add_i32 s22, s1, 0
	s_lshl_b32 s1, s28, 18
	v_lshl_add_u32 v164, v5, 10, v4
	v_lshl_add_u32 v165, v7, 10, v3
	s_ashr_i32 s7, s6, 31
	v_lshlrev_b32_e32 v8, 1, v7
	s_waitcnt vmcnt(4)
	v_lshrrev_b32_e32 v10, 2, v7
	v_and_or_b32 v9, v7, s0, v9
	s_ashr_i32 s0, s2, 8
	v_add_u32_e32 v174, s1, v164
	v_add_u32_e32 v175, s1, v165
	s_bitset1_b32 s1, 17
	s_lshl_b64 s[4:5], s[6:7], 18
	v_and_b32_e32 v8, 24, v8
	v_and_b32_e32 v10, 4, v10
	s_add_u32 s8, s20, s4
	v_or3_b32 v8, v9, v10, v8
	v_add_u32_e32 v177, s1, v164
	v_add_u32_e32 v176, s1, v165
	s_addc_u32 s9, s21, s5
	s_add_i32 s23, s22, 0x10000
	s_mov_b32 m0, s23
	s_nop 0
	global_load_lds_dwordx4 v0, s[8:9]
	s_add_i32 s24, s22, 0x12000
	v_lshl_add_u32 v147, v8, 10, v3
	s_mov_b32 m0, s24
	s_nop 0
	global_load_lds_dwordx4 v147, s[8:9]
	s_add_u32 s4, s8, 0x20000
	s_addc_u32 s5, s9, 0
	s_add_i32 s25, s22, 0x14000
	s_mov_b32 m0, s25
	s_nop 0
	global_load_lds_dwordx4 v0, s[4:5]
	s_add_i32 s51, s22, 0x16000
	s_mov_b32 m0, s51
	s_nop 0
	global_load_lds_dwordx4 v147, s[4:5]
	s_add_i32 s52, s22, 0x2000
	s_mov_b32 m0, s22
	s_nop 0
	global_load_lds_dwordx4 v174, s[80:81]
	s_add_i32 s53, s22, 0x4000
	s_mov_b32 m0, s52
	s_nop 0
	global_load_lds_dwordx4 v175, s[80:81]
	s_add_i32 s54, s22, 0x6000
	s_mov_b32 m0, s53
	s_nop 0
	global_load_lds_dwordx4 v177, s[80:81]
	s_cmp_eq_u32 s0, 1
	s_mov_b32 m0, s54
	s_nop 0
	global_load_lds_dwordx4 v176, s[80:81]
	s_cselect_b64 s[82:83], -1, 0
	s_cmp_lg_u32 s0, 1
	s_cbranch_scc1 .LBB0_452
	s_barrier
.LBB0_452:
	v_bfe_u32 v167, v2, 4, 2
	s_add_u32 s84, s94, 0x9d400000
	v_and_b32_e32 v166, 15, v2
	v_lshlrev_b32_e32 v3, 4, v167
	v_lshlrev_b32_e32 v2, 2, v2
	s_addc_u32 s85, s95, 0
	s_and_b32 s18, s3, 3
	s_lshl_b32 s55, s0, 6
	v_lshl_or_b32 v3, v166, 6, v3
	s_lshl_b32 s0, s0, 13
	v_and_b32_e32 v2, 32, v2
	v_bitop3_b32 v4, v3, s0, v2 bitop3:0xde
	s_lshl_b32 s56, s18, 5
	s_lshl_b32 s0, s18, 12
	v_bitop3_b32 v2, v3, s0, v2 bitop3:0xde
	s_add_u32 s0, s8, 0x80
	s_waitcnt vmcnt(2)
	s_barrier
	s_addc_u32 s1, s9, 0
	s_add_i32 s57, s22, 0x18000
	s_mov_b32 m0, s57
	s_nop 0
	global_load_lds_dwordx4 v0, s[0:1]
	s_add_i32 s58, s22, 0x1a000
	s_mov_b32 m0, s58
	s_nop 0
	global_load_lds_dwordx4 v147, s[0:1]
	s_add_u32 s0, s94, 0x99000080
	v_writelane_b32 v232, s92, 18
	s_addc_u32 s1, s95, 0
	s_add_i32 s59, s22, 0x8000
	s_mov_b32 m0, s59
	s_nop 0
	global_load_lds_dwordx4 v174, s[0:1]
	s_add_i32 s64, s22, 0xa000
	s_mov_b32 m0, s64
	s_nop 0
	global_load_lds_dwordx4 v175, s[0:1]
	s_add_u32 s0, s8, 0x20080
	s_addc_u32 s1, s9, 0
	s_add_i32 s65, s22, 0x1c000
	s_mov_b32 m0, s65
	s_nop 0
	global_load_lds_dwordx4 v0, s[0:1]
	s_add_i32 s66, s22, 0x1e000
	s_mov_b32 m0, s66
	s_nop 0
	global_load_lds_dwordx4 v147, s[0:1]
	v_writelane_b32 v232, s93, 19
	s_waitcnt vmcnt(6)
	s_add_i32 s67, s22, 0xc000
	s_add_i32 s72, s22, 0xe000
	v_writelane_b32 v232, s94, 20
	s_cmpk_lt_u32 s2, 0x100
	v_writelane_b32 v232, s95, 21
	s_cselect_b64 s[86:87], -1, 0
	s_ashr_i32 s73, s29, 31
	s_ashr_i32 s94, s38, 31
	s_mov_b32 s75, s19
	s_lshr_b32 s41, s41, 7
	s_mov_b32 s95, 0
	v_add_u32_e32 v168, 0, v2
	v_add_u32_e32 v169, 0, v4
	s_barrier
	s_waitcnt vmcnt(0)
	s_branch .LBB0_455

; #define PG8_STAGE(bufoff, gbase, v0, v1) do { glds16_s((gbase), (v0), ldsbase + (unsigned)(bufoff)); glds16_s((gbase), (v1), ldsbase + (unsigned)(bufoff) + 8192u); } while (0)
; #define PG8_LDA(dst, b, h) do { _Pragma("unroll") for (int m = 0; m < 4; ++m) _Pragma("unroll") for (int k = 0; k < 2; ++k) dst[m][k] = *(const LAS bf16x8*)(lds + PG8_SA(b, h) + aoff + m * 2048 + k * 1024); } while (0)
; #define PG8_LDB(dst, b, h) do { _Pragma("unroll") for (int n = 0; n < 2; ++n) _Pragma("unroll") for (int k = 0; k < 2; ++k) dst[n][k] = *(const LAS bf16x8*)(lds + PG8_SB(b, h) + boff + n * 2048 + k * 1024); } while (0)
; #define PG8_WAIT_V(n) asm volatile("s_waitcnt vmcnt(" #n ")" ::: "memory")
; #define PG8_WAIT_L(n) asm volatile("s_waitcnt lgkmcnt(" #n ")" ::: "memory")
; #define PG8_BAR __builtin_amdgcn_s_barrier()
; #define PG8_SCHED __builtin_amdgcn_sched_barrier(0)
; template <class Epi, class Sched, bool ALIGN_EPI, bool FP8 = false>
; __device__ __forceinline__ void gemm_phase(LAS unsigned char* lds, const bf16_t* A, const bf16_t* Bt, const int K, const Sched& S, const Epi& E, const int wave_in) {
;     ...
;             const unsigned w00 = last ? vN[0][0] : vA[0][0], w01 = last ? vN[0][1] : vA[0][1], w10 = last ? vN[1][0] : vA[1][0], w11 = last ? vN[1][1] : vA[1][1];
;             PG8_LDB(B0, 0, 0); PG8_LDB(B1, 0, 1); PG8_SCHED; PG8_LDA(At, 0, 0); PG8_STAGE(PG8_SA(1, 1), a1, vA[1][0], vA[1][1]);
;             PG8_WAIT_V(8); PG8_WAIT_L(0); PG8_BAR; PG8_MMA(0, 0, At, B0); PG8_MMA(0, 1, At, B1); PG8_BAR; PG8_SCHED;
;     ...
; #pragma unroll
;         for (int a = 0; a < 2; ++a)
; #pragma unroll
;             for (int b = 0; b < 2; ++b)
; #pragma unroll
;                 for (int m = 0; m < 4; ++m)
; #pragma unroll
;                     for (int n = 0; n < 2; ++n) acc[a][b][m][n] = (f32x4){0.f, 0.f, 0.f, 0.f};
.LBB0_459:
	s_add_u32 s0, s8, 0x100
	v_mov_b32_e32 v34, 0
	s_addc_u32 s1, s9, 0
	s_mov_b32 s7, -2
	s_mov_b64 s[26:27], s[80:81]
	v_mov_b32_e32 v35, 0
	v_mov_b64_e32 v[36:37], 0
	v_mov_b64_e32 v[38:39], 0
	v_mov_b64_e32 v[40:41], 0
	v_mov_b64_e32 v[50:51], 0
	v_mov_b64_e32 v[52:53], 0
	v_mov_b64_e32 v[54:55], 0
	v_mov_b64_e32 v[56:57], 0
	v_mov_b64_e32 v[66:67], 0
	v_mov_b64_e32 v[68:69], 0
	v_mov_b64_e32 v[70:71], 0
	v_mov_b64_e32 v[72:73], 0
	v_mov_b64_e32 v[82:83], 0
	v_mov_b64_e32 v[84:85], 0
	v_mov_b64_e32 v[86:87], 0
	v_mov_b64_e32 v[88:89], 0
	v_mov_b64_e32 v[42:43], 0
	v_mov_b64_e32 v[44:45], 0
	v_mov_b64_e32 v[46:47], 0
	v_mov_b64_e32 v[48:49], 0
	v_mov_b64_e32 v[58:59], 0
	v_mov_b64_e32 v[60:61], 0
	v_mov_b64_e32 v[62:63], 0
	v_mov_b64_e32 v[64:65], 0
	v_mov_b64_e32 v[74:75], 0
	v_mov_b64_e32 v[76:77], 0
	v_mov_b64_e32 v[78:79], 0
	v_mov_b64_e32 v[80:81], 0
	v_mov_b64_e32 v[90:91], 0
	v_mov_b64_e32 v[92:93], 0
	v_mov_b64_e32 v[94:95], 0
	v_mov_b64_e32 v[96:97], 0
	v_mov_b64_e32 v[98:99], 0
	v_mov_b64_e32 v[100:101], 0
	v_mov_b64_e32 v[102:103], 0
	v_mov_b64_e32 v[104:105], 0
	v_mov_b64_e32 v[114:115], 0
	v_mov_b64_e32 v[116:117], 0
	v_mov_b64_e32 v[118:119], 0
	v_mov_b64_e32 v[120:121], 0
	v_mov_b64_e32 v[130:131], 0
	v_mov_b64_e32 v[132:133], 0
	v_mov_b64_e32 v[134:135], 0
	v_mov_b64_e32 v[136:137], 0
	v_mov_b64_e32 v[148:149], 0
	v_mov_b64_e32 v[150:151], 0
	v_mov_b64_e32 v[152:153], 0
	v_mov_b64_e32 v[154:155], 0
	v_mov_b64_e32 v[106:107], 0
	v_mov_b64_e32 v[108:109], 0
	v_mov_b64_e32 v[110:111], 0
	v_mov_b64_e32 v[112:113], 0
	v_mov_b64_e32 v[122:123], 0
	v_mov_b64_e32 v[124:125], 0
	v_mov_b64_e32 v[126:127], 0
	v_mov_b64_e32 v[128:129], 0
	v_mov_b64_e32 v[138:139], 0
	v_mov_b64_e32 v[140:141], 0
	v_mov_b64_e32 v[142:143], 0
	v_mov_b64_e32 v[144:145], 0
	v_mov_b64_e32 v[156:157], 0
	v_mov_b64_e32 v[158:159], 0
	v_mov_b64_e32 v[160:161], 0
	v_mov_b64_e32 v[162:163], 0
.LBB0_460:
	s_add_u32 s4, s26, 0x100
	s_addc_u32 s5, s27, 0
	v_add_u32_e32 v2, 0x10000, v168
	v_add_u32_e32 v6, 0x14000, v168
	s_cmp_eq_u32 s7, 4
	ds_read_b128 v[26:29], v2
	ds_read_b128 v[30:33], v2 offset:1024
	ds_read_b128 v[18:21], v2 offset:2048
	ds_read_b128 v[22:25], v2 offset:3072
	ds_read_b128 v[10:13], v6
	ds_read_b128 v[14:17], v6 offset:1024
	ds_read_b128 v[2:5], v6 offset:2048
	ds_read_b128 v[6:9], v6 offset:3072
	s_cselect_b64 vcc, -1, 0
	s_and_b64 s[8:9], vcc, exec
	s_cselect_b32 s60, s80, s4
	s_cselect_b32 s61, s81, s5
	s_cselect_b32 s16, s90, s0
	s_cselect_b32 s17, s91, s1
	s_add_u32 s10, s60, 0x80
	s_addc_u32 s11, s61, 0
	s_add_u32 s8, s26, 0x80
	v_cndmask_b32_e32 v178, v174, v170, vcc
	v_cndmask_b32_e32 v180, v177, v172, vcc
	s_addc_u32 s9, s27, 0
	v_cndmask_b32_e32 v179, v175, v171, vcc
	ds_read_b128 v[198:201], v169
	ds_read_b128 v[202:205], v169 offset:1024
	ds_read_b128 v[206:209], v169 offset:2048
	ds_read_b128 v[210:213], v169 offset:3072
	ds_read_b128 v[214:217], v169 offset:4096
	ds_read_b128 v[218:221], v169 offset:5120
	ds_read_b128 v[222:225], v169 offset:6144
	ds_read_b128 v[226:229], v169 offset:7168
	s_mov_b32 m0, s67
	s_nop 0
	global_load_lds_dwordx4 v177, s[8:9]
	s_add_u32 s26, s16, 0x80
	s_mov_b32 m0, s72
	s_nop 0
	global_load_lds_dwordx4 v176, s[8:9]
	s_waitcnt vmcnt(8)
	s_waitcnt lgkmcnt(0)
	s_addc_u32 s27, s17, 0
	s_barrier
	s_setprio 1
	s_waitcnt lgkmcnt(6)
	v_mfma_scale_f32_16x16x128_f8f6f4 v[160:163], v[26:33], v[198:205], v[160:163], v186, v187 op_sel_hi:[0,0,0]
	v_mfma_scale_f32_16x16x128_f8f6f4 v[156:159], v[18:25], v[198:205], v[156:159], v186, v187 op_sel_hi:[0,0,0]
	s_waitcnt lgkmcnt(4)
	v_mfma_scale_f32_16x16x128_f8f6f4 v[142:145], v[26:33], v[206:213], v[142:145], v186, v187 op_sel_hi:[0,0,0]
	v_mfma_scale_f32_16x16x128_f8f6f4 v[138:141], v[18:25], v[206:213], v[138:141], v186, v187 op_sel_hi:[0,0,0]
	s_waitcnt lgkmcnt(2)
	v_mfma_scale_f32_16x16x128_f8f6f4 v[126:129], v[26:33], v[214:221], v[126:129], v186, v187 op_sel_hi:[0,0,0]
	v_mfma_scale_f32_16x16x128_f8f6f4 v[122:125], v[18:25], v[214:221], v[122:125], v186, v187 op_sel_hi:[0,0,0]
	s_waitcnt lgkmcnt(0)
	v_mfma_scale_f32_16x16x128_f8f6f4 v[110:113], v[26:33], v[222:229], v[110:113], v186, v187 op_sel_hi:[0,0,0]
	v_mfma_scale_f32_16x16x128_f8f6f4 v[106:109], v[18:25], v[222:229], v[106:109], v186, v187 op_sel_hi:[0,0,0]
	s_setprio 0
	s_setprio 1
	v_mfma_scale_f32_16x16x128_f8f6f4 v[152:155], v[10:17], v[198:205], v[152:155], v186, v187 op_sel_hi:[0,0,0]
	v_mfma_scale_f32_16x16x128_f8f6f4 v[148:151], v[2:9], v[198:205], v[148:151], v186, v187 op_sel_hi:[0,0,0]
	v_mfma_scale_f32_16x16x128_f8f6f4 v[134:137], v[10:17], v[206:213], v[134:137], v186, v187 op_sel_hi:[0,0,0]
	v_mfma_scale_f32_16x16x128_f8f6f4 v[130:133], v[2:9], v[206:213], v[130:133], v186, v187 op_sel_hi:[0,0,0]
	v_mfma_scale_f32_16x16x128_f8f6f4 v[118:121], v[10:17], v[214:221], v[118:121], v186, v187 op_sel_hi:[0,0,0]
	v_mfma_scale_f32_16x16x128_f8f6f4 v[114:117], v[2:9], v[214:221], v[114:117], v186, v187 op_sel_hi:[0,0,0]
	v_mfma_scale_f32_16x16x128_f8f6f4 v[102:105], v[10:17], v[222:229], v[102:105], v186, v187 op_sel_hi:[0,0,0]
	v_mfma_scale_f32_16x16x128_f8f6f4 v[98:101], v[2:9], v[222:229], v[98:101], v186, v187 op_sel_hi:[0,0,0]
	s_setprio 0
	s_barrier
; #define PG8_STAGE(bufoff, gbase, v0, v1) do { glds16_s((gbase), (v0), ldsbase + (unsigned)(bufoff)); glds16_s((gbase), (v1), ldsbase + (unsigned)(bufoff) + 8192u); } while (0)
; #define PG8_LDA(dst, b, h) do { _Pragma("unroll") for (int m = 0; m < 4; ++m) _Pragma("unroll") for (int k = 0; k < 2; ++k) dst[m][k] = *(const LAS bf16x8*)(lds + PG8_SA(b, h) + aoff + m * 2048 + k * 1024); } while (0)
; #define PG8_LDB(dst, b, h) do { _Pragma("unroll") for (int n = 0; n < 2; ++n) _Pragma("unroll") for (int k = 0; k < 2; ++k) dst[n][k] = *(const LAS bf16x8*)(lds + PG8_SB(b, h) + boff + n * 2048 + k * 1024); } while (0)
; #define PG8_WAIT_V(n) asm volatile("s_waitcnt vmcnt(" #n ")" ::: "memory")
; #define PG8_WAIT_L(n) asm volatile("s_waitcnt lgkmcnt(" #n ")" ::: "memory")
; #define PG8_BAR __builtin_amdgcn_s_barrier()
; #define PG8_SCHED __builtin_amdgcn_sched_barrier(0)
; template <class Epi, class Sched, bool ALIGN_EPI, bool FP8 = false>
; __device__ __forceinline__ void gemm_phase(LAS unsigned char* lds, const bf16_t* A, const bf16_t* Bt, const int K, const Sched& S, const Epi& E, const int wave_in) {
;     ...
;             PG8_WAIT_V(8); PG8_WAIT_L(0); PG8_BAR; PG8_MMA(0, 0, At, B0); PG8_MMA(0, 1, At, B1); PG8_BAR; PG8_SCHED;
;             PG8_LDA(At, 0, 1); PG8_STAGE(PG8_SB(0, 0), b2, voffB[0], voffB[1]); PG8_STAGE(PG8_SB(0, 1), b2 + hstep, voffB[0], voffB[1]); PG8_STAGE(PG8_SA(0, 0), a2, w00, w01);
;             PG8_WAIT_V(8); PG8_WAIT_L(0); PG8_BAR; PG8_MMA(1, 0, At, B0); PG8_MMA(1, 1, At, B1); PG8_BAR; PG8_SCHED;
;             PG8_LDB(B0, 1, 0); PG8_LDB(B1, 1, 1); PG8_SCHED; PG8_LDA(At, 1, 0); PG8_STAGE(PG8_SA(0, 1), a2, w10, w11);
;             PG8_WAIT_V(8); PG8_WAIT_L(0); PG8_BAR; PG8_MMA(0, 0, At, B0); PG8_MMA(0, 1, At, B1); PG8_BAR; PG8_SCHED;
	ds_read_b128 v[198:201], v169 offset:16384
	ds_read_b128 v[202:205], v169 offset:17408
	ds_read_b128 v[206:209], v169 offset:18432
	ds_read_b128 v[210:213], v169 offset:19456
	ds_read_b128 v[214:217], v169 offset:20480
	ds_read_b128 v[218:221], v169 offset:21504
	ds_read_b128 v[222:225], v169 offset:22528
	ds_read_b128 v[226:229], v169 offset:23552
	s_mov_b32 m0, s23
	s_nop 0
	global_load_lds_dwordx4 v0, s[16:17]
	s_nop 0
	s_mov_b32 m0, s24
	s_nop 0
	global_load_lds_dwordx4 v147, s[16:17]
	s_add_u32 s8, s16, 0x20000
	s_addc_u32 s9, s17, 0
	s_mov_b32 m0, s25
	s_nop 0
	global_load_lds_dwordx4 v0, s[8:9]
	s_nop 0
	s_mov_b32 m0, s51
	s_nop 0
	global_load_lds_dwordx4 v147, s[8:9]
	s_mov_b32 m0, s22
	s_nop 0
	global_load_lds_dwordx4 v178, s[60:61]
	s_nop 0
	s_mov_b32 m0, s52
	s_nop 0
	global_load_lds_dwordx4 v179, s[60:61]
	s_waitcnt vmcnt(8)
	s_waitcnt lgkmcnt(0)
	s_barrier
	s_setprio 1
	s_waitcnt lgkmcnt(6)
	v_mfma_scale_f32_16x16x128_f8f6f4 v[94:97], v[26:33], v[198:205], v[94:97], v186, v187 op_sel_hi:[0,0,0]
	v_mfma_scale_f32_16x16x128_f8f6f4 v[90:93], v[18:25], v[198:205], v[90:93], v186, v187 op_sel_hi:[0,0,0]
	s_waitcnt lgkmcnt(4)
	v_mfma_scale_f32_16x16x128_f8f6f4 v[78:81], v[26:33], v[206:213], v[78:81], v186, v187 op_sel_hi:[0,0,0]
	v_mfma_scale_f32_16x16x128_f8f6f4 v[74:77], v[18:25], v[206:213], v[74:77], v186, v187 op_sel_hi:[0,0,0]
	s_waitcnt lgkmcnt(2)
	v_mfma_scale_f32_16x16x128_f8f6f4 v[62:65], v[26:33], v[214:221], v[62:65], v186, v187 op_sel_hi:[0,0,0]
	v_mfma_scale_f32_16x16x128_f8f6f4 v[58:61], v[18:25], v[214:221], v[58:61], v186, v187 op_sel_hi:[0,0,0]
	s_waitcnt lgkmcnt(0)
	v_mfma_scale_f32_16x16x128_f8f6f4 v[46:49], v[26:33], v[222:229], v[46:49], v186, v187 op_sel_hi:[0,0,0]
	v_mfma_scale_f32_16x16x128_f8f6f4 v[42:45], v[18:25], v[222:229], v[42:45], v186, v187 op_sel_hi:[0,0,0]
	s_setprio 0
	s_setprio 1
	v_mfma_scale_f32_16x16x128_f8f6f4 v[86:89], v[10:17], v[198:205], v[86:89], v186, v187 op_sel_hi:[0,0,0]
	v_mfma_scale_f32_16x16x128_f8f6f4 v[82:85], v[2:9], v[198:205], v[82:85], v186, v187 op_sel_hi:[0,0,0]
	v_mfma_scale_f32_16x16x128_f8f6f4 v[70:73], v[10:17], v[206:213], v[70:73], v186, v187 op_sel_hi:[0,0,0]
	v_mfma_scale_f32_16x16x128_f8f6f4 v[66:69], v[2:9], v[206:213], v[66:69], v186, v187 op_sel_hi:[0,0,0]
	v_mfma_scale_f32_16x16x128_f8f6f4 v[54:57], v[10:17], v[214:221], v[54:57], v186, v187 op_sel_hi:[0,0,0]
	v_mfma_scale_f32_16x16x128_f8f6f4 v[50:53], v[2:9], v[214:221], v[50:53], v186, v187 op_sel_hi:[0,0,0]
	v_mfma_scale_f32_16x16x128_f8f6f4 v[38:41], v[10:17], v[222:229], v[38:41], v186, v187 op_sel_hi:[0,0,0]
	v_mfma_scale_f32_16x16x128_f8f6f4 v[34:37], v[2:9], v[222:229], v[34:37], v186, v187 op_sel_hi:[0,0,0]
	s_setprio 0
	s_barrier
	v_add_u32_e32 v14, 0x18000, v168
	v_add_u32_e32 v30, 0x1c000, v168
	ds_read_b128 v[2:5], v14
	ds_read_b128 v[6:9], v14 offset:1024
	ds_read_b128 v[10:13], v14 offset:2048
	ds_read_b128 v[14:17], v14 offset:3072
	ds_read_b128 v[18:21], v30
	ds_read_b128 v[22:25], v30 offset:1024
	ds_read_b128 v[26:29], v30 offset:2048
	ds_read_b128 v[30:33], v30 offset:3072
	ds_read_b128 v[198:201], v169 offset:32768
	ds_read_b128 v[202:205], v169 offset:33792
	ds_read_b128 v[206:209], v169 offset:34816
	ds_read_b128 v[210:213], v169 offset:35840
	ds_read_b128 v[214:217], v169 offset:36864
	ds_read_b128 v[218:221], v169 offset:37888
	ds_read_b128 v[222:225], v169 offset:38912
	ds_read_b128 v[226:229], v169 offset:39936
	s_mov_b32 m0, s53
	s_nop 0
	global_load_lds_dwordx4 v180, s[60:61]
	v_cndmask_b32_e32 v181, v176, v173, vcc
	s_mov_b32 m0, s54
	s_nop 0
	global_load_lds_dwordx4 v181, s[60:61]
	s_waitcnt vmcnt(8)
	s_waitcnt lgkmcnt(0)
	s_barrier
; #define PG8_STAGE(bufoff, gbase, v0, v1) do { glds16_s((gbase), (v0), ldsbase + (unsigned)(bufoff)); glds16_s((gbase), (v1), ldsbase + (unsigned)(bufoff) + 8192u); } while (0)
; #define PG8_LDA(dst, b, h) do { _Pragma("unroll") for (int m = 0; m < 4; ++m) _Pragma("unroll") for (int k = 0; k < 2; ++k) dst[m][k] = *(const LAS bf16x8*)(lds + PG8_SA(b, h) + aoff + m * 2048 + k * 1024); } while (0)
; #define PG8_WAIT_V(n) asm volatile("s_waitcnt vmcnt(" #n ")" ::: "memory")
; #define PG8_WAIT_L(n) asm volatile("s_waitcnt lgkmcnt(" #n ")" ::: "memory")
; #define PG8_BAR __builtin_amdgcn_s_barrier()
; #define PG8_SCHED __builtin_amdgcn_sched_barrier(0)
; template <class Epi, class Sched, bool ALIGN_EPI, bool FP8 = false>
; __device__ __forceinline__ void gemm_phase(LAS unsigned char* lds, const bf16_t* A, const bf16_t* Bt, const int K, const Sched& S, const Epi& E, const int wave_in) {
;     ...
;             PG8_WAIT_V(8); PG8_WAIT_L(0); PG8_BAR; PG8_MMA(0, 0, At, B0); PG8_MMA(0, 1, At, B1); PG8_BAR; PG8_SCHED;
;             PG8_LDA(At, 1, 1); PG8_STAGE(PG8_SB(1, 0), b3, voffB[0], voffB[1]); PG8_STAGE(PG8_SB(1, 1), b3 + hstep, voffB[0], voffB[1]); PG8_STAGE(PG8_SA(1, 0), a3, w00, w01);
;             PG8_WAIT_V(8); PG8_WAIT_L(0); PG8_BAR; PG8_MMA(1, 0, At, B0); PG8_MMA(1, 1, At, B1); PG8_BAR; PG8_SCHED;
;         }
;         if constexpr (FP8) asm volatile("s_nop 15\n\ts_nop 15" ::: "memory");
;         if constexpr (ALIGN_EPI) { if (wr == 0) PG8_BAR; }
	s_setprio 1
	s_waitcnt lgkmcnt(6)
	v_mfma_scale_f32_16x16x128_f8f6f4 v[160:163], v[2:9], v[198:205], v[160:163], v186, v187 op_sel_hi:[0,0,0]
	v_mfma_scale_f32_16x16x128_f8f6f4 v[156:159], v[10:17], v[198:205], v[156:159], v186, v187 op_sel_hi:[0,0,0]
	s_waitcnt lgkmcnt(4)
	v_mfma_scale_f32_16x16x128_f8f6f4 v[142:145], v[2:9], v[206:213], v[142:145], v186, v187 op_sel_hi:[0,0,0]
	v_mfma_scale_f32_16x16x128_f8f6f4 v[138:141], v[10:17], v[206:213], v[138:141], v186, v187 op_sel_hi:[0,0,0]
	s_waitcnt lgkmcnt(2)
	v_mfma_scale_f32_16x16x128_f8f6f4 v[126:129], v[2:9], v[214:221], v[126:129], v186, v187 op_sel_hi:[0,0,0]
	v_mfma_scale_f32_16x16x128_f8f6f4 v[122:125], v[10:17], v[214:221], v[122:125], v186, v187 op_sel_hi:[0,0,0]
	s_waitcnt lgkmcnt(0)
	v_mfma_scale_f32_16x16x128_f8f6f4 v[110:113], v[2:9], v[222:229], v[110:113], v186, v187 op_sel_hi:[0,0,0]
	v_mfma_scale_f32_16x16x128_f8f6f4 v[106:109], v[10:17], v[222:229], v[106:109], v186, v187 op_sel_hi:[0,0,0]
	s_setprio 0
	s_setprio 1
	v_mfma_scale_f32_16x16x128_f8f6f4 v[152:155], v[18:25], v[198:205], v[152:155], v186, v187 op_sel_hi:[0,0,0]
	v_mfma_scale_f32_16x16x128_f8f6f4 v[148:151], v[26:33], v[198:205], v[148:151], v186, v187 op_sel_hi:[0,0,0]
	v_mfma_scale_f32_16x16x128_f8f6f4 v[134:137], v[18:25], v[206:213], v[134:137], v186, v187 op_sel_hi:[0,0,0]
	v_mfma_scale_f32_16x16x128_f8f6f4 v[130:133], v[26:33], v[206:213], v[130:133], v186, v187 op_sel_hi:[0,0,0]
	v_mfma_scale_f32_16x16x128_f8f6f4 v[118:121], v[18:25], v[214:221], v[118:121], v186, v187 op_sel_hi:[0,0,0]
	v_mfma_scale_f32_16x16x128_f8f6f4 v[114:117], v[26:33], v[214:221], v[114:117], v186, v187 op_sel_hi:[0,0,0]
	v_mfma_scale_f32_16x16x128_f8f6f4 v[102:105], v[18:25], v[222:229], v[102:105], v186, v187 op_sel_hi:[0,0,0]
	v_mfma_scale_f32_16x16x128_f8f6f4 v[98:101], v[26:33], v[222:229], v[98:101], v186, v187 op_sel_hi:[0,0,0]
	s_setprio 0
	s_barrier
	ds_read_b128 v[198:201], v169 offset:49152
	ds_read_b128 v[202:205], v169 offset:50176
	ds_read_b128 v[206:209], v169 offset:51200
	ds_read_b128 v[210:213], v169 offset:52224
	ds_read_b128 v[214:217], v169 offset:53248
	ds_read_b128 v[218:221], v169 offset:54272
	ds_read_b128 v[222:225], v169 offset:55296
	ds_read_b128 v[226:229], v169 offset:56320
	s_mov_b32 m0, s57
	s_nop 0
	global_load_lds_dwordx4 v0, s[26:27]
	s_nop 0
	s_mov_b32 m0, s58
	s_nop 0
	global_load_lds_dwordx4 v147, s[26:27]
	s_add_u32 s8, s16, 0x20080
	s_addc_u32 s9, s17, 0
	s_mov_b32 m0, s65
	s_nop 0
	global_load_lds_dwordx4 v0, s[8:9]
	s_nop 0
	s_mov_b32 m0, s66
	s_nop 0
	global_load_lds_dwordx4 v147, s[8:9]
	s_mov_b32 m0, s59
	s_nop 0
	global_load_lds_dwordx4 v178, s[10:11]
	s_nop 0
	s_mov_b32 m0, s64
	s_nop 0
	global_load_lds_dwordx4 v179, s[10:11]
	s_waitcnt vmcnt(8)
	s_waitcnt lgkmcnt(0)
	s_barrier
	s_setprio 1
	s_waitcnt lgkmcnt(6)
	v_mfma_scale_f32_16x16x128_f8f6f4 v[94:97], v[2:9], v[198:205], v[94:97], v186, v187 op_sel_hi:[0,0,0]
	v_mfma_scale_f32_16x16x128_f8f6f4 v[90:93], v[10:17], v[198:205], v[90:93], v186, v187 op_sel_hi:[0,0,0]
	s_waitcnt lgkmcnt(4)
	v_mfma_scale_f32_16x16x128_f8f6f4 v[78:81], v[2:9], v[206:213], v[78:81], v186, v187 op_sel_hi:[0,0,0]
	v_mfma_scale_f32_16x16x128_f8f6f4 v[74:77], v[10:17], v[206:213], v[74:77], v186, v187 op_sel_hi:[0,0,0]
	s_waitcnt lgkmcnt(2)
	v_mfma_scale_f32_16x16x128_f8f6f4 v[62:65], v[2:9], v[214:221], v[62:65], v186, v187 op_sel_hi:[0,0,0]
	v_mfma_scale_f32_16x16x128_f8f6f4 v[58:61], v[10:17], v[214:221], v[58:61], v186, v187 op_sel_hi:[0,0,0]
	s_waitcnt lgkmcnt(0)
	v_mfma_scale_f32_16x16x128_f8f6f4 v[46:49], v[2:9], v[222:229], v[46:49], v186, v187 op_sel_hi:[0,0,0]
	v_mfma_scale_f32_16x16x128_f8f6f4 v[42:45], v[10:17], v[222:229], v[42:45], v186, v187 op_sel_hi:[0,0,0]
	s_setprio 0
	s_setprio 1
	v_mfma_scale_f32_16x16x128_f8f6f4 v[86:89], v[18:25], v[198:205], v[86:89], v186, v187 op_sel_hi:[0,0,0]
	v_mfma_scale_f32_16x16x128_f8f6f4 v[82:85], v[26:33], v[198:205], v[82:85], v186, v187 op_sel_hi:[0,0,0]
	v_mfma_scale_f32_16x16x128_f8f6f4 v[70:73], v[18:25], v[206:213], v[70:73], v186, v187 op_sel_hi:[0,0,0]
	v_mfma_scale_f32_16x16x128_f8f6f4 v[66:69], v[26:33], v[206:213], v[66:69], v186, v187 op_sel_hi:[0,0,0]
	v_mfma_scale_f32_16x16x128_f8f6f4 v[54:57], v[18:25], v[214:221], v[54:57], v186, v187 op_sel_hi:[0,0,0]
	v_mfma_scale_f32_16x16x128_f8f6f4 v[50:53], v[26:33], v[214:221], v[50:53], v186, v187 op_sel_hi:[0,0,0]
	v_mfma_scale_f32_16x16x128_f8f6f4 v[38:41], v[18:25], v[222:229], v[38:41], v186, v187 op_sel_hi:[0,0,0]
	v_mfma_scale_f32_16x16x128_f8f6f4 v[34:37], v[26:33], v[222:229], v[34:37], v186, v187 op_sel_hi:[0,0,0]
	s_setprio 0
	s_barrier
	s_add_i32 s7, s7, 2
	s_add_u32 s0, s0, 0x100
	s_addc_u32 s1, s1, 0
	s_cmp_gt_u32 s7, 5
	s_mov_b64 s[26:27], s[4:5]
	s_cbranch_scc0 .LBB0_460
	s_nop 15
	s_nop 15
	s_and_b64 vcc, exec, s[86:87]
	s_cbranch_vccz .LBB0_463
	s_barrier

; template <int M> __device__ __forceinline__ float swz_xor_f(float v) { return __builtin_bit_cast(float, __builtin_amdgcn_ds_swizzle(__builtin_bit_cast(int, v), (M << 10) | 0x1f)); }
; __device__ __forceinline__ int v_st(int k, int c) { const int kk = (k & ~0xC) | ((k & 4) << 1) | ((k & 8) >> 1); return ((kk >> 3) * 4 + (c >> 5)) * 512 + ((kk & 7) * 32 + (c & 31)) * 2; }
; __device__ __forceinline__ void gmlp_spatial_fused(Frame& F, int j, int row0) {
;     ...
;         unsigned woff[4];
; #pragma unroll
;         for (int i = 0; i < 4; ++i) { const int row = 4 * (4 * wave + i) + (lane >> 4), cpos = (lane & 15) << 4; woff[i] = (unsigned)(row * 256 + (cpos ^ ((row & 7) << 4))); }
;         int sto[8];
; #pragma unroll
;         for (int i = 0; i < 8; ++i) { const int q = q0 + 16 * i, e = 8 * c8; sto[i] = ((q >> 6) * 2 + (e >> 7)) * 16384 + att::v_st(q & 63, e & 127); }
;         if (tid < 128) bsl[tid] = bs[g * 128 + tid];
;         { const char* wg = (const char*)(WSb + (size_t)g * 128 * 128);
; #pragma unroll
;           for (int i = 0; i < 4; ++i) pg8::glds16_s(wg, woff[i], wlds + (unsigned)i * 1024u); }
;         { float sm = (pin[0][0] + pin[0][2]) + (pin[1][0] + pin[1][2]) + (pin[2][0] + pin[2][2]) + (pin[3][0] + pin[3][2]), sq = (pin[0][1] + pin[0][3]) + (pin[1][1] + pin[1][3]) + (pin[2][1] + pin[2][3]) + (pin[3][1] + pin[3][3]);
;           sm += swz_xor_f<1>(sm); sq += swz_xor_f<1>(sq); sm += swz_xor_f<2>(sm); sq += swz_xor_f<2>(sq);
;           const float mean = sm * (1.0f / 2048.0f), var = __builtin_fmaxf(sq * (1.0f / 2048.0f) - mean * mean, 0.f);
;           if ((tid & 3) == 0) stl[tid >> 2] = (f32x2){mean, 1.0f / sqrtf(var + LN_EPS)}; }
.LBB0_585:
	s_or_b64 exec, exec, s[0:1]
	v_bfe_u32 v0, v18, 4, 2
	v_or_b32_e32 v0, s29, v0
	v_lshlrev_b32_e32 v149, 4, v18
	v_and_b32_e32 v2, 0xf0, v149
	v_lshlrev_b32_e32 v3, 8, v0
	v_and_b32_e32 v4, 48, v18
	v_bitop3_b32 v3, v3, v2, v4 bitop3:0xf6
	v_or_b32_e32 v4, 4, v0
	s_lshl_b32 s0, s18, 15
	v_lshlrev_b32_e32 v5, 8, v4
	v_lshlrev_b32_e32 v4, 4, v4
	v_or_b32_e32 v0, 12, v0
	s_add_u32 s0, s21, s0
	v_and_b32_e32 v4, 0x70, v4
	v_lshlrev_b32_e32 v6, 8, v0
	v_lshlrev_b32_e32 v0, 4, v0
	s_addc_u32 s1, s22, 0
	s_mov_b32 m0, s27
	s_nop 0
	global_load_lds_dwordx4 v3, s[0:1]
	v_bitop3_b32 v4, v4, v5, v2 bitop3:0xde
	v_or_b32_e32 v5, 0x800, v3
	v_and_b32_e32 v0, 0x70, v0
	s_mov_b32 m0, s39
	s_nop 0
	global_load_lds_dwordx4 v4, s[0:1]
	v_bitop3_b32 v0, v0, v6, v2 bitop3:0xde
	s_mov_b32 m0, s41
	s_nop 0
	global_load_lds_dwordx4 v5, s[0:1]
	s_waitcnt vmcnt(0)
	v_pk_add_f32 v[2:3], v[110:111], v[112:113]
	v_pk_add_f32 v[4:5], v[106:107], v[108:109]
	s_mov_b32 m0, s48
	s_nop 0
	global_load_lds_dwordx4 v0, s[0:1]
	v_and_b32_e32 v20, 3, v18
	v_pk_add_f32 v[2:3], v[2:3], v[4:5]
	v_pk_add_f32 v[4:5], v[102:103], v[104:105]
	v_cmp_eq_u32_e32 vcc, 0, v20
	v_pk_add_f32 v[2:3], v[2:3], v[4:5]
	v_pk_add_f32 v[4:5], v[98:99], v[100:101]
	s_nop 0
	v_pk_add_f32 v[2:3], v[2:3], v[4:5]
	ds_swizzle_b32 v4, v2 offset:swizzle(SWAP,1)
	ds_swizzle_b32 v5, v3 offset:swizzle(SWAP,1)
	s_waitcnt lgkmcnt(0)
	v_pk_add_f32 v[2:3], v[2:3], v[4:5]
	ds_swizzle_b32 v4, v2 offset:swizzle(SWAP,2)
	ds_swizzle_b32 v5, v3 offset:swizzle(SWAP,2)
	s_and_saveexec_b64 s[0:1], vcc
	s_cbranch_execz .LBB0_587
	s_waitcnt lgkmcnt(0)
	v_pk_add_f32 v[2:3], v[2:3], v[4:5]
	s_mov_b32 s2, 0x3a000000
	v_pk_mul_f32 v[2:3], v[2:3], s[2:3] op_sel_hi:[1,0]
	s_nop 0
	v_fma_f32 v0, -v2, v2, v3
	v_max_f32_e32 v0, 0, v0
	v_add_f32_e32 v0, 0x3727c5ac, v0
	v_mul_f32_e32 v3, 0x4f800000, v0
	v_cmp_gt_f32_e32 vcc, s71, v0
	s_nop 1
	v_cndmask_b32_e32 v0, v0, v3, vcc
	v_sqrt_f32_e32 v3, v0
	s_nop 0
	v_add_u32_e32 v4, -1, v3
	v_fma_f32 v6, -v4, v3, v0
	v_add_u32_e32 v5, 1, v3
	v_cmp_ge_f32_e64 s[2:3], 0, v6
	s_nop 1
	v_cndmask_b32_e64 v4, v3, v4, s[2:3]
	v_fma_f32 v3, -v5, v3, v0
	v_cmp_lt_f32_e64 s[2:3], 0, v3
	s_nop 1
	v_cndmask_b32_e64 v3, v4, v5, s[2:3]
	v_mul_f32_e32 v4, 0x37800000, v3
	v_cndmask_b32_e32 v3, v3, v4, vcc
	v_cmp_class_f32_e32 vcc, v0, v189
	s_nop 1
	v_cndmask_b32_e32 v0, v3, v0, vcc
	v_div_scale_f32 v3, s[2:3], v0, v0, 1.0
	v_rcp_f32_e32 v4, v3
	s_nop 0
	v_fma_f32 v5, -v3, v4, 1.0
	v_fmac_f32_e32 v4, v5, v4
	v_div_scale_f32 v5, vcc, 1.0, v0, 1.0
	v_mul_f32_e32 v6, v5, v4
	v_fma_f32 v7, -v3, v6, v5
	v_fmac_f32_e32 v6, v7, v4
	v_fma_f32 v3, -v3, v6, v5
	v_div_fmas_f32 v3, v3, v4, v6
	v_div_fixup_f32 v3, v3, v0, 1.0
	v_lshl_add_u32 v0, v19, 1, 0
	v_add_u32_e32 v0, 0x20400, v0
	ds_write_b64 v0, v[2:3]

; template <class Epi, class Sched, bool ALIGN_EPI, bool FP8 = false>
; __device__ __forceinline__ void gemm_phase(LAS unsigned char* lds, const bf16_t* A, const bf16_t* Bt, const int K, const Sched& S, const Epi& E, const int wave_in) {
;     const int tid = opaque_tid(wave_in); const int wid = __builtin_amdgcn_readfirstlane(tid >> 6), lane = tid & 63, wr = wid >> 2, wc = wid & 3, fr = lane & 15, fq = lane >> 4;
;     const int nt = K / BK;
;     int sR[2], sC[2]; unsigned voffB[2];
; #pragma unroll
;     for (int i = 0; i < 2; ++i) { stage_rc(tid * 16 + i * 8192, sR[i], sC[i]); const int Rb = Epi::PERM ? ((sR[i] & ~31) + perm32(sR[i] & 31)) : sR[i];
;         voffB[i] = (unsigned)(Rb * K + sC[i]) * 2u; }
;     const size_t kstep = (size_t)(BK * 2);
;     const size_t hstep = (size_t)HALF * K * 2;
;     const unsigned ldsw = (unsigned)wid * 1024u;
;     const unsigned ldsbase = (unsigned)__builtin_amdgcn_readfirstlane((int)((unsigned)(uintptr_t)lds + ldsw));
;     const int aoff = lds_byte(wr * 64 + fr, fq * 8), boff = lds_byte(wc * 32 + fr, fq * 8);
;     ...
;     Unit cur, nxt; int ui = 0;
;     if (!S.next(0, cur)) return;
;     f32x4 acc[2][2][4][2];
; #pragma unroll
;     for (int a = 0; a < 2; ++a)
; #pragma unroll
;         for (int b = 0; b < 2; ++b)
; #pragma unroll
;             for (int m = 0; m < 4; ++m)
; #pragma unroll
;                 for (int n = 0; n < 2; ++n) acc[a][b][m][n] = (f32x4){0.f, 0.f, 0.f, 0.f};
;     bf16x8 At[4][2], B0[2][2], B1[2][2];
;     const int sclW = W8_E8M0, sclA = A8_E8M0;
;     unsigned vA[2][2], vN[2][2];
;     PG8_AOFF(vA, cur);
;     const char* const cA = (const char*)A;
;     const char* cB = (const char*)Bt + S.b_off(cur) * 2;
;     PG8_STAGE(PG8_SB(0, 0), cB, voffB[0], voffB[1]); PG8_STAGE(PG8_SB(0, 1), cB + hstep, voffB[0], voffB[1]); PG8_STAGE(PG8_SA(0, 0), cA, vA[0][0], vA[0][1]); PG8_STAGE(PG8_SA(0, 1), cA, vA[1][0], vA[1][1]);
;     if (wr == 1) PG8_BAR;
; __global__ void __launch_bounds__(NWAVES * 64, 2) fwd_kernel(Args args) {
;     ...
;         { pg8::DenseSched S; S.o.init(nPan, 1024 / 256, F.G, F.bid, pan0); S.K = yK;
;           pg8::EpiBf16<0> E{Y, 1024};
;           if (kind == 1) pg8::gemm_phase<pg8::EpiBf16<0>, pg8::DenseSched, true, true>(F.lds, yA, yW, yK, S, E, F.wave0);
;           else pg8::gemm_phase<pg8::EpiBf16<0>, pg8::DenseSched, true>(F.lds, yA, yW, yK, S, E, F.wave0); }
.LBB0_659:
	s_cmp_lg_u32 s37, 0
	s_cselect_b64 s[76:77], -1, 0
	s_cmp_eq_u32 s37, 0
	s_cselect_b64 s[0:1], -1, 0
	v_writelane_b32 v232, s0, 24
	s_mov_b64 s[4:5], s[92:93]
	s_mov_b32 s13, 0x40000
	v_writelane_b32 v232, s1, 25
	s_and_b64 s[0:1], s[0:1], exec
	s_cselect_b32 s0, 0, 0x800
	s_xor_b32 s29, s0, 0x10800
	v_writelane_b32 v232, s0, 22
	s_lshr_b32 s6, s29, 6
	v_writelane_b32 v232, s4, 18
	s_lshr_b32 s22, s29, 8
	s_lshr_b32 s23, s0, 8
	v_writelane_b32 v232, s5, 19
	v_writelane_b32 v232, s6, 20
	v_writelane_b32 v232, s7, 21
	s_cmp_lg_u32 s97, 1
	s_mov_b64 s[0:1], -1
	v_readlane_b32 s41, v232, 14
	s_mov_b32 s31, 0x10000
	s_mov_b32 s47, 0x18000
	s_mov_b32 s71, 0x8000
	s_cbranch_scc0 .LBB0_679
	v_readlane_b32 s0, v232, 0
	s_waitcnt vmcnt(6)
	v_mbcnt_lo_u32_b32 v2, -1, 0
	v_mbcnt_hi_u32_b32 v2, -1, v2
	s_nop 0
	v_add_u32_e32 v0, s0, v2
	s_nop 0
	v_readfirstlane_b32 s2, v0
	s_ashr_i32 s3, s2, 6
	s_cmp_ge_i32 s18, s6
	s_cbranch_scc1 .LBB0_678
	v_ashrrev_i32_e32 v4, 31, v0
	v_lshrrev_b32_e32 v4, 26, v4
	v_lshlrev_b32_e32 v3, 4, v0
	v_add_u32_e32 v4, v0, v4
	v_bfe_i32 v0, v0, 27, 1
	v_lshrrev_b32_e32 v0, 22, v0
	v_add_u32_e32 v0, v3, v0
	v_and_b32_e32 v0, 0xfffffc00, v0
	v_sub_u32_e32 v0, v3, v0
	v_lshrrev_b32_e32 v5, 4, v0
	v_bitop3_b32 v5, v5, v0, 32 bitop3:0x6c
	s_waitcnt vmcnt(5)
	v_ashrrev_i32_e32 v6, 31, v5
	v_lshrrev_b32_e32 v6, 26, v6
	v_ashrrev_i32_e32 v4, 6, v4
	v_add_u32_e32 v6, v5, v6
	v_lshlrev_b32_e32 v0, 3, v4
	v_ashrrev_i32_e32 v7, 6, v6
	v_and_b32_e32 v6, 0xc0, v6
	v_and_b32_e32 v0, -16, v0
	v_lshlrev_b32_e32 v4, 5, v4
	v_sub_u32_e32 v5, v5, v6
	v_add_u32_e32 v0, v7, v0
	v_and_b32_e32 v4, 32, v4
	v_ashrrev_i16_sdwa v5, v185, sext(v5) dst_sel:DWORD dst_unused:UNUSED_PAD src0_sel:DWORD src1_sel:BYTE_0
	v_add_u32_sdwa v132, v4, sext(v5) dst_sel:DWORD dst_unused:UNUSED_PAD src0_sel:DWORD src1_sel:WORD_0
	v_lshlrev_b32_e32 v4, 1, v0
	v_lshrrev_b32_e32 v5, 2, v0
	v_and_b32_e32 v6, 3, v7
	s_mov_b32 s0, 0x7fffffe0
	v_and_b32_e32 v4, 24, v4
	v_and_b32_e32 v5, 4, v5
	v_and_or_b32 v6, v0, s0, v6
	v_or3_b32 v4, v6, v5, v4
	v_mul_lo_u32 v4, v4, s21
	v_add_u32_e32 v3, 0x2000, v3
	v_add_lshl_u32 v133, v4, v132, 1
	v_ashrrev_i32_e32 v4, 31, v3
	v_lshrrev_b32_e32 v4, 22, v4
	v_add_u32_e32 v4, v3, v4
	v_ashrrev_i32_e32 v4, 10, v4
	v_mul_i32_i24_e32 v5, 0x400, v4
	v_sub_u32_e32 v3, v3, v5
	v_lshrrev_b32_e32 v5, 4, v3
	v_bitop3_b32 v3, v5, v3, 32 bitop3:0x6c
	v_ashrrev_i32_e32 v6, 31, v3
	v_lshrrev_b32_e32 v6, 26, v6
	v_lshlrev_b32_e32 v5, 3, v4
	v_add_u32_e32 v6, v3, v6
	v_and_b32_e32 v5, -16, v5
	v_ashrrev_i32_e32 v7, 6, v6
	v_add_u32_e32 v134, v7, v5
	v_and_b32_e32 v5, 0xc0, v6
	v_sub_u32_e32 v3, v3, v5
	v_and_b32_e32 v5, 3, v7
	s_ashr_i32 s25, s18, 31
	v_and_or_b32 v5, v134, s0, v5
	s_lshr_b32 s0, s25, 29
	s_add_i32 s0, s18, s0
	s_lshl_b32 s17, s3, 10
	s_lshr_b32 s24, s29, 9
	s_ashr_i32 s1, s0, 3
	s_and_b32 s0, s0, -8
	s_ashr_i32 s4, s2, 8
	s_lshl_b32 s16, s21, 8
	s_add_i32 s17, s17, 0
	s_sub_i32 s0, s18, s0
	s_or_b32 s28, s24, 1
	s_cmp_lt_i32 s0, 0
	s_cselect_b32 s5, s28, s24
	s_mul_i32 s0, s0, s5
	s_add_i32 s0, s0, s1
	s_ashr_i32 s1, s0, 31
	s_lshr_b32 s1, s1, 27
	v_lshlrev_b32_e32 v4, 5, v4
	s_add_i32 s1, s0, s1
	v_and_b32_e32 v4, 32, v4
	v_ashrrev_i16_sdwa v3, v185, sext(v3) dst_sel:DWORD dst_unused:UNUSED_PAD src0_sel:DWORD src1_sel:BYTE_0
	s_ashr_i32 s5, s1, 5
	v_add_u32_sdwa v135, v4, sext(v3) dst_sel:DWORD dst_unused:UNUSED_PAD src0_sel:DWORD src1_sel:WORD_0
	v_lshlrev_b32_e32 v3, 1, v134
	v_lshrrev_b32_e32 v4, 2, v134
	s_lshl_b32 s5, s5, 3
	v_and_b32_e32 v3, 24, v3
	v_and_b32_e32 v4, 4, v4
	s_sub_i32 s7, s22, s5
	v_or3_b32 v3, v5, v4, v3
	s_min_i32 s7, s7, 8
	v_mul_lo_u32 v3, v3, s21
	s_abs_i32 s9, s7
	v_add_lshl_u32 v136, v3, v135, 1
	v_cvt_f32_u32_e32 v3, s9
	s_sub_i32 s10, 0, s9
	s_andn2_b32 s1, s1, 31
	s_sub_i32 s0, s0, s1
	v_rcp_iflag_f32_e32 v3, v3
	s_abs_i32 s8, s0
	s_xor_b32 s1, s0, s7
	s_ashr_i32 s1, s1, 31
	v_mul_f32_e32 v3, 0x4f7ffffe, v3
	v_cvt_u32_f32_e32 v3, v3
	s_nop 0
	v_readfirstlane_b32 s11, v3
	s_mul_i32 s10, s10, s11
	s_mul_hi_u32 s10, s11, s10
	s_add_i32 s11, s11, s10
	s_mul_hi_u32 s10, s8, s11
	s_mul_i32 s11, s10, s9
	s_sub_i32 s8, s8, s11
	s_add_i32 s11, s10, 1
	s_sub_i32 s12, s8, s9
	s_cmp_ge_u32 s8, s9
	s_cselect_b32 s10, s11, s10
	s_cselect_b32 s8, s12, s8
	s_add_i32 s11, s10, 1
	s_cmp_ge_u32 s8, s9
	s_cselect_b32 s8, s11, s10
	s_xor_b32 s8, s8, s1
	s_sub_i32 s92, s8, s1
	s_mul_i32 s1, s92, s7
	s_sub_i32 s0, s0, s1
	s_add_i32 s0, s0, s23
	s_add_i32 s93, s0, s5
	s_lshl_b32 s0, s93, 8
	v_add_u32_e32 v3, s0, v0
	v_mul_lo_u32 v3, v3, s21
	v_add_lshl_u32 v130, v3, v132, 1
	v_add_u32_e32 v3, s0, v134
	v_mul_lo_u32 v3, v3, s21
	s_bitset1_b32 s0, 7
	v_add_lshl_u32 v131, v3, v135, 1
	v_add_u32_e32 v3, s0, v0
	s_lshl_b32 s38, s21, 9
	v_mul_lo_u32 v3, v3, s21
	s_mul_i32 s1, s38, s92
	v_add_lshl_u32 v145, v3, v132, 1
	v_add_u32_e32 v3, s0, v134
	s_mul_hi_i32 s0, s38, s92
	s_add_u32 s80, s86, s1
	s_addc_u32 s81, s87, s0
	s_add_i32 s39, s17, 0x10000
	s_mov_b32 m0, s39
	s_nop 0
	global_load_lds_dwordx4 v133, s[80:81]
	s_add_i32 s48, s17, 0x12000
	s_mov_b32 m0, s48
	s_nop 0
	global_load_lds_dwordx4 v136, s[80:81]
	s_add_u32 s0, s80, s16
	s_addc_u32 s1, s81, 0
	s_add_i32 s49, s17, 0x14000
	s_mov_b32 m0, s49
	s_nop 0
	global_load_lds_dwordx4 v133, s[0:1]
	s_add_i32 s50, s17, 0x16000
	s_mov_b32 m0, s50
	s_nop 0
	global_load_lds_dwordx4 v136, s[0:1]
	s_add_i32 s51, s17, 0x2000
	s_mov_b32 m0, s17
	s_nop 0
	global_load_lds_dwordx4 v130, s[84:85]
	v_mul_lo_u32 v3, v3, s21
	s_mov_b32 m0, s51
	s_nop 0
	global_load_lds_dwordx4 v131, s[84:85]
	s_add_i32 s52, s17, 0x4000
	s_mov_b32 m0, s52
	s_nop 0
	global_load_lds_dwordx4 v145, s[84:85]
	v_add_lshl_u32 v147, v3, v135, 1
	s_add_i32 s53, s17, 0x6000
	s_mov_b32 m0, s53
	s_nop 0
	global_load_lds_dwordx4 v147, s[84:85]
	s_cmp_eq_u32 s4, 1
	s_cselect_b64 s[26:27], -1, 0
	s_cmp_lg_u32 s4, 1
	s_cbranch_scc1 .LBB0_663
	s_barrier
; #define PG8_STAGE(bufoff, gbase, v0, v1) do { glds16_s((gbase), (v0), ldsbase + (unsigned)(bufoff)); glds16_s((gbase), (v1), ldsbase + (unsigned)(bufoff) + 8192u); } while (0)
; #define PG8_WAIT_V(n) asm volatile("s_waitcnt vmcnt(" #n ")" ::: "memory")
; #define PG8_BAR __builtin_amdgcn_s_barrier()
; template <class Epi, class Sched, bool ALIGN_EPI, bool FP8 = false>
; __device__ __forceinline__ void gemm_phase(LAS unsigned char* lds, const bf16_t* A, const bf16_t* Bt, const int K, const Sched& S, const Epi& E, const int wave_in) {
;     ...
;     if (wr == 1) PG8_BAR;
;     PG8_WAIT_V(2); PG8_BAR;
;     PG8_STAGE(PG8_SB(1, 0), cB + kstep, voffB[0], voffB[1]); PG8_STAGE(PG8_SA(1, 0), cA + kstep, vA[0][0], vA[0][1]); PG8_STAGE(PG8_SB(1, 1), cB + hstep + kstep, voffB[0], voffB[1]);
;     PG8_WAIT_V(6); PG8_BAR;
.LBB0_663:
	v_bfe_u32 v137, v2, 4, 2
	s_lshl_b32 s3, s3, 5
	v_and_b32_e32 v138, 15, v2
	v_lshlrev_b32_e32 v3, 4, v137
	v_lshlrev_b32_e32 v2, 2, v2
	s_and_b32 s56, s3, 0x60
	s_lshr_b32 s54, s21, 6
	s_lshl_b32 s55, s4, 6
	v_lshl_or_b32 v3, v138, 6, v3
	s_lshl_b32 s4, s4, 13
	v_and_b32_e32 v2, 32, v2
	s_lshl_b32 s3, s56, 7
	v_bitop3_b32 v4, v3, s4, v2 bitop3:0xde
	s_add_u32 s4, s80, 0x80
	v_bitop3_b32 v2, v3, s3, v2 bitop3:0xde
	s_waitcnt vmcnt(2)
	s_barrier
	s_addc_u32 s5, s81, 0
	s_add_i32 s57, s17, 0x18000
	s_mov_b32 m0, s57
	s_nop 0
	global_load_lds_dwordx4 v133, s[4:5]
	s_add_i32 s58, s17, 0x1a000
	s_mov_b32 m0, s58
	s_nop 0
	global_load_lds_dwordx4 v136, s[4:5]
	s_add_u32 s4, s84, 0x80
	s_addc_u32 s5, s85, 0
	s_add_i32 s59, s17, 0x8000
	s_mov_b32 m0, s59
	s_nop 0
	global_load_lds_dwordx4 v130, s[4:5]
	s_add_i32 s64, s17, 0xa000
	s_mov_b32 m0, s64
	s_nop 0
	global_load_lds_dwordx4 v131, s[4:5]
	s_add_u32 s0, s0, 0x80
	s_addc_u32 s1, s1, 0
	s_add_i32 s65, s17, 0x1c000
	s_mov_b32 m0, s65
	s_nop 0
	global_load_lds_dwordx4 v133, s[0:1]
	s_add_i32 s66, s17, 0x1e000
	s_mov_b32 m0, s66
	s_nop 0
	global_load_lds_dwordx4 v136, s[0:1]
	s_waitcnt vmcnt(6)
	s_add_i32 s67, s54, -2
	s_add_i32 s72, s17, 0xc000
	s_add_i32 s73, s17, 0xe000
	s_cmpk_lt_u32 s2, 0x100
	s_cselect_b64 s[78:79], -1, 0
	s_ashr_i32 s88, s20, 31
	s_mov_b32 s7, s19
	s_mov_b32 s89, 0
	v_add_u32_e32 v139, 0, v2
	v_add_u32_e32 v140, 0, v4
	s_barrier
	s_waitcnt vmcnt(0)
	s_branch .LBB0_666

; #define PG8_STAGE(bufoff, gbase, v0, v1) do { glds16_s((gbase), (v0), ldsbase + (unsigned)(bufoff)); glds16_s((gbase), (v1), ldsbase + (unsigned)(bufoff) + 8192u); } while (0)
; #define PG8_LDA(dst, b, h) do { _Pragma("unroll") for (int m = 0; m < 4; ++m) _Pragma("unroll") for (int k = 0; k < 2; ++k) dst[m][k] = *(const LAS bf16x8*)(lds + PG8_SA(b, h) + aoff + m * 2048 + k * 1024); } while (0)
; #define PG8_LDB(dst, b, h) do { _Pragma("unroll") for (int n = 0; n < 2; ++n) _Pragma("unroll") for (int k = 0; k < 2; ++k) dst[n][k] = *(const LAS bf16x8*)(lds + PG8_SB(b, h) + boff + n * 2048 + k * 1024); } while (0)
; #define PG8_WAIT_V(n) asm volatile("s_waitcnt vmcnt(" #n ")" ::: "memory")
; #define PG8_WAIT_L(n) asm volatile("s_waitcnt lgkmcnt(" #n ")" ::: "memory")
; #define PG8_BAR __builtin_amdgcn_s_barrier()
; #define PG8_SCHED __builtin_amdgcn_sched_barrier(0)
; template <class Epi, class Sched, bool ALIGN_EPI, bool FP8 = false>
; __device__ __forceinline__ void gemm_phase(LAS unsigned char* lds, const bf16_t* A, const bf16_t* Bt, const int K, const Sched& S, const Epi& E, const int wave_in) {
;     ...
;             const unsigned w00 = last ? vN[0][0] : vA[0][0], w01 = last ? vN[0][1] : vA[0][1], w10 = last ? vN[1][0] : vA[1][0], w11 = last ? vN[1][1] : vA[1][1];
;             PG8_LDB(B0, 0, 0); PG8_LDB(B1, 0, 1); PG8_SCHED; PG8_LDA(At, 0, 0); PG8_STAGE(PG8_SA(1, 1), a1, vA[1][0], vA[1][1]);
;             PG8_WAIT_V(8); PG8_WAIT_L(0); PG8_BAR; PG8_MMA(0, 0, At, B0); PG8_MMA(0, 1, At, B1); PG8_BAR; PG8_SCHED;
;     ...
; #pragma unroll
;         for (int a = 0; a < 2; ++a)
; #pragma unroll
;             for (int b = 0; b < 2; ++b)
; #pragma unroll
;                 for (int m = 0; m < 4; ++m)
; #pragma unroll
;                     for (int n = 0; n < 2; ++n) acc[a][b][m][n] = (f32x4){0.f, 0.f, 0.f, 0.f};
.LBB0_670:
	v_mov_b32_e32 v2, 0
	s_mov_b32 s0, 0
	s_mov_b64 s[60:61], 0x100
	v_mov_b32_e32 v3, 0
	v_mov_b64_e32 v[4:5], 0
	v_mov_b64_e32 v[6:7], 0
	v_mov_b64_e32 v[8:9], 0
	v_mov_b64_e32 v[10:11], 0
	v_mov_b64_e32 v[12:13], 0
	v_mov_b64_e32 v[18:19], 0
	v_mov_b64_e32 v[20:21], 0
	v_mov_b64_e32 v[26:27], 0
	v_mov_b64_e32 v[28:29], 0
	v_mov_b64_e32 v[34:35], 0
	v_mov_b64_e32 v[36:37], 0
	v_mov_b64_e32 v[42:43], 0
	v_mov_b64_e32 v[44:45], 0
	v_mov_b64_e32 v[50:51], 0
	v_mov_b64_e32 v[52:53], 0
	v_mov_b64_e32 v[14:15], 0
	v_mov_b64_e32 v[16:17], 0
	v_mov_b64_e32 v[22:23], 0
	v_mov_b64_e32 v[24:25], 0
	v_mov_b64_e32 v[30:31], 0
	v_mov_b64_e32 v[32:33], 0
	v_mov_b64_e32 v[38:39], 0
	v_mov_b64_e32 v[40:41], 0
	v_mov_b64_e32 v[46:47], 0
	v_mov_b64_e32 v[48:49], 0
	v_mov_b64_e32 v[54:55], 0
	v_mov_b64_e32 v[56:57], 0
	v_mov_b64_e32 v[58:59], 0
	v_mov_b64_e32 v[60:61], 0
	v_mov_b64_e32 v[62:63], 0
	v_mov_b64_e32 v[64:65], 0
	v_mov_b64_e32 v[66:67], 0
	v_mov_b64_e32 v[68:69], 0
	v_mov_b64_e32 v[70:71], 0
	v_mov_b64_e32 v[72:73], 0
	v_mov_b64_e32 v[74:75], 0
	v_mov_b64_e32 v[76:77], 0
	v_mov_b64_e32 v[82:83], 0
	v_mov_b64_e32 v[84:85], 0
	v_mov_b64_e32 v[90:91], 0
	v_mov_b64_e32 v[92:93], 0
	v_mov_b64_e32 v[98:99], 0
	v_mov_b64_e32 v[100:101], 0
	v_mov_b64_e32 v[106:107], 0
	v_mov_b64_e32 v[108:109], 0
	v_mov_b64_e32 v[114:115], 0
	v_mov_b64_e32 v[116:117], 0
	v_mov_b64_e32 v[78:79], 0
	v_mov_b64_e32 v[80:81], 0
	v_mov_b64_e32 v[86:87], 0
	v_mov_b64_e32 v[88:89], 0
	v_mov_b64_e32 v[94:95], 0
	v_mov_b64_e32 v[96:97], 0
	v_mov_b64_e32 v[102:103], 0
	v_mov_b64_e32 v[104:105], 0
	v_mov_b64_e32 v[110:111], 0
	v_mov_b64_e32 v[112:113], 0
	v_mov_b64_e32 v[118:119], 0
	v_mov_b64_e32 v[120:121], 0
	v_mov_b64_e32 v[122:123], 0
	v_mov_b64_e32 v[124:125], 0
	v_mov_b64_e32 v[126:127], 0
	v_mov_b64_e32 v[128:129], 0
.LBB0_671:
	s_cmp_eq_u32 s67, s0
	v_add_u32_e32 v160, 0x10000, v139
	v_add_u32_e32 v176, 0x14000, v139
	s_cselect_b64 vcc, -1, 0
	s_add_i32 s0, s0, 2
	ds_read_b128 v[148:151], v160
	ds_read_b128 v[152:155], v160 offset:1024
	ds_read_b128 v[156:159], v160 offset:2048
	ds_read_b128 v[160:163], v160 offset:3072
	ds_read_b128 v[164:167], v176
	ds_read_b128 v[168:171], v176 offset:1024
	ds_read_b128 v[172:175], v176 offset:2048
	ds_read_b128 v[176:179], v176 offset:3072
	s_and_b64 s[8:9], vcc, exec
	s_cselect_b32 s8, 0, s60
	s_cselect_b32 s1, 0, s61
	s_add_u32 s14, s84, s8
	s_addc_u32 s15, s85, s1
	s_add_u32 s1, s80, s60
	s_addc_u32 s12, s81, s61
	s_add_u32 s8, s14, 0x80
	s_addc_u32 s9, s15, 0
	s_and_b64 s[10:11], vcc, exec
	s_cselect_b32 s94, s4, s1
	s_cselect_b32 s95, s5, s12
	s_add_u32 s10, s94, 0x80
	v_cndmask_b32_e32 v180, v130, v141, vcc
	v_cndmask_b32_e32 v181, v145, v143, vcc
	v_cndmask_b32_e32 v197, v131, v142, vcc
	s_addc_u32 s11, s95, 0
	ds_read_b128 v[198:201], v140
	ds_read_b128 v[202:205], v140 offset:1024
	ds_read_b128 v[206:209], v140 offset:2048
	ds_read_b128 v[210:213], v140 offset:3072
	ds_read_b128 v[214:217], v140 offset:4096
	ds_read_b128 v[218:221], v140 offset:5120
	ds_read_b128 v[222:225], v140 offset:6144
	ds_read_b128 v[226:229], v140 offset:7168
	s_add_u32 s1, s84, s60
	s_addc_u32 s12, s85, s61
	s_add_u32 s96, s1, 0xffffff80
	s_addc_u32 s97, s12, -1
	s_mov_b32 m0, s72
	s_nop 0
	global_load_lds_dwordx4 v145, s[96:97]
	s_nop 0
	s_mov_b32 m0, s73
	s_nop 0
	global_load_lds_dwordx4 v147, s[96:97]
	s_waitcnt vmcnt(8)
	s_waitcnt lgkmcnt(0)
	s_barrier
	s_setprio 1
	s_waitcnt lgkmcnt(7)
	v_mfma_f32_16x16x32_bf16 v[126:129], v[148:151], v[198:201], v[126:129]
	v_mfma_f32_16x16x32_bf16 v[122:125], v[156:159], v[198:201], v[122:125]
	s_waitcnt lgkmcnt(5)
	v_mfma_f32_16x16x32_bf16 v[118:121], v[148:151], v[206:209], v[118:121]
	v_mfma_f32_16x16x32_bf16 v[110:113], v[156:159], v[206:209], v[110:113]
	s_waitcnt lgkmcnt(3)
	v_mfma_f32_16x16x32_bf16 v[102:105], v[148:151], v[214:217], v[102:105]
	v_mfma_f32_16x16x32_bf16 v[94:97], v[156:159], v[214:217], v[94:97]
	s_waitcnt lgkmcnt(1)
	v_mfma_f32_16x16x32_bf16 v[86:89], v[148:151], v[222:225], v[86:89]
	v_mfma_f32_16x16x32_bf16 v[78:81], v[156:159], v[222:225], v[78:81]
	v_mfma_f32_16x16x32_bf16 v[126:129], v[152:155], v[202:205], v[126:129]
	v_mfma_f32_16x16x32_bf16 v[122:125], v[160:163], v[202:205], v[122:125]
	v_mfma_f32_16x16x32_bf16 v[118:121], v[152:155], v[210:213], v[118:121]
	v_mfma_f32_16x16x32_bf16 v[110:113], v[160:163], v[210:213], v[110:113]
	v_mfma_f32_16x16x32_bf16 v[102:105], v[152:155], v[218:221], v[102:105]
	v_mfma_f32_16x16x32_bf16 v[94:97], v[160:163], v[218:221], v[94:97]
	s_waitcnt lgkmcnt(0)
	v_mfma_f32_16x16x32_bf16 v[86:89], v[152:155], v[226:229], v[86:89]
	v_mfma_f32_16x16x32_bf16 v[78:81], v[160:163], v[226:229], v[78:81]
	s_setprio 0
	s_setprio 1
	v_mfma_f32_16x16x32_bf16 v[114:117], v[164:167], v[198:201], v[114:117]
	v_mfma_f32_16x16x32_bf16 v[106:109], v[172:175], v[198:201], v[106:109]
	v_mfma_f32_16x16x32_bf16 v[98:101], v[164:167], v[206:209], v[98:101]
	v_mfma_f32_16x16x32_bf16 v[90:93], v[172:175], v[206:209], v[90:93]
	v_mfma_f32_16x16x32_bf16 v[82:85], v[164:167], v[214:217], v[82:85]
	v_mfma_f32_16x16x32_bf16 v[74:77], v[172:175], v[214:217], v[74:77]
	v_mfma_f32_16x16x32_bf16 v[70:73], v[164:167], v[222:225], v[70:73]
	v_mfma_f32_16x16x32_bf16 v[66:69], v[172:175], v[222:225], v[66:69]
	v_mfma_f32_16x16x32_bf16 v[114:117], v[168:171], v[202:205], v[114:117]
	v_mfma_f32_16x16x32_bf16 v[106:109], v[176:179], v[202:205], v[106:109]
	v_mfma_f32_16x16x32_bf16 v[98:101], v[168:171], v[210:213], v[98:101]
	v_mfma_f32_16x16x32_bf16 v[90:93], v[176:179], v[210:213], v[90:93]
	v_mfma_f32_16x16x32_bf16 v[82:85], v[168:171], v[218:221], v[82:85]
	v_mfma_f32_16x16x32_bf16 v[74:77], v[176:179], v[218:221], v[74:77]
	v_mfma_f32_16x16x32_bf16 v[70:73], v[168:171], v[226:229], v[70:73]
	v_mfma_f32_16x16x32_bf16 v[66:69], v[176:179], v[226:229], v[66:69]
	s_setprio 0
	s_barrier
; #define PG8_STAGE(bufoff, gbase, v0, v1) do { glds16_s((gbase), (v0), ldsbase + (unsigned)(bufoff)); glds16_s((gbase), (v1), ldsbase + (unsigned)(bufoff) + 8192u); } while (0)
; #define PG8_LDA(dst, b, h) do { _Pragma("unroll") for (int m = 0; m < 4; ++m) _Pragma("unroll") for (int k = 0; k < 2; ++k) dst[m][k] = *(const LAS bf16x8*)(lds + PG8_SA(b, h) + aoff + m * 2048 + k * 1024); } while (0)
; #define PG8_LDB(dst, b, h) do { _Pragma("unroll") for (int n = 0; n < 2; ++n) _Pragma("unroll") for (int k = 0; k < 2; ++k) dst[n][k] = *(const LAS bf16x8*)(lds + PG8_SB(b, h) + boff + n * 2048 + k * 1024); } while (0)
; #define PG8_WAIT_V(n) asm volatile("s_waitcnt vmcnt(" #n ")" ::: "memory")
; #define PG8_WAIT_L(n) asm volatile("s_waitcnt lgkmcnt(" #n ")" ::: "memory")
; #define PG8_BAR __builtin_amdgcn_s_barrier()
; #define PG8_SCHED __builtin_amdgcn_sched_barrier(0)
; template <class Epi, class Sched, bool ALIGN_EPI, bool FP8 = false>
; __device__ __forceinline__ void gemm_phase(LAS unsigned char* lds, const bf16_t* A, const bf16_t* Bt, const int K, const Sched& S, const Epi& E, const int wave_in) {
;     ...
;             PG8_WAIT_V(8); PG8_WAIT_L(0); PG8_BAR; PG8_MMA(0, 0, At, B0); PG8_MMA(0, 1, At, B1); PG8_BAR; PG8_SCHED;
;             PG8_LDA(At, 0, 1); PG8_STAGE(PG8_SB(0, 0), b2, voffB[0], voffB[1]); PG8_STAGE(PG8_SB(0, 1), b2 + hstep, voffB[0], voffB[1]); PG8_STAGE(PG8_SA(0, 0), a2, w00, w01);
;             PG8_WAIT_V(8); PG8_WAIT_L(0); PG8_BAR; PG8_MMA(1, 0, At, B0); PG8_MMA(1, 1, At, B1); PG8_BAR; PG8_SCHED;
;             PG8_LDB(B0, 1, 0); PG8_LDB(B1, 1, 1); PG8_SCHED; PG8_LDA(At, 1, 0); PG8_STAGE(PG8_SA(0, 1), a2, w10, w11);
;             PG8_WAIT_V(8); PG8_WAIT_L(0); PG8_BAR; PG8_MMA(0, 0, At, B0); PG8_MMA(0, 1, At, B1); PG8_BAR; PG8_SCHED;
	ds_read_b128 v[198:201], v140 offset:16384
	ds_read_b128 v[202:205], v140 offset:17408
	ds_read_b128 v[206:209], v140 offset:18432
	ds_read_b128 v[210:213], v140 offset:19456
	ds_read_b128 v[214:217], v140 offset:20480
	ds_read_b128 v[218:221], v140 offset:21504
	ds_read_b128 v[222:225], v140 offset:22528
	ds_read_b128 v[226:229], v140 offset:23552
	s_mov_b32 m0, s39
	s_nop 0
	global_load_lds_dwordx4 v133, s[94:95]
	s_nop 0
	s_mov_b32 m0, s48
	s_nop 0
	global_load_lds_dwordx4 v136, s[94:95]
	s_add_u32 s94, s94, s16
	s_addc_u32 s95, s95, 0
	s_mov_b32 m0, s49
	s_nop 0
	global_load_lds_dwordx4 v133, s[94:95]
	s_nop 0
	s_mov_b32 m0, s50
	s_nop 0
	global_load_lds_dwordx4 v136, s[94:95]
	s_nop 0
	s_mov_b32 m0, s17
	s_nop 0
	global_load_lds_dwordx4 v180, s[14:15]
	s_nop 0
	s_mov_b32 m0, s51
	s_nop 0
	global_load_lds_dwordx4 v197, s[14:15]
	s_waitcnt vmcnt(8)
	s_waitcnt lgkmcnt(0)
	s_barrier
	s_setprio 1
	s_waitcnt lgkmcnt(7)
	v_mfma_f32_16x16x32_bf16 v[62:65], v[148:151], v[198:201], v[62:65]
	v_mfma_f32_16x16x32_bf16 v[58:61], v[156:159], v[198:201], v[58:61]
	s_waitcnt lgkmcnt(5)
	v_mfma_f32_16x16x32_bf16 v[54:57], v[148:151], v[206:209], v[54:57]
	v_mfma_f32_16x16x32_bf16 v[46:49], v[156:159], v[206:209], v[46:49]
	s_waitcnt lgkmcnt(3)
	v_mfma_f32_16x16x32_bf16 v[38:41], v[148:151], v[214:217], v[38:41]
	v_mfma_f32_16x16x32_bf16 v[30:33], v[156:159], v[214:217], v[30:33]
	s_waitcnt lgkmcnt(1)
	v_mfma_f32_16x16x32_bf16 v[22:25], v[148:151], v[222:225], v[22:25]
	v_mfma_f32_16x16x32_bf16 v[14:17], v[156:159], v[222:225], v[14:17]
	v_mfma_f32_16x16x32_bf16 v[62:65], v[152:155], v[202:205], v[62:65]
	v_mfma_f32_16x16x32_bf16 v[58:61], v[160:163], v[202:205], v[58:61]
	v_mfma_f32_16x16x32_bf16 v[54:57], v[152:155], v[210:213], v[54:57]
	v_mfma_f32_16x16x32_bf16 v[46:49], v[160:163], v[210:213], v[46:49]
	v_mfma_f32_16x16x32_bf16 v[38:41], v[152:155], v[218:221], v[38:41]
	v_mfma_f32_16x16x32_bf16 v[30:33], v[160:163], v[218:221], v[30:33]
	s_waitcnt lgkmcnt(0)
	v_mfma_f32_16x16x32_bf16 v[22:25], v[152:155], v[226:229], v[22:25]
	v_mfma_f32_16x16x32_bf16 v[14:17], v[160:163], v[226:229], v[14:17]
	s_setprio 0
	s_setprio 1
	v_mfma_f32_16x16x32_bf16 v[50:53], v[164:167], v[198:201], v[50:53]
	v_mfma_f32_16x16x32_bf16 v[42:45], v[172:175], v[198:201], v[42:45]
	v_mfma_f32_16x16x32_bf16 v[34:37], v[164:167], v[206:209], v[34:37]
	v_mfma_f32_16x16x32_bf16 v[26:29], v[172:175], v[206:209], v[26:29]
	v_mfma_f32_16x16x32_bf16 v[18:21], v[164:167], v[214:217], v[18:21]
	v_mfma_f32_16x16x32_bf16 v[10:13], v[172:175], v[214:217], v[10:13]
	v_mfma_f32_16x16x32_bf16 v[6:9], v[164:167], v[222:225], v[6:9]
	v_mfma_f32_16x16x32_bf16 v[2:5], v[172:175], v[222:225], v[2:5]
	v_mfma_f32_16x16x32_bf16 v[50:53], v[168:171], v[202:205], v[50:53]
	v_mfma_f32_16x16x32_bf16 v[42:45], v[176:179], v[202:205], v[42:45]
	v_mfma_f32_16x16x32_bf16 v[34:37], v[168:171], v[210:213], v[34:37]
	v_mfma_f32_16x16x32_bf16 v[26:29], v[176:179], v[210:213], v[26:29]
	v_mfma_f32_16x16x32_bf16 v[18:21], v[168:171], v[218:221], v[18:21]
	v_mfma_f32_16x16x32_bf16 v[10:13], v[176:179], v[218:221], v[10:13]
	v_mfma_f32_16x16x32_bf16 v[6:9], v[168:171], v[226:229], v[6:9]
	v_mfma_f32_16x16x32_bf16 v[2:5], v[176:179], v[226:229], v[2:5]
	s_setprio 0
	s_barrier
	v_add_u32_e32 v160, 0x18000, v139
	v_add_u32_e32 v176, 0x1c000, v139
	ds_read_b128 v[148:151], v160
	ds_read_b128 v[152:155], v160 offset:1024
	ds_read_b128 v[156:159], v160 offset:2048
	ds_read_b128 v[160:163], v160 offset:3072
	ds_read_b128 v[164:167], v176
	ds_read_b128 v[168:171], v176 offset:1024
	ds_read_b128 v[172:175], v176 offset:2048
	ds_read_b128 v[176:179], v176 offset:3072
	ds_read_b128 v[198:201], v140 offset:32768
	ds_read_b128 v[202:205], v140 offset:33792
	ds_read_b128 v[206:209], v140 offset:34816
	ds_read_b128 v[210:213], v140 offset:35840
	ds_read_b128 v[214:217], v140 offset:36864
	ds_read_b128 v[218:221], v140 offset:37888
	ds_read_b128 v[222:225], v140 offset:38912
	ds_read_b128 v[226:229], v140 offset:39936
	s_mov_b32 m0, s52
	s_nop 0
	global_load_lds_dwordx4 v181, s[14:15]
	v_cndmask_b32_e32 v230, v147, v144, vcc
	s_mov_b32 m0, s53
	s_nop 0
	global_load_lds_dwordx4 v230, s[14:15]
	s_waitcnt vmcnt(8)
	s_waitcnt lgkmcnt(0)
	s_barrier
; #define PG8_STAGE(bufoff, gbase, v0, v1) do { glds16_s((gbase), (v0), ldsbase + (unsigned)(bufoff)); glds16_s((gbase), (v1), ldsbase + (unsigned)(bufoff) + 8192u); } while (0)
; #define PG8_LDA(dst, b, h) do { _Pragma("unroll") for (int m = 0; m < 4; ++m) _Pragma("unroll") for (int k = 0; k < 2; ++k) dst[m][k] = *(const LAS bf16x8*)(lds + PG8_SA(b, h) + aoff + m * 2048 + k * 1024); } while (0)
; #define PG8_WAIT_V(n) asm volatile("s_waitcnt vmcnt(" #n ")" ::: "memory")
; #define PG8_WAIT_L(n) asm volatile("s_waitcnt lgkmcnt(" #n ")" ::: "memory")
; #define PG8_BAR __builtin_amdgcn_s_barrier()
; #define PG8_SCHED __builtin_amdgcn_sched_barrier(0)
; template <class Epi, class Sched, bool ALIGN_EPI, bool FP8 = false>
; __device__ __forceinline__ void gemm_phase(LAS unsigned char* lds, const bf16_t* A, const bf16_t* Bt, const int K, const Sched& S, const Epi& E, const int wave_in) {
;     ...
;             PG8_WAIT_V(8); PG8_WAIT_L(0); PG8_BAR; PG8_MMA(0, 0, At, B0); PG8_MMA(0, 1, At, B1); PG8_BAR; PG8_SCHED;
;             PG8_LDA(At, 1, 1); PG8_STAGE(PG8_SB(1, 0), b3, voffB[0], voffB[1]); PG8_STAGE(PG8_SB(1, 1), b3 + hstep, voffB[0], voffB[1]); PG8_STAGE(PG8_SA(1, 0), a3, w00, w01);
;             PG8_WAIT_V(8); PG8_WAIT_L(0); PG8_BAR; PG8_MMA(1, 0, At, B0); PG8_MMA(1, 1, At, B1); PG8_BAR; PG8_SCHED;
;         }
	s_setprio 1
	s_waitcnt lgkmcnt(7)
	v_mfma_f32_16x16x32_bf16 v[126:129], v[148:151], v[198:201], v[126:129]
	v_mfma_f32_16x16x32_bf16 v[122:125], v[156:159], v[198:201], v[122:125]
	s_waitcnt lgkmcnt(5)
	v_mfma_f32_16x16x32_bf16 v[118:121], v[148:151], v[206:209], v[118:121]
	v_mfma_f32_16x16x32_bf16 v[110:113], v[156:159], v[206:209], v[110:113]
	s_waitcnt lgkmcnt(3)
	v_mfma_f32_16x16x32_bf16 v[102:105], v[148:151], v[214:217], v[102:105]
	v_mfma_f32_16x16x32_bf16 v[94:97], v[156:159], v[214:217], v[94:97]
	s_waitcnt lgkmcnt(1)
	v_mfma_f32_16x16x32_bf16 v[86:89], v[148:151], v[222:225], v[86:89]
	v_mfma_f32_16x16x32_bf16 v[78:81], v[156:159], v[222:225], v[78:81]
	v_mfma_f32_16x16x32_bf16 v[126:129], v[152:155], v[202:205], v[126:129]
	v_mfma_f32_16x16x32_bf16 v[122:125], v[160:163], v[202:205], v[122:125]
	v_mfma_f32_16x16x32_bf16 v[118:121], v[152:155], v[210:213], v[118:121]
	v_mfma_f32_16x16x32_bf16 v[110:113], v[160:163], v[210:213], v[110:113]
	v_mfma_f32_16x16x32_bf16 v[102:105], v[152:155], v[218:221], v[102:105]
	v_mfma_f32_16x16x32_bf16 v[94:97], v[160:163], v[218:221], v[94:97]
	s_waitcnt lgkmcnt(0)
	v_mfma_f32_16x16x32_bf16 v[86:89], v[152:155], v[226:229], v[86:89]
	v_mfma_f32_16x16x32_bf16 v[78:81], v[160:163], v[226:229], v[78:81]
	s_setprio 0
	s_setprio 1
	v_mfma_f32_16x16x32_bf16 v[114:117], v[164:167], v[198:201], v[114:117]
	v_mfma_f32_16x16x32_bf16 v[106:109], v[172:175], v[198:201], v[106:109]
	v_mfma_f32_16x16x32_bf16 v[98:101], v[164:167], v[206:209], v[98:101]
	v_mfma_f32_16x16x32_bf16 v[90:93], v[172:175], v[206:209], v[90:93]
	v_mfma_f32_16x16x32_bf16 v[82:85], v[164:167], v[214:217], v[82:85]
	v_mfma_f32_16x16x32_bf16 v[74:77], v[172:175], v[214:217], v[74:77]
	v_mfma_f32_16x16x32_bf16 v[70:73], v[164:167], v[222:225], v[70:73]
	v_mfma_f32_16x16x32_bf16 v[66:69], v[172:175], v[222:225], v[66:69]
	v_mfma_f32_16x16x32_bf16 v[114:117], v[168:171], v[202:205], v[114:117]
	v_mfma_f32_16x16x32_bf16 v[106:109], v[176:179], v[202:205], v[106:109]
	v_mfma_f32_16x16x32_bf16 v[98:101], v[168:171], v[210:213], v[98:101]
	v_mfma_f32_16x16x32_bf16 v[90:93], v[176:179], v[210:213], v[90:93]
	v_mfma_f32_16x16x32_bf16 v[82:85], v[168:171], v[218:221], v[82:85]
	v_mfma_f32_16x16x32_bf16 v[74:77], v[176:179], v[218:221], v[74:77]
	v_mfma_f32_16x16x32_bf16 v[70:73], v[168:171], v[226:229], v[70:73]
	v_mfma_f32_16x16x32_bf16 v[66:69], v[176:179], v[226:229], v[66:69]
	s_setprio 0
	s_barrier
	ds_read_b128 v[198:201], v140 offset:49152
	ds_read_b128 v[202:205], v140 offset:50176
	ds_read_b128 v[206:209], v140 offset:51200
	ds_read_b128 v[210:213], v140 offset:52224
	ds_read_b128 v[214:217], v140 offset:53248
	ds_read_b128 v[218:221], v140 offset:54272
	ds_read_b128 v[222:225], v140 offset:55296
	ds_read_b128 v[226:229], v140 offset:56320
	s_mov_b32 m0, s57
	s_nop 0
	global_load_lds_dwordx4 v133, s[10:11]
	s_nop 0
	s_mov_b32 m0, s58
	s_nop 0
	global_load_lds_dwordx4 v136, s[10:11]
	s_add_u32 s10, s10, s16
	s_addc_u32 s11, s11, 0
	s_mov_b32 m0, s65
	s_nop 0
	global_load_lds_dwordx4 v133, s[10:11]
	s_nop 0
	s_mov_b32 m0, s66
	s_nop 0
	global_load_lds_dwordx4 v136, s[10:11]
	s_nop 0
	s_mov_b32 m0, s59
	s_nop 0
	global_load_lds_dwordx4 v180, s[8:9]
	s_nop 0
	s_mov_b32 m0, s64
	s_nop 0
	global_load_lds_dwordx4 v197, s[8:9]
	s_waitcnt vmcnt(8)
	s_waitcnt lgkmcnt(0)
	s_barrier
	s_setprio 1
	s_waitcnt lgkmcnt(7)
	v_mfma_f32_16x16x32_bf16 v[62:65], v[148:151], v[198:201], v[62:65]
	v_mfma_f32_16x16x32_bf16 v[58:61], v[156:159], v[198:201], v[58:61]
	s_waitcnt lgkmcnt(5)
	v_mfma_f32_16x16x32_bf16 v[54:57], v[148:151], v[206:209], v[54:57]
	v_mfma_f32_16x16x32_bf16 v[46:49], v[156:159], v[206:209], v[46:49]
	s_waitcnt lgkmcnt(3)
	v_mfma_f32_16x16x32_bf16 v[38:41], v[148:151], v[214:217], v[38:41]
	v_mfma_f32_16x16x32_bf16 v[30:33], v[156:159], v[214:217], v[30:33]
	s_waitcnt lgkmcnt(1)
	v_mfma_f32_16x16x32_bf16 v[22:25], v[148:151], v[222:225], v[22:25]
	v_mfma_f32_16x16x32_bf16 v[14:17], v[156:159], v[222:225], v[14:17]
	v_mfma_f32_16x16x32_bf16 v[62:65], v[152:155], v[202:205], v[62:65]
	v_mfma_f32_16x16x32_bf16 v[58:61], v[160:163], v[202:205], v[58:61]
	v_mfma_f32_16x16x32_bf16 v[54:57], v[152:155], v[210:213], v[54:57]
	v_mfma_f32_16x16x32_bf16 v[46:49], v[160:163], v[210:213], v[46:49]
	v_mfma_f32_16x16x32_bf16 v[38:41], v[152:155], v[218:221], v[38:41]
	v_mfma_f32_16x16x32_bf16 v[30:33], v[160:163], v[218:221], v[30:33]
	s_waitcnt lgkmcnt(0)
	v_mfma_f32_16x16x32_bf16 v[22:25], v[152:155], v[226:229], v[22:25]
	v_mfma_f32_16x16x32_bf16 v[14:17], v[160:163], v[226:229], v[14:17]
	s_setprio 0
	s_setprio 1
	v_mfma_f32_16x16x32_bf16 v[50:53], v[164:167], v[198:201], v[50:53]
	v_mfma_f32_16x16x32_bf16 v[42:45], v[172:175], v[198:201], v[42:45]
	v_mfma_f32_16x16x32_bf16 v[34:37], v[164:167], v[206:209], v[34:37]
	v_mfma_f32_16x16x32_bf16 v[26:29], v[172:175], v[206:209], v[26:29]
	v_mfma_f32_16x16x32_bf16 v[18:21], v[164:167], v[214:217], v[18:21]
	v_mfma_f32_16x16x32_bf16 v[10:13], v[172:175], v[214:217], v[10:13]
	v_mfma_f32_16x16x32_bf16 v[6:9], v[164:167], v[222:225], v[6:9]
	v_mfma_f32_16x16x32_bf16 v[2:5], v[172:175], v[222:225], v[2:5]
	v_mfma_f32_16x16x32_bf16 v[50:53], v[168:171], v[202:205], v[50:53]
	v_mfma_f32_16x16x32_bf16 v[42:45], v[176:179], v[202:205], v[42:45]
	v_mfma_f32_16x16x32_bf16 v[34:37], v[168:171], v[210:213], v[34:37]
	v_mfma_f32_16x16x32_bf16 v[26:29], v[176:179], v[210:213], v[26:29]
	v_mfma_f32_16x16x32_bf16 v[18:21], v[168:171], v[218:221], v[18:21]
	v_mfma_f32_16x16x32_bf16 v[10:13], v[176:179], v[218:221], v[10:13]
	v_mfma_f32_16x16x32_bf16 v[6:9], v[168:171], v[226:229], v[6:9]
	v_mfma_f32_16x16x32_bf16 v[2:5], v[176:179], v[226:229], v[2:5]
	s_setprio 0
	s_barrier
	s_add_u32 s60, s60, 0x100
	s_addc_u32 s61, s61, 0
	s_cmp_ge_u32 s0, s54
	s_cbranch_scc0 .LBB0_671
	s_and_b64 vcc, exec, s[78:79]
	s_cbranch_vccz .LBB0_674
	s_barrier

; __device__ __forceinline__ int opaque_tid(int wave) { int l; asm volatile("v_mbcnt_lo_u32_b32 %0, -1, 0\n\tv_mbcnt_hi_u32_b32 %0, -1, %0" : "=v"(l)); return wave * 64 + l; }
; template <class Epi, class Sched, bool ALIGN_EPI, bool FP8 = false>
; __device__ __forceinline__ void gemm_phase(LAS unsigned char* lds, const bf16_t* A, const bf16_t* Bt, const int K, const Sched& S, const Epi& E, const int wave_in) {
;     const int tid = opaque_tid(wave_in); const int wid = __builtin_amdgcn_readfirstlane(tid >> 6), lane = tid & 63, wr = wid >> 2, wc = wid & 3, fr = lane & 15, fq = lane >> 4;
;     const int nt = K / BK;
;     int sR[2], sC[2]; unsigned voffB[2];
; #pragma unroll
;     for (int i = 0; i < 2; ++i) { stage_rc(tid * 16 + i * 8192, sR[i], sC[i]); const int Rb = Epi::PERM ? ((sR[i] & ~31) + perm32(sR[i] & 31)) : sR[i];
;         voffB[i] = (unsigned)(Rb * K + sC[i]) * 2u; }
;     const size_t kstep = (size_t)(BK * 2);
;     const size_t hstep = (size_t)HALF * K * 2;
;     const unsigned ldsw = (unsigned)wid * 1024u;
;     const unsigned ldsbase = (unsigned)__builtin_amdgcn_readfirstlane((int)((unsigned)(uintptr_t)lds + ldsw));
;     const int aoff = lds_byte(wr * 64 + fr, fq * 8), boff = lds_byte(wc * 32 + fr, fq * 8);
;     ...
;     Unit cur, nxt; int ui = 0;
;     if (!S.next(0, cur)) return;
;     f32x4 acc[2][2][4][2];
; #pragma unroll
;     for (int a = 0; a < 2; ++a)
; #pragma unroll
;         for (int b = 0; b < 2; ++b)
; #pragma unroll
;             for (int m = 0; m < 4; ++m)
; #pragma unroll
;                 for (int n = 0; n < 2; ++n) acc[a][b][m][n] = (f32x4){0.f, 0.f, 0.f, 0.f};
;     bf16x8 At[4][2], B0[2][2], B1[2][2];
;     const int sclW = W8_E8M0, sclA = A8_E8M0;
;     unsigned vA[2][2], vN[2][2];
;     PG8_AOFF(vA, cur);
;     const char* const cA = (const char*)A;
;     const char* cB = (const char*)Bt + S.b_off(cur) * 2;
;     PG8_STAGE(PG8_SB(0, 0), cB, voffB[0], voffB[1]); PG8_STAGE(PG8_SB(0, 1), cB + hstep, voffB[0], voffB[1]); PG8_STAGE(PG8_SA(0, 0), cA, vA[0][0], vA[0][1]); PG8_STAGE(PG8_SA(0, 1), cA, vA[1][0], vA[1][1]);
;     if (wr == 1) PG8_BAR;
;     PG8_WAIT_V(2); PG8_BAR;
;     PG8_STAGE(PG8_SB(1, 0), cB + kstep, voffB[0], voffB[1]); PG8_STAGE(PG8_SA(1, 0), cA + kstep, vA[0][0], vA[0][1]); PG8_STAGE(PG8_SB(1, 1), cB + hstep + kstep, voffB[0], voffB[1]);
;     PG8_WAIT_V(6); PG8_BAR;
.LBB0_679:
	s_andn2_b64 vcc, exec, s[0:1]
	s_cbranch_vccnz .LBB0_698
	v_readlane_b32 s0, v232, 0
	s_waitcnt vmcnt(6)
	v_mbcnt_lo_u32_b32 v2, -1, 0
	v_mbcnt_hi_u32_b32 v2, -1, v2
	s_nop 0
	v_add_u32_e32 v0, s0, v2
	s_nop 0
	v_readfirstlane_b32 s2, v0
	s_ashr_i32 s3, s2, 6
	s_cmp_ge_i32 s18, s6
	s_cbranch_scc1 .LBB0_698
	v_ashrrev_i32_e32 v4, 31, v0
	v_lshrrev_b32_e32 v4, 26, v4
	v_lshlrev_b32_e32 v3, 4, v0
	v_add_u32_e32 v4, v0, v4
	v_bfe_i32 v0, v0, 27, 1
	v_lshrrev_b32_e32 v0, 22, v0
	v_add_u32_e32 v0, v3, v0
	v_and_b32_e32 v0, 0xfffffc00, v0
	v_sub_u32_e32 v0, v3, v0
	v_lshrrev_b32_e32 v5, 4, v0
	v_bitop3_b32 v5, v5, v0, 32 bitop3:0x6c
	s_waitcnt vmcnt(5)
	v_ashrrev_i32_e32 v6, 31, v5
	v_lshrrev_b32_e32 v6, 26, v6
	v_ashrrev_i32_e32 v4, 6, v4
	v_add_u32_e32 v6, v5, v6
	v_lshlrev_b32_e32 v0, 3, v4
	v_ashrrev_i32_e32 v7, 6, v6
	v_and_b32_e32 v6, 0xc0, v6
	v_and_b32_e32 v0, -16, v0
	v_lshlrev_b32_e32 v4, 5, v4
	v_sub_u32_e32 v5, v5, v6
	v_add_u32_e32 v0, v7, v0
	v_and_b32_e32 v4, 32, v4
	v_ashrrev_i16_sdwa v5, v185, sext(v5) dst_sel:DWORD dst_unused:UNUSED_PAD src0_sel:DWORD src1_sel:BYTE_0
	v_add_u32_sdwa v147, v4, sext(v5) dst_sel:DWORD dst_unused:UNUSED_PAD src0_sel:DWORD src1_sel:WORD_0
	v_lshlrev_b32_e32 v4, 1, v0
	v_lshrrev_b32_e32 v5, 2, v0
	v_and_b32_e32 v6, 3, v7
	s_mov_b32 s0, 0x7fffffe0
	v_and_b32_e32 v4, 24, v4
	v_and_b32_e32 v5, 4, v5
	v_and_or_b32 v6, v0, s0, v6
	v_or3_b32 v4, v6, v5, v4
	v_mul_lo_u32 v4, v4, s21
	v_add_u32_e32 v3, 0x2000, v3
	v_add_lshl_u32 v164, v4, v147, 1
	v_ashrrev_i32_e32 v4, 31, v3
	v_lshrrev_b32_e32 v4, 22, v4
	v_add_u32_e32 v4, v3, v4
	v_ashrrev_i32_e32 v4, 10, v4
	v_mul_i32_i24_e32 v5, 0x400, v4
	v_sub_u32_e32 v3, v3, v5
	v_lshrrev_b32_e32 v5, 4, v3
	v_bitop3_b32 v3, v5, v3, 32 bitop3:0x6c
	v_ashrrev_i32_e32 v6, 31, v3
	v_lshrrev_b32_e32 v6, 26, v6
	v_lshlrev_b32_e32 v5, 3, v4
	v_add_u32_e32 v6, v3, v6
	v_and_b32_e32 v5, -16, v5
	v_ashrrev_i32_e32 v7, 6, v6
	v_add_u32_e32 v165, v7, v5
	v_and_b32_e32 v5, 0xc0, v6
	v_sub_u32_e32 v3, v3, v5
	v_and_b32_e32 v5, 3, v7
	v_and_or_b32 v5, v165, s0, v5
	s_lshl_b32 s0, s3, 10
	s_ashr_i32 s38, s18, 31
	s_add_i32 s25, s0, 0
	s_lshr_b32 s0, s38, 29
	s_add_i32 s0, s18, s0
	s_lshr_b32 s28, s29, 9
	s_ashr_i32 s1, s0, 3
	s_and_b32 s0, s0, -8
	s_ashr_i32 s4, s2, 8
	s_lshl_b32 s24, s21, 8
	s_sub_i32 s0, s18, s0
	s_or_b32 s39, s28, 1
	s_cmp_lt_i32 s0, 0
	s_cselect_b32 s5, s39, s28
	s_mul_i32 s0, s0, s5
	s_add_i32 s0, s0, s1
	s_ashr_i32 s1, s0, 31
	s_lshr_b32 s1, s1, 27
	v_lshlrev_b32_e32 v4, 5, v4
	s_add_i32 s1, s0, s1
	v_and_b32_e32 v4, 32, v4
	v_ashrrev_i16_sdwa v3, v185, sext(v3) dst_sel:DWORD dst_unused:UNUSED_PAD src0_sel:DWORD src1_sel:BYTE_0
	s_ashr_i32 s5, s1, 5
	v_add_u32_sdwa v166, v4, sext(v3) dst_sel:DWORD dst_unused:UNUSED_PAD src0_sel:DWORD src1_sel:WORD_0
	v_lshlrev_b32_e32 v3, 1, v165
	v_lshrrev_b32_e32 v4, 2, v165
	s_lshl_b32 s5, s5, 3
	v_and_b32_e32 v3, 24, v3
	v_and_b32_e32 v4, 4, v4
	s_sub_i32 s7, s22, s5
	v_or3_b32 v3, v5, v4, v3
	s_min_i32 s7, s7, 8
	v_mul_lo_u32 v3, v3, s21
	s_abs_i32 s9, s7
	v_add_lshl_u32 v167, v3, v166, 1
	v_cvt_f32_u32_e32 v3, s9
	s_sub_i32 s10, 0, s9
	s_andn2_b32 s1, s1, 31
	s_sub_i32 s0, s0, s1
	v_rcp_iflag_f32_e32 v3, v3
	s_abs_i32 s8, s0
	s_xor_b32 s1, s0, s7
	s_ashr_i32 s1, s1, 31
	v_mul_f32_e32 v3, 0x4f7ffffe, v3
	v_cvt_u32_f32_e32 v3, v3
	s_nop 0
	v_readfirstlane_b32 s11, v3
	s_mul_i32 s10, s10, s11
	s_mul_hi_u32 s10, s11, s10
	s_add_i32 s11, s11, s10
	s_mul_hi_u32 s10, s8, s11
	s_mul_i32 s11, s10, s9
	s_sub_i32 s8, s8, s11
	s_add_i32 s11, s10, 1
	s_sub_i32 s12, s8, s9
	s_cmp_ge_u32 s8, s9
	s_cselect_b32 s10, s11, s10
	s_cselect_b32 s8, s12, s8
	s_add_i32 s11, s10, 1
	s_cmp_ge_u32 s8, s9
	s_cselect_b32 s8, s11, s10
	s_xor_b32 s8, s8, s1
	s_sub_i32 s94, s8, s1
	s_mul_i32 s1, s94, s7
	s_sub_i32 s0, s0, s1
	s_add_i32 s0, s0, s23
	s_add_i32 s95, s0, s5
	s_lshl_b32 s0, s95, 8
	v_add_u32_e32 v3, s0, v0
	v_mul_lo_u32 v3, v3, s21
	v_add_lshl_u32 v176, v3, v147, 1
	v_add_u32_e32 v3, s0, v165
	v_mul_lo_u32 v3, v3, s21
	s_bitset1_b32 s0, 7
	v_add_lshl_u32 v177, v3, v166, 1
	v_add_u32_e32 v3, s0, v0
	s_lshl_b32 s48, s21, 9
	v_mul_lo_u32 v3, v3, s21
	s_mul_i32 s1, s48, s94
	v_add_lshl_u32 v178, v3, v147, 1
	v_add_u32_e32 v3, s0, v165
	s_mul_hi_i32 s0, s48, s94
	s_add_u32 s80, s86, s1
	s_addc_u32 s81, s87, s0
	s_add_i32 s49, s25, 0x10000
	s_mov_b32 m0, s49
	s_nop 0
	global_load_lds_dwordx4 v164, s[80:81]
	s_add_i32 s50, s25, 0x12000
	s_mov_b32 m0, s50
	s_nop 0
	global_load_lds_dwordx4 v167, s[80:81]
	s_add_u32 s0, s80, s24
	s_addc_u32 s1, s81, 0
	s_add_i32 s51, s25, 0x14000
	s_mov_b32 m0, s51
	s_nop 0
	global_load_lds_dwordx4 v164, s[0:1]
	s_add_i32 s52, s25, 0x16000
	s_mov_b32 m0, s52
	s_nop 0
	global_load_lds_dwordx4 v167, s[0:1]
	s_add_i32 s53, s25, 0x2000
	s_mov_b32 m0, s25
	s_nop 0
	global_load_lds_dwordx4 v176, s[84:85]
	v_mul_lo_u32 v3, v3, s21
	s_mov_b32 m0, s53
	s_nop 0
	global_load_lds_dwordx4 v177, s[84:85]
	s_add_i32 s54, s25, 0x4000
	s_mov_b32 m0, s54
	s_nop 0
	global_load_lds_dwordx4 v178, s[84:85]
	v_add_lshl_u32 v179, v3, v166, 1
	s_add_i32 s55, s25, 0x6000
	s_mov_b32 m0, s55
	s_nop 0
	global_load_lds_dwordx4 v179, s[84:85]
	s_cmp_eq_u32 s4, 1
	s_cselect_b64 s[26:27], -1, 0
	s_cmp_lg_u32 s4, 1
	s_cbranch_scc1 .LBB0_683
	s_barrier
.LBB0_683:
	v_bfe_u32 v168, v2, 4, 2
	s_lshl_b32 s3, s3, 5
	v_and_b32_e32 v169, 15, v2
	v_lshlrev_b32_e32 v3, 4, v168
	v_lshlrev_b32_e32 v2, 2, v2
	s_and_b32 s58, s3, 0x60
	s_lshr_b32 s56, s21, 6
	s_lshl_b32 s57, s4, 6
	v_lshl_or_b32 v3, v169, 6, v3
	s_lshl_b32 s4, s4, 13
	v_and_b32_e32 v2, 32, v2
	s_lshl_b32 s3, s58, 7
	v_bitop3_b32 v4, v3, s4, v2 bitop3:0xde
	s_add_u32 s4, s80, 0x80
	v_bitop3_b32 v2, v3, s3, v2 bitop3:0xde
	s_waitcnt vmcnt(2)
	s_barrier
	s_addc_u32 s5, s81, 0
	s_add_i32 s59, s25, 0x18000
	s_mov_b32 m0, s59
	s_nop 0
	global_load_lds_dwordx4 v164, s[4:5]
	s_add_i32 s64, s25, 0x1a000
	s_mov_b32 m0, s64
	s_nop 0
	global_load_lds_dwordx4 v167, s[4:5]
	s_add_u32 s4, s84, 0x80
	s_addc_u32 s5, s85, 0
	s_add_i32 s65, s25, 0x8000
	s_mov_b32 m0, s65
	s_nop 0
	global_load_lds_dwordx4 v176, s[4:5]
	s_add_i32 s66, s25, 0xa000
	s_mov_b32 m0, s66
	s_nop 0
	global_load_lds_dwordx4 v177, s[4:5]
	s_add_u32 s0, s0, 0x80
	s_addc_u32 s1, s1, 0
	s_add_i32 s67, s25, 0x1c000
	s_mov_b32 m0, s67
	s_nop 0
	global_load_lds_dwordx4 v164, s[0:1]
	s_add_i32 s72, s25, 0x1e000
	s_mov_b32 m0, s72
	s_nop 0
	global_load_lds_dwordx4 v167, s[0:1]
	s_waitcnt vmcnt(6)
	s_add_i32 s73, s56, -2
	s_add_i32 s88, s25, 0xc000
	s_add_i32 s89, s25, 0xe000
	s_cmpk_lt_u32 s2, 0x100
	s_cselect_b64 s[78:79], -1, 0
	s_ashr_i32 s90, s20, 31
	s_mov_b32 s7, s19
	s_mov_b32 s91, 0
	v_add_u32_e32 v170, 0, v2
	v_add_u32_e32 v171, 0, v4
	s_barrier
	s_waitcnt vmcnt(0)
	s_branch .LBB0_686

; #define PG8_STAGE(bufoff, gbase, v0, v1) do { glds16_s((gbase), (v0), ldsbase + (unsigned)(bufoff)); glds16_s((gbase), (v1), ldsbase + (unsigned)(bufoff) + 8192u); } while (0)
; #define PG8_LDA(dst, b, h) do { _Pragma("unroll") for (int m = 0; m < 4; ++m) _Pragma("unroll") for (int k = 0; k < 2; ++k) dst[m][k] = *(const LAS bf16x8*)(lds + PG8_SA(b, h) + aoff + m * 2048 + k * 1024); } while (0)
; #define PG8_LDB(dst, b, h) do { _Pragma("unroll") for (int n = 0; n < 2; ++n) _Pragma("unroll") for (int k = 0; k < 2; ++k) dst[n][k] = *(const LAS bf16x8*)(lds + PG8_SB(b, h) + boff + n * 2048 + k * 1024); } while (0)
; #define PG8_WAIT_V(n) asm volatile("s_waitcnt vmcnt(" #n ")" ::: "memory")
; #define PG8_WAIT_L(n) asm volatile("s_waitcnt lgkmcnt(" #n ")" ::: "memory")
; #define PG8_BAR __builtin_amdgcn_s_barrier()
; #define PG8_SCHED __builtin_amdgcn_sched_barrier(0)
; template <class Epi, class Sched, bool ALIGN_EPI, bool FP8 = false>
; __device__ __forceinline__ void gemm_phase(LAS unsigned char* lds, const bf16_t* A, const bf16_t* Bt, const int K, const Sched& S, const Epi& E, const int wave_in) {
;     ...
;             const unsigned w00 = last ? vN[0][0] : vA[0][0], w01 = last ? vN[0][1] : vA[0][1], w10 = last ? vN[1][0] : vA[1][0], w11 = last ? vN[1][1] : vA[1][1];
;             PG8_LDB(B0, 0, 0); PG8_LDB(B1, 0, 1); PG8_SCHED; PG8_LDA(At, 0, 0); PG8_STAGE(PG8_SA(1, 1), a1, vA[1][0], vA[1][1]);
;             PG8_WAIT_V(8); PG8_WAIT_L(0); PG8_BAR; PG8_MMA(0, 0, At, B0); PG8_MMA(0, 1, At, B1); PG8_BAR; PG8_SCHED;
;     ...
; #pragma unroll
;         for (int a = 0; a < 2; ++a)
; #pragma unroll
;             for (int b = 0; b < 2; ++b)
; #pragma unroll
;                 for (int m = 0; m < 4; ++m)
; #pragma unroll
;                     for (int n = 0; n < 2; ++n) acc[a][b][m][n] = (f32x4){0.f, 0.f, 0.f, 0.f};
.LBB0_690:
	v_mov_b32_e32 v34, 0
	s_mov_b32 s0, 0
	s_mov_b64 s[60:61], 0x100
	v_mov_b32_e32 v35, 0
	v_mov_b64_e32 v[36:37], 0
	v_mov_b64_e32 v[38:39], 0
	v_mov_b64_e32 v[40:41], 0
	v_mov_b64_e32 v[42:43], 0
	v_mov_b64_e32 v[44:45], 0
	v_mov_b64_e32 v[50:51], 0
	v_mov_b64_e32 v[52:53], 0
	v_mov_b64_e32 v[58:59], 0
	v_mov_b64_e32 v[60:61], 0
	v_mov_b64_e32 v[66:67], 0
	v_mov_b64_e32 v[68:69], 0
	v_mov_b64_e32 v[74:75], 0
	v_mov_b64_e32 v[76:77], 0
	v_mov_b64_e32 v[82:83], 0
	v_mov_b64_e32 v[84:85], 0
	v_mov_b64_e32 v[46:47], 0
	v_mov_b64_e32 v[48:49], 0
	v_mov_b64_e32 v[54:55], 0
	v_mov_b64_e32 v[56:57], 0
	v_mov_b64_e32 v[62:63], 0
	v_mov_b64_e32 v[64:65], 0
	v_mov_b64_e32 v[70:71], 0
	v_mov_b64_e32 v[72:73], 0
	v_mov_b64_e32 v[78:79], 0
	v_mov_b64_e32 v[80:81], 0
	v_mov_b64_e32 v[86:87], 0
	v_mov_b64_e32 v[88:89], 0
	v_mov_b64_e32 v[90:91], 0
	v_mov_b64_e32 v[92:93], 0
	v_mov_b64_e32 v[94:95], 0
	v_mov_b64_e32 v[96:97], 0
	v_mov_b64_e32 v[98:99], 0
	v_mov_b64_e32 v[100:101], 0
	v_mov_b64_e32 v[102:103], 0
	v_mov_b64_e32 v[104:105], 0
	v_mov_b64_e32 v[106:107], 0
	v_mov_b64_e32 v[108:109], 0
	v_mov_b64_e32 v[114:115], 0
	v_mov_b64_e32 v[116:117], 0
	v_mov_b64_e32 v[122:123], 0
	v_mov_b64_e32 v[124:125], 0
	v_mov_b64_e32 v[130:131], 0
	v_mov_b64_e32 v[132:133], 0
	v_mov_b64_e32 v[138:139], 0
	v_mov_b64_e32 v[140:141], 0
	v_mov_b64_e32 v[148:149], 0
	v_mov_b64_e32 v[150:151], 0
	v_mov_b64_e32 v[110:111], 0
	v_mov_b64_e32 v[112:113], 0
	v_mov_b64_e32 v[118:119], 0
	v_mov_b64_e32 v[120:121], 0
	v_mov_b64_e32 v[126:127], 0
	v_mov_b64_e32 v[128:129], 0
	v_mov_b64_e32 v[134:135], 0
	v_mov_b64_e32 v[136:137], 0
	v_mov_b64_e32 v[142:143], 0
	v_mov_b64_e32 v[144:145], 0
	v_mov_b64_e32 v[152:153], 0
	v_mov_b64_e32 v[154:155], 0
	v_mov_b64_e32 v[156:157], 0
	v_mov_b64_e32 v[158:159], 0
	v_mov_b64_e32 v[160:161], 0
	v_mov_b64_e32 v[162:163], 0
.LBB0_691:
	s_cmp_eq_u32 s73, s0
	s_cselect_b64 vcc, -1, 0
	s_add_i32 s0, s0, 2
	s_and_b64 s[8:9], vcc, exec
	s_cselect_b32 s8, 0, s60
	s_cselect_b32 s1, 0, s61
	s_add_u32 s16, s84, s8
	s_addc_u32 s17, s85, s1
	v_add_u32_e32 v2, 0x10000, v170
	v_add_u32_e32 v6, 0x14000, v170
	s_add_u32 s1, s80, s60
	ds_read_b128 v[26:29], v2
	ds_read_b128 v[30:33], v2 offset:1024
	ds_read_b128 v[18:21], v2 offset:2048
	ds_read_b128 v[22:25], v2 offset:3072
	ds_read_b128 v[10:13], v6
	ds_read_b128 v[14:17], v6 offset:1024
	ds_read_b128 v[2:5], v6 offset:2048
	ds_read_b128 v[6:9], v6 offset:3072
	s_addc_u32 s12, s81, s61
	s_add_u32 s10, s16, 0x80
	s_addc_u32 s11, s17, 0
	s_and_b64 s[8:9], vcc, exec
	s_cselect_b32 s9, s5, s12
	s_cselect_b32 s8, s4, s1
	s_add_u32 s1, s84, s60
	s_addc_u32 s12, s85, s61
	s_add_u32 s96, s1, 0xffffff80
	v_cndmask_b32_e32 v180, v176, v172, vcc
	v_cndmask_b32_e32 v197, v178, v174, vcc
	v_cndmask_b32_e32 v181, v177, v173, vcc
	s_addc_u32 s97, s12, -1
	ds_read_b128 v[198:201], v171
	ds_read_b128 v[202:205], v171 offset:1024
	ds_read_b128 v[206:209], v171 offset:2048
	ds_read_b128 v[210:213], v171 offset:3072
	ds_read_b128 v[214:217], v171 offset:4096
	ds_read_b128 v[218:221], v171 offset:5120
	ds_read_b128 v[222:225], v171 offset:6144
	ds_read_b128 v[226:229], v171 offset:7168
	s_mov_b32 m0, s88
	s_nop 0
	global_load_lds_dwordx4 v178, s[96:97]
	s_add_u32 s14, s8, 0x80
	s_mov_b32 m0, s89
	s_nop 0
	global_load_lds_dwordx4 v179, s[96:97]
	s_waitcnt vmcnt(8)
	s_waitcnt lgkmcnt(0)
	s_addc_u32 s15, s9, 0
	s_barrier
	s_setprio 1
	s_waitcnt lgkmcnt(6)
	v_mfma_scale_f32_16x16x128_f8f6f4 v[160:163], v[26:33], v[198:205], v[160:163], v186, v187 op_sel_hi:[0,0,0]
	v_mfma_scale_f32_16x16x128_f8f6f4 v[156:159], v[18:25], v[198:205], v[156:159], v186, v187 op_sel_hi:[0,0,0]
	s_waitcnt lgkmcnt(4)
	v_mfma_scale_f32_16x16x128_f8f6f4 v[152:155], v[26:33], v[206:213], v[152:155], v186, v187 op_sel_hi:[0,0,0]
	v_mfma_scale_f32_16x16x128_f8f6f4 v[142:145], v[18:25], v[206:213], v[142:145], v186, v187 op_sel_hi:[0,0,0]
	s_waitcnt lgkmcnt(2)
	v_mfma_scale_f32_16x16x128_f8f6f4 v[134:137], v[26:33], v[214:221], v[134:137], v186, v187 op_sel_hi:[0,0,0]
	v_mfma_scale_f32_16x16x128_f8f6f4 v[126:129], v[18:25], v[214:221], v[126:129], v186, v187 op_sel_hi:[0,0,0]
	s_waitcnt lgkmcnt(0)
	v_mfma_scale_f32_16x16x128_f8f6f4 v[118:121], v[26:33], v[222:229], v[118:121], v186, v187 op_sel_hi:[0,0,0]
	v_mfma_scale_f32_16x16x128_f8f6f4 v[110:113], v[18:25], v[222:229], v[110:113], v186, v187 op_sel_hi:[0,0,0]
	s_setprio 0
	s_setprio 1
	v_mfma_scale_f32_16x16x128_f8f6f4 v[148:151], v[10:17], v[198:205], v[148:151], v186, v187 op_sel_hi:[0,0,0]
	v_mfma_scale_f32_16x16x128_f8f6f4 v[138:141], v[2:9], v[198:205], v[138:141], v186, v187 op_sel_hi:[0,0,0]
	v_mfma_scale_f32_16x16x128_f8f6f4 v[130:133], v[10:17], v[206:213], v[130:133], v186, v187 op_sel_hi:[0,0,0]
	v_mfma_scale_f32_16x16x128_f8f6f4 v[122:125], v[2:9], v[206:213], v[122:125], v186, v187 op_sel_hi:[0,0,0]
	v_mfma_scale_f32_16x16x128_f8f6f4 v[114:117], v[10:17], v[214:221], v[114:117], v186, v187 op_sel_hi:[0,0,0]
	v_mfma_scale_f32_16x16x128_f8f6f4 v[106:109], v[2:9], v[214:221], v[106:109], v186, v187 op_sel_hi:[0,0,0]
	v_mfma_scale_f32_16x16x128_f8f6f4 v[102:105], v[10:17], v[222:229], v[102:105], v186, v187 op_sel_hi:[0,0,0]
	v_mfma_scale_f32_16x16x128_f8f6f4 v[98:101], v[2:9], v[222:229], v[98:101], v186, v187 op_sel_hi:[0,0,0]
	s_setprio 0
	s_barrier
; #define PG8_STAGE(bufoff, gbase, v0, v1) do { glds16_s((gbase), (v0), ldsbase + (unsigned)(bufoff)); glds16_s((gbase), (v1), ldsbase + (unsigned)(bufoff) + 8192u); } while (0)
; #define PG8_LDA(dst, b, h) do { _Pragma("unroll") for (int m = 0; m < 4; ++m) _Pragma("unroll") for (int k = 0; k < 2; ++k) dst[m][k] = *(const LAS bf16x8*)(lds + PG8_SA(b, h) + aoff + m * 2048 + k * 1024); } while (0)
; #define PG8_LDB(dst, b, h) do { _Pragma("unroll") for (int n = 0; n < 2; ++n) _Pragma("unroll") for (int k = 0; k < 2; ++k) dst[n][k] = *(const LAS bf16x8*)(lds + PG8_SB(b, h) + boff + n * 2048 + k * 1024); } while (0)
; #define PG8_WAIT_V(n) asm volatile("s_waitcnt vmcnt(" #n ")" ::: "memory")
; #define PG8_WAIT_L(n) asm volatile("s_waitcnt lgkmcnt(" #n ")" ::: "memory")
; #define PG8_BAR __builtin_amdgcn_s_barrier()
; #define PG8_SCHED __builtin_amdgcn_sched_barrier(0)
; __device__ __forceinline__ void glds16_s(const char* gbase, unsigned voff, unsigned lds_dst) { unsigned keep;
;     asm volatile("s_mov_b32 %0, m0\n\ts_mov_b32 m0, %3\n\ts_nop 0\n\tglobal_load_lds_dwordx4 %1, %2\n\ts_mov_b32 m0, %0" : "=&s"(keep) : "v"(voff), "s"(gbase), "s"(lds_dst) : "memory"); }
; template <class Epi, class Sched, bool ALIGN_EPI, bool FP8 = false>
; __device__ __forceinline__ void gemm_phase(LAS unsigned char* lds, const bf16_t* A, const bf16_t* Bt, const int K, const Sched& S, const Epi& E, const int wave_in) {
;     ...
;             PG8_LDA(At, 0, 1); PG8_STAGE(PG8_SB(0, 0), b2, voffB[0], voffB[1]); PG8_STAGE(PG8_SB(0, 1), b2 + hstep, voffB[0], voffB[1]); PG8_STAGE(PG8_SA(0, 0), a2, w00, w01);
;             PG8_WAIT_V(8); PG8_WAIT_L(0); PG8_BAR; PG8_MMA(1, 0, At, B0); PG8_MMA(1, 1, At, B1); PG8_BAR; PG8_SCHED;
;             PG8_LDB(B0, 1, 0); PG8_LDB(B1, 1, 1); PG8_SCHED; PG8_LDA(At, 1, 0); PG8_STAGE(PG8_SA(0, 1), a2, w10, w11);
;             PG8_WAIT_V(8); PG8_WAIT_L(0); PG8_BAR; PG8_MMA(0, 0, At, B0); PG8_MMA(0, 1, At, B1); PG8_BAR; PG8_SCHED;
	ds_read_b128 v[198:201], v171 offset:16384
	ds_read_b128 v[202:205], v171 offset:17408
	ds_read_b128 v[206:209], v171 offset:18432
	ds_read_b128 v[210:213], v171 offset:19456
	ds_read_b128 v[214:217], v171 offset:20480
	ds_read_b128 v[218:221], v171 offset:21504
	ds_read_b128 v[222:225], v171 offset:22528
	ds_read_b128 v[226:229], v171 offset:23552
	s_mov_b32 m0, s49
	s_nop 0
	global_load_lds_dwordx4 v164, s[8:9]
	s_nop 0
	s_mov_b32 m0, s50
	s_nop 0
	global_load_lds_dwordx4 v167, s[8:9]
	s_add_u32 s8, s8, s24
	s_addc_u32 s9, s9, 0
	s_mov_b32 m0, s51
	s_nop 0
	global_load_lds_dwordx4 v164, s[8:9]
	s_nop 0
	s_mov_b32 m0, s52
	s_nop 0
	global_load_lds_dwordx4 v167, s[8:9]
	s_nop 0
	s_mov_b32 m0, s25
	s_nop 0
	global_load_lds_dwordx4 v180, s[16:17]
	s_nop 0
	s_mov_b32 m0, s53
	s_nop 0
	global_load_lds_dwordx4 v181, s[16:17]
	s_waitcnt vmcnt(8)
	s_waitcnt lgkmcnt(0)
	s_barrier
	s_setprio 1
	s_waitcnt lgkmcnt(6)
	v_mfma_scale_f32_16x16x128_f8f6f4 v[94:97], v[26:33], v[198:205], v[94:97], v186, v187 op_sel_hi:[0,0,0]
	v_mfma_scale_f32_16x16x128_f8f6f4 v[90:93], v[18:25], v[198:205], v[90:93], v186, v187 op_sel_hi:[0,0,0]
	s_waitcnt lgkmcnt(4)
	v_mfma_scale_f32_16x16x128_f8f6f4 v[86:89], v[26:33], v[206:213], v[86:89], v186, v187 op_sel_hi:[0,0,0]
	v_mfma_scale_f32_16x16x128_f8f6f4 v[78:81], v[18:25], v[206:213], v[78:81], v186, v187 op_sel_hi:[0,0,0]
	s_waitcnt lgkmcnt(2)
	v_mfma_scale_f32_16x16x128_f8f6f4 v[70:73], v[26:33], v[214:221], v[70:73], v186, v187 op_sel_hi:[0,0,0]
	v_mfma_scale_f32_16x16x128_f8f6f4 v[62:65], v[18:25], v[214:221], v[62:65], v186, v187 op_sel_hi:[0,0,0]
	s_waitcnt lgkmcnt(0)
	v_mfma_scale_f32_16x16x128_f8f6f4 v[54:57], v[26:33], v[222:229], v[54:57], v186, v187 op_sel_hi:[0,0,0]
	v_mfma_scale_f32_16x16x128_f8f6f4 v[46:49], v[18:25], v[222:229], v[46:49], v186, v187 op_sel_hi:[0,0,0]
	s_setprio 0
	s_setprio 1
	v_mfma_scale_f32_16x16x128_f8f6f4 v[82:85], v[10:17], v[198:205], v[82:85], v186, v187 op_sel_hi:[0,0,0]
	v_mfma_scale_f32_16x16x128_f8f6f4 v[74:77], v[2:9], v[198:205], v[74:77], v186, v187 op_sel_hi:[0,0,0]
	v_mfma_scale_f32_16x16x128_f8f6f4 v[66:69], v[10:17], v[206:213], v[66:69], v186, v187 op_sel_hi:[0,0,0]
	v_mfma_scale_f32_16x16x128_f8f6f4 v[58:61], v[2:9], v[206:213], v[58:61], v186, v187 op_sel_hi:[0,0,0]
	v_mfma_scale_f32_16x16x128_f8f6f4 v[50:53], v[10:17], v[214:221], v[50:53], v186, v187 op_sel_hi:[0,0,0]
	v_mfma_scale_f32_16x16x128_f8f6f4 v[42:45], v[2:9], v[214:221], v[42:45], v186, v187 op_sel_hi:[0,0,0]
	v_mfma_scale_f32_16x16x128_f8f6f4 v[38:41], v[10:17], v[222:229], v[38:41], v186, v187 op_sel_hi:[0,0,0]
	v_mfma_scale_f32_16x16x128_f8f6f4 v[34:37], v[2:9], v[222:229], v[34:37], v186, v187 op_sel_hi:[0,0,0]
	s_setprio 0
	s_barrier
	v_add_u32_e32 v14, 0x18000, v170
	v_add_u32_e32 v30, 0x1c000, v170
	ds_read_b128 v[2:5], v14
	ds_read_b128 v[6:9], v14 offset:1024
	ds_read_b128 v[10:13], v14 offset:2048
	ds_read_b128 v[14:17], v14 offset:3072
	ds_read_b128 v[18:21], v30
	ds_read_b128 v[22:25], v30 offset:1024
	ds_read_b128 v[26:29], v30 offset:2048
	ds_read_b128 v[30:33], v30 offset:3072
	ds_read_b128 v[198:201], v171 offset:32768
	ds_read_b128 v[202:205], v171 offset:33792
	ds_read_b128 v[206:209], v171 offset:34816
	ds_read_b128 v[210:213], v171 offset:35840
	ds_read_b128 v[214:217], v171 offset:36864
	ds_read_b128 v[218:221], v171 offset:37888
	ds_read_b128 v[222:225], v171 offset:38912
	ds_read_b128 v[226:229], v171 offset:39936
	s_mov_b32 m0, s54
	s_nop 0
	global_load_lds_dwordx4 v197, s[16:17]
	v_cndmask_b32_e32 v230, v179, v175, vcc
	s_mov_b32 m0, s55
	s_nop 0
	global_load_lds_dwordx4 v230, s[16:17]
	s_waitcnt vmcnt(8)
	s_waitcnt lgkmcnt(0)
	s_barrier
; #define PG8_STAGE(bufoff, gbase, v0, v1) do { glds16_s((gbase), (v0), ldsbase + (unsigned)(bufoff)); glds16_s((gbase), (v1), ldsbase + (unsigned)(bufoff) + 8192u); } while (0)
; #define PG8_LDA(dst, b, h) do { _Pragma("unroll") for (int m = 0; m < 4; ++m) _Pragma("unroll") for (int k = 0; k < 2; ++k) dst[m][k] = *(const LAS bf16x8*)(lds + PG8_SA(b, h) + aoff + m * 2048 + k * 1024); } while (0)
; #define PG8_WAIT_V(n) asm volatile("s_waitcnt vmcnt(" #n ")" ::: "memory")
; #define PG8_WAIT_L(n) asm volatile("s_waitcnt lgkmcnt(" #n ")" ::: "memory")
; #define PG8_BAR __builtin_amdgcn_s_barrier()
; #define PG8_SCHED __builtin_amdgcn_sched_barrier(0)
; __device__ __forceinline__ void glds16_s(const char* gbase, unsigned voff, unsigned lds_dst) { unsigned keep;
;     asm volatile("s_mov_b32 %0, m0\n\ts_mov_b32 m0, %3\n\ts_nop 0\n\tglobal_load_lds_dwordx4 %1, %2\n\ts_mov_b32 m0, %0" : "=&s"(keep) : "v"(voff), "s"(gbase), "s"(lds_dst) : "memory"); }
; template <class Epi, class Sched, bool ALIGN_EPI, bool FP8 = false>
; __device__ __forceinline__ void gemm_phase(LAS unsigned char* lds, const bf16_t* A, const bf16_t* Bt, const int K, const Sched& S, const Epi& E, const int wave_in) {
;     ...
;             PG8_WAIT_V(8); PG8_WAIT_L(0); PG8_BAR; PG8_MMA(0, 0, At, B0); PG8_MMA(0, 1, At, B1); PG8_BAR; PG8_SCHED;
;             PG8_LDA(At, 1, 1); PG8_STAGE(PG8_SB(1, 0), b3, voffB[0], voffB[1]); PG8_STAGE(PG8_SB(1, 1), b3 + hstep, voffB[0], voffB[1]); PG8_STAGE(PG8_SA(1, 0), a3, w00, w01);
;             PG8_WAIT_V(8); PG8_WAIT_L(0); PG8_BAR; PG8_MMA(1, 0, At, B0); PG8_MMA(1, 1, At, B1); PG8_BAR; PG8_SCHED;
;         }
;         if constexpr (FP8) asm volatile("s_nop 15\n\ts_nop 15" ::: "memory");
;         if constexpr (ALIGN_EPI) { if (wr == 0) PG8_BAR; }
	s_setprio 1
	s_waitcnt lgkmcnt(6)
	v_mfma_scale_f32_16x16x128_f8f6f4 v[160:163], v[2:9], v[198:205], v[160:163], v186, v187 op_sel_hi:[0,0,0]
	v_mfma_scale_f32_16x16x128_f8f6f4 v[156:159], v[10:17], v[198:205], v[156:159], v186, v187 op_sel_hi:[0,0,0]
	s_waitcnt lgkmcnt(4)
	v_mfma_scale_f32_16x16x128_f8f6f4 v[152:155], v[2:9], v[206:213], v[152:155], v186, v187 op_sel_hi:[0,0,0]
	v_mfma_scale_f32_16x16x128_f8f6f4 v[142:145], v[10:17], v[206:213], v[142:145], v186, v187 op_sel_hi:[0,0,0]
	s_waitcnt lgkmcnt(2)
	v_mfma_scale_f32_16x16x128_f8f6f4 v[134:137], v[2:9], v[214:221], v[134:137], v186, v187 op_sel_hi:[0,0,0]
	v_mfma_scale_f32_16x16x128_f8f6f4 v[126:129], v[10:17], v[214:221], v[126:129], v186, v187 op_sel_hi:[0,0,0]
	s_waitcnt lgkmcnt(0)
	v_mfma_scale_f32_16x16x128_f8f6f4 v[118:121], v[2:9], v[222:229], v[118:121], v186, v187 op_sel_hi:[0,0,0]
	v_mfma_scale_f32_16x16x128_f8f6f4 v[110:113], v[10:17], v[222:229], v[110:113], v186, v187 op_sel_hi:[0,0,0]
	s_setprio 0
	s_setprio 1
	v_mfma_scale_f32_16x16x128_f8f6f4 v[148:151], v[18:25], v[198:205], v[148:151], v186, v187 op_sel_hi:[0,0,0]
	v_mfma_scale_f32_16x16x128_f8f6f4 v[138:141], v[26:33], v[198:205], v[138:141], v186, v187 op_sel_hi:[0,0,0]
	v_mfma_scale_f32_16x16x128_f8f6f4 v[130:133], v[18:25], v[206:213], v[130:133], v186, v187 op_sel_hi:[0,0,0]
	v_mfma_scale_f32_16x16x128_f8f6f4 v[122:125], v[26:33], v[206:213], v[122:125], v186, v187 op_sel_hi:[0,0,0]
	v_mfma_scale_f32_16x16x128_f8f6f4 v[114:117], v[18:25], v[214:221], v[114:117], v186, v187 op_sel_hi:[0,0,0]
	v_mfma_scale_f32_16x16x128_f8f6f4 v[106:109], v[26:33], v[214:221], v[106:109], v186, v187 op_sel_hi:[0,0,0]
	v_mfma_scale_f32_16x16x128_f8f6f4 v[102:105], v[18:25], v[222:229], v[102:105], v186, v187 op_sel_hi:[0,0,0]
	v_mfma_scale_f32_16x16x128_f8f6f4 v[98:101], v[26:33], v[222:229], v[98:101], v186, v187 op_sel_hi:[0,0,0]
	s_setprio 0
	s_barrier
	ds_read_b128 v[198:201], v171 offset:49152
	ds_read_b128 v[202:205], v171 offset:50176
	ds_read_b128 v[206:209], v171 offset:51200
	ds_read_b128 v[210:213], v171 offset:52224
	ds_read_b128 v[214:217], v171 offset:53248
	ds_read_b128 v[218:221], v171 offset:54272
	ds_read_b128 v[222:225], v171 offset:55296
	ds_read_b128 v[226:229], v171 offset:56320
	s_mov_b32 m0, s59
	s_nop 0
	global_load_lds_dwordx4 v164, s[14:15]
	s_add_u32 s8, s14, s24
	s_mov_b32 m0, s64
	s_nop 0
	global_load_lds_dwordx4 v167, s[14:15]
	s_addc_u32 s9, s15, 0
	s_mov_b32 m0, s67
	s_nop 0
	global_load_lds_dwordx4 v164, s[8:9]
	s_nop 0
	s_mov_b32 m0, s72
	s_nop 0
	global_load_lds_dwordx4 v167, s[8:9]
	s_nop 0
	s_mov_b32 m0, s65
	s_nop 0
	global_load_lds_dwordx4 v180, s[10:11]
	s_nop 0
	s_mov_b32 m0, s66
	s_nop 0
	global_load_lds_dwordx4 v181, s[10:11]
	s_waitcnt vmcnt(8)
	s_waitcnt lgkmcnt(0)
	s_barrier
	s_setprio 1
	s_waitcnt lgkmcnt(6)
	v_mfma_scale_f32_16x16x128_f8f6f4 v[94:97], v[2:9], v[198:205], v[94:97], v186, v187 op_sel_hi:[0,0,0]
	v_mfma_scale_f32_16x16x128_f8f6f4 v[90:93], v[10:17], v[198:205], v[90:93], v186, v187 op_sel_hi:[0,0,0]
	s_waitcnt lgkmcnt(4)
	v_mfma_scale_f32_16x16x128_f8f6f4 v[86:89], v[2:9], v[206:213], v[86:89], v186, v187 op_sel_hi:[0,0,0]
	v_mfma_scale_f32_16x16x128_f8f6f4 v[78:81], v[10:17], v[206:213], v[78:81], v186, v187 op_sel_hi:[0,0,0]
	s_waitcnt lgkmcnt(2)
	v_mfma_scale_f32_16x16x128_f8f6f4 v[70:73], v[2:9], v[214:221], v[70:73], v186, v187 op_sel_hi:[0,0,0]
	v_mfma_scale_f32_16x16x128_f8f6f4 v[62:65], v[10:17], v[214:221], v[62:65], v186, v187 op_sel_hi:[0,0,0]
	s_waitcnt lgkmcnt(0)
	v_mfma_scale_f32_16x16x128_f8f6f4 v[54:57], v[2:9], v[222:229], v[54:57], v186, v187 op_sel_hi:[0,0,0]
	v_mfma_scale_f32_16x16x128_f8f6f4 v[46:49], v[10:17], v[222:229], v[46:49], v186, v187 op_sel_hi:[0,0,0]
	s_setprio 0
	s_setprio 1
	v_mfma_scale_f32_16x16x128_f8f6f4 v[82:85], v[18:25], v[198:205], v[82:85], v186, v187 op_sel_hi:[0,0,0]
	v_mfma_scale_f32_16x16x128_f8f6f4 v[74:77], v[26:33], v[198:205], v[74:77], v186, v187 op_sel_hi:[0,0,0]
	v_mfma_scale_f32_16x16x128_f8f6f4 v[66:69], v[18:25], v[206:213], v[66:69], v186, v187 op_sel_hi:[0,0,0]
	v_mfma_scale_f32_16x16x128_f8f6f4 v[58:61], v[26:33], v[206:213], v[58:61], v186, v187 op_sel_hi:[0,0,0]
	v_mfma_scale_f32_16x16x128_f8f6f4 v[50:53], v[18:25], v[214:221], v[50:53], v186, v187 op_sel_hi:[0,0,0]
	v_mfma_scale_f32_16x16x128_f8f6f4 v[42:45], v[26:33], v[214:221], v[42:45], v186, v187 op_sel_hi:[0,0,0]
	v_mfma_scale_f32_16x16x128_f8f6f4 v[38:41], v[18:25], v[222:229], v[38:41], v186, v187 op_sel_hi:[0,0,0]
	v_mfma_scale_f32_16x16x128_f8f6f4 v[34:37], v[26:33], v[222:229], v[34:37], v186, v187 op_sel_hi:[0,0,0]
	s_setprio 0
	s_barrier
	s_add_u32 s60, s60, 0x100
	s_addc_u32 s61, s61, 0
	s_cmp_ge_u32 s0, s56
	s_cbranch_scc0 .LBB0_691
	s_nop 15
	s_nop 15
	s_and_b64 vcc, exec, s[78:79]
	s_cbranch_vccz .LBB0_694
	s_barrier

; __device__ __forceinline__ int opaque_tid(int wave) { int l; asm volatile("v_mbcnt_lo_u32_b32 %0, -1, 0\n\tv_mbcnt_hi_u32_b32 %0, -1, %0" : "=v"(l)); return wave * 64 + l; }
;     __device__ __forceinline__ bool next(int i, Unit& u) const { u.e = 0; return o.tile(i, u.pm, u.pn); }
;     __device__ __forceinline__ size_t b_off(const Unit& u) const { return (size_t)u.pn * BM * K; }
; #define PG8_BAR __builtin_amdgcn_s_barrier()
; template <class Epi, class Sched, bool ALIGN_EPI, bool FP8 = false>
; __device__ __forceinline__ void gemm_phase(LAS unsigned char* lds, const bf16_t* A, const bf16_t* Bt, const int K, const Sched& S, const Epi& E, const int wave_in) {
;     const int tid = opaque_tid(wave_in); const int wid = __builtin_amdgcn_readfirstlane(tid >> 6), lane = tid & 63, wr = wid >> 2, wc = wid & 3, fr = lane & 15, fq = lane >> 4;
;     const int nt = K / BK;
;     int sR[2], sC[2]; unsigned voffB[2];
; #pragma unroll
;     for (int i = 0; i < 2; ++i) { stage_rc(tid * 16 + i * 8192, sR[i], sC[i]); const int Rb = Epi::PERM ? ((sR[i] & ~31) + perm32(sR[i] & 31)) : sR[i];
;         voffB[i] = (unsigned)(Rb * K + sC[i]) * 2u; }
;     const size_t kstep = (size_t)(BK * 2);
;     const size_t hstep = (size_t)HALF * K * 2;
;     const unsigned ldsw = (unsigned)wid * 1024u;
;     const unsigned ldsbase = (unsigned)__builtin_amdgcn_readfirstlane((int)((unsigned)(uintptr_t)lds + ldsw));
;     const int aoff = lds_byte(wr * 64 + fr, fq * 8), boff = lds_byte(wc * 32 + fr, fq * 8);
;     ...
;     Unit cur, nxt; int ui = 0;
;     if (!S.next(0, cur)) return;
;     f32x4 acc[2][2][4][2];
; #pragma unroll
;     for (int a = 0; a < 2; ++a)
; #pragma unroll
;         for (int b = 0; b < 2; ++b)
; #pragma unroll
;             for (int m = 0; m < 4; ++m)
; #pragma unroll
;                 for (int n = 0; n < 2; ++n) acc[a][b][m][n] = (f32x4){0.f, 0.f, 0.f, 0.f};
;     bf16x8 At[4][2], B0[2][2], B1[2][2];
;     const int sclW = W8_E8M0, sclA = A8_E8M0;
;     unsigned vA[2][2], vN[2][2];
;     PG8_AOFF(vA, cur);
;     const char* const cA = (const char*)A;
;     const char* cB = (const char*)Bt + S.b_off(cur) * 2;
;     PG8_STAGE(PG8_SB(0, 0), cB, voffB[0], voffB[1]); PG8_STAGE(PG8_SB(0, 1), cB + hstep, voffB[0], voffB[1]); PG8_STAGE(PG8_SA(0, 0), cA, vA[0][0], vA[0][1]); PG8_STAGE(PG8_SA(0, 1), cA, vA[1][0], vA[1][1]);
;     if (wr == 1) PG8_BAR;
.LBB0_1039:
	s_or_b64 exec, exec, s[2:3]
	s_mov_b64 s[0:1], s[88:89]
	v_readlane_b32 s2, v232, 0
	s_waitcnt lgkmcnt(0)
	s_barrier
	v_mbcnt_lo_u32_b32 v2, -1, 0
	v_mbcnt_hi_u32_b32 v2, -1, v2
	s_lshl_b32 s76, s28, 3
	v_add_u32_e32 v0, s2, v2
	s_nop 0
	v_readfirstlane_b32 s4, v0
	s_ashr_i32 s5, s4, 6
	s_cmp_ge_i32 s20, s76
	s_cbranch_scc1 .LBB0_1061
	v_ashrrev_i32_e32 v3, 31, v0
	v_lshrrev_b32_e32 v3, 26, v3
	v_lshlrev_b32_e32 v4, 4, v0
	v_add_u32_e32 v3, v0, v3
	v_bfe_i32 v0, v0, 27, 1
	v_lshrrev_b32_e32 v0, 22, v0
	v_add_u32_e32 v0, v4, v0
	v_and_b32_e32 v0, 0xfffffc00, v0
	v_sub_u32_e32 v0, v4, v0
	v_ashrrev_i32_e32 v5, 6, v3
	v_lshrrev_b32_e32 v3, 4, v0
	v_bitop3_b32 v0, v3, v0, 32 bitop3:0x6c
	v_ashrrev_i32_e32 v6, 31, v0
	v_lshrrev_b32_e32 v6, 26, v6
	s_add_u32 s78, s74, 0x1100000
	v_add_u32_e32 v6, v0, v6
	s_addc_u32 s79, s75, 0
	v_ashrrev_i32_e32 v7, 6, v6
	v_and_b32_e32 v6, 0xc0, v6
	s_add_u32 s60, s74, 0x99000000
	v_sub_u32_e32 v0, v0, v6
	s_load_dwordx2 s[2:3], s[0:1], 0xc0
	s_addc_u32 s61, s75, 0
	s_lshl_b64 s[0:1], s[18:19], 21
	v_lshlrev_b32_e32 v3, 3, v5
	v_lshlrev_b32_e32 v5, 5, v5
	v_ashrrev_i16_sdwa v0, v185, sext(v0) dst_sel:DWORD dst_unused:UNUSED_PAD src0_sel:DWORD src1_sel:BYTE_0
	s_add_u32 s0, s74, s0
	v_and_b32_e32 v3, -16, v3
	v_and_b32_e32 v5, 32, v5
	v_bfe_i32 v0, v0, 0, 16
	v_add_u32_e32 v4, 0x2000, v4
	s_addc_u32 s1, s75, s1
	v_add_u32_e32 v3, v7, v3
	v_add_lshl_u32 v0, v5, v0, 1
	v_ashrrev_i32_e32 v5, 31, v4
	s_add_u32 s8, s0, 0x4400000
	v_lshlrev_b32_e32 v6, 1, v3
	v_lshrrev_b32_e32 v8, 2, v3
	v_and_b32_e32 v7, 3, v7
	s_mov_b32 s0, 0x3fffe0
	v_lshrrev_b32_e32 v5, 22, v5
	v_and_b32_e32 v6, 24, v6
	v_and_b32_e32 v8, 4, v8
	v_and_or_b32 v7, v3, s0, v7
	v_add_u32_e32 v5, v4, v5
	v_or3_b32 v6, v7, v8, v6
	v_ashrrev_i32_e32 v5, 10, v5
	v_lshl_add_u32 v147, v6, 10, v0
	v_mul_i32_i24_e32 v6, 0x400, v5
	v_sub_u32_e32 v4, v4, v6
	v_lshrrev_b32_e32 v6, 4, v4
	v_bitop3_b32 v6, v6, v4, 32 bitop3:0x6c
	v_ashrrev_i32_e32 v7, 31, v6
	s_addc_u32 s9, s1, 0
	v_lshrrev_b32_e32 v7, 26, v7
	s_lshl_b32 s1, s5, 10
	s_ashr_i32 s25, s20, 31
	v_lshlrev_b32_e32 v4, 3, v5
	v_add_u32_e32 v7, v6, v7
	s_add_i32 s24, s1, 0
	s_lshr_b32 s1, s25, 29
	v_and_b32_e32 v4, -16, v4
	v_ashrrev_i32_e32 v8, 6, v7
	s_add_i32 s1, s20, s1
	v_add_u32_e32 v4, v8, v4
	v_and_b32_e32 v8, 3, v8
	s_ashr_i32 s6, s1, 3
	s_and_b32 s1, s1, -8
	v_and_or_b32 v8, v4, s0, v8
	s_ashr_i32 s0, s4, 8
	s_sub_i32 s1, s20, s1
	s_add_i32 s29, s28, 1
	s_cmp_lt_i32 s1, 0
	s_cselect_b32 s7, s29, s28
	s_mul_i32 s1, s7, s1
	s_add_i32 s1, s1, s6
	s_ashr_i32 s6, s1, 31
	s_lshr_b32 s6, s6, 26
	s_add_i32 s6, s1, s6
	s_ashr_i32 s7, s6, 6
	v_and_b32_e32 v7, 0xc0, v7
	s_lshl_b32 s7, s7, 3
	v_sub_u32_e32 v6, v6, v7
	s_sub_i32 s10, s28, s7
	v_lshlrev_b32_e32 v5, 5, v5
	v_ashrrev_i16_sdwa v6, v185, sext(v6) dst_sel:DWORD dst_unused:UNUSED_PAD src0_sel:DWORD src1_sel:BYTE_0
	s_min_i32 s10, s10, 8
	v_and_b32_e32 v5, 32, v5
	v_bfe_i32 v6, v6, 0, 16
	s_abs_i32 s12, s10
	v_add_lshl_u32 v164, v5, v6, 1
	v_cvt_f32_u32_e32 v5, s12
	s_sub_i32 s13, 0, s12
	s_andn2_b32 s6, s6, 63
	s_sub_i32 s1, s1, s6
	v_rcp_iflag_f32_e32 v5, v5
	s_abs_i32 s11, s1
	s_xor_b32 s6, s1, s10
	s_ashr_i32 s6, s6, 31
	v_mul_f32_e32 v5, 0x4f7ffffe, v5
	v_cvt_u32_f32_e32 v5, v5
	v_lshlrev_b32_e32 v7, 1, v4
	v_lshrrev_b32_e32 v9, 2, v4
	v_and_b32_e32 v7, 24, v7
	v_readfirstlane_b32 s14, v5
	s_mul_i32 s13, s13, s14
	s_mul_hi_u32 s13, s14, s13
	s_add_i32 s14, s14, s13
	s_mul_hi_u32 s13, s11, s14
	s_mul_i32 s14, s13, s12
	s_sub_i32 s11, s11, s14
	s_add_i32 s14, s13, 1
	s_sub_i32 s15, s11, s12
	s_cmp_ge_u32 s11, s12
	s_cselect_b32 s13, s14, s13
	s_cselect_b32 s11, s15, s11
	s_add_i32 s14, s13, 1
	s_cmp_ge_u32 s11, s12
	s_cselect_b32 s11, s14, s13
	s_xor_b32 s11, s11, s6
	s_sub_i32 s92, s11, s6
	s_mul_i32 s6, s92, s10
	s_sub_i32 s1, s1, s6
	s_add_i32 s73, s7, s1
	s_lshl_b32 s1, s73, 2
	s_add_i32 s1, s1, 0
	s_add_i32 s1, s1, 0x21000
	v_mov_b32_e32 v5, s1
	ds_read_b32 v5, v5
	v_and_b32_e32 v9, 4, v9
	s_lshl_b32 s1, s73, 8
	v_or3_b32 v7, v8, v9, v7
	v_add_u32_e32 v6, s1, v3
	v_lshl_add_u32 v165, v7, 10, v164
	v_ashrrev_i32_e32 v7, 31, v6
	v_lshl_add_u64 v[6:7], v[6:7], 2, s[78:79]
	s_waitcnt lgkmcnt(0)
	v_readfirstlane_b32 s6, v5
	global_load_dword v5, v[6:7], off
	v_add_u32_e32 v6, s1, v4
	v_ashrrev_i32_e32 v7, 31, v6
	v_lshl_add_u64 v[6:7], v[6:7], 2, s[78:79]
	s_bitset1_b32 s1, 7
	s_ashr_i32 s7, s6, 31
	s_ashr_i32 s93, s92, 31
	s_lshl_b64 s[10:11], s[92:93], 18
	s_lshl_b64 s[14:15], s[6:7], 21
	s_waitcnt vmcnt(0)
	v_lshl_add_u32 v177, v5, 10, v0
	global_load_dword v5, v[6:7], off
	v_add_u32_e32 v6, s1, v3
	v_ashrrev_i32_e32 v7, 31, v6
	v_lshl_add_u64 v[6:7], v[6:7], 2, s[78:79]
	s_waitcnt vmcnt(0)
	v_lshl_add_u32 v178, v5, 10, v164
	global_load_dword v5, v[6:7], off
	v_add_u32_e32 v6, s1, v4
	v_ashrrev_i32_e32 v7, 31, v6
	v_lshl_add_u64 v[6:7], v[6:7], 2, s[78:79]
	s_add_u32 s1, s8, s14
	s_addc_u32 s7, s9, s15
	s_add_u32 s10, s1, s10
	s_addc_u32 s11, s7, s11
	s_add_i32 s38, s24, 0x10000
	s_add_i32 s39, s24, 0x12000
	s_add_u32 s14, s10, 0x20000
	s_addc_u32 s15, s11, 0
	s_add_i32 s48, s24, 0x14000
	s_add_i32 s49, s24, 0x16000
	s_add_i32 s50, s24, 0x2000
	s_add_i32 s51, s24, 0x4000
	s_add_i32 s52, s24, 0x6000
	s_cmp_eq_u32 s0, 1
	s_cselect_b64 s[82:83], -1, 0
	s_cmp_lg_u32 s0, 1
	s_waitcnt vmcnt(0)
	v_lshl_add_u32 v179, v5, 10, v0
	global_load_dword v5, v[6:7], off
	s_mov_b32 m0, s38
	s_nop 0
	global_load_lds_dwordx4 v147, s[10:11]
	s_waitcnt vmcnt(0)
	v_lshl_add_u32 v180, v5, 10, v164
	s_mov_b32 m0, s39
	s_nop 0
	global_load_lds_dwordx4 v165, s[10:11]
	s_nop 0
	s_mov_b32 m0, s48
	s_nop 0
	global_load_lds_dwordx4 v147, s[14:15]
	s_nop 0
	s_mov_b32 m0, s49
	s_nop 0
	global_load_lds_dwordx4 v165, s[14:15]
	s_nop 0
	s_mov_b32 m0, s24
	s_nop 0
	global_load_lds_dwordx4 v177, s[60:61]
	s_nop 0
	s_mov_b32 m0, s50
	s_nop 0
	global_load_lds_dwordx4 v178, s[60:61]
	s_nop 0
	s_mov_b32 m0, s51
	s_nop 0
	global_load_lds_dwordx4 v179, s[60:61]
	s_nop 0
	s_mov_b32 m0, s52
	s_nop 0
	global_load_lds_dwordx4 v180, s[60:61]
	s_cbranch_scc1 .LBB0_1042
	s_barrier
;     __device__ __forceinline__ bool next(int i, Unit& u) const { u.e = 0; return o.tile(i, u.pm, u.pn); }
;     __device__ __forceinline__ size_t b_off(const Unit& u) const { return (size_t)u.pn * BM * K; }
;     __device__ __forceinline__ size_t b_off(const Unit& u) const { return ((size_t)u.e * N + (size_t)u.pn * BM) * K; }
; #define PG8_STAGE(bufoff, gbase, v0, v1) do { glds16_s((gbase), (v0), ldsbase + (unsigned)(bufoff)); glds16_s((gbase), (v1), ldsbase + (unsigned)(bufoff) + 8192u); } while (0)
; #define PG8_WAIT_V(n) asm volatile("s_waitcnt vmcnt(" #n ")" ::: "memory")
; #define PG8_BAR __builtin_amdgcn_s_barrier()
; template <class Epi, class Sched, bool ALIGN_EPI, bool FP8 = false>
; __device__ __forceinline__ void gemm_phase(LAS unsigned char* lds, const bf16_t* A, const bf16_t* Bt, const int K, const Sched& S, const Epi& E, const int wave_in) {
;     ...
;     if (wr == 1) PG8_BAR;
;     PG8_WAIT_V(2); PG8_BAR;
;     PG8_STAGE(PG8_SB(1, 0), cB + kstep, voffB[0], voffB[1]); PG8_STAGE(PG8_SA(1, 0), cA + kstep, vA[0][0], vA[0][1]); PG8_STAGE(PG8_SB(1, 1), cB + hstep + kstep, voffB[0], voffB[1]);
;     PG8_WAIT_V(6); PG8_BAR;
;     for (;;) {
;         const bool has_next = S.next(ui + 1, nxt);
;         const char* nB = cB;
;         E.prefetch(cur, (unsigned)__builtin_amdgcn_readfirstlane((int)((unsigned)(uintptr_t)lds + (unsigned)(EPI_LDS_OFF - 0) + (unsigned)((ui & 1) * EPI_LDS_BUF))), wid, lane);
;         if (has_next) { nB = (const char*)Bt + S.b_off(nxt) * 2;
.LBB0_1042:
	s_lshl_b64 s[14:15], s[18:19], 13
	s_add_u32 s84, s2, s14
	v_and_b32_e32 v166, 15, v2
	v_and_b32_e32 v5, 48, v2
	v_lshlrev_b32_e32 v6, 2, v2
	s_addc_u32 s85, s3, s15
	s_lshl_b32 s53, s0, 6
	s_lshl_b32 s0, s0, 13
	v_lshl_or_b32 v5, v166, 6, v5
	v_and_b32_e32 v6, 32, v6
	v_bitop3_b32 v7, v5, s0, v6 bitop3:0xde
	s_lshl_b32 s0, s5, 5
	s_and_b32 s54, s0, 0x60
	s_lshl_b32 s0, s54, 7
	s_add_u32 s86, s74, 0x55800000
	s_addc_u32 s87, s75, 0
	v_bitop3_b32 v5, s0, v5, v6 bitop3:0xf6
	s_add_u32 s0, s10, 0x80
	s_waitcnt vmcnt(2)
	s_barrier
	s_addc_u32 s1, s11, 0
	s_add_i32 s55, s24, 0x18000
	s_mov_b32 m0, s55
	s_nop 0
	global_load_lds_dwordx4 v147, s[0:1]
	s_add_i32 s56, s24, 0x1a000
	s_mov_b32 m0, s56
	s_nop 0
	global_load_lds_dwordx4 v165, s[0:1]
	s_add_u32 s0, s74, 0x99000080
	s_addc_u32 s1, s75, 0
	s_add_i32 s57, s24, 0x8000
	s_mov_b32 m0, s57
	s_nop 0
	global_load_lds_dwordx4 v177, s[0:1]
	s_add_i32 s58, s24, 0xa000
	s_mov_b32 m0, s58
	s_nop 0
	global_load_lds_dwordx4 v178, s[0:1]
	s_add_u32 s0, s10, 0x20080
	s_addc_u32 s1, s11, 0
	s_add_i32 s59, s24, 0x1c000
	s_mov_b32 m0, s59
	s_nop 0
	global_load_lds_dwordx4 v147, s[0:1]
	s_add_i32 s64, s24, 0x1e000
	s_mov_b32 m0, s64
	s_nop 0
	global_load_lds_dwordx4 v165, s[0:1]
	s_cmp_lt_u32 s4, 64
	s_waitcnt vmcnt(6)
	s_cselect_b64 s[88:89], -1, 0
	v_lshlrev_b32_e32 v6, 7, v2
	s_add_i32 s65, s24, 0xc000
	s_add_i32 s66, s24, 0xe000
	v_bfe_u32 v167, v2, 4, 2
	v_and_b32_e32 v6, 0x1000, v6
	v_lshlrev_b32_e32 v2, 4, v2
	s_movk_i32 s0, 0x1f0
	s_cmpk_lt_u32 s4, 0x100
	v_and_or_b32 v168, v2, s0, v6
	s_cselect_b64 s[90:91], -1, 0
	v_lshlrev_b32_e32 v169, 2, v3
	v_lshlrev_b32_e32 v170, 2, v4
	s_ashr_i32 s67, s21, 31
	s_ashr_i32 s77, s76, 31
	s_mov_b32 s2, 0
	v_add_u32_e32 v171, 0, v5
	v_add_u32_e32 v172, 0, v7
	s_barrier
	s_branch .LBB0_1045

;     __device__ __forceinline__ void prefetch(const Unit& u, unsigned lds_dst, int wid, int lane) const {
;         if (wid == 0) { const unsigned off = (unsigned)((u.e * 2048 + (lane >> 5) * 1024 + u.pn * HALF) * 4 + (lane & 31) * 16); glds16_s((const char*)bgu, off, lds_dst); } }
; template <class Epi, class Sched, bool ALIGN_EPI, bool FP8 = false>
; __device__ __forceinline__ void gemm_phase(LAS unsigned char* lds, const bf16_t* A, const bf16_t* Bt, const int K, const Sched& S, const Epi& E, const int wave_in) {
;     ...
;         E.prefetch(cur, (unsigned)__builtin_amdgcn_readfirstlane((int)((unsigned)(uintptr_t)lds + (unsigned)(EPI_LDS_OFF - 0) + (unsigned)((ui & 1) * EPI_LDS_BUF))), wid, lane);
.LBB0_1047:
	s_bitcmp1_b32 s2, 0
	s_cselect_b32 s0, 0xc00, 0
	s_andn2_b64 vcc, exec, s[88:89]
	s_cbranch_vccnz .LBB0_1049
	v_lshl_or_b32 v2, s6, 13, v168
	s_add_i32 s1, s0, 0
	v_lshl_add_u32 v2, s92, 9, v2
	s_add_i32 s1, s1, 0x22200
	s_mov_b32 m0, s1
	s_nop 0
	global_load_lds_dwordx4 v2, s[84:85]

; #define PG8_STAGE(bufoff, gbase, v0, v1) do { glds16_s((gbase), (v0), ldsbase + (unsigned)(bufoff)); glds16_s((gbase), (v1), ldsbase + (unsigned)(bufoff) + 8192u); } while (0)
; #define PG8_LDA(dst, b, h) do { _Pragma("unroll") for (int m = 0; m < 4; ++m) _Pragma("unroll") for (int k = 0; k < 2; ++k) dst[m][k] = *(const LAS bf16x8*)(lds + PG8_SA(b, h) + aoff + m * 2048 + k * 1024); } while (0)
; #define PG8_LDB(dst, b, h) do { _Pragma("unroll") for (int n = 0; n < 2; ++n) _Pragma("unroll") for (int k = 0; k < 2; ++k) dst[n][k] = *(const LAS bf16x8*)(lds + PG8_SB(b, h) + boff + n * 2048 + k * 1024); } while (0)
; #define PG8_WAIT_V(n) asm volatile("s_waitcnt vmcnt(" #n ")" ::: "memory")
; #define PG8_BAR __builtin_amdgcn_s_barrier()
; template <class Epi, class Sched, bool ALIGN_EPI, bool FP8 = false>
; __device__ __forceinline__ void gemm_phase(LAS unsigned char* lds, const bf16_t* A, const bf16_t* Bt, const int K, const Sched& S, const Epi& E, const int wave_in) {
;     ...
;         for (int t = 0; t < nt; t += 2) {
;             const bool last = (t == nt - 2);
;             const char* a1 = cA + (size_t)(t + 1) * kstep;
;             const char* a2 = last ? cA : cA + (size_t)(t + 2) * kstep; const char* b2 = last ? nB : cB + (size_t)(t + 2) * kstep;
;             const char* a3 = a2 + kstep; const char* b3 = b2 + kstep;
;             if constexpr (Sched::ASYNC_ROWS) { if (last && has_next) { asm volatile("" : "+v"(vN[0][0]), "+v"(vN[0][1]), "+v"(vN[1][0]), "+v"(vN[1][1]));
; #pragma unroll
;                 for (int h = 0; h < 2; ++h)
; #pragma unroll
;                     for (int i = 0; i < 2; ++i) vN[h][i] = (vN[h][i] * (unsigned)K + (unsigned)sC[i]) * 2u; } }
;             const unsigned w00 = last ? vN[0][0] : vA[0][0], w01 = last ? vN[0][1] : vA[0][1], w10 = last ? vN[1][0] : vA[1][0], w11 = last ? vN[1][1] : vA[1][1];
;             PG8_LDB(B0, 0, 0); PG8_LDB(B1, 0, 1); PG8_SCHED; PG8_LDA(At, 0, 0); PG8_STAGE(PG8_SA(1, 1), a1, vA[1][0], vA[1][1]);
;             PG8_WAIT_V(8); PG8_WAIT_L(0); PG8_BAR; PG8_MMA(0, 0, At, B0); PG8_MMA(0, 1, At, B1); PG8_BAR; PG8_SCHED;
;     ...
;         for (int a = 0; a < 2; ++a)
; #pragma unroll
;             for (int b = 0; b < 2; ++b)
; #pragma unroll
;                 for (int m = 0; m < 4; ++m)
; #pragma unroll
;                     for (int n = 0; n < 2; ++n) acc[a][b][m][n] = (f32x4){0.f, 0.f, 0.f, 0.f};
.LBB0_1051:
	s_add_u32 s1, s10, 0x100
	v_mov_b32_e32 v34, 0
	s_addc_u32 s27, s11, 0
	s_mov_b32 s95, -2
	s_mov_b64 s[80:81], s[60:61]
	v_mov_b32_e32 v35, 0
	v_mov_b64_e32 v[36:37], 0
	v_mov_b64_e32 v[42:43], 0
	v_mov_b64_e32 v[44:45], 0
	v_mov_b64_e32 v[50:51], 0
	v_mov_b64_e32 v[52:53], 0
	v_mov_b64_e32 v[58:59], 0
	v_mov_b64_e32 v[60:61], 0
	v_mov_b64_e32 v[66:67], 0
	v_mov_b64_e32 v[68:69], 0
	v_mov_b64_e32 v[74:75], 0
	v_mov_b64_e32 v[76:77], 0
	v_mov_b64_e32 v[82:83], 0
	v_mov_b64_e32 v[84:85], 0
	v_mov_b64_e32 v[90:91], 0
	v_mov_b64_e32 v[92:93], 0
	v_mov_b64_e32 v[38:39], 0
	v_mov_b64_e32 v[40:41], 0
	v_mov_b64_e32 v[46:47], 0
	v_mov_b64_e32 v[48:49], 0
	v_mov_b64_e32 v[54:55], 0
	v_mov_b64_e32 v[56:57], 0
	v_mov_b64_e32 v[62:63], 0
	v_mov_b64_e32 v[64:65], 0
	v_mov_b64_e32 v[70:71], 0
	v_mov_b64_e32 v[72:73], 0
	v_mov_b64_e32 v[78:79], 0
	v_mov_b64_e32 v[80:81], 0
	v_mov_b64_e32 v[86:87], 0
	v_mov_b64_e32 v[88:89], 0
	v_mov_b64_e32 v[94:95], 0
	v_mov_b64_e32 v[96:97], 0
	v_mov_b64_e32 v[98:99], 0
	v_mov_b64_e32 v[100:101], 0
	v_mov_b64_e32 v[106:107], 0
	v_mov_b64_e32 v[108:109], 0
	v_mov_b64_e32 v[114:115], 0
	v_mov_b64_e32 v[116:117], 0
	v_mov_b64_e32 v[122:123], 0
	v_mov_b64_e32 v[124:125], 0
	v_mov_b64_e32 v[130:131], 0
	v_mov_b64_e32 v[132:133], 0
	v_mov_b64_e32 v[138:139], 0
	v_mov_b64_e32 v[140:141], 0
	v_mov_b64_e32 v[148:149], 0
	v_mov_b64_e32 v[150:151], 0
	v_mov_b64_e32 v[156:157], 0
	v_mov_b64_e32 v[158:159], 0
	v_mov_b64_e32 v[102:103], 0
	v_mov_b64_e32 v[104:105], 0
	v_mov_b64_e32 v[110:111], 0
	v_mov_b64_e32 v[112:113], 0
	v_mov_b64_e32 v[118:119], 0
	v_mov_b64_e32 v[120:121], 0
	v_mov_b64_e32 v[126:127], 0
	v_mov_b64_e32 v[128:129], 0
	v_mov_b64_e32 v[134:135], 0
	v_mov_b64_e32 v[136:137], 0
	v_mov_b64_e32 v[142:143], 0
	v_mov_b64_e32 v[144:145], 0
	v_mov_b64_e32 v[152:153], 0
	v_mov_b64_e32 v[154:155], 0
	v_mov_b64_e32 v[160:161], 0
	v_mov_b64_e32 v[162:163], 0
	s_branch .LBB0_1053
.LBB0_1052:
	s_add_u32 s12, s80, 0x80
	s_addc_u32 s13, s81, 0
	v_add_u32_e32 v2, 0x10000, v171
	v_add_u32_e32 v6, 0x14000, v171
	s_add_u32 s80, s80, 0x100
	ds_read_b128 v[26:29], v2
	ds_read_b128 v[30:33], v2 offset:1024
	ds_read_b128 v[18:21], v2 offset:2048
	ds_read_b128 v[22:25], v2 offset:3072
	ds_read_b128 v[10:13], v6
	ds_read_b128 v[14:17], v6 offset:1024
	ds_read_b128 v[2:5], v6 offset:2048
	ds_read_b128 v[6:9], v6 offset:3072
	s_addc_u32 s81, s81, 0
	s_and_b64 s[10:11], s[6:7], exec
	s_cselect_b32 s22, s60, s80
	s_cselect_b32 s23, s61, s81
	s_cselect_b32 s17, s97, s27
	s_cselect_b32 s16, s96, s1
	s_add_u32 s10, s22, 0x80
	s_addc_u32 s11, s23, 0
	s_add_u32 s14, s16, 0x80
	s_addc_u32 s15, s17, 0
	v_cndmask_b32_e64 v181, v177, v173, s[6:7]
	v_cndmask_b32_e64 v230, v179, v175, s[6:7]
	v_cndmask_b32_e64 v197, v178, v174, s[6:7]
	ds_read_b128 v[198:201], v172
	ds_read_b128 v[202:205], v172 offset:1024
	ds_read_b128 v[206:209], v172 offset:2048
	ds_read_b128 v[210:213], v172 offset:3072
	ds_read_b128 v[214:217], v172 offset:4096
	ds_read_b128 v[218:221], v172 offset:5120
	ds_read_b128 v[222:225], v172 offset:6144
	ds_read_b128 v[226:229], v172 offset:7168
	s_mov_b32 m0, s65
	s_nop 0
	global_load_lds_dwordx4 v179, s[12:13]
	s_nop 0
	s_mov_b32 m0, s66
	s_nop 0
	global_load_lds_dwordx4 v180, s[12:13]
	s_waitcnt vmcnt(8)
	s_waitcnt lgkmcnt(0)
	s_barrier
	s_setprio 1
	s_waitcnt lgkmcnt(6)
	v_mfma_scale_f32_16x16x128_f8f6f4 v[160:163], v[26:33], v[198:205], v[160:163], v186, v187 op_sel_hi:[0,0,0]
	v_mfma_scale_f32_16x16x128_f8f6f4 v[152:155], v[18:25], v[198:205], v[152:155], v186, v187 op_sel_hi:[0,0,0]
	s_waitcnt lgkmcnt(4)
	v_mfma_scale_f32_16x16x128_f8f6f4 v[142:145], v[26:33], v[206:213], v[142:145], v186, v187 op_sel_hi:[0,0,0]
	v_mfma_scale_f32_16x16x128_f8f6f4 v[134:137], v[18:25], v[206:213], v[134:137], v186, v187 op_sel_hi:[0,0,0]
	s_waitcnt lgkmcnt(2)
	v_mfma_scale_f32_16x16x128_f8f6f4 v[126:129], v[26:33], v[214:221], v[126:129], v186, v187 op_sel_hi:[0,0,0]
	v_mfma_scale_f32_16x16x128_f8f6f4 v[118:121], v[18:25], v[214:221], v[118:121], v186, v187 op_sel_hi:[0,0,0]
	s_waitcnt lgkmcnt(0)
	v_mfma_scale_f32_16x16x128_f8f6f4 v[110:113], v[26:33], v[222:229], v[110:113], v186, v187 op_sel_hi:[0,0,0]
	v_mfma_scale_f32_16x16x128_f8f6f4 v[102:105], v[18:25], v[222:229], v[102:105], v186, v187 op_sel_hi:[0,0,0]
	s_setprio 0
	s_setprio 1
	v_mfma_scale_f32_16x16x128_f8f6f4 v[156:159], v[10:17], v[198:205], v[156:159], v186, v187 op_sel_hi:[0,0,0]
	v_mfma_scale_f32_16x16x128_f8f6f4 v[148:151], v[2:9], v[198:205], v[148:151], v186, v187 op_sel_hi:[0,0,0]
	v_mfma_scale_f32_16x16x128_f8f6f4 v[138:141], v[10:17], v[206:213], v[138:141], v186, v187 op_sel_hi:[0,0,0]
	v_mfma_scale_f32_16x16x128_f8f6f4 v[130:133], v[2:9], v[206:213], v[130:133], v186, v187 op_sel_hi:[0,0,0]
	v_mfma_scale_f32_16x16x128_f8f6f4 v[122:125], v[10:17], v[214:221], v[122:125], v186, v187 op_sel_hi:[0,0,0]
	v_mfma_scale_f32_16x16x128_f8f6f4 v[114:117], v[2:9], v[214:221], v[114:117], v186, v187 op_sel_hi:[0,0,0]
	v_mfma_scale_f32_16x16x128_f8f6f4 v[106:109], v[10:17], v[222:229], v[106:109], v186, v187 op_sel_hi:[0,0,0]
	v_mfma_scale_f32_16x16x128_f8f6f4 v[98:101], v[2:9], v[222:229], v[98:101], v186, v187 op_sel_hi:[0,0,0]
	s_setprio 0
	s_barrier
; #define PG8_STAGE(bufoff, gbase, v0, v1) do { glds16_s((gbase), (v0), ldsbase + (unsigned)(bufoff)); glds16_s((gbase), (v1), ldsbase + (unsigned)(bufoff) + 8192u); } while (0)
; #define PG8_LDA(dst, b, h) do { _Pragma("unroll") for (int m = 0; m < 4; ++m) _Pragma("unroll") for (int k = 0; k < 2; ++k) dst[m][k] = *(const LAS bf16x8*)(lds + PG8_SA(b, h) + aoff + m * 2048 + k * 1024); } while (0)
; #define PG8_LDB(dst, b, h) do { _Pragma("unroll") for (int n = 0; n < 2; ++n) _Pragma("unroll") for (int k = 0; k < 2; ++k) dst[n][k] = *(const LAS bf16x8*)(lds + PG8_SB(b, h) + boff + n * 2048 + k * 1024); } while (0)
; #define PG8_WAIT_V(n) asm volatile("s_waitcnt vmcnt(" #n ")" ::: "memory")
; #define PG8_WAIT_L(n) asm volatile("s_waitcnt lgkmcnt(" #n ")" ::: "memory")
; #define PG8_BAR __builtin_amdgcn_s_barrier()
; #define PG8_SCHED __builtin_amdgcn_sched_barrier(0)
; template <class Epi, class Sched, bool ALIGN_EPI, bool FP8 = false>
; __device__ __forceinline__ void gemm_phase(LAS unsigned char* lds, const bf16_t* A, const bf16_t* Bt, const int K, const Sched& S, const Epi& E, const int wave_in) {
;     ...
;             PG8_LDA(At, 0, 1); PG8_STAGE(PG8_SB(0, 0), b2, voffB[0], voffB[1]); PG8_STAGE(PG8_SB(0, 1), b2 + hstep, voffB[0], voffB[1]); PG8_STAGE(PG8_SA(0, 0), a2, w00, w01);
;             PG8_WAIT_V(8); PG8_WAIT_L(0); PG8_BAR; PG8_MMA(1, 0, At, B0); PG8_MMA(1, 1, At, B1); PG8_BAR; PG8_SCHED;
;             PG8_LDB(B0, 1, 0); PG8_LDB(B1, 1, 1); PG8_SCHED; PG8_LDA(At, 1, 0); PG8_STAGE(PG8_SA(0, 1), a2, w10, w11);
;             PG8_WAIT_V(8); PG8_WAIT_L(0); PG8_BAR; PG8_MMA(0, 0, At, B0); PG8_MMA(0, 1, At, B1); PG8_BAR; PG8_SCHED;
	ds_read_b128 v[198:201], v172 offset:16384
	ds_read_b128 v[202:205], v172 offset:17408
	ds_read_b128 v[206:209], v172 offset:18432
	ds_read_b128 v[210:213], v172 offset:19456
	ds_read_b128 v[214:217], v172 offset:20480
	ds_read_b128 v[218:221], v172 offset:21504
	ds_read_b128 v[222:225], v172 offset:22528
	ds_read_b128 v[226:229], v172 offset:23552
	s_mov_b32 m0, s38
	s_nop 0
	global_load_lds_dwordx4 v147, s[16:17]
	s_nop 0
	s_mov_b32 m0, s39
	s_nop 0
	global_load_lds_dwordx4 v165, s[16:17]
	s_add_u32 s12, s16, 0x20000
	s_addc_u32 s13, s17, 0
	s_mov_b32 m0, s48
	s_nop 0
	global_load_lds_dwordx4 v147, s[12:13]
	s_nop 0
	s_mov_b32 m0, s49
	s_nop 0
	global_load_lds_dwordx4 v165, s[12:13]
	s_mov_b32 m0, s24
	s_nop 0
	global_load_lds_dwordx4 v181, s[22:23]
	s_nop 0
	s_mov_b32 m0, s50
	s_nop 0
	global_load_lds_dwordx4 v197, s[22:23]
	s_waitcnt vmcnt(8)
	s_waitcnt lgkmcnt(0)
	s_barrier
	s_setprio 1
	s_waitcnt lgkmcnt(6)
	v_mfma_scale_f32_16x16x128_f8f6f4 v[94:97], v[26:33], v[198:205], v[94:97], v186, v187 op_sel_hi:[0,0,0]
	v_mfma_scale_f32_16x16x128_f8f6f4 v[86:89], v[18:25], v[198:205], v[86:89], v186, v187 op_sel_hi:[0,0,0]
	s_waitcnt lgkmcnt(4)
	v_mfma_scale_f32_16x16x128_f8f6f4 v[78:81], v[26:33], v[206:213], v[78:81], v186, v187 op_sel_hi:[0,0,0]
	v_mfma_scale_f32_16x16x128_f8f6f4 v[70:73], v[18:25], v[206:213], v[70:73], v186, v187 op_sel_hi:[0,0,0]
	s_waitcnt lgkmcnt(2)
	v_mfma_scale_f32_16x16x128_f8f6f4 v[62:65], v[26:33], v[214:221], v[62:65], v186, v187 op_sel_hi:[0,0,0]
	v_mfma_scale_f32_16x16x128_f8f6f4 v[54:57], v[18:25], v[214:221], v[54:57], v186, v187 op_sel_hi:[0,0,0]
	s_waitcnt lgkmcnt(0)
	v_mfma_scale_f32_16x16x128_f8f6f4 v[46:49], v[26:33], v[222:229], v[46:49], v186, v187 op_sel_hi:[0,0,0]
	v_mfma_scale_f32_16x16x128_f8f6f4 v[38:41], v[18:25], v[222:229], v[38:41], v186, v187 op_sel_hi:[0,0,0]
	s_setprio 0
	s_setprio 1
	v_mfma_scale_f32_16x16x128_f8f6f4 v[90:93], v[10:17], v[198:205], v[90:93], v186, v187 op_sel_hi:[0,0,0]
	v_mfma_scale_f32_16x16x128_f8f6f4 v[82:85], v[2:9], v[198:205], v[82:85], v186, v187 op_sel_hi:[0,0,0]
	v_mfma_scale_f32_16x16x128_f8f6f4 v[74:77], v[10:17], v[206:213], v[74:77], v186, v187 op_sel_hi:[0,0,0]
	v_mfma_scale_f32_16x16x128_f8f6f4 v[66:69], v[2:9], v[206:213], v[66:69], v186, v187 op_sel_hi:[0,0,0]
	v_mfma_scale_f32_16x16x128_f8f6f4 v[58:61], v[10:17], v[214:221], v[58:61], v186, v187 op_sel_hi:[0,0,0]
	v_mfma_scale_f32_16x16x128_f8f6f4 v[50:53], v[2:9], v[214:221], v[50:53], v186, v187 op_sel_hi:[0,0,0]
	v_mfma_scale_f32_16x16x128_f8f6f4 v[42:45], v[10:17], v[222:229], v[42:45], v186, v187 op_sel_hi:[0,0,0]
	v_mfma_scale_f32_16x16x128_f8f6f4 v[34:37], v[2:9], v[222:229], v[34:37], v186, v187 op_sel_hi:[0,0,0]
	s_setprio 0
	s_barrier
	v_add_u32_e32 v14, 0x18000, v171
	v_add_u32_e32 v30, 0x1c000, v171
	ds_read_b128 v[2:5], v14
	ds_read_b128 v[6:9], v14 offset:1024
	ds_read_b128 v[10:13], v14 offset:2048
	ds_read_b128 v[14:17], v14 offset:3072
	ds_read_b128 v[18:21], v30
	ds_read_b128 v[22:25], v30 offset:1024
	ds_read_b128 v[26:29], v30 offset:2048
	ds_read_b128 v[30:33], v30 offset:3072
	ds_read_b128 v[198:201], v172 offset:32768
	ds_read_b128 v[202:205], v172 offset:33792
	ds_read_b128 v[206:209], v172 offset:34816
	ds_read_b128 v[210:213], v172 offset:35840
	ds_read_b128 v[214:217], v172 offset:36864
	ds_read_b128 v[218:221], v172 offset:37888
	ds_read_b128 v[222:225], v172 offset:38912
	ds_read_b128 v[226:229], v172 offset:39936
	v_cndmask_b32_e64 v231, v180, v176, s[6:7]
	s_mov_b32 m0, s51
	s_nop 0
	global_load_lds_dwordx4 v230, s[22:23]
	s_nop 0
	s_mov_b32 m0, s52
	s_nop 0
	global_load_lds_dwordx4 v231, s[22:23]
	s_waitcnt vmcnt(8)
	s_waitcnt lgkmcnt(0)
	s_barrier
; #define PG8_STAGE(bufoff, gbase, v0, v1) do { glds16_s((gbase), (v0), ldsbase + (unsigned)(bufoff)); glds16_s((gbase), (v1), ldsbase + (unsigned)(bufoff) + 8192u); } while (0)
; #define PG8_LDA(dst, b, h) do { _Pragma("unroll") for (int m = 0; m < 4; ++m) _Pragma("unroll") for (int k = 0; k < 2; ++k) dst[m][k] = *(const LAS bf16x8*)(lds + PG8_SA(b, h) + aoff + m * 2048 + k * 1024); } while (0)
; #define PG8_WAIT_V(n) asm volatile("s_waitcnt vmcnt(" #n ")" ::: "memory")
; #define PG8_WAIT_L(n) asm volatile("s_waitcnt lgkmcnt(" #n ")" ::: "memory")
; #define PG8_BAR __builtin_amdgcn_s_barrier()
; #define PG8_SCHED __builtin_amdgcn_sched_barrier(0)
; template <class Epi, class Sched, bool ALIGN_EPI, bool FP8 = false>
; __device__ __forceinline__ void gemm_phase(LAS unsigned char* lds, const bf16_t* A, const bf16_t* Bt, const int K, const Sched& S, const Epi& E, const int wave_in) {
;     ...
;             PG8_WAIT_V(8); PG8_WAIT_L(0); PG8_BAR; PG8_MMA(0, 0, At, B0); PG8_MMA(0, 1, At, B1); PG8_BAR; PG8_SCHED;
;             PG8_LDA(At, 1, 1); PG8_STAGE(PG8_SB(1, 0), b3, voffB[0], voffB[1]); PG8_STAGE(PG8_SB(1, 1), b3 + hstep, voffB[0], voffB[1]); PG8_STAGE(PG8_SA(1, 0), a3, w00, w01);
;             PG8_WAIT_V(8); PG8_WAIT_L(0); PG8_BAR; PG8_MMA(1, 0, At, B0); PG8_MMA(1, 1, At, B1); PG8_BAR; PG8_SCHED;
;         }
	s_setprio 1
	s_waitcnt lgkmcnt(6)
	v_mfma_scale_f32_16x16x128_f8f6f4 v[160:163], v[2:9], v[198:205], v[160:163], v186, v187 op_sel_hi:[0,0,0]
	v_mfma_scale_f32_16x16x128_f8f6f4 v[152:155], v[10:17], v[198:205], v[152:155], v186, v187 op_sel_hi:[0,0,0]
	s_waitcnt lgkmcnt(4)
	v_mfma_scale_f32_16x16x128_f8f6f4 v[142:145], v[2:9], v[206:213], v[142:145], v186, v187 op_sel_hi:[0,0,0]
	v_mfma_scale_f32_16x16x128_f8f6f4 v[134:137], v[10:17], v[206:213], v[134:137], v186, v187 op_sel_hi:[0,0,0]
	s_waitcnt lgkmcnt(2)
	v_mfma_scale_f32_16x16x128_f8f6f4 v[126:129], v[2:9], v[214:221], v[126:129], v186, v187 op_sel_hi:[0,0,0]
	v_mfma_scale_f32_16x16x128_f8f6f4 v[118:121], v[10:17], v[214:221], v[118:121], v186, v187 op_sel_hi:[0,0,0]
	s_waitcnt lgkmcnt(0)
	v_mfma_scale_f32_16x16x128_f8f6f4 v[110:113], v[2:9], v[222:229], v[110:113], v186, v187 op_sel_hi:[0,0,0]
	v_mfma_scale_f32_16x16x128_f8f6f4 v[102:105], v[10:17], v[222:229], v[102:105], v186, v187 op_sel_hi:[0,0,0]
	s_setprio 0
	s_setprio 1
	v_mfma_scale_f32_16x16x128_f8f6f4 v[156:159], v[18:25], v[198:205], v[156:159], v186, v187 op_sel_hi:[0,0,0]
	v_mfma_scale_f32_16x16x128_f8f6f4 v[148:151], v[26:33], v[198:205], v[148:151], v186, v187 op_sel_hi:[0,0,0]
	v_mfma_scale_f32_16x16x128_f8f6f4 v[138:141], v[18:25], v[206:213], v[138:141], v186, v187 op_sel_hi:[0,0,0]
	v_mfma_scale_f32_16x16x128_f8f6f4 v[130:133], v[26:33], v[206:213], v[130:133], v186, v187 op_sel_hi:[0,0,0]
	v_mfma_scale_f32_16x16x128_f8f6f4 v[122:125], v[18:25], v[214:221], v[122:125], v186, v187 op_sel_hi:[0,0,0]
	v_mfma_scale_f32_16x16x128_f8f6f4 v[114:117], v[26:33], v[214:221], v[114:117], v186, v187 op_sel_hi:[0,0,0]
	v_mfma_scale_f32_16x16x128_f8f6f4 v[106:109], v[18:25], v[222:229], v[106:109], v186, v187 op_sel_hi:[0,0,0]
	v_mfma_scale_f32_16x16x128_f8f6f4 v[98:101], v[26:33], v[222:229], v[98:101], v186, v187 op_sel_hi:[0,0,0]
	s_setprio 0
	s_barrier
	ds_read_b128 v[198:201], v172 offset:49152
	ds_read_b128 v[202:205], v172 offset:50176
	ds_read_b128 v[206:209], v172 offset:51200
	ds_read_b128 v[210:213], v172 offset:52224
	ds_read_b128 v[214:217], v172 offset:53248
	ds_read_b128 v[218:221], v172 offset:54272
	ds_read_b128 v[222:225], v172 offset:55296
	ds_read_b128 v[226:229], v172 offset:56320
	s_mov_b32 m0, s55
	s_nop 0
	global_load_lds_dwordx4 v147, s[14:15]
	s_nop 0
	s_mov_b32 m0, s56
	s_nop 0
	global_load_lds_dwordx4 v165, s[14:15]
	s_add_u32 s6, s16, 0x20080
	s_addc_u32 s7, s17, 0
	s_mov_b32 m0, s59
	s_nop 0
	global_load_lds_dwordx4 v147, s[6:7]
	s_nop 0
	s_mov_b32 m0, s64
	s_nop 0
	global_load_lds_dwordx4 v165, s[6:7]
	s_mov_b32 m0, s57
	s_nop 0
	global_load_lds_dwordx4 v181, s[10:11]
	s_nop 0
	s_mov_b32 m0, s58
	s_nop 0
	global_load_lds_dwordx4 v197, s[10:11]
	s_waitcnt vmcnt(8)
	s_waitcnt lgkmcnt(0)
	s_barrier
	s_setprio 1
	s_waitcnt lgkmcnt(6)
	v_mfma_scale_f32_16x16x128_f8f6f4 v[94:97], v[2:9], v[198:205], v[94:97], v186, v187 op_sel_hi:[0,0,0]
	v_mfma_scale_f32_16x16x128_f8f6f4 v[86:89], v[10:17], v[198:205], v[86:89], v186, v187 op_sel_hi:[0,0,0]
	s_waitcnt lgkmcnt(4)
	v_mfma_scale_f32_16x16x128_f8f6f4 v[78:81], v[2:9], v[206:213], v[78:81], v186, v187 op_sel_hi:[0,0,0]
	v_mfma_scale_f32_16x16x128_f8f6f4 v[70:73], v[10:17], v[206:213], v[70:73], v186, v187 op_sel_hi:[0,0,0]
	s_waitcnt lgkmcnt(2)
	v_mfma_scale_f32_16x16x128_f8f6f4 v[62:65], v[2:9], v[214:221], v[62:65], v186, v187 op_sel_hi:[0,0,0]
	v_mfma_scale_f32_16x16x128_f8f6f4 v[54:57], v[10:17], v[214:221], v[54:57], v186, v187 op_sel_hi:[0,0,0]
	s_waitcnt lgkmcnt(0)
	v_mfma_scale_f32_16x16x128_f8f6f4 v[46:49], v[2:9], v[222:229], v[46:49], v186, v187 op_sel_hi:[0,0,0]
	v_mfma_scale_f32_16x16x128_f8f6f4 v[38:41], v[10:17], v[222:229], v[38:41], v186, v187 op_sel_hi:[0,0,0]
	s_setprio 0
	s_setprio 1
	v_mfma_scale_f32_16x16x128_f8f6f4 v[90:93], v[18:25], v[198:205], v[90:93], v186, v187 op_sel_hi:[0,0,0]
	v_mfma_scale_f32_16x16x128_f8f6f4 v[82:85], v[26:33], v[198:205], v[82:85], v186, v187 op_sel_hi:[0,0,0]
	v_mfma_scale_f32_16x16x128_f8f6f4 v[74:77], v[18:25], v[206:213], v[74:77], v186, v187 op_sel_hi:[0,0,0]
	v_mfma_scale_f32_16x16x128_f8f6f4 v[66:69], v[26:33], v[206:213], v[66:69], v186, v187 op_sel_hi:[0,0,0]
	v_mfma_scale_f32_16x16x128_f8f6f4 v[58:61], v[18:25], v[214:221], v[58:61], v186, v187 op_sel_hi:[0,0,0]
	v_mfma_scale_f32_16x16x128_f8f6f4 v[50:53], v[26:33], v[214:221], v[50:53], v186, v187 op_sel_hi:[0,0,0]
	v_mfma_scale_f32_16x16x128_f8f6f4 v[42:45], v[18:25], v[222:229], v[42:45], v186, v187 op_sel_hi:[0,0,0]
	v_mfma_scale_f32_16x16x128_f8f6f4 v[34:37], v[26:33], v[222:229], v[34:37], v186, v187 op_sel_hi:[0,0,0]
	s_setprio 0
	s_barrier
	s_add_i32 s95, s95, 2
	s_add_u32 s1, s1, 0x100
	s_addc_u32 s27, s27, 0
	s_cmp_gt_u32 s95, 5
	s_cbranch_scc1 .LBB0_1055

; __device__ __forceinline__ int opaque_tid(int wave) { int l; asm volatile("v_mbcnt_lo_u32_b32 %0, -1, 0\n\tv_mbcnt_hi_u32_b32 %0, -1, %0" : "=v"(l)); return wave * 64 + l; }
; template <class Epi, class Sched, bool ALIGN_EPI, bool FP8 = false>
; __device__ __forceinline__ void gemm_phase(LAS unsigned char* lds, const bf16_t* A, const bf16_t* Bt, const int K, const Sched& S, const Epi& E, const int wave_in) {
;     const int tid = opaque_tid(wave_in); const int wid = __builtin_amdgcn_readfirstlane(tid >> 6), lane = tid & 63, wr = wid >> 2, wc = wid & 3, fr = lane & 15, fq = lane >> 4;
;     const int nt = K / BK;
;     int sR[2], sC[2]; unsigned voffB[2];
; #pragma unroll
;     for (int i = 0; i < 2; ++i) { stage_rc(tid * 16 + i * 8192, sR[i], sC[i]); const int Rb = Epi::PERM ? ((sR[i] & ~31) + perm32(sR[i] & 31)) : sR[i];
;         voffB[i] = (unsigned)(Rb * K + sC[i]) * 2u; }
;     const size_t kstep = (size_t)(BK * 2);
;     const size_t hstep = (size_t)HALF * K * 2;
;     const unsigned ldsw = (unsigned)wid * 1024u;
;     const unsigned ldsbase = (unsigned)__builtin_amdgcn_readfirstlane((int)((unsigned)(uintptr_t)lds + ldsw));
;     const int aoff = lds_byte(wr * 64 + fr, fq * 8), boff = lds_byte(wc * 32 + fr, fq * 8);
;     ...
;     Unit cur, nxt; int ui = 0;
;     if (!S.next(0, cur)) return;
;     f32x4 acc[2][2][4][2];
; #pragma unroll
;     for (int a = 0; a < 2; ++a)
; #pragma unroll
;         for (int b = 0; b < 2; ++b)
; #pragma unroll
;             for (int m = 0; m < 4; ++m)
; #pragma unroll
;                 for (int n = 0; n < 2; ++n) acc[a][b][m][n] = (f32x4){0.f, 0.f, 0.f, 0.f};
;     bf16x8 At[4][2], B0[2][2], B1[2][2];
;     const int sclW = W8_E8M0, sclA = A8_E8M0;
;     unsigned vA[2][2], vN[2][2];
;     PG8_AOFF(vA, cur);
;     const char* const cA = (const char*)A;
;     const char* cB = (const char*)Bt + S.b_off(cur) * 2;
;     PG8_STAGE(PG8_SB(0, 0), cB, voffB[0], voffB[1]); PG8_STAGE(PG8_SB(0, 1), cB + hstep, voffB[0], voffB[1]); PG8_STAGE(PG8_SA(0, 0), cA, vA[0][0], vA[0][1]); PG8_STAGE(PG8_SA(0, 1), cA, vA[1][0], vA[1][1]);
;     if (wr == 1) PG8_BAR;
;     PG8_WAIT_V(2); PG8_BAR;
;     PG8_STAGE(PG8_SB(1, 0), cB + kstep, voffB[0], voffB[1]); PG8_STAGE(PG8_SA(1, 0), cA + kstep, vA[0][0], vA[0][1]); PG8_STAGE(PG8_SB(1, 1), cB + hstep + kstep, voffB[0], voffB[1]);
;     PG8_WAIT_V(6); PG8_BAR;
.LBB0_1118:
	v_ashrrev_i32_e32 v4, 31, v0
	v_lshrrev_b32_e32 v4, 26, v4
	v_lshlrev_b32_e32 v3, 4, v0
	v_add_u32_e32 v4, v0, v4
	v_bfe_i32 v0, v0, 27, 1
	v_lshrrev_b32_e32 v0, 22, v0
	v_add_u32_e32 v0, v3, v0
	v_and_b32_e32 v0, 0xfffffc00, v0
	v_sub_u32_e32 v0, v3, v0
	v_lshrrev_b32_e32 v5, 4, v0
	v_bitop3_b32 v0, v5, v0, 32 bitop3:0x6c
	v_ashrrev_i32_e32 v6, 31, v0
	s_add_u32 s76, s74, 0x55800000
	v_ashrrev_i32_e32 v4, 6, v4
	v_lshrrev_b32_e32 v6, 26, v6
	s_addc_u32 s77, s75, 0
	s_lshl_b64 s[2:3], s[18:19], 20
	v_lshlrev_b32_e32 v5, 3, v4
	v_add_u32_e32 v6, v0, v6
	s_add_u32 s0, s74, s2
	v_and_b32_e32 v5, -16, v5
	v_ashrrev_i32_e32 v7, 6, v6
	v_and_b32_e32 v6, 0xc0, v6
	s_addc_u32 s2, s75, s3
	v_add_u32_e32 v5, v7, v5
	v_sub_u32_e32 v0, v0, v6
	s_add_u32 s29, s0, 0x24400000
	v_lshlrev_b32_e32 v4, 5, v4
	v_ashrrev_i16_sdwa v0, v185, sext(v0) dst_sel:DWORD dst_unused:UNUSED_PAD src0_sel:DWORD src1_sel:BYTE_0
	v_lshlrev_b32_e32 v6, 1, v5
	v_lshrrev_b32_e32 v8, 2, v5
	v_and_b32_e32 v7, 3, v7
	s_mov_b32 s0, 0x3fffe0
	v_and_b32_e32 v4, 32, v4
	v_bfe_i32 v0, v0, 0, 16
	v_and_b32_e32 v6, 24, v6
	v_and_b32_e32 v8, 4, v8
	v_and_or_b32 v7, v5, s0, v7
	v_or3_b32 v6, v7, v8, v6
	v_add_lshl_u32 v4, v4, v0, 1
	v_add_u32_e32 v3, 0x2000, v3
	v_lshl_add_u32 v0, v6, 10, v4
	v_ashrrev_i32_e32 v6, 31, v3
	v_lshrrev_b32_e32 v6, 22, v6
	v_add_u32_e32 v6, v3, v6
	v_ashrrev_i32_e32 v6, 10, v6
	v_mul_i32_i24_e32 v7, 0x400, v6
	v_sub_u32_e32 v3, v3, v7
	s_addc_u32 s38, s2, 0
	v_lshrrev_b32_e32 v7, 4, v3
	s_lshl_b32 s2, s20, 10
	s_add_i32 s1, s10, s1
	v_bitop3_b32 v3, v7, v3, 32 bitop3:0x6c
	s_add_i32 s39, s2, 0
	s_ashr_i32 s2, s1, 31
	v_ashrrev_i32_e32 v8, 31, v3
	s_lshr_b32 s2, s2, 27
	v_lshrrev_b32_e32 v8, 26, v8
	s_add_i32 s2, s1, s2
	v_add_u32_e32 v8, v3, v8
	s_ashr_i32 s3, s2, 5
	v_ashrrev_i32_e32 v9, 6, v8
	v_and_b32_e32 v8, 0xc0, v8
	s_lshl_b32 s3, s3, 3
	v_sub_u32_e32 v3, v3, v8
	s_sub_i32 s10, s28, s3
	v_lshlrev_b32_e32 v7, 3, v6
	v_lshlrev_b32_e32 v6, 5, v6
	v_ashrrev_i16_sdwa v3, v185, sext(v3) dst_sel:DWORD dst_unused:UNUSED_PAD src0_sel:DWORD src1_sel:BYTE_0
	s_min_i32 s10, s10, 8
	v_and_b32_e32 v6, 32, v6
	v_bfe_i32 v3, v3, 0, 16
	s_abs_i32 s12, s10
	v_add_lshl_u32 v3, v6, v3, 1
	v_cvt_f32_u32_e32 v6, s12
	s_sub_i32 s13, 0, s12
	s_andn2_b32 s2, s2, 31
	s_sub_i32 s1, s1, s2
	v_rcp_iflag_f32_e32 v6, v6
	s_abs_i32 s11, s1
	v_and_b32_e32 v7, -16, v7
	v_add_u32_e32 v7, v9, v7
	v_mul_f32_e32 v6, 0x4f7ffffe, v6
	v_cvt_u32_f32_e32 v6, v6
	v_and_b32_e32 v9, 3, v9
	s_xor_b32 s2, s1, s10
	v_and_or_b32 v9, v7, s0, v9
	v_readfirstlane_b32 s15, v6
	s_mul_i32 s13, s13, s15
	s_mul_hi_u32 s13, s15, s13
	s_add_i32 s15, s15, s13
	s_mul_hi_u32 s13, s11, s15
	s_mul_i32 s15, s13, s12
	s_sub_i32 s11, s11, s15
	s_ashr_i32 s0, s14, 8
	s_ashr_i32 s2, s2, 31
	s_add_i32 s15, s13, 1
	s_sub_i32 s16, s11, s12
	s_cmp_ge_u32 s11, s12
	s_cselect_b32 s13, s15, s13
	s_cselect_b32 s11, s16, s11
	s_add_i32 s15, s13, 1
	s_cmp_ge_u32 s11, s12
	s_cselect_b32 s11, s15, s13
	s_xor_b32 s11, s11, s2
	s_sub_i32 s26, s11, s2
	s_mul_i32 s2, s26, s10
	s_sub_i32 s1, s1, s2
	s_add_i32 s94, s3, s1
	s_lshl_b32 s1, s94, 2
	s_add_i32 s1, s1, 0
	s_add_i32 s1, s1, 0x21000
	v_mov_b32_e32 v6, s1
	ds_read_b32 v6, v6
	s_lshl_b32 s1, s94, 18
	v_lshl_add_u32 v164, v5, 10, v4
	v_lshl_add_u32 v165, v7, 10, v3
	s_ashr_i32 s27, s26, 31
	s_waitcnt lgkmcnt(0)
	v_readfirstlane_b32 s2, v6
	s_ashr_i32 s3, s2, 31
	v_add_u32_e32 v175, s1, v164
	v_add_u32_e32 v176, s1, v165
	s_bitset1_b32 s1, 17
	s_lshl_b64 s[10:11], s[26:27], 18
	s_lshl_b64 s[12:13], s[2:3], 20
	v_add_u32_e32 v178, s1, v164
	v_add_u32_e32 v177, s1, v165
	s_add_u32 s1, s29, s12
	v_lshlrev_b32_e32 v8, 1, v7
	v_lshrrev_b32_e32 v10, 2, v7
	s_addc_u32 s3, s38, s13
	v_and_b32_e32 v8, 24, v8
	v_and_b32_e32 v10, 4, v10
	s_add_u32 s10, s1, s10
	v_or3_b32 v8, v9, v10, v8
	s_addc_u32 s11, s3, s11
	s_add_i32 s27, s39, 0x10000
	s_mov_b32 m0, s27
	s_nop 0
	global_load_lds_dwordx4 v0, s[10:11]
	s_add_i32 s48, s39, 0x12000
	v_lshl_add_u32 v147, v8, 10, v3
	s_mov_b32 m0, s48
	s_nop 0
	global_load_lds_dwordx4 v147, s[10:11]
	s_add_u32 s12, s10, 0x20000
	s_addc_u32 s13, s11, 0
	s_add_i32 s49, s39, 0x14000
	s_mov_b32 m0, s49
	s_nop 0
	global_load_lds_dwordx4 v0, s[12:13]
	s_add_i32 s50, s39, 0x16000
	s_mov_b32 m0, s50
	s_nop 0
	global_load_lds_dwordx4 v147, s[12:13]
	s_add_i32 s51, s39, 0x2000
	s_mov_b32 m0, s39
	s_nop 0
	global_load_lds_dwordx4 v175, s[76:77]
	s_add_i32 s52, s39, 0x4000
	s_mov_b32 m0, s51
	s_nop 0
	global_load_lds_dwordx4 v176, s[76:77]
	s_add_i32 s53, s39, 0x6000
	s_mov_b32 m0, s52
	s_nop 0
	global_load_lds_dwordx4 v178, s[76:77]
	s_cmp_eq_u32 s0, 1
	s_mov_b32 m0, s53
	s_nop 0
	global_load_lds_dwordx4 v177, s[76:77]
	s_cselect_b64 s[78:79], -1, 0
	s_cmp_lg_u32 s0, 1
	s_cbranch_scc1 .LBB0_1120
	s_barrier
.LBB0_1120:
	s_add_u32 s80, s74, 0x67800000
	s_addc_u32 s81, s75, 0
	s_lshl_b64 s[12:13], s[18:19], 12
	s_add_u32 s82, s4, s12
	s_addc_u32 s83, s5, s13
	s_add_u32 s84, s74, 0x1300000
	v_and_b32_e32 v3, 63, v2
	v_and_b32_e32 v166, 15, v2
	v_bfe_u32 v167, v2, 4, 2
	v_and_b32_e32 v4, 48, v2
	v_lshlrev_b32_e32 v2, 2, v2
	s_addc_u32 s85, s75, 0
	s_lshl_b32 s18, s0, 6
	s_lshl_b32 s0, s0, 13
	v_lshl_or_b32 v4, v166, 6, v4
	v_and_b32_e32 v2, 32, v2
	v_bitop3_b32 v5, v4, s0, v2 bitop3:0xde
	s_lshl_b32 s0, s20, 5
	s_and_b32 s54, s0, 0x60
	s_lshl_b32 s0, s54, 7
	v_bitop3_b32 v2, s0, v4, v2 bitop3:0xf6
	s_add_u32 s0, s10, 0x80
	s_waitcnt vmcnt(2)
	s_barrier
	s_addc_u32 s1, s11, 0
	s_add_i32 s55, s39, 0x18000
	s_mov_b32 m0, s55
	s_nop 0
	global_load_lds_dwordx4 v0, s[0:1]
	s_add_i32 s56, s39, 0x1a000
	s_mov_b32 m0, s56
	s_nop 0
	global_load_lds_dwordx4 v147, s[0:1]
	s_add_u32 s0, s76, 0x80
	s_addc_u32 s1, s77, 0
	s_add_i32 s57, s39, 0x8000
	s_mov_b32 m0, s57
	s_nop 0
	global_load_lds_dwordx4 v175, s[0:1]
	s_add_i32 s58, s39, 0xa000
	s_mov_b32 m0, s58
	s_nop 0
	global_load_lds_dwordx4 v176, s[0:1]
	s_add_u32 s0, s10, 0x20080
	s_addc_u32 s1, s11, 0
	s_add_i32 s59, s39, 0x1c000
	s_mov_b32 m0, s59
	s_nop 0
	global_load_lds_dwordx4 v0, s[0:1]
	s_add_i32 s64, s39, 0x1e000
	s_mov_b32 m0, s64
	s_nop 0
	global_load_lds_dwordx4 v147, s[0:1]
	s_waitcnt vmcnt(6)
	s_add_i32 s65, s39, 0xc000
	s_add_i32 s66, s39, 0xe000
	s_cmpk_lt_u32 s14, 0x100
	v_lshlrev_b32_e32 v168, 4, v3
	s_cselect_b64 s[86:87], -1, 0
	s_ashr_i32 s67, s8, 31
	s_mov_b32 s3, 0
	v_add_u32_e32 v169, 0, v2
	v_add_u32_e32 v170, 0, v5
	s_barrier
	s_waitcnt vmcnt(0)
	s_branch .LBB0_1123

;     __device__ __forceinline__ void prefetch(const Unit& u, unsigned lds_dst, int wid, int lane) const {
;         if (wid == 0) glds16_s((const char*)bdn, (unsigned)((u.e * 1024 + u.pn * BM) * 4 + lane * 16), lds_dst);
;         else if (wid == 2) glds16_s((const char*)slot_gate, (unsigned)(u.pm * BM * 4 + lane * 16), lds_dst + 2048u); }
; template <class Epi, class Sched, bool ALIGN_EPI, bool FP8 = false>
; __device__ __forceinline__ void gemm_phase(LAS unsigned char* lds, const bf16_t* A, const bf16_t* Bt, const int K, const Sched& S, const Epi& E, const int wave_in) {
;     ...
;         E.prefetch(cur, (unsigned)__builtin_amdgcn_readfirstlane((int)((unsigned)(uintptr_t)lds + (unsigned)(EPI_LDS_OFF - 0) + (unsigned)((ui & 1) * EPI_LDS_BUF))), wid, lane);
.LBB0_1129:
	s_bitcmp1_b32 s3, 0
	s_cselect_b32 s95, 0xc00, 0
	s_cmp_lt_i32 s20, 2
	s_mov_b64 s[0:1], -1
	s_cbranch_scc1 .LBB0_1133
	s_cmp_eq_u32 s20, 2
	s_cbranch_scc0 .LBB0_1132
	s_add_i32 s0, s95, 0
	v_lshl_or_b32 v2, s94, 10, v168
	s_add_i32 s0, s0, 0x22a00
	s_mov_b32 m0, s0
	s_nop 0
	global_load_lds_dwordx4 v2, s[84:85]

;     __device__ __forceinline__ void prefetch(const Unit& u, unsigned lds_dst, int wid, int lane) const {
;         if (wid == 0) glds16_s((const char*)bdn, (unsigned)((u.e * 1024 + u.pn * BM) * 4 + lane * 16), lds_dst);
;         else if (wid == 2) glds16_s((const char*)slot_gate, (unsigned)(u.pm * BM * 4 + lane * 16), lds_dst + 2048u); }
; template <class Epi, class Sched, bool ALIGN_EPI, bool FP8 = false>
; __device__ __forceinline__ void gemm_phase(LAS unsigned char* lds, const bf16_t* A, const bf16_t* Bt, const int K, const Sched& S, const Epi& E, const int wave_in) {
;     ...
;         E.prefetch(cur, (unsigned)__builtin_amdgcn_readfirstlane((int)((unsigned)(uintptr_t)lds + (unsigned)(EPI_LDS_OFF - 0) + (unsigned)((ui & 1) * EPI_LDS_BUF))), wid, lane);
.LBB0_1133:
	s_andn2_b64 vcc, exec, s[0:1]
	s_cbranch_vccnz .LBB0_1136
	s_cmp_lg_u32 s20, 0
	s_cbranch_scc1 .LBB0_1136
	s_lshl_b32 s1, s26, 10
	s_lshl_b32 s2, s2, 12
	s_add_i32 s0, s95, 0
	s_add_i32 s1, s1, s2
	s_add_i32 s0, s0, 0x22200
	v_or_b32_e32 v2, s1, v168
	s_mov_b32 m0, s0
	s_nop 0
	global_load_lds_dwordx4 v2, s[82:83]

; #define PG8_STAGE(bufoff, gbase, v0, v1) do { glds16_s((gbase), (v0), ldsbase + (unsigned)(bufoff)); glds16_s((gbase), (v1), ldsbase + (unsigned)(bufoff) + 8192u); } while (0)
; #define PG8_LDA(dst, b, h) do { _Pragma("unroll") for (int m = 0; m < 4; ++m) _Pragma("unroll") for (int k = 0; k < 2; ++k) dst[m][k] = *(const LAS bf16x8*)(lds + PG8_SA(b, h) + aoff + m * 2048 + k * 1024); } while (0)
; #define PG8_LDB(dst, b, h) do { _Pragma("unroll") for (int n = 0; n < 2; ++n) _Pragma("unroll") for (int k = 0; k < 2; ++k) dst[n][k] = *(const LAS bf16x8*)(lds + PG8_SB(b, h) + boff + n * 2048 + k * 1024); } while (0)
; #define PG8_WAIT_V(n) asm volatile("s_waitcnt vmcnt(" #n ")" ::: "memory")
; #define PG8_BAR __builtin_amdgcn_s_barrier()
; template <class Epi, class Sched, bool ALIGN_EPI, bool FP8 = false>
; __device__ __forceinline__ void gemm_phase(LAS unsigned char* lds, const bf16_t* A, const bf16_t* Bt, const int K, const Sched& S, const Epi& E, const int wave_in) {
;     ...
;         for (int t = 0; t < nt; t += 2) {
;             const bool last = (t == nt - 2);
;             const char* a1 = cA + (size_t)(t + 1) * kstep;
;             const char* a2 = last ? cA : cA + (size_t)(t + 2) * kstep; const char* b2 = last ? nB : cB + (size_t)(t + 2) * kstep;
;             const char* a3 = a2 + kstep; const char* b3 = b2 + kstep;
;             if constexpr (Sched::ASYNC_ROWS) { if (last && has_next) { asm volatile("" : "+v"(vN[0][0]), "+v"(vN[0][1]), "+v"(vN[1][0]), "+v"(vN[1][1]));
; #pragma unroll
;                 for (int h = 0; h < 2; ++h)
; #pragma unroll
;                     for (int i = 0; i < 2; ++i) vN[h][i] = (vN[h][i] * (unsigned)K + (unsigned)sC[i]) * 2u; } }
;             const unsigned w00 = last ? vN[0][0] : vA[0][0], w01 = last ? vN[0][1] : vA[0][1], w10 = last ? vN[1][0] : vA[1][0], w11 = last ? vN[1][1] : vA[1][1];
;             PG8_LDB(B0, 0, 0); PG8_LDB(B1, 0, 1); PG8_SCHED; PG8_LDA(At, 0, 0); PG8_STAGE(PG8_SA(1, 1), a1, vA[1][0], vA[1][1]);
;             PG8_WAIT_V(8); PG8_WAIT_L(0); PG8_BAR; PG8_MMA(0, 0, At, B0); PG8_MMA(0, 1, At, B1); PG8_BAR; PG8_SCHED;
;     ...
;         for (int a = 0; a < 2; ++a)
; #pragma unroll
;             for (int b = 0; b < 2; ++b)
; #pragma unroll
;                 for (int m = 0; m < 4; ++m)
; #pragma unroll
;                     for (int n = 0; n < 2; ++n) acc[a][b][m][n] = (f32x4){0.f, 0.f, 0.f, 0.f};
.LBB0_1138:
	s_add_u32 s0, s10, 0x100
	v_mov_b32_e32 v34, 0
	s_addc_u32 s1, s11, 0
	s_mov_b32 s89, -2
	s_mov_b64 s[14:15], s[76:77]
	v_mov_b32_e32 v35, 0
	v_mov_b64_e32 v[36:37], 0
	v_mov_b64_e32 v[38:39], 0
	v_mov_b64_e32 v[40:41], 0
	v_mov_b64_e32 v[50:51], 0
	v_mov_b64_e32 v[52:53], 0
	v_mov_b64_e32 v[54:55], 0
	v_mov_b64_e32 v[56:57], 0
	v_mov_b64_e32 v[66:67], 0
	v_mov_b64_e32 v[68:69], 0
	v_mov_b64_e32 v[70:71], 0
	v_mov_b64_e32 v[72:73], 0
	v_mov_b64_e32 v[82:83], 0
	v_mov_b64_e32 v[84:85], 0
	v_mov_b64_e32 v[86:87], 0
	v_mov_b64_e32 v[88:89], 0
	v_mov_b64_e32 v[42:43], 0
	v_mov_b64_e32 v[44:45], 0
	v_mov_b64_e32 v[46:47], 0
	v_mov_b64_e32 v[48:49], 0
	v_mov_b64_e32 v[58:59], 0
	v_mov_b64_e32 v[60:61], 0
	v_mov_b64_e32 v[62:63], 0
	v_mov_b64_e32 v[64:65], 0
	v_mov_b64_e32 v[74:75], 0
	v_mov_b64_e32 v[76:77], 0
	v_mov_b64_e32 v[78:79], 0
	v_mov_b64_e32 v[80:81], 0
	v_mov_b64_e32 v[90:91], 0
	v_mov_b64_e32 v[92:93], 0
	v_mov_b64_e32 v[94:95], 0
	v_mov_b64_e32 v[96:97], 0
	v_mov_b64_e32 v[98:99], 0
	v_mov_b64_e32 v[100:101], 0
	v_mov_b64_e32 v[102:103], 0
	v_mov_b64_e32 v[104:105], 0
	v_mov_b64_e32 v[114:115], 0
	v_mov_b64_e32 v[116:117], 0
	v_mov_b64_e32 v[118:119], 0
	v_mov_b64_e32 v[120:121], 0
	v_mov_b64_e32 v[130:131], 0
	v_mov_b64_e32 v[132:133], 0
	v_mov_b64_e32 v[134:135], 0
	v_mov_b64_e32 v[136:137], 0
	v_mov_b64_e32 v[148:149], 0
	v_mov_b64_e32 v[150:151], 0
	v_mov_b64_e32 v[152:153], 0
	v_mov_b64_e32 v[154:155], 0
	v_mov_b64_e32 v[106:107], 0
	v_mov_b64_e32 v[108:109], 0
	v_mov_b64_e32 v[110:111], 0
	v_mov_b64_e32 v[112:113], 0
	v_mov_b64_e32 v[122:123], 0
	v_mov_b64_e32 v[124:125], 0
	v_mov_b64_e32 v[126:127], 0
	v_mov_b64_e32 v[128:129], 0
	v_mov_b64_e32 v[138:139], 0
	v_mov_b64_e32 v[140:141], 0
	v_mov_b64_e32 v[142:143], 0
	v_mov_b64_e32 v[144:145], 0
	v_mov_b64_e32 v[156:157], 0
	v_mov_b64_e32 v[158:159], 0
	v_mov_b64_e32 v[160:161], 0
	v_mov_b64_e32 v[162:163], 0
.LBB0_1139:
	s_add_u32 s60, s14, 0x100
	s_addc_u32 s61, s15, 0
	v_add_u32_e32 v2, 0x10000, v169
	v_add_u32_e32 v6, 0x14000, v169
	s_cmp_eq_u32 s89, 4
	ds_read_b128 v[26:29], v2
	ds_read_b128 v[30:33], v2 offset:1024
	ds_read_b128 v[18:21], v2 offset:2048
	ds_read_b128 v[22:25], v2 offset:3072
	ds_read_b128 v[10:13], v6
	ds_read_b128 v[14:17], v6 offset:1024
	ds_read_b128 v[2:5], v6 offset:2048
	ds_read_b128 v[6:9], v6 offset:3072
	s_cselect_b64 vcc, -1, 0
	s_and_b64 s[10:11], vcc, exec
	s_cselect_b32 s92, s76, s60
	s_cselect_b32 s93, s77, s61
	s_cselect_b32 s16, s4, s0
	s_cselect_b32 s17, s5, s1
	s_add_u32 s10, s92, 0x80
	s_addc_u32 s11, s93, 0
	s_add_u32 s12, s14, 0x80
	v_cndmask_b32_e32 v179, v175, v171, vcc
	v_cndmask_b32_e32 v181, v178, v173, vcc
	s_addc_u32 s13, s15, 0
	v_cndmask_b32_e32 v180, v176, v172, vcc
	ds_read_b128 v[198:201], v170
	ds_read_b128 v[202:205], v170 offset:1024
	ds_read_b128 v[206:209], v170 offset:2048
	ds_read_b128 v[210:213], v170 offset:3072
	ds_read_b128 v[214:217], v170 offset:4096
	ds_read_b128 v[218:221], v170 offset:5120
	ds_read_b128 v[222:225], v170 offset:6144
	ds_read_b128 v[226:229], v170 offset:7168
	s_mov_b32 m0, s65
	s_nop 0
	global_load_lds_dwordx4 v178, s[12:13]
	s_add_u32 s14, s16, 0x80
	s_mov_b32 m0, s66
	s_nop 0
	global_load_lds_dwordx4 v177, s[12:13]
	s_waitcnt vmcnt(8)
	s_waitcnt lgkmcnt(0)
	s_addc_u32 s15, s17, 0
	s_barrier
	s_setprio 1
	s_waitcnt lgkmcnt(6)
	v_mfma_scale_f32_16x16x128_f8f6f4 v[160:163], v[26:33], v[198:205], v[160:163], v186, v187 op_sel_hi:[0,0,0]
	v_mfma_scale_f32_16x16x128_f8f6f4 v[156:159], v[18:25], v[198:205], v[156:159], v186, v187 op_sel_hi:[0,0,0]
	s_waitcnt lgkmcnt(4)
	v_mfma_scale_f32_16x16x128_f8f6f4 v[142:145], v[26:33], v[206:213], v[142:145], v186, v187 op_sel_hi:[0,0,0]
	v_mfma_scale_f32_16x16x128_f8f6f4 v[138:141], v[18:25], v[206:213], v[138:141], v186, v187 op_sel_hi:[0,0,0]
	s_waitcnt lgkmcnt(2)
	v_mfma_scale_f32_16x16x128_f8f6f4 v[126:129], v[26:33], v[214:221], v[126:129], v186, v187 op_sel_hi:[0,0,0]
	v_mfma_scale_f32_16x16x128_f8f6f4 v[122:125], v[18:25], v[214:221], v[122:125], v186, v187 op_sel_hi:[0,0,0]
	s_waitcnt lgkmcnt(0)
	v_mfma_scale_f32_16x16x128_f8f6f4 v[110:113], v[26:33], v[222:229], v[110:113], v186, v187 op_sel_hi:[0,0,0]
	v_mfma_scale_f32_16x16x128_f8f6f4 v[106:109], v[18:25], v[222:229], v[106:109], v186, v187 op_sel_hi:[0,0,0]
	s_setprio 0
	s_setprio 1
	v_mfma_scale_f32_16x16x128_f8f6f4 v[152:155], v[10:17], v[198:205], v[152:155], v186, v187 op_sel_hi:[0,0,0]
	v_mfma_scale_f32_16x16x128_f8f6f4 v[148:151], v[2:9], v[198:205], v[148:151], v186, v187 op_sel_hi:[0,0,0]
	v_mfma_scale_f32_16x16x128_f8f6f4 v[134:137], v[10:17], v[206:213], v[134:137], v186, v187 op_sel_hi:[0,0,0]
	v_mfma_scale_f32_16x16x128_f8f6f4 v[130:133], v[2:9], v[206:213], v[130:133], v186, v187 op_sel_hi:[0,0,0]
	v_mfma_scale_f32_16x16x128_f8f6f4 v[118:121], v[10:17], v[214:221], v[118:121], v186, v187 op_sel_hi:[0,0,0]
	v_mfma_scale_f32_16x16x128_f8f6f4 v[114:117], v[2:9], v[214:221], v[114:117], v186, v187 op_sel_hi:[0,0,0]
	v_mfma_scale_f32_16x16x128_f8f6f4 v[102:105], v[10:17], v[222:229], v[102:105], v186, v187 op_sel_hi:[0,0,0]
	v_mfma_scale_f32_16x16x128_f8f6f4 v[98:101], v[2:9], v[222:229], v[98:101], v186, v187 op_sel_hi:[0,0,0]
	s_setprio 0
	s_barrier
; #define PG8_STAGE(bufoff, gbase, v0, v1) do { glds16_s((gbase), (v0), ldsbase + (unsigned)(bufoff)); glds16_s((gbase), (v1), ldsbase + (unsigned)(bufoff) + 8192u); } while (0)
; #define PG8_LDA(dst, b, h) do { _Pragma("unroll") for (int m = 0; m < 4; ++m) _Pragma("unroll") for (int k = 0; k < 2; ++k) dst[m][k] = *(const LAS bf16x8*)(lds + PG8_SA(b, h) + aoff + m * 2048 + k * 1024); } while (0)
; #define PG8_LDB(dst, b, h) do { _Pragma("unroll") for (int n = 0; n < 2; ++n) _Pragma("unroll") for (int k = 0; k < 2; ++k) dst[n][k] = *(const LAS bf16x8*)(lds + PG8_SB(b, h) + boff + n * 2048 + k * 1024); } while (0)
; #define PG8_WAIT_V(n) asm volatile("s_waitcnt vmcnt(" #n ")" ::: "memory")
; #define PG8_WAIT_L(n) asm volatile("s_waitcnt lgkmcnt(" #n ")" ::: "memory")
; #define PG8_BAR __builtin_amdgcn_s_barrier()
; #define PG8_SCHED __builtin_amdgcn_sched_barrier(0)
; template <class Epi, class Sched, bool ALIGN_EPI, bool FP8 = false>
; __device__ __forceinline__ void gemm_phase(LAS unsigned char* lds, const bf16_t* A, const bf16_t* Bt, const int K, const Sched& S, const Epi& E, const int wave_in) {
;     ...
;             PG8_LDA(At, 0, 1); PG8_STAGE(PG8_SB(0, 0), b2, voffB[0], voffB[1]); PG8_STAGE(PG8_SB(0, 1), b2 + hstep, voffB[0], voffB[1]); PG8_STAGE(PG8_SA(0, 0), a2, w00, w01);
;             PG8_WAIT_V(8); PG8_WAIT_L(0); PG8_BAR; PG8_MMA(1, 0, At, B0); PG8_MMA(1, 1, At, B1); PG8_BAR; PG8_SCHED;
;             PG8_LDB(B0, 1, 0); PG8_LDB(B1, 1, 1); PG8_SCHED; PG8_LDA(At, 1, 0); PG8_STAGE(PG8_SA(0, 1), a2, w10, w11);
;             PG8_WAIT_V(8); PG8_WAIT_L(0); PG8_BAR; PG8_MMA(0, 0, At, B0); PG8_MMA(0, 1, At, B1); PG8_BAR; PG8_SCHED;
	ds_read_b128 v[198:201], v170 offset:16384
	ds_read_b128 v[202:205], v170 offset:17408
	ds_read_b128 v[206:209], v170 offset:18432
	ds_read_b128 v[210:213], v170 offset:19456
	ds_read_b128 v[214:217], v170 offset:20480
	ds_read_b128 v[218:221], v170 offset:21504
	ds_read_b128 v[222:225], v170 offset:22528
	ds_read_b128 v[226:229], v170 offset:23552
	s_mov_b32 m0, s27
	s_nop 0
	global_load_lds_dwordx4 v0, s[16:17]
	s_nop 0
	s_mov_b32 m0, s48
	s_nop 0
	global_load_lds_dwordx4 v147, s[16:17]
	s_add_u32 s12, s16, 0x20000
	s_addc_u32 s13, s17, 0
	s_mov_b32 m0, s49
	s_nop 0
	global_load_lds_dwordx4 v0, s[12:13]
	s_nop 0
	s_mov_b32 m0, s50
	s_nop 0
	global_load_lds_dwordx4 v147, s[12:13]
	s_mov_b32 m0, s39
	s_nop 0
	global_load_lds_dwordx4 v179, s[92:93]
	s_nop 0
	s_mov_b32 m0, s51
	s_nop 0
	global_load_lds_dwordx4 v180, s[92:93]
	s_waitcnt vmcnt(8)
	s_waitcnt lgkmcnt(0)
	s_barrier
	s_setprio 1
	s_waitcnt lgkmcnt(6)
	v_mfma_scale_f32_16x16x128_f8f6f4 v[94:97], v[26:33], v[198:205], v[94:97], v186, v187 op_sel_hi:[0,0,0]
	v_mfma_scale_f32_16x16x128_f8f6f4 v[90:93], v[18:25], v[198:205], v[90:93], v186, v187 op_sel_hi:[0,0,0]
	s_waitcnt lgkmcnt(4)
	v_mfma_scale_f32_16x16x128_f8f6f4 v[78:81], v[26:33], v[206:213], v[78:81], v186, v187 op_sel_hi:[0,0,0]
	v_mfma_scale_f32_16x16x128_f8f6f4 v[74:77], v[18:25], v[206:213], v[74:77], v186, v187 op_sel_hi:[0,0,0]
	s_waitcnt lgkmcnt(2)
	v_mfma_scale_f32_16x16x128_f8f6f4 v[62:65], v[26:33], v[214:221], v[62:65], v186, v187 op_sel_hi:[0,0,0]
	v_mfma_scale_f32_16x16x128_f8f6f4 v[58:61], v[18:25], v[214:221], v[58:61], v186, v187 op_sel_hi:[0,0,0]
	s_waitcnt lgkmcnt(0)
	v_mfma_scale_f32_16x16x128_f8f6f4 v[46:49], v[26:33], v[222:229], v[46:49], v186, v187 op_sel_hi:[0,0,0]
	v_mfma_scale_f32_16x16x128_f8f6f4 v[42:45], v[18:25], v[222:229], v[42:45], v186, v187 op_sel_hi:[0,0,0]
	s_setprio 0
	s_setprio 1
	v_mfma_scale_f32_16x16x128_f8f6f4 v[86:89], v[10:17], v[198:205], v[86:89], v186, v187 op_sel_hi:[0,0,0]
	v_mfma_scale_f32_16x16x128_f8f6f4 v[82:85], v[2:9], v[198:205], v[82:85], v186, v187 op_sel_hi:[0,0,0]
	v_mfma_scale_f32_16x16x128_f8f6f4 v[70:73], v[10:17], v[206:213], v[70:73], v186, v187 op_sel_hi:[0,0,0]
	v_mfma_scale_f32_16x16x128_f8f6f4 v[66:69], v[2:9], v[206:213], v[66:69], v186, v187 op_sel_hi:[0,0,0]
	v_mfma_scale_f32_16x16x128_f8f6f4 v[54:57], v[10:17], v[214:221], v[54:57], v186, v187 op_sel_hi:[0,0,0]
	v_mfma_scale_f32_16x16x128_f8f6f4 v[50:53], v[2:9], v[214:221], v[50:53], v186, v187 op_sel_hi:[0,0,0]
	v_mfma_scale_f32_16x16x128_f8f6f4 v[38:41], v[10:17], v[222:229], v[38:41], v186, v187 op_sel_hi:[0,0,0]
	v_mfma_scale_f32_16x16x128_f8f6f4 v[34:37], v[2:9], v[222:229], v[34:37], v186, v187 op_sel_hi:[0,0,0]
	s_setprio 0
	s_barrier
	v_add_u32_e32 v14, 0x18000, v169
	v_add_u32_e32 v30, 0x1c000, v169
	ds_read_b128 v[2:5], v14
	ds_read_b128 v[6:9], v14 offset:1024
	ds_read_b128 v[10:13], v14 offset:2048
	ds_read_b128 v[14:17], v14 offset:3072
	ds_read_b128 v[18:21], v30
	ds_read_b128 v[22:25], v30 offset:1024
	ds_read_b128 v[26:29], v30 offset:2048
	ds_read_b128 v[30:33], v30 offset:3072
	ds_read_b128 v[198:201], v170 offset:32768
	ds_read_b128 v[202:205], v170 offset:33792
	ds_read_b128 v[206:209], v170 offset:34816
	ds_read_b128 v[210:213], v170 offset:35840
	ds_read_b128 v[214:217], v170 offset:36864
	ds_read_b128 v[218:221], v170 offset:37888
	ds_read_b128 v[222:225], v170 offset:38912
	ds_read_b128 v[226:229], v170 offset:39936
	s_mov_b32 m0, s52
	s_nop 0
	global_load_lds_dwordx4 v181, s[92:93]
	v_cndmask_b32_e32 v197, v177, v174, vcc
	s_mov_b32 m0, s53
	s_nop 0
	global_load_lds_dwordx4 v197, s[92:93]
	s_waitcnt vmcnt(8)
	s_waitcnt lgkmcnt(0)
	s_barrier
; #define PG8_STAGE(bufoff, gbase, v0, v1) do { glds16_s((gbase), (v0), ldsbase + (unsigned)(bufoff)); glds16_s((gbase), (v1), ldsbase + (unsigned)(bufoff) + 8192u); } while (0)
; #define PG8_LDA(dst, b, h) do { _Pragma("unroll") for (int m = 0; m < 4; ++m) _Pragma("unroll") for (int k = 0; k < 2; ++k) dst[m][k] = *(const LAS bf16x8*)(lds + PG8_SA(b, h) + aoff + m * 2048 + k * 1024); } while (0)
; #define PG8_WAIT_V(n) asm volatile("s_waitcnt vmcnt(" #n ")" ::: "memory")
; #define PG8_WAIT_L(n) asm volatile("s_waitcnt lgkmcnt(" #n ")" ::: "memory")
; #define PG8_BAR __builtin_amdgcn_s_barrier()
; #define PG8_SCHED __builtin_amdgcn_sched_barrier(0)
; template <class Epi, class Sched, bool ALIGN_EPI, bool FP8 = false>
; __device__ __forceinline__ void gemm_phase(LAS unsigned char* lds, const bf16_t* A, const bf16_t* Bt, const int K, const Sched& S, const Epi& E, const int wave_in) {
;     ...
;             PG8_WAIT_V(8); PG8_WAIT_L(0); PG8_BAR; PG8_MMA(0, 0, At, B0); PG8_MMA(0, 1, At, B1); PG8_BAR; PG8_SCHED;
;             PG8_LDA(At, 1, 1); PG8_STAGE(PG8_SB(1, 0), b3, voffB[0], voffB[1]); PG8_STAGE(PG8_SB(1, 1), b3 + hstep, voffB[0], voffB[1]); PG8_STAGE(PG8_SA(1, 0), a3, w00, w01);
;             PG8_WAIT_V(8); PG8_WAIT_L(0); PG8_BAR; PG8_MMA(1, 0, At, B0); PG8_MMA(1, 1, At, B1); PG8_BAR; PG8_SCHED;
;         }
;         if constexpr (FP8) asm volatile("s_nop 15\n\ts_nop 15" ::: "memory");
;         if constexpr (ALIGN_EPI) { if (wr == 0) PG8_BAR; }
	s_setprio 1
	s_waitcnt lgkmcnt(6)
	v_mfma_scale_f32_16x16x128_f8f6f4 v[160:163], v[2:9], v[198:205], v[160:163], v186, v187 op_sel_hi:[0,0,0]
	v_mfma_scale_f32_16x16x128_f8f6f4 v[156:159], v[10:17], v[198:205], v[156:159], v186, v187 op_sel_hi:[0,0,0]
	s_waitcnt lgkmcnt(4)
	v_mfma_scale_f32_16x16x128_f8f6f4 v[142:145], v[2:9], v[206:213], v[142:145], v186, v187 op_sel_hi:[0,0,0]
	v_mfma_scale_f32_16x16x128_f8f6f4 v[138:141], v[10:17], v[206:213], v[138:141], v186, v187 op_sel_hi:[0,0,0]
	s_waitcnt lgkmcnt(2)
	v_mfma_scale_f32_16x16x128_f8f6f4 v[126:129], v[2:9], v[214:221], v[126:129], v186, v187 op_sel_hi:[0,0,0]
	v_mfma_scale_f32_16x16x128_f8f6f4 v[122:125], v[10:17], v[214:221], v[122:125], v186, v187 op_sel_hi:[0,0,0]
	s_waitcnt lgkmcnt(0)
	v_mfma_scale_f32_16x16x128_f8f6f4 v[110:113], v[2:9], v[222:229], v[110:113], v186, v187 op_sel_hi:[0,0,0]
	v_mfma_scale_f32_16x16x128_f8f6f4 v[106:109], v[10:17], v[222:229], v[106:109], v186, v187 op_sel_hi:[0,0,0]
	s_setprio 0
	s_setprio 1
	v_mfma_scale_f32_16x16x128_f8f6f4 v[152:155], v[18:25], v[198:205], v[152:155], v186, v187 op_sel_hi:[0,0,0]
	v_mfma_scale_f32_16x16x128_f8f6f4 v[148:151], v[26:33], v[198:205], v[148:151], v186, v187 op_sel_hi:[0,0,0]
	v_mfma_scale_f32_16x16x128_f8f6f4 v[134:137], v[18:25], v[206:213], v[134:137], v186, v187 op_sel_hi:[0,0,0]
	v_mfma_scale_f32_16x16x128_f8f6f4 v[130:133], v[26:33], v[206:213], v[130:133], v186, v187 op_sel_hi:[0,0,0]
	v_mfma_scale_f32_16x16x128_f8f6f4 v[118:121], v[18:25], v[214:221], v[118:121], v186, v187 op_sel_hi:[0,0,0]
	v_mfma_scale_f32_16x16x128_f8f6f4 v[114:117], v[26:33], v[214:221], v[114:117], v186, v187 op_sel_hi:[0,0,0]
	v_mfma_scale_f32_16x16x128_f8f6f4 v[102:105], v[18:25], v[222:229], v[102:105], v186, v187 op_sel_hi:[0,0,0]
	v_mfma_scale_f32_16x16x128_f8f6f4 v[98:101], v[26:33], v[222:229], v[98:101], v186, v187 op_sel_hi:[0,0,0]
	s_setprio 0
	s_barrier
	ds_read_b128 v[198:201], v170 offset:49152
	ds_read_b128 v[202:205], v170 offset:50176
	ds_read_b128 v[206:209], v170 offset:51200
	ds_read_b128 v[210:213], v170 offset:52224
	ds_read_b128 v[214:217], v170 offset:53248
	ds_read_b128 v[218:221], v170 offset:54272
	ds_read_b128 v[222:225], v170 offset:55296
	ds_read_b128 v[226:229], v170 offset:56320
	s_mov_b32 m0, s55
	s_nop 0
	global_load_lds_dwordx4 v0, s[14:15]
	s_nop 0
	s_mov_b32 m0, s56
	s_nop 0
	global_load_lds_dwordx4 v147, s[14:15]
	s_add_u32 s12, s16, 0x20080
	s_addc_u32 s13, s17, 0
	s_mov_b32 m0, s59
	s_nop 0
	global_load_lds_dwordx4 v0, s[12:13]
	s_nop 0
	s_mov_b32 m0, s64
	s_nop 0
	global_load_lds_dwordx4 v147, s[12:13]
	s_mov_b32 m0, s57
	s_nop 0
	global_load_lds_dwordx4 v179, s[10:11]
	s_nop 0
	s_mov_b32 m0, s58
	s_nop 0
	global_load_lds_dwordx4 v180, s[10:11]
	s_waitcnt vmcnt(8)
	s_waitcnt lgkmcnt(0)
	s_barrier
	s_setprio 1
	s_waitcnt lgkmcnt(6)
	v_mfma_scale_f32_16x16x128_f8f6f4 v[94:97], v[2:9], v[198:205], v[94:97], v186, v187 op_sel_hi:[0,0,0]
	v_mfma_scale_f32_16x16x128_f8f6f4 v[90:93], v[10:17], v[198:205], v[90:93], v186, v187 op_sel_hi:[0,0,0]
	s_waitcnt lgkmcnt(4)
	v_mfma_scale_f32_16x16x128_f8f6f4 v[78:81], v[2:9], v[206:213], v[78:81], v186, v187 op_sel_hi:[0,0,0]
	v_mfma_scale_f32_16x16x128_f8f6f4 v[74:77], v[10:17], v[206:213], v[74:77], v186, v187 op_sel_hi:[0,0,0]
	s_waitcnt lgkmcnt(2)
	v_mfma_scale_f32_16x16x128_f8f6f4 v[62:65], v[2:9], v[214:221], v[62:65], v186, v187 op_sel_hi:[0,0,0]
	v_mfma_scale_f32_16x16x128_f8f6f4 v[58:61], v[10:17], v[214:221], v[58:61], v186, v187 op_sel_hi:[0,0,0]
	s_waitcnt lgkmcnt(0)
	v_mfma_scale_f32_16x16x128_f8f6f4 v[46:49], v[2:9], v[222:229], v[46:49], v186, v187 op_sel_hi:[0,0,0]
	v_mfma_scale_f32_16x16x128_f8f6f4 v[42:45], v[10:17], v[222:229], v[42:45], v186, v187 op_sel_hi:[0,0,0]
	s_setprio 0
	s_setprio 1
	v_mfma_scale_f32_16x16x128_f8f6f4 v[86:89], v[18:25], v[198:205], v[86:89], v186, v187 op_sel_hi:[0,0,0]
	v_mfma_scale_f32_16x16x128_f8f6f4 v[82:85], v[26:33], v[198:205], v[82:85], v186, v187 op_sel_hi:[0,0,0]
	v_mfma_scale_f32_16x16x128_f8f6f4 v[70:73], v[18:25], v[206:213], v[70:73], v186, v187 op_sel_hi:[0,0,0]
	v_mfma_scale_f32_16x16x128_f8f6f4 v[66:69], v[26:33], v[206:213], v[66:69], v186, v187 op_sel_hi:[0,0,0]
	v_mfma_scale_f32_16x16x128_f8f6f4 v[54:57], v[18:25], v[214:221], v[54:57], v186, v187 op_sel_hi:[0,0,0]
	v_mfma_scale_f32_16x16x128_f8f6f4 v[50:53], v[26:33], v[214:221], v[50:53], v186, v187 op_sel_hi:[0,0,0]
	v_mfma_scale_f32_16x16x128_f8f6f4 v[38:41], v[18:25], v[222:229], v[38:41], v186, v187 op_sel_hi:[0,0,0]
	v_mfma_scale_f32_16x16x128_f8f6f4 v[34:37], v[26:33], v[222:229], v[34:37], v186, v187 op_sel_hi:[0,0,0]
	s_setprio 0
	s_barrier
	s_add_i32 s89, s89, 2
	s_add_u32 s0, s0, 0x100
	s_addc_u32 s1, s1, 0
	s_cmp_gt_u32 s89, 5
	s_mov_b64 s[14:15], s[60:61]
	s_cbranch_scc0 .LBB0_1139
	s_nop 15
	s_nop 15
	s_and_b64 vcc, exec, s[86:87]
	s_cbranch_vccz .LBB0_1142
	s_barrier

; #define ISSUE_L(t, so) do { const unsigned so_ = (unsigned)(so); \
;     if ((t) < NT) { const char* kb_ = Kh + KROWB(t); pg8::glds16_s(kb_, koff[0], ldsK + so_); pg8::glds16_s(kb_, koff[1], ldsK + so_ + 1024u); } \
;     if ((t) >= 1) { const char* vb_ = Vh + KROWB((t) - 1); pg8::glds16_s(vb_, voff[0], ldsV + so_); pg8::glds16_s(vb_, voff[1], ldsV + so_ + 1024u); } } while (0)
; #define PBAR() asm volatile("s_waitcnt lgkmcnt(0)\n\ts_barrier" ::: "memory")
; #define PBAR_V0() asm volatile("s_waitcnt vmcnt(0) lgkmcnt(0)\n\ts_barrier" ::: "memory")
; #define ISSUE_L(t, sl) do { \
;     if ((t) < NT) pg8::glds16_s(Kh + KROWB(t), koff, ldsK + (unsigned)(sl) * 8192u); \
;     if ((t) >= 1 && (t) <= NT) pg8::glds16_s((const char*)V8 + (size_t)((t) - 1) * 8192, voff, ldsV + (unsigned)(sl) * 8192u); } while (0)
; #define PBAR() asm volatile("s_waitcnt lgkmcnt(0)\n\ts_barrier" ::: "memory")
; __device__ __forceinline__ void attn_unit_f8(const bf16_t* __restrict__ Q, const bf16_t* __restrict__ Kb, const unsigned char* __restrict__ V8, bf16_t* __restrict__ O, ...
;     ...
;   unsigned koff, voff;
;   { const int row = 8 * wid + (lane >> 3), cpos = lane & 7;
;     const int key = 16 * (row & 3) + 8 * ((row >> 2) & 1) + ((row >> 3) & 3) + 4 * (row >> 5);
;     koff = (unsigned)(key * DM + 16 * (cpos ^ ((row >> 1) & 7))); }
;   { const int e = 16 * wid + (lane >> 2), cpos = lane & 3; voff = (unsigned)(e * 64 + 16 * (cpos ^ ((e >> 2) & 3))); }
;   const unsigned ldsK = (unsigned)__builtin_amdgcn_readfirstlane((int)((unsigned)(uintptr_t)K_lds + (unsigned)wid * 1024u));
;   const unsigned ldsV = (unsigned)__builtin_amdgcn_readfirstlane((int)((unsigned)(uintptr_t)V_lds + (unsigned)wid * 1024u));
;   const char* Kh = (const char*)Kb + h * 128;
;   const int fsw = (r32 >> 2) & 3;
;   const char* vfa = V_lds + r32 * 64 + 16 * ((2 * hi) ^ fsw); const char* vfb = V_lds + r32 * 64 + 16 * ((2 * hi + 1) ^ fsw);
;     ...
;   f32x16 p0, p1; i32x8 p8 = i32x8{};
;   i32x8 onesf = (i32x8){0x38383838, 0x38383838, 0x38383838, 0x38383838, 0x38383838, 0x38383838, 0x38383838, 0x38383838}; asm volatile("" : "+v"(onesf));
;   f32x16 negm = f32x16{}; asm volatile("" : "+v"(negm));
;   const int scl1 = 0x7F7F7F7F;
;     ...
;   if (!pref_in) { ISSUE_L(0, 0); ISSUE_L(1, 1); PBAR_V3(); }
;   else PBAR_V0();
;   int sx = 1, si = 2;
;   if (cq == 0) {
;     QKT(0); ISSUE_L(2, si); si = NEXT3(si); PBAR();
.LBB0_1297:
	v_lshrrev_b32_e32 v2, 2, v16
	v_lshlrev_b32_e32 v0, 1, v179
	v_and_b32_e32 v3, 8, v2
	v_and_b32_e32 v0, 48, v0
	v_add_u32_e32 v3, s50, v3
	v_add_lshl_u32 v0, v3, v0, 10
	s_lshl_b32 s2, s50, 2
	v_bfe_u32 v3, v179, 4, 2
	v_bitop3_b32 v3, v3, v179, s2 bitop3:0x36
	v_lshlrev_b32_e32 v3, 4, v3
	s_movk_i32 s2, 0x70
	v_and_or_b32 v148, v3, s2, v0
	v_lshlrev_b32_e32 v0, 4, v179
	v_and_b32_e32 v3, 0x3c0, v0
	v_bitop3_b32 v0, v0, 48, v179 bitop3:0x48
	s_lshl_b32 s84, s27, 8
	v_or3_b32 v147, v3, v0, s55
	s_andn2_b64 vcc, exec, s[0:1]
	s_add_i32 s57, s55, s28
	s_cbranch_vccnz .LBB0_1299
	s_ashr_i32 s85, s84, 31
	s_lshl_b64 s[0:1], s[84:85], 10
	s_add_u32 s0, s59, s0
	s_addc_u32 s1, s60, s1
	s_mov_b32 m0, s57
	s_nop 0
	global_load_lds_dwordx4 v148, s[0:1]
	s_or_b32 s0, s84, 64
	s_ashr_i32 s1, s0, 31
	s_lshl_b64 s[0:1], s[0:1], 10
	s_add_u32 s0, s59, s0
	s_addc_u32 s1, s60, s1
	s_cmp_lg_u32 s56, -1
	s_cselect_b32 s2, s56, 0
	s_add_i32 s2, s2, s55
	s_addk_i32 s2, 0x2000
	s_cmp_lg_u32 0, -1
	s_mov_b32 m0, s2
	s_nop 0
	global_load_lds_dwordx4 v148, s[0:1]
	s_cselect_b32 s0, 0, 0
	s_add_i32 s0, s0, s55
	s_addk_i32 s0, 0x2000
	s_mov_b32 m0, s0
	s_nop 0
	global_load_lds_dwordx4 v147, s[82:83]
	s_waitcnt vmcnt(2) lgkmcnt(0)
	s_barrier
.LBB0_1299:
	s_cmp_lg_u32 0, -1
	v_and_b32_e32 v181, 63, v179
	s_cselect_b32 s0, 0, 0
	v_lshrrev_b32_e32 v0, 5, v181
	s_add_i32 s58, s55, s0
	s_and_b32 s0, s26, 0x3fffffc0
	v_lshlrev_b32_e32 v198, 6, v178
	v_lshlrev_b32_e32 v199, 1, v0
	s_lshl_b32 s0, s0, 2
	v_and_b32_e32 v3, 3, v2
	v_add_u32_e32 v200, 0, v198
	v_bitop3_b32 v2, v199, v2, 3 bitop3:0x78
	s_add_i32 s66, s0, 0
	v_lshl_add_u32 v149, v2, 4, v200
	v_bitop3_b32 v2, v199, v3, 1 bitop3:0x36
	s_cmpk_lt_u32 s26, 0x100
	v_lshlrev_b32_e32 v152, 7, v178
	v_lshl_add_u32 v150, v2, 4, v200
	s_cselect_b64 s[80:81], -1, 0
	s_cmpk_gt_u32 s26, 0xff
	s_mov_b64 s[0:1], -1
	v_cmp_gt_u32_e64 s[2:3], 32, v181
	v_add_u32_e32 v153, 0, v152
	v_lshl_add_u32 v151, v178, 2, s66
	s_cbranch_scc0 .LBB0_1327
	s_or_b32 s0, s84, 0x80
	s_ashr_i32 s1, s0, 31
	s_lshl_b64 s[0:1], s[0:1], 10
	s_add_u32 s0, s59, s0
	s_addc_u32 s1, s60, s1
	s_cmp_lg_u32 s56, -1
	s_cselect_b32 s12, s56, 0
	s_add_i32 s12, s12, s55
	s_addk_i32 s12, 0x4000
	s_mov_b32 m0, s12
	s_nop 0
	global_load_lds_dwordx4 v148, s[0:1]
	s_add_u32 s0, s82, 0x2000
	s_addc_u32 s1, s83, 0
	s_cmp_lg_u32 0, -1
	s_cselect_b32 s12, 0, 0
	s_add_i32 s12, s12, s55
	s_addk_i32 s12, 0x4000
	s_mov_b32 m0, s12
	s_nop 0
	global_load_lds_dwordx4 v147, s[0:1]
	s_lshl_b32 s0, s51, 2
	v_or_b32_e32 v2, s0, v199
	v_bfe_u32 v3, v179, 1, 3
	v_bitop3_b32 v2, v2, v3, 1 bitop3:0x36
	v_bitop3_b32 v4, s0, v3, v199 bitop3:0x36
	v_lshlrev_b32_e32 v203, 4, v2
	s_waitcnt lgkmcnt(0)
	s_barrier
	v_lshlrev_b32_e32 v202, 4, v4
	v_add_u32_e32 v35, v153, v203
	v_add_u32_e32 v34, v153, v202
	ds_read_b128 v[6:9], v35 offset:24576
	ds_read_b128 v[2:5], v34 offset:24576
	ds_read_b128 v[18:21], v34 offset:28672
	ds_read_b128 v[22:25], v35 offset:28672
	s_waitcnt vmcnt(0) lgkmcnt(2)
	v_mfma_scale_f32_32x32x64_f8f6f4 v[2:17], v[2:9], v[154:161], v[82:97], v187, v187 op_sel_hi:[0,0,0]
	v_mov_b32_e32 v170, v1
	v_mov_b32_e32 v174, v1
	v_mov_b32_e32 v171, v1
	v_mov_b32_e32 v175, v1
	v_mov_b32_e32 v172, v1
	v_mov_b32_e32 v176, v1
	v_mov_b32_e32 v173, v1
	v_mov_b32_e32 v177, v1
	s_mov_b32 s72, 0
	s_mov_b32 s28, 2
	s_mov_b32 s67, 1
	s_nop 8
	v_max_f32_e32 v36, v3, v3
	s_waitcnt lgkmcnt(0)
	v_mfma_scale_f32_32x32x64_f8f6f4 v[18:33], v[18:25], v[154:161], v[82:97], v187, v187 op_sel_hi:[0,0,0]
	v_max_f32_e32 v37, v2, v2
	v_max_f32_e32 v36, v37, v36
	s_waitcnt vmcnt(2) lgkmcnt(0)
	s_barrier
; #define ISSUE_L(t, so) do { const unsigned so_ = (unsigned)(so); \
;     if ((t) < NT) { const char* kb_ = Kh + KROWB(t); pg8::glds16_s(kb_, koff[0], ldsK + so_); pg8::glds16_s(kb_, koff[1], ldsK + so_ + 1024u); } \
;     if ((t) >= 1) { const char* vb_ = Vh + KROWB((t) - 1); pg8::glds16_s(vb_, voff[0], ldsV + so_); pg8::glds16_s(vb_, voff[1], ldsV + so_ + 1024u); } } while (0)
; #define PBAR() asm volatile("s_waitcnt lgkmcnt(0)\n\ts_barrier" ::: "memory")
; #define PBAR_V0() asm volatile("s_waitcnt vmcnt(0) lgkmcnt(0)\n\ts_barrier" ::: "memory")
; #define ISSUE_L(t, sl) do { \
;     if ((t) < NT) pg8::glds16_s(Kh + KROWB(t), koff, ldsK + (unsigned)(sl) * 8192u); \
;     if ((t) >= 1 && (t) <= NT) pg8::glds16_s((const char*)V8 + (size_t)((t) - 1) * 8192, voff, ldsV + (unsigned)(sl) * 8192u); } while (0)
; #define PBAR() asm volatile("s_waitcnt lgkmcnt(0)\n\ts_barrier" ::: "memory")
; #define PBAR_V0() asm volatile("s_waitcnt vmcnt(0) lgkmcnt(0)\n\ts_barrier" ::: "memory")
; #define PBAR_V3() asm volatile("s_waitcnt vmcnt(2) lgkmcnt(0)\n\ts_barrier" ::: "memory")
; __device__ __forceinline__ void attn_unit_f8(const bf16_t* __restrict__ Q, const bf16_t* __restrict__ Kb, const unsigned char* __restrict__ V8, bf16_t* __restrict__ O, ...
;     ...
;   if (!pref_in) { ISSUE_L(0, 0); ISSUE_L(1, 1); PBAR_V3(); }
;   else PBAR_V0();
;   int sx = 1, si = 2;
;   if (cq == 0) {
;     QKT(0); ISSUE_L(2, si); si = NEXT3(si); PBAR();
;     YSOFT(true); PBAR_V3();
;     for (int t = 1; t < NT; ++t) {
;       __builtin_amdgcn_s_setprio(1); QKT(sx); PV8(sx); sx = NEXT3(sx);
;       if (t + 2 <= NT) { ISSUE_L(t + 2, si); si = NEXT3(si); }
;       __builtin_amdgcn_s_setprio(0);
;       PBAR();
	s_nop 15
	s_nop 1
	v_max3_f32 v38, v4, v5, v19
	v_max3_f32 v36, v36, v18, v20
	v_max3_f32 v37, v38, v8, v9
	v_max3_f32 v36, v36, v21, v6
	v_max3_f32 v37, v37, v24, v25
	v_max3_f32 v36, v36, v7, v22
	v_max3_f32 v37, v37, v12, v13
	v_max3_f32 v36, v36, v23, v10
	v_max3_f32 v36, v36, v11, v26
	v_max3_f32 v37, v37, v28, v29
	v_max3_f32 v36, v36, v27, v14
	v_max3_f32 v37, v37, v16, v17
	v_max3_f32 v36, v36, v15, v30
	v_max3_f32 v37, v37, v32, v33
	v_max3_f32 v36, v36, v31, v37
	v_mov_b32_e32 v37, v36
	s_nop 1
	v_permlane32_swap_b32_e32 v36, v37
	v_max_f32_e32 v37, v37, v37
	v_max_f32_e32 v36, v36, v36
	v_max_f32_e32 v36, v36, v37
	v_add_f32_e32 v201, 0xc0c00000, v36
	v_sub_f32_e32 v2, v2, v201
	v_sub_f32_e32 v18, v18, v201
	v_sub_f32_e32 v3, v3, v201
	v_sub_f32_e32 v19, v19, v201
	v_sub_f32_e32 v6, v6, v201
	v_sub_f32_e32 v22, v22, v201
	v_sub_f32_e32 v7, v7, v201
	v_sub_f32_e32 v23, v23, v201
	v_sub_f32_e32 v10, v10, v201
	v_sub_f32_e32 v26, v26, v201
	v_sub_f32_e32 v11, v11, v201
	v_sub_f32_e32 v27, v27, v201
	v_sub_f32_e32 v14, v14, v201
	v_sub_f32_e32 v30, v30, v201
	v_sub_f32_e32 v15, v15, v201
	v_sub_f32_e32 v31, v31, v201
	v_exp_f32_e32 v2, v2
	v_exp_f32_e32 v3, v3
	v_exp_f32_e32 v6, v6
	v_exp_f32_e32 v7, v7
	v_exp_f32_e32 v10, v10
	v_exp_f32_e32 v11, v11
	v_exp_f32_e32 v14, v14
	v_exp_f32_e32 v15, v15
	v_exp_f32_e32 v18, v18
	v_exp_f32_e32 v19, v19
	v_exp_f32_e32 v22, v22
	v_exp_f32_e32 v23, v23
	v_exp_f32_e32 v26, v26
	v_exp_f32_e32 v27, v27
	v_exp_f32_e32 v30, v30
	v_exp_f32_e32 v31, v31
	v_sub_f32_e32 v4, v4, v201
	v_sub_f32_e32 v20, v20, v201
	v_sub_f32_e32 v5, v5, v201
	v_sub_f32_e32 v21, v21, v201
	v_sub_f32_e32 v8, v8, v201
	v_sub_f32_e32 v24, v24, v201
	v_sub_f32_e32 v9, v9, v201
	v_sub_f32_e32 v25, v25, v201
	v_sub_f32_e32 v12, v12, v201
	v_sub_f32_e32 v28, v28, v201
	v_sub_f32_e32 v13, v13, v201
	v_sub_f32_e32 v29, v29, v201
	v_sub_f32_e32 v16, v16, v201
	v_sub_f32_e32 v32, v32, v201
	v_sub_f32_e32 v17, v17, v201
	v_sub_f32_e32 v33, v33, v201
	v_exp_f32_e32 v4, v4
	v_exp_f32_e32 v5, v5
	v_exp_f32_e32 v8, v8
	v_exp_f32_e32 v9, v9
	v_exp_f32_e32 v12, v12
	v_exp_f32_e32 v13, v13
	v_exp_f32_e32 v16, v16
	v_exp_f32_e32 v17, v17
	v_exp_f32_e32 v20, v20
	v_exp_f32_e32 v21, v21
	v_exp_f32_e32 v24, v24
	v_exp_f32_e32 v25, v25
	v_exp_f32_e32 v28, v28
	v_exp_f32_e32 v29, v29
	v_exp_f32_e32 v32, v32
	v_exp_f32_e32 v33, v33
	v_cvt_pk_fp8_f32 v170, v2, v3
	v_cvt_pk_fp8_f32 v174, v18, v19
	v_cvt_pk_fp8_f32 v171, v6, v7
	v_cvt_pk_fp8_f32 v175, v22, v23
	v_cvt_pk_fp8_f32 v172, v10, v11
	v_cvt_pk_fp8_f32 v176, v26, v27
	v_cvt_pk_fp8_f32 v173, v14, v15
	v_cvt_pk_fp8_f32 v177, v30, v31
	v_xor_b32_e32 v98, 0x80000000, v201
	v_mov_b32_e32 v99, v98
	v_mov_b32_e32 v100, v98
	v_mov_b32_e32 v101, v98
	v_mov_b32_e32 v102, v98
	v_mov_b32_e32 v103, v98
	v_mov_b32_e32 v104, v98
	v_mov_b32_e32 v105, v98
	v_mov_b32_e32 v106, v98
	v_mov_b32_e32 v107, v98
	v_mov_b32_e32 v108, v98
	v_mov_b32_e32 v109, v98
	v_mov_b32_e32 v110, v98
	v_mov_b32_e32 v111, v98
	v_mov_b32_e32 v112, v98
	v_mov_b32_e32 v113, v98
	v_cvt_pk_fp8_f32 v170, v4, v5 op_sel:[0,0,1]
	v_cvt_pk_fp8_f32 v174, v20, v21 op_sel:[0,0,1]
	v_cvt_pk_fp8_f32 v171, v8, v9 op_sel:[0,0,1]
	v_cvt_pk_fp8_f32 v175, v24, v25 op_sel:[0,0,1]
	v_cvt_pk_fp8_f32 v172, v12, v13 op_sel:[0,0,1]
	v_cvt_pk_fp8_f32 v176, v28, v29 op_sel:[0,0,1]
	v_cvt_pk_fp8_f32 v173, v16, v17 op_sel:[0,0,1]
	v_cvt_pk_fp8_f32 v177, v32, v33 op_sel:[0,0,1]
	s_waitcnt lgkmcnt(0)
	s_barrier
	s_setprio 1
	ds_read_b128 v[6:9], v35 offset:32768
	ds_read_b128 v[2:5], v34 offset:32768
	ds_read_b128 v[66:69], v34 offset:36864
	ds_read_b128 v[70:73], v35 offset:36864
	v_mov_b64_e32 v[144:145], v[112:113]
	v_mov_b64_e32 v[142:143], v[110:111]
	s_waitcnt lgkmcnt(2)
	v_mfma_scale_f32_32x32x64_f8f6f4 v[114:129], v[2:9], v[154:161], v[98:113], v187, v187 op_sel_hi:[0,0,0]
	ds_read_b128 v[6:9], v150 offset:8192
	ds_read_b128 v[2:5], v149 offset:8192
	ds_read_b128 v[18:21], v149 offset:10240
	ds_read_b128 v[22:25], v150 offset:10240
	ds_read_b128 v[38:41], v150 offset:12288
	ds_read_b128 v[34:37], v149 offset:12288
	ds_read_b128 v[50:53], v149 offset:14336
	ds_read_b128 v[54:57], v150 offset:14336
	v_mov_b64_e32 v[140:141], v[108:109]
	v_mov_b64_e32 v[138:139], v[106:107]
	v_mov_b64_e32 v[136:137], v[104:105]
	v_mov_b64_e32 v[134:135], v[102:103]
	v_mov_b64_e32 v[132:133], v[100:101]
	v_mov_b64_e32 v[130:131], v[98:99]
	s_waitcnt lgkmcnt(6)
	v_mfma_scale_f32_32x32x64_f8f6f4 v[2:17], v[170:177], v[2:9], 0, v187, v187 op_sel_hi:[0,0,0]
	s_waitcnt lgkmcnt(4)
	v_mfma_scale_f32_32x32x64_f8f6f4 v[18:33], v[170:177], v[18:25], 0, v187, v187 op_sel_hi:[0,0,0]
	s_waitcnt lgkmcnt(2)
	v_mfma_scale_f32_32x32x64_f8f6f4 v[34:49], v[170:177], v[34:41], 0, v187, v187 op_sel_hi:[0,0,0]
	s_waitcnt lgkmcnt(0)
	v_mfma_scale_f32_32x32x64_f8f6f4 v[50:65], v[170:177], v[50:57], 0, v187, v187 op_sel_hi:[0,0,0]
	v_mfma_scale_f32_32x32x64_f8f6f4 v[130:145], v[66:73], v[154:161], v[130:145], v187, v187 op_sel_hi:[0,0,0]
	v_mfma_scale_f32_32x32x64_f8f6f4 v[66:81], v[170:177], v[162:169], 0, v187, v187 op_sel_hi:[0,0,0]
	s_setprio 0
	s_or_b32 s0, s84, 0xc0
	s_ashr_i32 s1, s0, 31
	s_lshl_b64 s[0:1], s[0:1], 10
	s_add_u32 s0, s59, s0
	s_addc_u32 s1, s60, s1
	s_mov_b32 m0, s57
	s_nop 0
	global_load_lds_dwordx4 v148, s[0:1]
	s_add_u32 s0, s82, 0x4000
	s_addc_u32 s1, s83, 0
	s_mov_b32 m0, s58
	s_nop 0
	global_load_lds_dwordx4 v147, s[0:1]
	s_waitcnt vmcnt(2) lgkmcnt(0)
	s_barrier
	s_add_i32 s47, s61, 0x800
	s_add_u32 s26, s22, s65
	v_lshlrev_b32_e32 v204, 4, v0
	s_addc_u32 s27, s23, s64
	s_branch .LBB0_1304

; #define ISSUE_L(t, so) do { const unsigned so_ = (unsigned)(so); \
;     if ((t) < NT) { const char* kb_ = Kh + KROWB(t); pg8::glds16_s(kb_, koff[0], ldsK + so_); pg8::glds16_s(kb_, koff[1], ldsK + so_ + 1024u); } \
;     if ((t) >= 1) { const char* vb_ = Vh + KROWB((t) - 1); pg8::glds16_s(vb_, voff[0], ldsV + so_); pg8::glds16_s(vb_, voff[1], ldsV + so_ + 1024u); } } while (0)
; #define PBAR() asm volatile("s_waitcnt lgkmcnt(0)\n\ts_barrier" ::: "memory")
; #define PBAR_V0() asm volatile("s_waitcnt vmcnt(0) lgkmcnt(0)\n\ts_barrier" ::: "memory")
; #define YPH() YSOFT(false)
; #define ISSUE_L(t, sl) do { \
;     if ((t) < NT) pg8::glds16_s(Kh + KROWB(t), koff, ldsK + (unsigned)(sl) * 8192u); \
;     if ((t) >= 1 && (t) <= NT) pg8::glds16_s((const char*)V8 + (size_t)((t) - 1) * 8192, voff, ldsV + (unsigned)(sl) * 8192u); } while (0)
; #define PBAR() asm volatile("s_waitcnt lgkmcnt(0)\n\ts_barrier" ::: "memory")
; #define PBAR_V0() asm volatile("s_waitcnt vmcnt(0) lgkmcnt(0)\n\ts_barrier" ::: "memory")
; #define PBAR_V3() asm volatile("s_waitcnt vmcnt(2) lgkmcnt(0)\n\ts_barrier" ::: "memory")
; #define YPH() YSOFT(false)
; __device__ __forceinline__ void attn_unit_f8(const bf16_t* __restrict__ Q, const bf16_t* __restrict__ Kb, const unsigned char* __restrict__ V8, bf16_t* __restrict__ O, ...
;     ...
;   if (!pref_in) { ISSUE_L(0, 0); ISSUE_L(1, 1); PBAR_V3(); }
;   else PBAR_V0();
;   int sx = 1, si = 2;
;   if (cq == 0) {
;     QKT(0); ISSUE_L(2, si); si = NEXT3(si); PBAR();
;     YSOFT(true); PBAR_V3();
;     for (int t = 1; t < NT; ++t) {
;       __builtin_amdgcn_s_setprio(1); QKT(sx); PV8(sx); sx = NEXT3(sx);
;       if (t + 2 <= NT) { ISSUE_L(t + 2, si); si = NEXT3(si); }
;       __builtin_amdgcn_s_setprio(0);
;       PBAR();
;       YPH(); if (t + 2 < NT) PBAR_V3(); else PBAR_V0();
.LBB0_1303:
	v_exp_f32_e32 v114, v114
	v_exp_f32_e32 v115, v115
	v_exp_f32_e32 v118, v118
	v_exp_f32_e32 v119, v119
	v_exp_f32_e32 v122, v122
	v_exp_f32_e32 v123, v123
	v_exp_f32_e32 v126, v126
	v_exp_f32_e32 v127, v127
	v_exp_f32_e32 v130, v130
	v_exp_f32_e32 v131, v131
	v_exp_f32_e32 v134, v134
	v_exp_f32_e32 v135, v135
	v_exp_f32_e32 v138, v138
	v_exp_f32_e32 v139, v139
	v_exp_f32_e32 v142, v142
	v_exp_f32_e32 v143, v143
	v_exp_f32_e32 v116, v116
	v_exp_f32_e32 v117, v117
	v_exp_f32_e32 v120, v120
	v_exp_f32_e32 v121, v121
	v_exp_f32_e32 v124, v124
	v_exp_f32_e32 v125, v125
	v_exp_f32_e32 v128, v128
	v_exp_f32_e32 v129, v129
	v_exp_f32_e32 v132, v132
	v_exp_f32_e32 v133, v133
	v_exp_f32_e32 v136, v136
	v_exp_f32_e32 v137, v137
	v_exp_f32_e32 v140, v140
	v_exp_f32_e32 v141, v141
	v_exp_f32_e32 v144, v144
	v_exp_f32_e32 v145, v145
	v_cvt_pk_fp8_f32 v170, v114, v115
	v_cvt_pk_fp8_f32 v174, v130, v131
	v_cvt_pk_fp8_f32 v171, v118, v119
	v_cvt_pk_fp8_f32 v175, v134, v135
	v_cvt_pk_fp8_f32 v172, v122, v123
	v_cvt_pk_fp8_f32 v176, v138, v139
	v_cvt_pk_fp8_f32 v173, v126, v127
	v_cvt_pk_fp8_f32 v177, v142, v143
	v_cvt_pk_fp8_f32 v170, v116, v117 op_sel:[0,0,1]
	v_cvt_pk_fp8_f32 v174, v132, v133 op_sel:[0,0,1]
	v_cvt_pk_fp8_f32 v171, v120, v121 op_sel:[0,0,1]
	v_cvt_pk_fp8_f32 v175, v136, v137 op_sel:[0,0,1]
	v_cvt_pk_fp8_f32 v172, v124, v125 op_sel:[0,0,1]
	v_cvt_pk_fp8_f32 v176, v140, v141 op_sel:[0,0,1]
	v_cvt_pk_fp8_f32 v173, v128, v129 op_sel:[0,0,1]
	v_cvt_pk_fp8_f32 v177, v144, v145 op_sel:[0,0,1]
	s_waitcnt lgkmcnt(0)
	s_barrier
	s_setprio 1
	s_lshl_b32 s0, s28, 13
	v_add_u32_e32 v114, s0, v153
	v_add_u32_e32 v139, v114, v203
	v_add_u32_e32 v138, v114, v202
	ds_read_b128 v[118:121], v139 offset:24576
	ds_read_b128 v[114:117], v138 offset:24576
	v_add_u32_e32 v141, s0, v150
	v_add_u32_e32 v140, s0, v149
	v_mfma_scale_f32_32x32x64_f8f6f4 v[66:81], v[170:177], v[162:169], v[66:81], v187, v187 op_sel_hi:[0,0,0]
	s_add_i32 s0, s28, 1
	s_cmp_lg_u32 s28, 2
	s_cselect_b32 s28, s0, 0
	s_add_i32 s0, s47, s72
	s_ashr_i32 s1, s0, 31
	s_lshl_b64 s[0:1], s[0:1], 10
	s_add_u32 s0, s59, s0
	s_addc_u32 s1, s60, s1
	s_lshl_b32 s12, s67, 13
	s_add_i32 s13, s12, s57
	s_add_u32 s26, s26, 0x2000
	s_addc_u32 s27, s27, 0
	s_add_i32 s12, s12, s58
	s_waitcnt lgkmcnt(0)
	v_mfma_scale_f32_32x32x64_f8f6f4 v[114:129], v[114:121], v[154:161], v[98:113], v187, v187 op_sel_hi:[0,0,0]
	ds_read_b128 v[134:137], v141
	ds_read_b128 v[130:133], v140
	s_waitcnt lgkmcnt(0)
	v_mfma_scale_f32_32x32x64_f8f6f4 v[2:17], v[170:177], v[130:137], v[2:17], v187, v187 op_sel_hi:[0,0,0]
	ds_read_b128 v[130:133], v140 offset:2048
	ds_read_b128 v[134:137], v141 offset:2048
	s_waitcnt lgkmcnt(0)
	v_mfma_scale_f32_32x32x64_f8f6f4 v[18:33], v[170:177], v[130:137], v[18:33], v187, v187 op_sel_hi:[0,0,0]
	ds_read_b128 v[134:137], v141 offset:4096
	ds_read_b128 v[130:133], v140 offset:4096
	s_waitcnt lgkmcnt(0)
	v_mfma_scale_f32_32x32x64_f8f6f4 v[34:49], v[170:177], v[130:137], v[34:49], v187, v187 op_sel_hi:[0,0,0]
	ds_read_b128 v[130:133], v140 offset:6144
	ds_read_b128 v[134:137], v141 offset:6144
	s_waitcnt lgkmcnt(0)
	v_mfma_scale_f32_32x32x64_f8f6f4 v[50:65], v[170:177], v[130:137], v[50:65], v187, v187 op_sel_hi:[0,0,0]
	ds_read_b128 v[130:133], v138 offset:28672
	ds_read_b128 v[134:137], v139 offset:28672
	s_waitcnt lgkmcnt(0)
	v_mfma_scale_f32_32x32x64_f8f6f4 v[130:145], v[130:137], v[154:161], v[98:113], v187, v187 op_sel_hi:[0,0,0]
	s_mov_b32 m0, s13
	s_nop 0
	global_load_lds_dwordx4 v148, s[0:1]
	s_mov_b32 m0, s12
	s_nop 0
	global_load_lds_dwordx4 v147, s[26:27]
	s_add_i32 s0, s67, 1
	s_cmp_lg_u32 s67, 2
	s_cselect_b32 s67, s0, 0
	s_setprio 0
	s_waitcnt vmcnt(2) lgkmcnt(0)
	s_barrier
	s_add_i32 s72, s72, 64
	s_cmpk_eq_i32 s72, 0x2000
	s_cbranch_scc1 .LBB0_1308

; #define ISSUE_L(t, so) do { const unsigned so_ = (unsigned)(so); \
;     if ((t) < NT) { const char* kb_ = Kh + KROWB(t); pg8::glds16_s(kb_, koff[0], ldsK + so_); pg8::glds16_s(kb_, koff[1], ldsK + so_ + 1024u); } \
;     if ((t) >= 1) { const char* vb_ = Vh + KROWB((t) - 1); pg8::glds16_s(vb_, voff[0], ldsV + so_); pg8::glds16_s(vb_, voff[1], ldsV + so_ + 1024u); } } while (0)
; #define PBAR() asm volatile("s_waitcnt lgkmcnt(0)\n\ts_barrier" ::: "memory")
; #define PBAR_V0() asm volatile("s_waitcnt vmcnt(0) lgkmcnt(0)\n\ts_barrier" ::: "memory")
; #define YPH() YSOFT(false)
; #define ISSUE_L(t, sl) do { \
;     if ((t) < NT) pg8::glds16_s(Kh + KROWB(t), koff, ldsK + (unsigned)(sl) * 8192u); \
;     if ((t) >= 1 && (t) <= NT) pg8::glds16_s((const char*)V8 + (size_t)((t) - 1) * 8192, voff, ldsV + (unsigned)(sl) * 8192u); } while (0)
; #define PBAR() asm volatile("s_waitcnt lgkmcnt(0)\n\ts_barrier" ::: "memory")
; #define PBAR_V0() asm volatile("s_waitcnt vmcnt(0) lgkmcnt(0)\n\ts_barrier" ::: "memory")
; #define PBAR_V3() asm volatile("s_waitcnt vmcnt(2) lgkmcnt(0)\n\ts_barrier" ::: "memory")
; #define YPH() YSOFT(false)
; __device__ __forceinline__ void attn_unit_f8(const bf16_t* __restrict__ Q, const bf16_t* __restrict__ Kb, const unsigned char* __restrict__ V8, bf16_t* __restrict__ O, ...
;     ...
;   if (!pref_in) { ISSUE_L(0, 0); ISSUE_L(1, 1); PBAR_V3(); }
;   else PBAR_V0();
;   int sx = 1, si = 2;
;   if (cq == 0) {
;     QKT(0); ISSUE_L(2, si); si = NEXT3(si); PBAR();
;     YSOFT(true); PBAR_V3();
;     for (int t = 1; t < NT; ++t) {
;       __builtin_amdgcn_s_setprio(1); QKT(sx); PV8(sx); sx = NEXT3(sx);
;       if (t + 2 <= NT) { ISSUE_L(t + 2, si); si = NEXT3(si); }
;       __builtin_amdgcn_s_setprio(0);
;       PBAR();
;       YPH(); if (t + 2 < NT) PBAR_V3(); else PBAR_V0();
.LBB0_1314:
	v_exp_f32_e32 v114, v114
	v_exp_f32_e32 v115, v115
	v_exp_f32_e32 v118, v118
	v_exp_f32_e32 v119, v119
	v_exp_f32_e32 v122, v122
	v_exp_f32_e32 v123, v123
	v_exp_f32_e32 v126, v126
	v_exp_f32_e32 v127, v127
	v_exp_f32_e32 v130, v130
	v_exp_f32_e32 v131, v131
	v_exp_f32_e32 v134, v134
	v_exp_f32_e32 v135, v135
	v_exp_f32_e32 v138, v138
	v_exp_f32_e32 v139, v139
	v_exp_f32_e32 v142, v142
	v_exp_f32_e32 v143, v143
	v_exp_f32_e32 v116, v116
	v_exp_f32_e32 v117, v117
	v_exp_f32_e32 v120, v120
	v_exp_f32_e32 v121, v121
	v_exp_f32_e32 v124, v124
	v_exp_f32_e32 v125, v125
	v_exp_f32_e32 v128, v128
	v_exp_f32_e32 v129, v129
	v_exp_f32_e32 v132, v132
	v_exp_f32_e32 v133, v133
	v_exp_f32_e32 v136, v136
	v_exp_f32_e32 v137, v137
	v_exp_f32_e32 v140, v140
	v_exp_f32_e32 v141, v141
	v_exp_f32_e32 v144, v144
	v_exp_f32_e32 v145, v145
	v_cvt_pk_fp8_f32 v170, v114, v115
	v_cvt_pk_fp8_f32 v174, v130, v131
	v_cvt_pk_fp8_f32 v171, v118, v119
	v_cvt_pk_fp8_f32 v175, v134, v135
	v_cvt_pk_fp8_f32 v172, v122, v123
	v_cvt_pk_fp8_f32 v176, v138, v139
	v_cvt_pk_fp8_f32 v173, v126, v127
	v_cvt_pk_fp8_f32 v177, v142, v143
	v_cvt_pk_fp8_f32 v170, v116, v117 op_sel:[0,0,1]
	v_cvt_pk_fp8_f32 v174, v132, v133 op_sel:[0,0,1]
	v_cvt_pk_fp8_f32 v171, v120, v121 op_sel:[0,0,1]
	v_cvt_pk_fp8_f32 v175, v136, v137 op_sel:[0,0,1]
	v_cvt_pk_fp8_f32 v172, v124, v125 op_sel:[0,0,1]
	v_cvt_pk_fp8_f32 v176, v140, v141 op_sel:[0,0,1]
	v_cvt_pk_fp8_f32 v173, v128, v129 op_sel:[0,0,1]
	v_cvt_pk_fp8_f32 v177, v144, v145 op_sel:[0,0,1]
	s_waitcnt lgkmcnt(0)
	s_barrier
	s_setprio 1
	s_lshl_b32 s0, s28, 13
	s_add_i32 s1, s0, 0
	v_add_u32_e32 v114, s1, v152
	v_add_u32_e32 v139, v114, v203
	v_add_u32_e32 v138, v114, v202
	ds_read_b128 v[118:121], v139 offset:24576
	ds_read_b128 v[114:117], v138 offset:24576
	v_add_u32_e32 v141, s0, v150
	v_add_u32_e32 v140, s0, v149
	v_mfma_scale_f32_32x32x64_f8f6f4 v[66:81], v[170:177], v[162:169], v[66:81], v187, v187 op_sel_hi:[0,0,0]
	s_lshl_b32 s12, s67, 13
	s_add_u32 s0, s82, 0x106000
	s_addc_u32 s1, s83, 0
	s_add_i32 s12, s12, s58
	s_waitcnt lgkmcnt(0)
	v_mfma_scale_f32_32x32x64_f8f6f4 v[114:129], v[114:121], v[154:161], v[98:113], v187, v187 op_sel_hi:[0,0,0]
	ds_read_b128 v[134:137], v141
	ds_read_b128 v[130:133], v140
	s_waitcnt lgkmcnt(0)
	v_mfma_scale_f32_32x32x64_f8f6f4 v[2:17], v[170:177], v[130:137], v[2:17], v187, v187 op_sel_hi:[0,0,0]
	ds_read_b128 v[130:133], v140 offset:2048
	ds_read_b128 v[134:137], v141 offset:2048
	s_waitcnt lgkmcnt(0)
	v_mfma_scale_f32_32x32x64_f8f6f4 v[18:33], v[170:177], v[130:137], v[18:33], v187, v187 op_sel_hi:[0,0,0]
	ds_read_b128 v[134:137], v141 offset:4096
	ds_read_b128 v[130:133], v140 offset:4096
	s_waitcnt lgkmcnt(0)
	v_mfma_scale_f32_32x32x64_f8f6f4 v[34:49], v[170:177], v[130:137], v[34:49], v187, v187 op_sel_hi:[0,0,0]
	ds_read_b128 v[130:133], v140 offset:6144
	ds_read_b128 v[134:137], v141 offset:6144
	s_waitcnt lgkmcnt(0)
	v_mfma_scale_f32_32x32x64_f8f6f4 v[50:65], v[170:177], v[130:137], v[50:65], v187, v187 op_sel_hi:[0,0,0]
	ds_read_b128 v[130:133], v138 offset:28672
	ds_read_b128 v[134:137], v139 offset:28672
	s_waitcnt lgkmcnt(0)
	v_mfma_scale_f32_32x32x64_f8f6f4 v[130:145], v[130:137], v[154:161], v[98:113], v187, v187 op_sel_hi:[0,0,0]
	s_mov_b32 m0, s12
	s_nop 0
	global_load_lds_dwordx4 v147, s[0:1]
	s_setprio 0
	v_max_f32_e32 v205, v115, v115
	v_max_f32_e32 v206, v114, v114
	v_max_f32_e32 v205, v206, v205
	s_nop 15
	v_max3_f32 v206, v116, v117, v131
	v_max3_f32 v205, v205, v130, v132
	v_max3_f32 v205, v205, v133, v118
	v_max3_f32 v206, v206, v120, v121
	v_max3_f32 v205, v205, v119, v134
	v_max3_f32 v206, v206, v136, v137
	v_max3_f32 v205, v205, v135, v122
	v_max3_f32 v206, v206, v124, v125
	v_max3_f32 v205, v205, v123, v138
	v_max3_f32 v206, v206, v140, v141
	v_max3_f32 v205, v205, v139, v126
	v_max3_f32 v206, v206, v128, v129
	v_max3_f32 v205, v205, v127, v142
	v_max3_f32 v206, v206, v144, v145
	v_max3_f32 v205, v205, v143, v206
	v_mov_b32_e32 v206, v205
	s_nop 1
	v_permlane32_swap_b32_e32 v205, v206
	s_waitcnt vmcnt(0) lgkmcnt(0)
	s_barrier
	v_max_f32_e32 v206, v206, v206
	v_max_f32_e32 v205, v205, v205
	v_max_f32_e32 v205, v205, v206
	v_cmp_lt_f32_e32 vcc, s69, v205
	s_cbranch_vccz .LBB0_1320
	v_add_f32_e32 v98, 0xc0c00000, v205
	v_max_f32_e32 v205, 0, v98
	v_exp_f32_e64 v206, -v205
	v_add_f32_e32 v201, v201, v205
	v_xor_b32_e32 v98, 0x80000000, v201
	v_mov_b32_e32 v99, v98
	v_mov_b32_e32 v100, v98
	v_mov_b32_e32 v101, v98
	v_mov_b32_e32 v102, v98
	v_mov_b32_e32 v103, v98
	v_mov_b32_e32 v104, v98
	v_mov_b32_e32 v105, v98
	v_mov_b32_e32 v106, v98
	v_mov_b32_e32 v107, v98
	v_mov_b32_e32 v108, v98
	v_mov_b32_e32 v109, v98
	v_mov_b32_e32 v110, v98
	v_mov_b32_e32 v111, v98
	v_mov_b32_e32 v112, v98
	v_mov_b32_e32 v113, v98
	v_cmp_gt_f32_e32 vcc, 1.0, v206
	s_cbranch_vccz .LBB0_1319
	s_and_saveexec_b64 s[0:1], s[2:3]
	ds_write_b32 v151, v206 offset:49280
	s_or_b64 exec, exec, s[0:1]
	s_waitcnt lgkmcnt(0)
	v_add_u32_e32 v218, s66, v204
	ds_read_b128 v[206:209], v218 offset:49376
	ds_read_b128 v[210:213], v218 offset:49344
	ds_read_b128 v[214:217], v218 offset:49312
	ds_read_b128 v[218:221], v218 offset:49280
	s_waitcnt lgkmcnt(3)
	v_pk_mul_f32 v[14:15], v[14:15], v[206:207]
	s_waitcnt lgkmcnt(2)
	v_pk_mul_f32 v[10:11], v[10:11], v[210:211]
	s_waitcnt lgkmcnt(1)
	v_pk_mul_f32 v[6:7], v[6:7], v[214:215]
	v_pk_mul_f32 v[16:17], v[16:17], v[208:209]
	v_pk_mul_f32 v[12:13], v[12:13], v[212:213]
	v_pk_mul_f32 v[8:9], v[8:9], v[216:217]
	s_waitcnt lgkmcnt(0)
	v_pk_mul_f32 v[4:5], v[4:5], v[220:221]
	v_pk_mul_f32 v[2:3], v[2:3], v[218:219]
	v_pk_mul_f32 v[30:31], v[30:31], v[206:207]
	v_pk_mul_f32 v[26:27], v[26:27], v[210:211]
	v_pk_mul_f32 v[22:23], v[22:23], v[214:215]
	v_pk_mul_f32 v[32:33], v[32:33], v[208:209]
	v_pk_mul_f32 v[28:29], v[28:29], v[212:213]
	v_pk_mul_f32 v[24:25], v[24:25], v[216:217]
	v_pk_mul_f32 v[20:21], v[20:21], v[220:221]
	v_pk_mul_f32 v[18:19], v[18:19], v[218:219]
	v_pk_mul_f32 v[46:47], v[46:47], v[206:207]
	v_pk_mul_f32 v[42:43], v[42:43], v[210:211]
	v_pk_mul_f32 v[38:39], v[38:39], v[214:215]
	v_pk_mul_f32 v[48:49], v[48:49], v[208:209]
	v_pk_mul_f32 v[44:45], v[44:45], v[212:213]
	v_pk_mul_f32 v[40:41], v[40:41], v[216:217]
	v_pk_mul_f32 v[36:37], v[36:37], v[220:221]
	v_pk_mul_f32 v[34:35], v[34:35], v[218:219]
	v_pk_mul_f32 v[62:63], v[62:63], v[206:207]
	v_pk_mul_f32 v[58:59], v[58:59], v[210:211]
	v_pk_mul_f32 v[54:55], v[54:55], v[214:215]
	v_pk_mul_f32 v[64:65], v[64:65], v[208:209]
	v_pk_mul_f32 v[60:61], v[60:61], v[212:213]
	v_pk_mul_f32 v[56:57], v[56:57], v[216:217]
	v_pk_mul_f32 v[52:53], v[52:53], v[220:221]
	v_pk_mul_f32 v[50:51], v[50:51], v[218:219]
	v_pk_mul_f32 v[78:79], v[78:79], v[206:207]
	v_pk_mul_f32 v[74:75], v[74:75], v[210:211]
	v_pk_mul_f32 v[70:71], v[70:71], v[214:215]
	v_pk_mul_f32 v[80:81], v[80:81], v[208:209]
	v_pk_mul_f32 v[76:77], v[76:77], v[212:213]
	v_pk_mul_f32 v[72:73], v[72:73], v[216:217]
	v_pk_mul_f32 v[68:69], v[68:69], v[220:221]
	v_pk_mul_f32 v[66:67], v[66:67], v[218:219]

; #define ISSUE_L(t, so) do { const unsigned so_ = (unsigned)(so); \
;     if ((t) < NT) { const char* kb_ = Kh + KROWB(t); pg8::glds16_s(kb_, koff[0], ldsK + so_); pg8::glds16_s(kb_, koff[1], ldsK + so_ + 1024u); } \
;     if ((t) >= 1) { const char* vb_ = Vh + KROWB((t) - 1); pg8::glds16_s(vb_, voff[0], ldsV + so_); pg8::glds16_s(vb_, voff[1], ldsV + so_ + 1024u); } } while (0)
; #define PBAR() asm volatile("s_waitcnt lgkmcnt(0)\n\ts_barrier" ::: "memory")
; #define ISSUE_L(t, sl) do { \
;     if ((t) < NT) pg8::glds16_s(Kh + KROWB(t), koff, ldsK + (unsigned)(sl) * 8192u); \
;     if ((t) >= 1 && (t) <= NT) pg8::glds16_s((const char*)V8 + (size_t)((t) - 1) * 8192, voff, ldsV + (unsigned)(sl) * 8192u); } while (0)
; #define PBAR() asm volatile("s_waitcnt lgkmcnt(0)\n\ts_barrier" ::: "memory")
; #define PBAR_V3() asm volatile("s_waitcnt vmcnt(2) lgkmcnt(0)\n\ts_barrier" ::: "memory")
; __device__ __forceinline__ void attn_unit_f8(const bf16_t* __restrict__ Q, const bf16_t* __restrict__ Kb, const unsigned char* __restrict__ V8, bf16_t* __restrict__ O, ...
;     ...
;     ISSUE_L(2, si); si = NEXT3(si); PBAR();
;     QKT(0); PBAR_V3();
;     YSOFT(true); PBAR();
.LBB0_1327:
	s_and_b64 vcc, exec, s[0:1]
	s_cbranch_vccz .LBB0_1355
	s_nop 5
	v_or_b32_e32 v2, 1, v199
	v_lshrrev_b32_e32 v4, 1, v179
	v_bitop3_b32 v2, v2, v4, 7 bitop3:0x78
	v_add_u32_e32 v3, v200, v198
	v_bitop3_b32 v5, v199, v4, 7 bitop3:0x78
	v_lshlrev_b32_e32 v140, 4, v2
	v_lshlrev_b32_e32 v139, 4, v5
	v_add_u32_e32 v27, v3, v140
	v_add_u32_e32 v26, v3, v139
	ds_read_b128 v[6:9], v27 offset:24576
	ds_read_b128 v[2:5], v26 offset:24576
	ds_read_b128 v[18:21], v26 offset:28672
	ds_read_b128 v[22:25], v27 offset:28672
	s_waitcnt vmcnt(0) lgkmcnt(2)
	v_mfma_scale_f32_32x32x64_f8f6f4 v[2:17], v[2:9], v[154:161], v[82:97], v187, v187 op_sel_hi:[0,0,0]
	s_or_b32 s0, s84, 0x80
	s_ashr_i32 s1, s0, 31
	s_lshl_b64 s[0:1], s[0:1], 10
	s_add_u32 s0, s59, s0
	s_addc_u32 s1, s60, s1
	s_cmp_lg_u32 s56, -1
	s_cselect_b32 s2, s56, 0
	s_add_i32 s2, s2, s55
	s_addk_i32 s2, 0x4000
	s_mov_b32 m0, s2
	s_nop 0
	global_load_lds_dwordx4 v148, s[0:1]
	s_add_u32 s0, s82, 0x2000
	v_mov_b32_e32 v130, v1
	v_mov_b32_e32 v134, v1
	v_mov_b32_e32 v131, v1
	v_mov_b32_e32 v135, v1
	s_waitcnt lgkmcnt(0)
	v_mfma_scale_f32_32x32x64_f8f6f4 v[82:97], v[18:25], v[154:161], v[82:97], v187, v187 op_sel_hi:[0,0,0]
	s_nop 3
	v_max_f32_e32 v18, v3, v3
	v_max_f32_e32 v19, v2, v2
	v_max_f32_e32 v18, v19, v18
	v_mov_b32_e32 v132, v1
	v_mov_b32_e32 v136, v1
	v_mov_b32_e32 v133, v1
	v_mov_b32_e32 v137, v1
	s_addc_u32 s1, s83, 0
	s_cmp_lg_u32 0, -1
	s_cselect_b32 s2, 0, 0
	s_add_i32 s2, s2, s55
	s_addk_i32 s2, 0x4000
	s_mov_b32 m0, s2
	s_nop 0
	global_load_lds_dwordx4 v147, s[0:1]
	s_waitcnt lgkmcnt(0)
	s_barrier
	v_lshlrev_b32_e32 v141, 2, v0
	s_nop 2
	v_max3_f32 v19, v4, v5, v83
	v_max3_f32 v18, v18, v82, v84
	v_max3_f32 v18, v18, v85, v6
	v_max3_f32 v19, v19, v8, v9
	v_max3_f32 v18, v18, v7, v86
	v_max3_f32 v19, v19, v88, v89
	v_max3_f32 v18, v18, v87, v10
	v_max3_f32 v19, v19, v12, v13
	v_max3_f32 v18, v18, v11, v90
	v_max3_f32 v19, v19, v92, v93
	v_max3_f32 v18, v18, v91, v14
	v_max3_f32 v19, v19, v16, v17
	v_max3_f32 v18, v18, v15, v94
	v_max3_f32 v19, v19, v96, v97
	v_max3_f32 v18, v18, v95, v19
	v_mov_b32_e32 v19, v18
	s_nop 1
	v_permlane32_swap_b32_e32 v18, v19
	v_max_f32_e32 v19, v19, v19
	v_max_f32_e32 v18, v18, v18
	v_max_f32_e32 v18, v18, v19
	v_add_f32_e32 v138, 0xc0c00000, v18
	v_sub_f32_e32 v2, v2, v138
	v_sub_f32_e32 v18, v82, v138
	v_sub_f32_e32 v3, v3, v138
	v_sub_f32_e32 v19, v83, v138
	v_sub_f32_e32 v6, v6, v138
	v_sub_f32_e32 v22, v86, v138
	v_sub_f32_e32 v7, v7, v138
	v_sub_f32_e32 v23, v87, v138
	v_sub_f32_e32 v10, v10, v138
	v_sub_f32_e32 v28, v90, v138
	v_sub_f32_e32 v11, v11, v138
	v_sub_f32_e32 v29, v91, v138
	v_sub_f32_e32 v14, v14, v138
	v_sub_f32_e32 v32, v94, v138
	v_sub_f32_e32 v15, v15, v138
	v_sub_f32_e32 v33, v95, v138
	v_exp_f32_e32 v2, v2
	v_exp_f32_e32 v3, v3
	v_exp_f32_e32 v6, v6
	v_exp_f32_e32 v7, v7
	v_exp_f32_e32 v10, v10
	v_exp_f32_e32 v11, v11
	v_exp_f32_e32 v14, v14
	v_exp_f32_e32 v15, v15
	v_exp_f32_e32 v18, v18
	v_exp_f32_e32 v19, v19
	v_exp_f32_e32 v22, v22
	v_exp_f32_e32 v23, v23
	v_exp_f32_e32 v28, v28
	v_exp_f32_e32 v29, v29
	v_exp_f32_e32 v32, v32
	v_exp_f32_e32 v33, v33
	v_sub_f32_e32 v4, v4, v138
	v_sub_f32_e32 v20, v84, v138
	v_sub_f32_e32 v5, v5, v138
	v_sub_f32_e32 v21, v85, v138
	v_sub_f32_e32 v8, v8, v138
	v_sub_f32_e32 v24, v88, v138
	v_sub_f32_e32 v9, v9, v138
	v_sub_f32_e32 v25, v89, v138
	v_sub_f32_e32 v12, v12, v138
	v_sub_f32_e32 v30, v92, v138
	v_sub_f32_e32 v13, v13, v138
	v_sub_f32_e32 v31, v93, v138
	v_sub_f32_e32 v16, v16, v138
	v_sub_f32_e32 v34, v96, v138
	v_sub_f32_e32 v17, v17, v138
	v_sub_f32_e32 v35, v97, v138
	v_exp_f32_e32 v4, v4
	v_exp_f32_e32 v5, v5
	v_exp_f32_e32 v8, v8
	v_exp_f32_e32 v9, v9
	v_exp_f32_e32 v12, v12
	v_exp_f32_e32 v13, v13
	v_exp_f32_e32 v16, v16
	v_exp_f32_e32 v17, v17
	v_exp_f32_e32 v20, v20
	v_exp_f32_e32 v21, v21
	v_exp_f32_e32 v24, v24
	v_exp_f32_e32 v25, v25
	v_exp_f32_e32 v30, v30
	v_exp_f32_e32 v31, v31
	v_exp_f32_e32 v34, v34
	v_exp_f32_e32 v35, v35
	v_cvt_pk_fp8_f32 v130, v2, v3
	v_cvt_pk_fp8_f32 v134, v18, v19
	v_cvt_pk_fp8_f32 v131, v6, v7
	v_cvt_pk_fp8_f32 v135, v22, v23
	v_cvt_pk_fp8_f32 v132, v10, v11
	v_cvt_pk_fp8_f32 v136, v28, v29
	v_cvt_pk_fp8_f32 v133, v14, v15
	v_cvt_pk_fp8_f32 v137, v32, v33
	v_xor_b32_e32 v82, 0x80000000, v138
	v_mov_b32_e32 v83, v82
	v_mov_b32_e32 v84, v82
	v_mov_b32_e32 v85, v82
	v_mov_b32_e32 v86, v82
	v_mov_b32_e32 v87, v82
	v_mov_b32_e32 v88, v82
	v_mov_b32_e32 v89, v82
	v_mov_b32_e32 v90, v82
	v_mov_b32_e32 v91, v82
	v_mov_b32_e32 v92, v82
	v_mov_b32_e32 v93, v82
	v_mov_b32_e32 v94, v82
	v_mov_b32_e32 v95, v82
	v_mov_b32_e32 v96, v82
	v_mov_b32_e32 v97, v82
	v_cvt_pk_fp8_f32 v130, v4, v5 op_sel:[0,0,1]
	v_cvt_pk_fp8_f32 v134, v20, v21 op_sel:[0,0,1]
	v_cvt_pk_fp8_f32 v131, v8, v9 op_sel:[0,0,1]
	v_cvt_pk_fp8_f32 v135, v24, v25 op_sel:[0,0,1]
	v_cvt_pk_fp8_f32 v132, v12, v13 op_sel:[0,0,1]
	v_cvt_pk_fp8_f32 v136, v30, v31 op_sel:[0,0,1]
	v_cvt_pk_fp8_f32 v133, v16, v17 op_sel:[0,0,1]
	v_cvt_pk_fp8_f32 v137, v34, v35 op_sel:[0,0,1]
	s_waitcnt vmcnt(2) lgkmcnt(0)
	s_barrier
; #define ISSUE_L(t, so) do { const unsigned so_ = (unsigned)(so); \
;     if ((t) < NT) { const char* kb_ = Kh + KROWB(t); pg8::glds16_s(kb_, koff[0], ldsK + so_); pg8::glds16_s(kb_, koff[1], ldsK + so_ + 1024u); } \
;     if ((t) >= 1) { const char* vb_ = Vh + KROWB((t) - 1); pg8::glds16_s(vb_, voff[0], ldsV + so_); pg8::glds16_s(vb_, voff[1], ldsV + so_ + 1024u); } } while (0)
; #define PBAR() asm volatile("s_waitcnt lgkmcnt(0)\n\ts_barrier" ::: "memory")
; #define PBAR_V0() asm volatile("s_waitcnt vmcnt(0) lgkmcnt(0)\n\ts_barrier" ::: "memory")
; #define YPH() YSOFT(false)
; #define ISSUE_L(t, sl) do { \
;     if ((t) < NT) pg8::glds16_s(Kh + KROWB(t), koff, ldsK + (unsigned)(sl) * 8192u); \
;     if ((t) >= 1 && (t) <= NT) pg8::glds16_s((const char*)V8 + (size_t)((t) - 1) * 8192, voff, ldsV + (unsigned)(sl) * 8192u); } while (0)
; #define PBAR() asm volatile("s_waitcnt lgkmcnt(0)\n\ts_barrier" ::: "memory")
; #define PBAR_V0() asm volatile("s_waitcnt vmcnt(0) lgkmcnt(0)\n\ts_barrier" ::: "memory")
; #define PBAR_V3() asm volatile("s_waitcnt vmcnt(2) lgkmcnt(0)\n\ts_barrier" ::: "memory")
; #define YPH() YSOFT(false)
; __device__ __forceinline__ void attn_unit_f8(const bf16_t* __restrict__ Q, const bf16_t* __restrict__ Kb, const unsigned char* __restrict__ V8, bf16_t* __restrict__ O, ...
;     ...
;   f32x16 p0, p1; i32x8 p8 = i32x8{};
;   i32x8 onesf = (i32x8){0x38383838, 0x38383838, 0x38383838, 0x38383838, 0x38383838, 0x38383838, 0x38383838, 0x38383838}; asm volatile("" : "+v"(onesf));
;   f32x16 negm = f32x16{}; asm volatile("" : "+v"(negm));
;   const int scl1 = 0x7F7F7F7F;
;     ...
;     __builtin_amdgcn_s_setprio(1); QKT(sx); PV8(sx); sx = NEXT3(sx); __builtin_amdgcn_s_setprio(0);
;     ISSUE_L(3, si); si = NEXT3(si); if (3 < NT) PBAR_V3(); else PBAR_V0();
;     for (int t = 2; t < NT; ++t) {
;       YPH(); PBAR();
;       __builtin_amdgcn_s_setprio(1); QKT(sx); PV8(sx); sx = NEXT3(sx);
	v_cmp_gt_u32_e64 s[2:3], 32, v181
	s_setprio 1
	ds_read_b128 v[6:9], v27 offset:32768
	ds_read_b128 v[2:5], v26 offset:32768
	ds_read_b128 v[66:69], v26 offset:36864
	ds_read_b128 v[70:73], v27 offset:36864
	s_or_b32 s0, s84, 0xc0
	s_ashr_i32 s1, s0, 31
	s_waitcnt lgkmcnt(2)
	v_mfma_scale_f32_32x32x64_f8f6f4 v[98:113], v[2:9], v[154:161], v[82:97], v187, v187 op_sel_hi:[0,0,0]
	ds_read_b128 v[6:9], v150 offset:8192
	ds_read_b128 v[2:5], v149 offset:8192
	ds_read_b128 v[18:21], v149 offset:10240
	ds_read_b128 v[22:25], v150 offset:10240
	ds_read_b128 v[38:41], v150 offset:12288
	ds_read_b128 v[34:37], v149 offset:12288
	ds_read_b128 v[50:53], v149 offset:14336
	ds_read_b128 v[54:57], v150 offset:14336
	s_lshl_b64 s[0:1], s[0:1], 10
	s_add_u32 s0, s59, s0
	s_addc_u32 s1, s60, s1
	s_waitcnt lgkmcnt(6)
	v_mfma_scale_f32_32x32x64_f8f6f4 v[2:17], v[130:137], v[2:9], 0, v187, v187 op_sel_hi:[0,0,0]
	s_waitcnt lgkmcnt(4)
	v_mfma_scale_f32_32x32x64_f8f6f4 v[18:33], v[130:137], v[18:25], 0, v187, v187 op_sel_hi:[0,0,0]
	s_waitcnt lgkmcnt(2)
	v_mfma_scale_f32_32x32x64_f8f6f4 v[34:49], v[130:137], v[34:41], 0, v187, v187 op_sel_hi:[0,0,0]
	s_waitcnt lgkmcnt(0)
	v_mfma_scale_f32_32x32x64_f8f6f4 v[50:65], v[130:137], v[50:57], 0, v187, v187 op_sel_hi:[0,0,0]
	v_mfma_scale_f32_32x32x64_f8f6f4 v[114:129], v[66:73], v[154:161], v[82:97], v187, v187 op_sel_hi:[0,0,0]
	s_mov_b32 m0, s57
	s_nop 0
	global_load_lds_dwordx4 v148, s[0:1]
	s_add_u32 s0, s82, 0x4000
	s_addc_u32 s1, s83, 0
	s_mov_b32 m0, s58
	s_nop 0
	global_load_lds_dwordx4 v147, s[0:1]
	v_mfma_scale_f32_32x32x64_f8f6f4 v[66:81], v[130:137], v[162:169], 0, v187, v187 op_sel_hi:[0,0,0]
	s_setprio 0
	v_max_f32_e32 v142, v99, v99
	v_max_f32_e32 v143, v98, v98
	v_max_f32_e32 v142, v143, v142
	s_nop 12
	v_max3_f32 v143, v100, v101, v115
	v_max3_f32 v142, v142, v114, v116
	v_max3_f32 v142, v142, v117, v102
	v_max3_f32 v143, v143, v104, v105
	v_max3_f32 v142, v142, v103, v118
	v_max3_f32 v143, v143, v120, v121
	v_max3_f32 v142, v142, v119, v106
	v_max3_f32 v143, v143, v108, v109
	v_max3_f32 v142, v142, v107, v122
	v_max3_f32 v143, v143, v124, v125
	v_max3_f32 v142, v142, v123, v110
	v_max3_f32 v143, v143, v112, v113
	v_max3_f32 v142, v142, v111, v126
	v_max3_f32 v143, v143, v128, v129
	v_max3_f32 v142, v142, v127, v143
	v_mov_b32_e32 v143, v142
	s_nop 1
	v_permlane32_swap_b32_e32 v142, v143
	s_waitcnt lgkmcnt(0)
	s_barrier
	v_max_f32_e32 v143, v143, v143
	v_max_f32_e32 v142, v142, v142
	v_max_f32_e32 v142, v142, v143
	v_cmp_lt_f32_e32 vcc, s69, v142
	s_cbranch_vccz .LBB0_1334
	v_add_f32_e32 v82, 0xc0c00000, v142
	v_max_f32_e32 v142, 0, v82
	v_exp_f32_e64 v143, -v142
	v_add_f32_e32 v138, v138, v142
	v_xor_b32_e32 v82, 0x80000000, v138
	v_mov_b32_e32 v83, v82
	v_mov_b32_e32 v84, v82
	v_mov_b32_e32 v85, v82
	v_mov_b32_e32 v86, v82
	v_mov_b32_e32 v87, v82
	v_mov_b32_e32 v88, v82
	v_mov_b32_e32 v89, v82
	v_mov_b32_e32 v90, v82
	v_mov_b32_e32 v91, v82
	v_mov_b32_e32 v92, v82
	v_mov_b32_e32 v93, v82
	v_mov_b32_e32 v94, v82
	v_mov_b32_e32 v95, v82
	v_mov_b32_e32 v96, v82
	v_mov_b32_e32 v97, v82
	v_cmp_gt_f32_e32 vcc, 1.0, v143
	s_cbranch_vccz .LBB0_1333
	s_and_saveexec_b64 s[0:1], s[2:3]
	ds_write_b32 v151, v143 offset:49280
	s_or_b64 exec, exec, s[0:1]
	s_waitcnt lgkmcnt(0)
	v_lshl_add_u32 v143, v141, 2, s66
	ds_read_b128 v[170:173], v143 offset:49376
	ds_read_b128 v[174:177], v143 offset:49344
	ds_read_b128 v[198:201], v143 offset:49312
	ds_read_b128 v[202:205], v143 offset:49280
	s_waitcnt lgkmcnt(3)
	v_pk_mul_f32 v[16:17], v[16:17], v[172:173]
	s_waitcnt lgkmcnt(2)
	v_pk_mul_f32 v[12:13], v[12:13], v[176:177]
	s_waitcnt lgkmcnt(1)
	v_pk_mul_f32 v[8:9], v[8:9], v[200:201]
	s_waitcnt lgkmcnt(0)
	v_pk_mul_f32 v[4:5], v[4:5], v[204:205]
	v_pk_mul_f32 v[14:15], v[14:15], v[170:171]
	v_pk_mul_f32 v[10:11], v[10:11], v[174:175]
	v_pk_mul_f32 v[6:7], v[6:7], v[198:199]
	v_pk_mul_f32 v[2:3], v[2:3], v[202:203]
	v_pk_mul_f32 v[32:33], v[32:33], v[172:173]
	v_pk_mul_f32 v[28:29], v[28:29], v[176:177]
	v_pk_mul_f32 v[24:25], v[24:25], v[200:201]
	v_pk_mul_f32 v[20:21], v[20:21], v[204:205]
	v_pk_mul_f32 v[30:31], v[30:31], v[170:171]
	v_pk_mul_f32 v[26:27], v[26:27], v[174:175]
	v_pk_mul_f32 v[22:23], v[22:23], v[198:199]
	v_pk_mul_f32 v[18:19], v[18:19], v[202:203]
	v_pk_mul_f32 v[48:49], v[48:49], v[172:173]
	v_pk_mul_f32 v[44:45], v[44:45], v[176:177]
	v_pk_mul_f32 v[40:41], v[40:41], v[200:201]
	v_pk_mul_f32 v[36:37], v[36:37], v[204:205]
	v_pk_mul_f32 v[46:47], v[46:47], v[170:171]
	v_pk_mul_f32 v[42:43], v[42:43], v[174:175]
	v_pk_mul_f32 v[38:39], v[38:39], v[198:199]
	v_pk_mul_f32 v[34:35], v[34:35], v[202:203]
	v_pk_mul_f32 v[64:65], v[64:65], v[172:173]
	v_pk_mul_f32 v[60:61], v[60:61], v[176:177]
	v_pk_mul_f32 v[56:57], v[56:57], v[200:201]
	v_pk_mul_f32 v[52:53], v[52:53], v[204:205]
	v_pk_mul_f32 v[62:63], v[62:63], v[170:171]
	v_pk_mul_f32 v[58:59], v[58:59], v[174:175]
	v_pk_mul_f32 v[54:55], v[54:55], v[198:199]
	v_pk_mul_f32 v[50:51], v[50:51], v[202:203]
	v_pk_mul_f32 v[80:81], v[80:81], v[172:173]
	v_pk_mul_f32 v[76:77], v[76:77], v[176:177]
	v_pk_mul_f32 v[72:73], v[72:73], v[200:201]
	v_pk_mul_f32 v[68:69], v[68:69], v[204:205]
	v_pk_mul_f32 v[78:79], v[78:79], v[170:171]
	v_pk_mul_f32 v[74:75], v[74:75], v[174:175]
	v_pk_mul_f32 v[70:71], v[70:71], v[198:199]
	v_pk_mul_f32 v[66:67], v[66:67], v[202:203]

; #define ISSUE_L(t, so) do { const unsigned so_ = (unsigned)(so); \
;     if ((t) < NT) { const char* kb_ = Kh + KROWB(t); pg8::glds16_s(kb_, koff[0], ldsK + so_); pg8::glds16_s(kb_, koff[1], ldsK + so_ + 1024u); } \
;     if ((t) >= 1) { const char* vb_ = Vh + KROWB((t) - 1); pg8::glds16_s(vb_, voff[0], ldsV + so_); pg8::glds16_s(vb_, voff[1], ldsV + so_ + 1024u); } } while (0)
; #define PBAR() asm volatile("s_waitcnt lgkmcnt(0)\n\ts_barrier" ::: "memory")
; #define PBAR_V0() asm volatile("s_waitcnt vmcnt(0) lgkmcnt(0)\n\ts_barrier" ::: "memory")
; #define YPH() YSOFT(false)
; #define ISSUE_L(t, sl) do { \
;     if ((t) < NT) pg8::glds16_s(Kh + KROWB(t), koff, ldsK + (unsigned)(sl) * 8192u); \
;     if ((t) >= 1 && (t) <= NT) pg8::glds16_s((const char*)V8 + (size_t)((t) - 1) * 8192, voff, ldsV + (unsigned)(sl) * 8192u); } while (0)
; #define PBAR() asm volatile("s_waitcnt lgkmcnt(0)\n\ts_barrier" ::: "memory")
; #define PBAR_V0() asm volatile("s_waitcnt vmcnt(0) lgkmcnt(0)\n\ts_barrier" ::: "memory")
; #define PBAR_V3() asm volatile("s_waitcnt vmcnt(2) lgkmcnt(0)\n\ts_barrier" ::: "memory")
; #define YPH() YSOFT(false)
; __device__ __forceinline__ void attn_unit_f8(const bf16_t* __restrict__ Q, const bf16_t* __restrict__ Kb, const unsigned char* __restrict__ V8, bf16_t* __restrict__ O, ...
;     ...
;     for (int t = 2; t < NT; ++t) {
;       YPH(); PBAR();
;       __builtin_amdgcn_s_setprio(1); QKT(sx); PV8(sx); sx = NEXT3(sx);
;       if (t + 2 <= NT) { ISSUE_L(t + 2, si); si = NEXT3(si); }
;       __builtin_amdgcn_s_setprio(0);
;       if (t + 2 < NT) PBAR_V3(); else PBAR_V0();
;     }
.LBB0_1338:
	s_setprio 1
	s_lshl_b32 s0, s26, 13
	v_add_u32_e32 v98, s0, v153
	v_add_u32_e32 v123, v98, v140
	v_add_u32_e32 v122, v98, v139
	ds_read_b128 v[102:105], v123 offset:24576
	ds_read_b128 v[98:101], v122 offset:24576
	v_add_u32_e32 v125, s0, v150
	v_add_u32_e32 v124, s0, v149
	v_mfma_scale_f32_32x32x64_f8f6f4 v[66:81], v[130:137], v[162:169], v[66:81], v187, v187 op_sel_hi:[0,0,0]
	s_add_i32 s0, s28, s64
	s_ashr_i32 s1, s0, 31
	s_lshl_b64 s[0:1], s[0:1], 10
	s_add_u32 s0, s59, s0
	s_addc_u32 s1, s60, s1
	s_lshl_b32 s12, s27, 13
	s_add_i32 s13, s12, s57
	s_waitcnt lgkmcnt(0)
	v_mfma_scale_f32_32x32x64_f8f6f4 v[98:113], v[98:105], v[154:161], v[82:97], v187, v187 op_sel_hi:[0,0,0]
	ds_read_b128 v[118:121], v125
	ds_read_b128 v[114:117], v124
	s_waitcnt lgkmcnt(0)
	v_mfma_scale_f32_32x32x64_f8f6f4 v[2:17], v[130:137], v[114:121], v[2:17], v187, v187 op_sel_hi:[0,0,0]
	ds_read_b128 v[114:117], v124 offset:2048
	ds_read_b128 v[118:121], v125 offset:2048
	s_waitcnt lgkmcnt(0)
	v_mfma_scale_f32_32x32x64_f8f6f4 v[18:33], v[130:137], v[114:121], v[18:33], v187, v187 op_sel_hi:[0,0,0]
	ds_read_b128 v[118:121], v125 offset:4096
	ds_read_b128 v[114:117], v124 offset:4096
	s_waitcnt lgkmcnt(0)
	v_mfma_scale_f32_32x32x64_f8f6f4 v[34:49], v[130:137], v[114:121], v[34:49], v187, v187 op_sel_hi:[0,0,0]
	ds_read_b128 v[114:117], v124 offset:6144
	ds_read_b128 v[118:121], v125 offset:6144
	s_waitcnt lgkmcnt(0)
	v_mfma_scale_f32_32x32x64_f8f6f4 v[50:65], v[130:137], v[114:121], v[50:65], v187, v187 op_sel_hi:[0,0,0]
	ds_read_b128 v[114:117], v122 offset:28672
	ds_read_b128 v[118:121], v123 offset:28672
	s_waitcnt lgkmcnt(0)
	v_mfma_scale_f32_32x32x64_f8f6f4 v[114:129], v[114:121], v[154:161], v[82:97], v187, v187 op_sel_hi:[0,0,0]
	s_mov_b32 m0, s13
	s_nop 0
	global_load_lds_dwordx4 v148, s[0:1]
	s_add_u32 s0, s47, 0x2000
	s_addc_u32 s1, s61, 0
	s_add_i32 s12, s12, s58
	s_mov_b32 m0, s12
	s_nop 0
	global_load_lds_dwordx4 v147, s[0:1]
	s_setprio 0
	v_max_f32_e32 v142, v99, v99
	v_max_f32_e32 v143, v98, v98
	v_max_f32_e32 v142, v143, v142
	s_nop 12
	v_max3_f32 v143, v100, v101, v115
	v_max3_f32 v142, v142, v114, v116
	v_max3_f32 v142, v142, v117, v102
	v_max3_f32 v143, v143, v104, v105
	v_max3_f32 v142, v142, v103, v118
	v_max3_f32 v143, v143, v120, v121
	v_max3_f32 v142, v142, v119, v106
	v_max3_f32 v143, v143, v108, v109
	v_max3_f32 v142, v142, v107, v122
	v_max3_f32 v143, v143, v124, v125
	v_max3_f32 v142, v142, v123, v110
	v_max3_f32 v143, v143, v112, v113
	v_max3_f32 v142, v142, v111, v126
	v_max3_f32 v143, v143, v128, v129
	v_max3_f32 v142, v142, v127, v143
	v_mov_b32_e32 v143, v142
	s_nop 1
	v_permlane32_swap_b32_e32 v142, v143
	s_waitcnt lgkmcnt(0)
	s_barrier
	v_max_f32_e32 v143, v143, v143
	v_max_f32_e32 v142, v142, v142
	v_max_f32_e32 v142, v142, v143
	v_cmp_lt_f32_e32 vcc, s69, v142
	s_cbranch_vccz .LBB0_1337
	v_add_f32_e32 v82, 0xc0c00000, v142
	v_max_f32_e32 v142, 0, v82
	v_exp_f32_e64 v143, -v142
	v_add_f32_e32 v138, v138, v142
	v_xor_b32_e32 v82, 0x80000000, v138
	v_mov_b32_e32 v83, v82
	v_mov_b32_e32 v84, v82
	v_mov_b32_e32 v85, v82
	v_mov_b32_e32 v86, v82
	v_mov_b32_e32 v87, v82
	v_mov_b32_e32 v88, v82
	v_mov_b32_e32 v89, v82
	v_mov_b32_e32 v90, v82
	v_mov_b32_e32 v91, v82
	v_mov_b32_e32 v92, v82
	v_mov_b32_e32 v93, v82
	v_mov_b32_e32 v94, v82
	v_mov_b32_e32 v95, v82
	v_mov_b32_e32 v96, v82
	v_mov_b32_e32 v97, v82
	v_cmp_gt_f32_e32 vcc, 1.0, v143
	s_cbranch_vccz .LBB0_1336
	s_and_saveexec_b64 s[0:1], s[2:3]
	s_cbranch_execz .LBB0_1335
	ds_write_b32 v151, v143 offset:49280
	s_branch .LBB0_1335
; #define ISSUE_L(t, so) do { const unsigned so_ = (unsigned)(so); \
;     if ((t) < NT) { const char* kb_ = Kh + KROWB(t); pg8::glds16_s(kb_, koff[0], ldsK + so_); pg8::glds16_s(kb_, koff[1], ldsK + so_ + 1024u); } \
;     if ((t) >= 1) { const char* vb_ = Vh + KROWB((t) - 1); pg8::glds16_s(vb_, voff[0], ldsV + so_); pg8::glds16_s(vb_, voff[1], ldsV + so_ + 1024u); } } while (0)
; #define PBAR() asm volatile("s_waitcnt lgkmcnt(0)\n\ts_barrier" ::: "memory")
; #define PBAR_V0() asm volatile("s_waitcnt vmcnt(0) lgkmcnt(0)\n\ts_barrier" ::: "memory")
; #define YPH() YSOFT(false)
; #define ISSUE_L(t, sl) do { \
;     if ((t) < NT) pg8::glds16_s(Kh + KROWB(t), koff, ldsK + (unsigned)(sl) * 8192u); \
;     if ((t) >= 1 && (t) <= NT) pg8::glds16_s((const char*)V8 + (size_t)((t) - 1) * 8192, voff, ldsV + (unsigned)(sl) * 8192u); } while (0)
; #define PBAR() asm volatile("s_waitcnt lgkmcnt(0)\n\ts_barrier" ::: "memory")
; #define PBAR_V0() asm volatile("s_waitcnt vmcnt(0) lgkmcnt(0)\n\ts_barrier" ::: "memory")
; #define PBAR_V3() asm volatile("s_waitcnt vmcnt(2) lgkmcnt(0)\n\ts_barrier" ::: "memory")
; #define YPH() YSOFT(false)
; __device__ __forceinline__ void attn_unit_f8(const bf16_t* __restrict__ Q, const bf16_t* __restrict__ Kb, const unsigned char* __restrict__ V8, bf16_t* __restrict__ O, ...
;     ...
;   f32x16 p0, p1; i32x8 p8 = i32x8{};
;   i32x8 onesf = (i32x8){0x38383838, 0x38383838, 0x38383838, 0x38383838, 0x38383838, 0x38383838, 0x38383838, 0x38383838}; asm volatile("" : "+v"(onesf));
;   f32x16 negm = f32x16{}; asm volatile("" : "+v"(negm));
;   const int scl1 = 0x7F7F7F7F;
;     ...
;     for (int t = 2; t < NT; ++t) {
;       YPH(); PBAR();
;       __builtin_amdgcn_s_setprio(1); QKT(sx); PV8(sx); sx = NEXT3(sx);
;       if (t + 2 <= NT) { ISSUE_L(t + 2, si); si = NEXT3(si); }
;       __builtin_amdgcn_s_setprio(0);
;       if (t + 2 < NT) PBAR_V3(); else PBAR_V0();
;     }
;     YPH(); PBAR();
.LBB0_1342:
	s_setprio 1
	s_lshl_b32 s0, s26, 13
	s_add_i32 s1, s0, 0
	v_add_u32_e32 v98, s1, v152
	v_add_u32_e32 v123, v98, v140
	v_add_u32_e32 v122, v98, v139
	ds_read_b128 v[102:105], v123 offset:24576
	ds_read_b128 v[98:101], v122 offset:24576
	v_add_u32_e32 v125, s0, v150
	v_add_u32_e32 v124, s0, v149
	v_mfma_scale_f32_32x32x64_f8f6f4 v[66:81], v[130:137], v[162:169], v[66:81], v187, v187 op_sel_hi:[0,0,0]
	s_lshl_b32 s12, s27, 13
	s_add_u32 s0, s82, 0x106000
	s_addc_u32 s1, s83, 0
	s_add_i32 s12, s12, s58
	s_waitcnt lgkmcnt(0)
	v_mfma_scale_f32_32x32x64_f8f6f4 v[98:113], v[98:105], v[154:161], v[82:97], v187, v187 op_sel_hi:[0,0,0]
	ds_read_b128 v[118:121], v125
	ds_read_b128 v[114:117], v124
	s_waitcnt lgkmcnt(0)
	v_mfma_scale_f32_32x32x64_f8f6f4 v[2:17], v[130:137], v[114:121], v[2:17], v187, v187 op_sel_hi:[0,0,0]
	ds_read_b128 v[114:117], v124 offset:2048
	ds_read_b128 v[118:121], v125 offset:2048
	s_waitcnt lgkmcnt(0)
	v_mfma_scale_f32_32x32x64_f8f6f4 v[18:33], v[130:137], v[114:121], v[18:33], v187, v187 op_sel_hi:[0,0,0]
	ds_read_b128 v[118:121], v125 offset:4096
	ds_read_b128 v[114:117], v124 offset:4096
	s_waitcnt lgkmcnt(0)
	v_mfma_scale_f32_32x32x64_f8f6f4 v[34:49], v[130:137], v[114:121], v[34:49], v187, v187 op_sel_hi:[0,0,0]
	ds_read_b128 v[114:117], v124 offset:6144
	ds_read_b128 v[118:121], v125 offset:6144
	s_waitcnt lgkmcnt(0)
	v_mfma_scale_f32_32x32x64_f8f6f4 v[50:65], v[130:137], v[114:121], v[50:65], v187, v187 op_sel_hi:[0,0,0]
	ds_read_b128 v[114:117], v122 offset:28672
	ds_read_b128 v[118:121], v123 offset:28672
	s_waitcnt lgkmcnt(0)
	v_mfma_scale_f32_32x32x64_f8f6f4 v[114:129], v[114:121], v[154:161], v[82:97], v187, v187 op_sel_hi:[0,0,0]
	s_mov_b32 m0, s12
	s_nop 0
	global_load_lds_dwordx4 v147, s[0:1]
	s_setprio 0
	v_max_f32_e32 v142, v99, v99
	v_max_f32_e32 v143, v98, v98
	v_max_f32_e32 v142, v143, v142
	s_nop 15
	v_max3_f32 v143, v100, v101, v115
	v_max3_f32 v142, v142, v114, v116
	v_max3_f32 v142, v142, v117, v102
	v_max3_f32 v143, v143, v104, v105
	v_max3_f32 v142, v142, v103, v118
	v_max3_f32 v143, v143, v120, v121
	v_max3_f32 v142, v142, v119, v106
	v_max3_f32 v143, v143, v108, v109
	v_max3_f32 v142, v142, v107, v122
	v_max3_f32 v143, v143, v124, v125
	v_max3_f32 v142, v142, v123, v110
	v_max3_f32 v143, v143, v112, v113
	v_max3_f32 v142, v142, v111, v126
	v_max3_f32 v143, v143, v128, v129
	v_max3_f32 v142, v142, v127, v143
	v_mov_b32_e32 v143, v142
	s_nop 1
	v_permlane32_swap_b32_e32 v142, v143
	s_waitcnt lgkmcnt(0)
	s_barrier
	v_max_f32_e32 v143, v143, v143
	v_max_f32_e32 v142, v142, v142
	v_max_f32_e32 v142, v142, v143
	v_cmp_lt_f32_e32 vcc, s69, v142
	s_cbranch_vccz .LBB0_1348
	v_add_f32_e32 v82, 0xc0c00000, v142
	v_max_f32_e32 v142, 0, v82
	v_exp_f32_e64 v143, -v142
	v_add_f32_e32 v138, v138, v142
	v_xor_b32_e32 v82, 0x80000000, v138
	v_mov_b32_e32 v83, v82
	v_mov_b32_e32 v84, v82
	v_mov_b32_e32 v85, v82
	v_mov_b32_e32 v86, v82
	v_mov_b32_e32 v87, v82
	v_mov_b32_e32 v88, v82
	v_mov_b32_e32 v89, v82
	v_mov_b32_e32 v90, v82
	v_mov_b32_e32 v91, v82
	v_mov_b32_e32 v92, v82
	v_mov_b32_e32 v93, v82
	v_mov_b32_e32 v94, v82
	v_mov_b32_e32 v95, v82
	v_mov_b32_e32 v96, v82
	v_mov_b32_e32 v97, v82
	v_cmp_gt_f32_e32 vcc, 1.0, v143
	s_cbranch_vccz .LBB0_1347
	s_and_saveexec_b64 s[0:1], s[2:3]
	ds_write_b32 v151, v143 offset:49280
	s_or_b64 exec, exec, s[0:1]
	s_waitcnt lgkmcnt(0)
	ds_read_b128 v[170:173], v141 offset:49376
	ds_read_b128 v[174:177], v141 offset:49344
	ds_read_b128 v[198:201], v141 offset:49312
	ds_read_b128 v[202:205], v141 offset:49280
	s_waitcnt lgkmcnt(3)
	v_pk_mul_f32 v[16:17], v[16:17], v[172:173]
	s_waitcnt lgkmcnt(2)
	v_pk_mul_f32 v[12:13], v[12:13], v[176:177]
	s_waitcnt lgkmcnt(1)
	v_pk_mul_f32 v[8:9], v[8:9], v[200:201]
	s_waitcnt lgkmcnt(0)
	v_pk_mul_f32 v[4:5], v[4:5], v[204:205]
	v_pk_mul_f32 v[14:15], v[14:15], v[170:171]
	v_pk_mul_f32 v[10:11], v[10:11], v[174:175]
	v_pk_mul_f32 v[6:7], v[6:7], v[198:199]
	v_pk_mul_f32 v[2:3], v[2:3], v[202:203]
	v_pk_mul_f32 v[32:33], v[32:33], v[172:173]
	v_pk_mul_f32 v[28:29], v[28:29], v[176:177]
	v_pk_mul_f32 v[24:25], v[24:25], v[200:201]
	v_pk_mul_f32 v[20:21], v[20:21], v[204:205]
	v_pk_mul_f32 v[30:31], v[30:31], v[170:171]
	v_pk_mul_f32 v[26:27], v[26:27], v[174:175]
	v_pk_mul_f32 v[22:23], v[22:23], v[198:199]
	v_pk_mul_f32 v[18:19], v[18:19], v[202:203]
	v_pk_mul_f32 v[48:49], v[48:49], v[172:173]
	v_pk_mul_f32 v[44:45], v[44:45], v[176:177]
	v_pk_mul_f32 v[40:41], v[40:41], v[200:201]
	v_pk_mul_f32 v[36:37], v[36:37], v[204:205]
	v_pk_mul_f32 v[46:47], v[46:47], v[170:171]
	v_pk_mul_f32 v[42:43], v[42:43], v[174:175]
	v_pk_mul_f32 v[38:39], v[38:39], v[198:199]
	v_pk_mul_f32 v[34:35], v[34:35], v[202:203]
	v_pk_mul_f32 v[64:65], v[64:65], v[172:173]
	v_pk_mul_f32 v[60:61], v[60:61], v[176:177]
	v_pk_mul_f32 v[56:57], v[56:57], v[200:201]
	v_pk_mul_f32 v[52:53], v[52:53], v[204:205]
	v_pk_mul_f32 v[62:63], v[62:63], v[170:171]
	v_pk_mul_f32 v[58:59], v[58:59], v[174:175]
	v_pk_mul_f32 v[54:55], v[54:55], v[198:199]
	v_pk_mul_f32 v[50:51], v[50:51], v[202:203]
	v_pk_mul_f32 v[80:81], v[80:81], v[172:173]
	v_pk_mul_f32 v[76:77], v[76:77], v[176:177]
	v_pk_mul_f32 v[72:73], v[72:73], v[200:201]
	v_pk_mul_f32 v[68:69], v[68:69], v[204:205]
	v_pk_mul_f32 v[78:79], v[78:79], v[170:171]
	v_pk_mul_f32 v[74:75], v[74:75], v[174:175]
	v_pk_mul_f32 v[70:71], v[70:71], v[198:199]
	v_pk_mul_f32 v[66:67], v[66:67], v[202:203]

; #define PBAR_V0() asm volatile("s_waitcnt vmcnt(0) lgkmcnt(0)\n\ts_barrier" ::: "memory")
; #define PBAR_V0() asm volatile("s_waitcnt vmcnt(0) lgkmcnt(0)\n\ts_barrier" ::: "memory")
; __device__ __forceinline__ void attn_unit_f8(const bf16_t* __restrict__ Q, const bf16_t* __restrict__ Kb, const unsigned char* __restrict__ V8, bf16_t* __restrict__ O, ...
;     ...
;   PBAR_V0();
;   if (pref_out) { const char* Khn = (const char*)Kb + hn * 128;
;     pg8::glds16_s(Khn + (size_t)kc0n * DM, koff, ldsK); pg8::glds16_s(Khn + (size_t)(kc0n + 64) * DM, koff, ldsK + 8192u); pg8::glds16_s((const char*)V8n, voff, ldsV + 8192u);
;     const unsigned char* Qw = (const unsigned char*)Q + (size_t)(qrow0n + wq * QBLK + r32) * DM + hn * 128 + cq * 64 + hi * 32;
;     const u32x4 qa = *reinterpret_cast<const u32x4*>(Qw), qb = *reinterpret_cast<const u32x4*>(Qw + 16); qf = (i32x8){(int)qa.x, (int)qa.y, (int)qa.z, (int)qa.w, (int)qb.x, (int)qb.y, (int)qb.z, (int)qb.w}; }
; __device__ __forceinline__ void attn_phase(Frame& F) {
;     ...
;     for (int id = vcu; id < 4096; id += F.G) {
;         { const int bh = id >> 6, qb = id & 63, b = bh >> 3, h = bh & 7;
;           const int idn = id + F.G; const bool hasn = idn < 4096; const int bhn = hasn ? (idn >> 6) : bh, bn = bhn >> 3, hn = bhn & 7, qbn = hasn ? (idn & 63) : qb;
;             att::attn_unit_f8(Q, Kb, V8 + (size_t)bh * 132 * 8192, O, NCTX + b * SEQ + qb * 128, b * CTXL, NCTX + b * SEQ, 4 + SEQ / 64, h, lam, subg, F.ldsg, F.wave0,
;                               id != vcu, hasn, V8 + (size_t)bhn * 132 * 8192, bn * CTXL, hn, NCTX + bn * SEQ + qbn * 128, qfu); }
.LBB0_1355:
	s_add_i32 s24, s24, s8
	s_cmpk_lt_i32 s24, 0x1000
	s_cselect_b64 s[0:1], -1, 0
	s_cmpk_gt_i32 s24, 0xfff
	s_waitcnt vmcnt(0) lgkmcnt(0)
	s_barrier
	s_cselect_b64 s[2:3], -1, 0
	s_and_b64 vcc, exec, s[2:3]
	s_cbranch_vccnz .LBB0_1357
	s_ashr_i32 s12, s24, 6
	s_and_b64 s[26:27], s[0:1], exec
	s_cselect_b32 s13, s12, s53
	s_ashr_i32 s14, s13, 3
	s_and_b32 s15, s24, 63
	s_and_b64 s[0:1], s[0:1], exec
	s_mul_hi_i32 s1, s13, 0x108000
	s_mul_i32 s13, s13, 0x108000
	s_cselect_b32 s15, s15, s54
	s_add_u32 s0, s20, s13
	s_addc_u32 s1, s21, s1
	s_lshl_b32 s26, s14, 8
	s_lshl_b32 s13, s14, 13
	s_lshl_b32 s14, s15, 7
	s_or_b32 s13, s14, s13
	s_lshl_b32 s14, s52, 5
	s_lshl_b32 s12, s12, 7
	s_or_b32 s13, s13, s14
	s_and_b32 s48, s12, 0x380
	s_add_u32 s12, s10, s48
	s_addc_u32 s14, s11, 0
	s_ashr_i32 s27, s26, 31
	s_lshl_b64 s[58:59], s[26:27], 10
	s_add_u32 s58, s12, s58
	s_addc_u32 s59, s14, s59
	s_or_b32 s26, s26, 64
	s_ashr_i32 s27, s26, 31
	s_lshl_b64 s[26:27], s[26:27], 10
	s_add_u32 s26, s12, s26
	s_addc_u32 s27, s14, s27
	s_cmp_lg_u32 s56, -1
	s_cselect_b32 s12, s56, 0
	s_add_i32 s12, s12, s55
	s_addk_i32 s12, 0x2000
	s_mov_b32 m0, s57
	s_nop 0
	global_load_lds_dwordx4 v148, s[58:59]
	s_cmp_lg_u32 0, -1
	s_mov_b32 m0, s12
	s_nop 0
	global_load_lds_dwordx4 v148, s[26:27]
	s_cselect_b32 s12, 0, 0
	s_addk_i32 s13, 0x800
	v_or_b32_e32 v82, s13, v178
	v_ashrrev_i32_e32 v83, 31, v82
	s_add_i32 s12, s12, s55
	v_lshlrev_b64 v[82:83], 10, v[82:83]
	s_mov_b32 s49, s19
	s_addk_i32 s12, 0x2000
	s_mov_b32 m0, s12
	s_nop 0
	global_load_lds_dwordx4 v147, s[0:1]
	v_lshl_add_u64 v[82:83], s[6:7], 0, v[82:83]
	s_lshl_b32 s0, s51, 6
	v_lshl_add_u64 v[82:83], v[82:83], 0, s[48:49]
	s_ashr_i32 s1, s0, 31
	v_lshl_add_u64 v[82:83], v[82:83], 0, s[0:1]
	v_mov_b32_e32 v181, v1
	v_lshl_add_u64 v[82:83], v[82:83], 0, v[180:181]
	global_load_dwordx4 v[154:157], v[82:83], off
	global_load_dwordx4 v[158:161], v[82:83], off offset:16
